# baseline (speedup 1.0000x reference)
.Lpf_kv:
	s_lshr_b32 s8, s3, 2
	s_add_u32 s21, s8, 1
	s_and_b32 s8, s3, 3
	s_and_b32 s9, s8, 1
	s_lshr_b32 s8, s8, 1
	s_lshl_b32 s8, s8, 1
	s_add_u32 s8, s8, s6
	s_mul_i32 s10, s8, 0x120
	s_lshl_b32 s11, s9, 11
	s_add_u32 s11, s11, s10
	s_cmp_eq_u32 s21, 1
	s_cselect_b32 s12, s26, s28
	s_cselect_b32 s13, s27, s29
	s_cselect_b32 s14, s36, s38
	s_cselect_b32 s15, s37, s39
	s_mov_b32 s16, s42
	s_mov_b32 s17, s43
	s_cselect_b32 s22, s46, s48
	s_cselect_b32 s23, s47, s49
	s_mov_b32 s19, 1.0
.Lpf_common:
	s_mul_i32 s8, s11, 0x880
	s_mul_hi_u32 s24, s11, 0x880
	s_add_u32 s12, s12, s8
	s_addc_u32 s13, s13, s24
	s_lshl_b32 s8, s21, 10
	s_lshl_b32 s24, s5, 7
	s_add_u32 s8, s8, s24
	s_mul_i32 s8, s8, 0x880
	s_add_u32 s6, s30, s8
	s_addc_u32 s7, s31, 0
	s_mov_b32 s4, s12
	s_mov_b32 s5, s13
	s_and_b32 s24, s18, 1
	s_lshr_b32 s25, s18, 1
	s_lshr_b32 s26, s2, 3
	s_and_b32 s26, s26, 7
	s_lshl_b32 s26, s26, 1
	s_add_u32 s26, s26, s24
	s_lshl_b32 s27, s9, 4
	s_add_u32 s27, s27, s26
	s_lshl_b32 s28, s18, 10
	s_lshl_b32 s8, s26, 8
	s_add_u32 s14, s14, s8
	s_addc_u32 s15, s15, 0
	s_lshl_b32 s8, s27, 18
	s_add_u32 s22, s22, s8
	s_addc_u32 s23, s23, 0
	v_lshrrev_b32_e32 v5, 3, v1
	v_lshl_add_u32 v5, v2, 3, v5
	v_mul_u32_u24_e32 v5, 0x880, v5
	v_and_b32_e32 v6, 7, v1
	v_lshrrev_b32_e32 v7, 4, v1
	v_and_b32_e32 v8, 1, v2
	v_lshl_or_b32 v7, v8, 2, v7
	v_xor_b32_e32 v6, v6, v7
	v_lshl_add_u32 v10, v6, 4, v5
	v_add_u32_e32 v11, 0x22000, v10
	v_add_u32_e32 v12, 0x44000, v10
	v_add_u32_e32 v13, 0x66000, v10
	v_add_u32_e32 v14, 0x88000, v10
	v_lshrrev_b32_e32 v5, 1, v3
	v_xor_b32_e32 v6, v4, v5
	v_lshlrev_b32_e32 v6, 4, v6
	v_or_b32_e32 v7, 4, v4
	v_xor_b32_e32 v7, v7, v5
	v_lshlrev_b32_e32 v7, 4, v7
	v_lshl_add_u32 v9, v8, 6, v3
	v_lshlrev_b32_e32 v9, 7, v9
	v_and_b32_e32 v5, 1, v4
	v_lshl_add_u32 v5, v5, 5, v3
	v_lshlrev_b32_e32 v5, 4, v5
	v_lshrrev_b32_e32 v8, 1, v4
	v_lshl_add_u32 v23, v8, 3, v5
	s_cmp_eq_u32 s21, 0
	s_cbranch_scc1 .Lpf_vQ
	s_cmp_lt_u32 s18, 4
	s_cselect_b32 s8, 1, 0
	s_cmp_eq_u32 s21, 1
	s_cbranch_scc0 .Lpf_vV
	s_cmp_eq_u32 s8, 1
	s_cbranch_scc1 .Lpf_vKA
	s_branch .Lpf_vKB

.Lpf_vQ:
	s_add_u32 m0, s28, 0x0
	s_nop 0
	global_load_lds_dwordx4 v10, s[4:5]
	s_add_u32 m0, s28, 0x2000
	s_nop 0
	global_load_lds_dwordx4 v11, s[4:5]
	s_add_u32 m0, s28, 0x4000
	s_nop 0
	global_load_lds_dwordx4 v12, s[4:5]
	s_add_u32 m0, s28, 0x6000
	s_nop 0
	global_load_lds_dwordx4 v13, s[4:5]
	s_add_u32 s4, s4, s20
	s_addc_u32 s5, s5, 0
	s_add_u32 m0, s28, 0x8000
	s_nop 0
	global_load_lds_dwordx4 v10, s[6:7]
	s_add_u32 m0, s28, 0xa000
	s_nop 0
	global_load_lds_dwordx4 v11, s[6:7]
	s_add_u32 s6, s6, s20
	s_addc_u32 s7, s7, 0
	s_add_u32 m0, s28, 0xc000
	s_nop 0
	global_load_lds_dwordx4 v10, s[4:5]
	s_add_u32 m0, s28, 0xe000
	s_nop 0
	global_load_lds_dwordx4 v11, s[4:5]
	s_add_u32 m0, s28, 0x10000
	s_nop 0
	global_load_lds_dwordx4 v12, s[4:5]
	s_add_u32 m0, s28, 0x12000
	s_nop 0
	global_load_lds_dwordx4 v13, s[4:5]
	s_add_u32 s4, s4, s20
	s_addc_u32 s5, s5, 0
	s_add_u32 m0, s28, 0x14000
	s_nop 0
	global_load_lds_dwordx4 v10, s[6:7]
	s_add_u32 m0, s28, 0x16000
	s_nop 0
	global_load_lds_dwordx4 v11, s[6:7]
	s_add_u32 s6, s6, s20
	s_addc_u32 s7, s7, 0
	s_add_u32 m0, s28, 0x18000
	s_nop 0
	global_load_lds_dwordx4 v10, s[4:5]
	s_add_u32 m0, s28, 0x1a000
	s_nop 0
	global_load_lds_dwordx4 v11, s[4:5]
	s_add_u32 m0, s28, 0x1c000
	s_nop 0
	global_load_lds_dwordx4 v12, s[4:5]
	s_add_u32 m0, s28, 0x1e000
	s_nop 0
	global_load_lds_dwordx4 v13, s[4:5]
	s_add_u32 s4, s4, s20
	s_addc_u32 s5, s5, 0
	s_add_u32 m0, s28, 0x20000
	s_nop 0
	global_load_lds_dwordx4 v10, s[6:7]
	s_add_u32 m0, s28, 0x22000
	s_nop 0
	global_load_lds_dwordx4 v11, s[6:7]
	s_add_u32 s6, s6, s20
	s_addc_u32 s7, s7, 0
	s_lshl_b32 s25, s25, 6
	s_add_u32 s29, s10, s25
	s_lshr_b32 s29, s29, 4
	v_add_u32_e32 v5, s25, v3
	v_lshlrev_b32_e32 v5, 7, v5
	v_add_u32_e32 v15, v5, v6
	v_add_u32_e32 v16, v5, v7
	v_add_u32_e32 v5, 0x8000, v9
	v_add_u32_e32 v17, v5, v6
	v_add_u32_e32 v18, v5, v7
	v_add_u32_e32 v19, 0x18000, v15
	v_add_u32_e32 v20, 0x18000, v16
	v_add_u32_e32 v21, 0x18000, v17
	v_add_u32_e32 v22, 0x18000, v18
	v_lshlrev_b32_e32 v5, 4, v4
	global_load_dwordx4 v[24:27], v5, s[14:15] offset:0
	global_load_dwordx4 v[28:31], v5, s[14:15] offset:64
	global_load_dwordx4 v[32:35], v5, s[14:15] offset:128
	global_load_dwordx4 v[36:39], v5, s[14:15] offset:192
	global_load_dwordx4 v[40:43], v5, s[16:17] offset:0
	global_load_dwordx4 v[44:47], v5, s[16:17] offset:64
	global_load_dwordx4 v[48:51], v5, s[16:17] offset:128
	global_load_dwordx4 v[52:55], v5, s[16:17] offset:192
	s_waitcnt vmcnt(20) lgkmcnt(0)
	s_barrier
	s_waitcnt lgkmcnt(7)
	ds_read_b128 v[136:139], v15
	ds_read_b128 v[156:159], v17
	ds_read_b128 v[160:163], v17 offset:2048
	ds_read_b128 v[164:167], v17 offset:4096
	ds_read_b128 v[168:171], v17 offset:6144
	ds_read_b128 v[140:143], v15 offset:2048
	ds_read_b128 v[144:147], v15 offset:4096
	ds_read_b128 v[148:151], v15 offset:6144
	s_waitcnt lgkmcnt(7)
	ds_read_b128 v[172:175], v16
	ds_read_b128 v[192:195], v18
	ds_read_b128 v[196:199], v18 offset:2048
	ds_read_b128 v[200:203], v18 offset:4096
	ds_read_b128 v[204:207], v18 offset:6144
	ds_read_b128 v[176:179], v16 offset:2048
	ds_read_b128 v[180:183], v16 offset:4096
	ds_read_b128 v[184:187], v16 offset:6144
	s_waitcnt lgkmcnt(14)
	v_mfma_f32_16x16x32_f16 v[56:59], v[156:159], v[136:139], 0
	s_waitcnt lgkmcnt(13)
	v_mfma_f32_16x16x32_f16 v[60:63], v[160:163], v[136:139], 0
	s_waitcnt lgkmcnt(12)
	v_mfma_f32_16x16x32_f16 v[64:67], v[164:167], v[136:139], 0
	s_waitcnt lgkmcnt(11)
	v_mfma_f32_16x16x32_f16 v[68:71], v[168:171], v[136:139], 0
	s_waitcnt lgkmcnt(10)
	v_mfma_f32_16x16x32_f16 v[72:75], v[156:159], v[140:143], 0
	v_mfma_f32_16x16x32_f16 v[76:79], v[160:163], v[140:143], 0
	v_mfma_f32_16x16x32_f16 v[80:83], v[164:167], v[140:143], 0
	v_mfma_f32_16x16x32_f16 v[84:87], v[168:171], v[140:143], 0
	s_waitcnt lgkmcnt(9)
	v_mfma_f32_16x16x32_f16 v[88:91], v[156:159], v[144:147], 0
	v_mfma_f32_16x16x32_f16 v[92:95], v[160:163], v[144:147], 0
	v_mfma_f32_16x16x32_f16 v[96:99], v[164:167], v[144:147], 0
	v_mfma_f32_16x16x32_f16 v[100:103], v[168:171], v[144:147], 0
	s_waitcnt lgkmcnt(8)
	v_mfma_f32_16x16x32_f16 v[104:107], v[156:159], v[148:151], 0
	v_mfma_f32_16x16x32_f16 v[108:111], v[160:163], v[148:151], 0
	v_mfma_f32_16x16x32_f16 v[112:115], v[164:167], v[148:151], 0
	v_mfma_f32_16x16x32_f16 v[116:119], v[168:171], v[148:151], 0
	s_waitcnt vmcnt(14) lgkmcnt(0)
	s_barrier
	s_waitcnt lgkmcnt(7)
	ds_read_b128 v[136:139], v15 offset:49152
	ds_read_b128 v[156:159], v17 offset:49152
	ds_read_b128 v[160:163], v17 offset:51200
	ds_read_b128 v[164:167], v17 offset:53248
	ds_read_b128 v[168:171], v17 offset:55296
	ds_read_b128 v[140:143], v15 offset:51200
	ds_read_b128 v[144:147], v15 offset:53248
	ds_read_b128 v[148:151], v15 offset:55296
	s_waitcnt lgkmcnt(14)
	v_mfma_f32_16x16x32_f16 v[56:59], v[192:195], v[172:175], v[56:59]
	s_add_u32 m0, s28, 0x0
	s_nop 0
	global_load_lds_dwordx4 v10, s[4:5]
	s_waitcnt lgkmcnt(13)
	v_mfma_f32_16x16x32_f16 v[60:63], v[196:199], v[172:175], v[60:63]
	s_waitcnt lgkmcnt(12)
	v_mfma_f32_16x16x32_f16 v[64:67], v[200:203], v[172:175], v[64:67]
	s_waitcnt lgkmcnt(11)
	v_mfma_f32_16x16x32_f16 v[68:71], v[204:207], v[172:175], v[68:71]
	s_waitcnt lgkmcnt(10)
	v_mfma_f32_16x16x32_f16 v[72:75], v[192:195], v[176:179], v[72:75]
	v_mfma_f32_16x16x32_f16 v[76:79], v[196:199], v[176:179], v[76:79]
	s_add_u32 m0, s28, 0x2000
	s_nop 0
	global_load_lds_dwordx4 v11, s[4:5]
	v_mfma_f32_16x16x32_f16 v[80:83], v[200:203], v[176:179], v[80:83]
	v_mfma_f32_16x16x32_f16 v[84:87], v[204:207], v[176:179], v[84:87]
	s_waitcnt lgkmcnt(9)
	v_mfma_f32_16x16x32_f16 v[88:91], v[192:195], v[180:183], v[88:91]
	v_mfma_f32_16x16x32_f16 v[92:95], v[196:199], v[180:183], v[92:95]
	v_mfma_f32_16x16x32_f16 v[96:99], v[200:203], v[180:183], v[96:99]
	s_add_u32 m0, s28, 0x4000
	s_nop 0
	global_load_lds_dwordx4 v12, s[4:5]
	v_mfma_f32_16x16x32_f16 v[100:103], v[204:207], v[180:183], v[100:103]
	s_waitcnt lgkmcnt(8)
	v_mfma_f32_16x16x32_f16 v[104:107], v[192:195], v[184:187], v[104:107]
	v_mfma_f32_16x16x32_f16 v[108:111], v[196:199], v[184:187], v[108:111]
	v_mfma_f32_16x16x32_f16 v[112:115], v[200:203], v[184:187], v[112:115]
	v_mfma_f32_16x16x32_f16 v[116:119], v[204:207], v[184:187], v[116:119]
	s_waitcnt lgkmcnt(7)
	ds_read_b128 v[172:175], v16 offset:49152
	ds_read_b128 v[192:195], v18 offset:49152
	ds_read_b128 v[196:199], v18 offset:51200
	ds_read_b128 v[200:203], v18 offset:53248
	ds_read_b128 v[204:207], v18 offset:55296
	ds_read_b128 v[176:179], v16 offset:51200
	ds_read_b128 v[180:183], v16 offset:53248
	ds_read_b128 v[184:187], v16 offset:55296
	s_waitcnt lgkmcnt(14)
	v_mfma_f32_16x16x32_f16 v[56:59], v[156:159], v[136:139], v[56:59]
	s_add_u32 m0, s28, 0x6000
	s_nop 0
	global_load_lds_dwordx4 v13, s[4:5]
	s_add_u32 s4, s4, s20
	s_addc_u32 s5, s5, 0
	s_waitcnt lgkmcnt(13)
	v_mfma_f32_16x16x32_f16 v[60:63], v[160:163], v[136:139], v[60:63]
	s_waitcnt lgkmcnt(12)
	v_mfma_f32_16x16x32_f16 v[64:67], v[164:167], v[136:139], v[64:67]
	s_waitcnt lgkmcnt(11)
	v_mfma_f32_16x16x32_f16 v[68:71], v[168:171], v[136:139], v[68:71]
	s_waitcnt lgkmcnt(10)
	v_mfma_f32_16x16x32_f16 v[72:75], v[156:159], v[140:143], v[72:75]
	v_mfma_f32_16x16x32_f16 v[76:79], v[160:163], v[140:143], v[76:79]
	s_add_u32 m0, s28, 0x8000
	s_nop 0
	global_load_lds_dwordx4 v10, s[6:7]
	v_mfma_f32_16x16x32_f16 v[80:83], v[164:167], v[140:143], v[80:83]
	v_mfma_f32_16x16x32_f16 v[84:87], v[168:171], v[140:143], v[84:87]
	s_waitcnt lgkmcnt(9)
	v_mfma_f32_16x16x32_f16 v[88:91], v[156:159], v[144:147], v[88:91]
	v_mfma_f32_16x16x32_f16 v[92:95], v[160:163], v[144:147], v[92:95]
	v_mfma_f32_16x16x32_f16 v[96:99], v[164:167], v[144:147], v[96:99]
	s_add_u32 m0, s28, 0xa000
	s_nop 0
	global_load_lds_dwordx4 v11, s[6:7]
	s_add_u32 s6, s6, s20
	s_addc_u32 s7, s7, 0
	v_mfma_f32_16x16x32_f16 v[100:103], v[168:171], v[144:147], v[100:103]
	s_waitcnt lgkmcnt(8)
	v_mfma_f32_16x16x32_f16 v[104:107], v[156:159], v[148:151], v[104:107]
	v_mfma_f32_16x16x32_f16 v[108:111], v[160:163], v[148:151], v[108:111]
	v_mfma_f32_16x16x32_f16 v[112:115], v[164:167], v[148:151], v[112:115]
	v_mfma_f32_16x16x32_f16 v[116:119], v[168:171], v[148:151], v[116:119]
	s_waitcnt vmcnt(6) lgkmcnt(0)
	s_barrier
	s_waitcnt lgkmcnt(7)
	ds_read_b128 v[136:139], v19
	ds_read_b128 v[156:159], v21
	ds_read_b128 v[160:163], v21 offset:2048
	ds_read_b128 v[164:167], v21 offset:4096
	ds_read_b128 v[168:171], v21 offset:6144
	ds_read_b128 v[140:143], v19 offset:2048
	ds_read_b128 v[144:147], v19 offset:4096
	ds_read_b128 v[148:151], v19 offset:6144
	s_waitcnt lgkmcnt(14)
	v_mfma_f32_16x16x32_f16 v[56:59], v[192:195], v[172:175], v[56:59]
	s_add_u32 m0, s28, 0xc000
	s_nop 0
	global_load_lds_dwordx4 v10, s[4:5]
	s_waitcnt lgkmcnt(13)
	v_mfma_f32_16x16x32_f16 v[60:63], v[196:199], v[172:175], v[60:63]
	s_waitcnt lgkmcnt(12)
	v_mfma_f32_16x16x32_f16 v[64:67], v[200:203], v[172:175], v[64:67]
	s_waitcnt lgkmcnt(11)
	v_mfma_f32_16x16x32_f16 v[68:71], v[204:207], v[172:175], v[68:71]
	s_waitcnt lgkmcnt(10)
	v_mfma_f32_16x16x32_f16 v[72:75], v[192:195], v[176:179], v[72:75]
	v_mfma_f32_16x16x32_f16 v[76:79], v[196:199], v[176:179], v[76:79]
	s_add_u32 m0, s28, 0xe000
	s_nop 0
	global_load_lds_dwordx4 v11, s[4:5]
	v_mfma_f32_16x16x32_f16 v[80:83], v[200:203], v[176:179], v[80:83]
	v_mfma_f32_16x16x32_f16 v[84:87], v[204:207], v[176:179], v[84:87]
	s_waitcnt lgkmcnt(9)
	v_mfma_f32_16x16x32_f16 v[88:91], v[192:195], v[180:183], v[88:91]
	v_mfma_f32_16x16x32_f16 v[92:95], v[196:199], v[180:183], v[92:95]
	v_mfma_f32_16x16x32_f16 v[96:99], v[200:203], v[180:183], v[96:99]
	s_add_u32 m0, s28, 0x10000
	s_nop 0
	global_load_lds_dwordx4 v12, s[4:5]
	v_mfma_f32_16x16x32_f16 v[100:103], v[204:207], v[180:183], v[100:103]
	s_waitcnt lgkmcnt(8)
	v_mfma_f32_16x16x32_f16 v[104:107], v[192:195], v[184:187], v[104:107]
	v_mfma_f32_16x16x32_f16 v[108:111], v[196:199], v[184:187], v[108:111]
	v_mfma_f32_16x16x32_f16 v[112:115], v[200:203], v[184:187], v[112:115]
	v_mfma_f32_16x16x32_f16 v[116:119], v[204:207], v[184:187], v[116:119]
	s_waitcnt lgkmcnt(7)
	ds_read_b128 v[172:175], v20
	ds_read_b128 v[192:195], v22
	ds_read_b128 v[196:199], v22 offset:2048
	ds_read_b128 v[200:203], v22 offset:4096
	ds_read_b128 v[204:207], v22 offset:6144
	ds_read_b128 v[176:179], v20 offset:2048
	ds_read_b128 v[180:183], v20 offset:4096
	ds_read_b128 v[184:187], v20 offset:6144
	s_waitcnt lgkmcnt(14)
	v_mfma_f32_16x16x32_f16 v[56:59], v[156:159], v[136:139], v[56:59]
	s_add_u32 m0, s28, 0x12000
	s_nop 0
	global_load_lds_dwordx4 v13, s[4:5]
	s_add_u32 s4, s4, s20
	s_addc_u32 s5, s5, 0
	s_waitcnt lgkmcnt(13)
	v_mfma_f32_16x16x32_f16 v[60:63], v[160:163], v[136:139], v[60:63]
	s_waitcnt lgkmcnt(12)
	v_mfma_f32_16x16x32_f16 v[64:67], v[164:167], v[136:139], v[64:67]
	s_waitcnt lgkmcnt(11)
	v_mfma_f32_16x16x32_f16 v[68:71], v[168:171], v[136:139], v[68:71]
	s_waitcnt lgkmcnt(10)
	v_mfma_f32_16x16x32_f16 v[72:75], v[156:159], v[140:143], v[72:75]
	v_mfma_f32_16x16x32_f16 v[76:79], v[160:163], v[140:143], v[76:79]
	s_add_u32 m0, s28, 0x14000
	s_nop 0
	global_load_lds_dwordx4 v10, s[6:7]
	v_mfma_f32_16x16x32_f16 v[80:83], v[164:167], v[140:143], v[80:83]
	v_mfma_f32_16x16x32_f16 v[84:87], v[168:171], v[140:143], v[84:87]
	s_waitcnt lgkmcnt(9)
	v_mfma_f32_16x16x32_f16 v[88:91], v[156:159], v[144:147], v[88:91]
	v_mfma_f32_16x16x32_f16 v[92:95], v[160:163], v[144:147], v[92:95]
	v_mfma_f32_16x16x32_f16 v[96:99], v[164:167], v[144:147], v[96:99]
	s_add_u32 m0, s28, 0x16000
	s_nop 0
	global_load_lds_dwordx4 v11, s[6:7]
	s_add_u32 s6, s6, s20
	s_addc_u32 s7, s7, 0
	v_mfma_f32_16x16x32_f16 v[100:103], v[168:171], v[144:147], v[100:103]
	s_waitcnt lgkmcnt(8)
	v_mfma_f32_16x16x32_f16 v[104:107], v[156:159], v[148:151], v[104:107]
	v_mfma_f32_16x16x32_f16 v[108:111], v[160:163], v[148:151], v[108:111]
	v_mfma_f32_16x16x32_f16 v[112:115], v[164:167], v[148:151], v[112:115]
	v_mfma_f32_16x16x32_f16 v[116:119], v[168:171], v[148:151], v[116:119]
	s_waitcnt vmcnt(6) lgkmcnt(0)
	s_barrier
	s_waitcnt lgkmcnt(7)
	ds_read_b128 v[136:139], v15
	ds_read_b128 v[156:159], v17
	ds_read_b128 v[160:163], v17 offset:2048
	ds_read_b128 v[164:167], v17 offset:4096
	ds_read_b128 v[168:171], v17 offset:6144
	ds_read_b128 v[140:143], v15 offset:2048
	ds_read_b128 v[144:147], v15 offset:4096
	ds_read_b128 v[148:151], v15 offset:6144
	s_waitcnt lgkmcnt(14)
	v_mfma_f32_16x16x32_f16 v[56:59], v[192:195], v[172:175], v[56:59]
	s_add_u32 m0, s28, 0x18000
	s_nop 0
	global_load_lds_dwordx4 v10, s[4:5]
	s_waitcnt lgkmcnt(13)
	v_mfma_f32_16x16x32_f16 v[60:63], v[196:199], v[172:175], v[60:63]
	s_waitcnt lgkmcnt(12)
	v_mfma_f32_16x16x32_f16 v[64:67], v[200:203], v[172:175], v[64:67]
	s_waitcnt lgkmcnt(11)
	v_mfma_f32_16x16x32_f16 v[68:71], v[204:207], v[172:175], v[68:71]
	s_waitcnt lgkmcnt(10)
	v_mfma_f32_16x16x32_f16 v[72:75], v[192:195], v[176:179], v[72:75]
	v_mfma_f32_16x16x32_f16 v[76:79], v[196:199], v[176:179], v[76:79]
	s_add_u32 m0, s28, 0x1a000
	s_nop 0
	global_load_lds_dwordx4 v11, s[4:5]
	v_mfma_f32_16x16x32_f16 v[80:83], v[200:203], v[176:179], v[80:83]
	v_mfma_f32_16x16x32_f16 v[84:87], v[204:207], v[176:179], v[84:87]
	s_waitcnt lgkmcnt(9)
	v_mfma_f32_16x16x32_f16 v[88:91], v[192:195], v[180:183], v[88:91]
	v_mfma_f32_16x16x32_f16 v[92:95], v[196:199], v[180:183], v[92:95]
	v_mfma_f32_16x16x32_f16 v[96:99], v[200:203], v[180:183], v[96:99]
	s_add_u32 m0, s28, 0x1c000
	s_nop 0
	global_load_lds_dwordx4 v12, s[4:5]
	v_mfma_f32_16x16x32_f16 v[100:103], v[204:207], v[180:183], v[100:103]
	s_waitcnt lgkmcnt(8)
	v_mfma_f32_16x16x32_f16 v[104:107], v[192:195], v[184:187], v[104:107]
	v_mfma_f32_16x16x32_f16 v[108:111], v[196:199], v[184:187], v[108:111]
	v_mfma_f32_16x16x32_f16 v[112:115], v[200:203], v[184:187], v[112:115]
	v_mfma_f32_16x16x32_f16 v[116:119], v[204:207], v[184:187], v[116:119]
	s_waitcnt lgkmcnt(7)
	ds_read_b128 v[172:175], v16
	ds_read_b128 v[192:195], v18
	ds_read_b128 v[196:199], v18 offset:2048
	ds_read_b128 v[200:203], v18 offset:4096
	ds_read_b128 v[204:207], v18 offset:6144
	ds_read_b128 v[176:179], v16 offset:2048
	ds_read_b128 v[180:183], v16 offset:4096
	ds_read_b128 v[184:187], v16 offset:6144
	s_waitcnt lgkmcnt(14)
	v_mfma_f32_16x16x32_f16 v[56:59], v[156:159], v[136:139], v[56:59]
	s_add_u32 m0, s28, 0x1e000
	s_nop 0
	global_load_lds_dwordx4 v13, s[4:5]
	s_add_u32 s4, s4, s20
	s_addc_u32 s5, s5, 0
	s_waitcnt lgkmcnt(13)
	v_mfma_f32_16x16x32_f16 v[60:63], v[160:163], v[136:139], v[60:63]
	s_waitcnt lgkmcnt(12)
	v_mfma_f32_16x16x32_f16 v[64:67], v[164:167], v[136:139], v[64:67]
	s_waitcnt lgkmcnt(11)
	v_mfma_f32_16x16x32_f16 v[68:71], v[168:171], v[136:139], v[68:71]
	s_waitcnt lgkmcnt(10)
	v_mfma_f32_16x16x32_f16 v[72:75], v[156:159], v[140:143], v[72:75]
	v_mfma_f32_16x16x32_f16 v[76:79], v[160:163], v[140:143], v[76:79]
	s_add_u32 m0, s28, 0x20000
	s_nop 0
	global_load_lds_dwordx4 v10, s[6:7]
	v_mfma_f32_16x16x32_f16 v[80:83], v[164:167], v[140:143], v[80:83]
	v_mfma_f32_16x16x32_f16 v[84:87], v[168:171], v[140:143], v[84:87]
	s_waitcnt lgkmcnt(9)
	v_mfma_f32_16x16x32_f16 v[88:91], v[156:159], v[144:147], v[88:91]
	v_mfma_f32_16x16x32_f16 v[92:95], v[160:163], v[144:147], v[92:95]
	v_mfma_f32_16x16x32_f16 v[96:99], v[164:167], v[144:147], v[96:99]
	s_add_u32 m0, s28, 0x22000
	s_nop 0
	global_load_lds_dwordx4 v11, s[6:7]
	s_add_u32 s6, s6, s20
	s_addc_u32 s7, s7, 0
	v_mfma_f32_16x16x32_f16 v[100:103], v[168:171], v[144:147], v[100:103]
	s_waitcnt lgkmcnt(8)
	v_mfma_f32_16x16x32_f16 v[104:107], v[156:159], v[148:151], v[104:107]
	v_mfma_f32_16x16x32_f16 v[108:111], v[160:163], v[148:151], v[108:111]
	v_mfma_f32_16x16x32_f16 v[112:115], v[164:167], v[148:151], v[112:115]
	v_mfma_f32_16x16x32_f16 v[116:119], v[168:171], v[148:151], v[116:119]
	s_waitcnt vmcnt(6) lgkmcnt(0)
	s_barrier
	s_waitcnt lgkmcnt(7)
	ds_read_b128 v[136:139], v15 offset:49152
	ds_read_b128 v[156:159], v17 offset:49152
	ds_read_b128 v[160:163], v17 offset:51200
	ds_read_b128 v[164:167], v17 offset:53248
	ds_read_b128 v[168:171], v17 offset:55296
	ds_read_b128 v[140:143], v15 offset:51200
	ds_read_b128 v[144:147], v15 offset:53248
	ds_read_b128 v[148:151], v15 offset:55296
	s_waitcnt lgkmcnt(14)
	v_mfma_f32_16x16x32_f16 v[56:59], v[192:195], v[172:175], v[56:59]
	s_add_u32 m0, s28, 0x0
	s_nop 0
	global_load_lds_dwordx4 v10, s[4:5]
	s_waitcnt lgkmcnt(13)
	v_mfma_f32_16x16x32_f16 v[60:63], v[196:199], v[172:175], v[60:63]
	s_waitcnt lgkmcnt(12)
	v_mfma_f32_16x16x32_f16 v[64:67], v[200:203], v[172:175], v[64:67]
	s_waitcnt lgkmcnt(11)
	v_mfma_f32_16x16x32_f16 v[68:71], v[204:207], v[172:175], v[68:71]
	s_waitcnt lgkmcnt(10)
	v_mfma_f32_16x16x32_f16 v[72:75], v[192:195], v[176:179], v[72:75]
	v_mfma_f32_16x16x32_f16 v[76:79], v[196:199], v[176:179], v[76:79]
	s_add_u32 m0, s28, 0x2000
	s_nop 0
	global_load_lds_dwordx4 v11, s[4:5]
	v_mfma_f32_16x16x32_f16 v[80:83], v[200:203], v[176:179], v[80:83]
	v_mfma_f32_16x16x32_f16 v[84:87], v[204:207], v[176:179], v[84:87]
	s_waitcnt lgkmcnt(9)
	v_mfma_f32_16x16x32_f16 v[88:91], v[192:195], v[180:183], v[88:91]
	v_mfma_f32_16x16x32_f16 v[92:95], v[196:199], v[180:183], v[92:95]
	v_mfma_f32_16x16x32_f16 v[96:99], v[200:203], v[180:183], v[96:99]
	s_add_u32 m0, s28, 0x4000
	s_nop 0
	global_load_lds_dwordx4 v12, s[4:5]
	v_mfma_f32_16x16x32_f16 v[100:103], v[204:207], v[180:183], v[100:103]
	s_waitcnt lgkmcnt(8)
	v_mfma_f32_16x16x32_f16 v[104:107], v[192:195], v[184:187], v[104:107]
	v_mfma_f32_16x16x32_f16 v[108:111], v[196:199], v[184:187], v[108:111]
	v_mfma_f32_16x16x32_f16 v[112:115], v[200:203], v[184:187], v[112:115]
	v_mfma_f32_16x16x32_f16 v[116:119], v[204:207], v[184:187], v[116:119]
	s_waitcnt lgkmcnt(7)
	ds_read_b128 v[172:175], v16 offset:49152
	ds_read_b128 v[192:195], v18 offset:49152
	ds_read_b128 v[196:199], v18 offset:51200
	ds_read_b128 v[200:203], v18 offset:53248
	ds_read_b128 v[204:207], v18 offset:55296
	ds_read_b128 v[176:179], v16 offset:51200
	ds_read_b128 v[180:183], v16 offset:53248
	ds_read_b128 v[184:187], v16 offset:55296
	s_waitcnt lgkmcnt(14)
	v_mfma_f32_16x16x32_f16 v[56:59], v[156:159], v[136:139], v[56:59]
	s_add_u32 m0, s28, 0x6000
	s_nop 0
	global_load_lds_dwordx4 v13, s[4:5]
	s_add_u32 s4, s4, s20
	s_addc_u32 s5, s5, 0
	s_waitcnt lgkmcnt(13)
	v_mfma_f32_16x16x32_f16 v[60:63], v[160:163], v[136:139], v[60:63]
	s_waitcnt lgkmcnt(12)
	v_mfma_f32_16x16x32_f16 v[64:67], v[164:167], v[136:139], v[64:67]
	s_waitcnt lgkmcnt(11)
	v_mfma_f32_16x16x32_f16 v[68:71], v[168:171], v[136:139], v[68:71]
	s_waitcnt lgkmcnt(10)
	v_mfma_f32_16x16x32_f16 v[72:75], v[156:159], v[140:143], v[72:75]
	v_mfma_f32_16x16x32_f16 v[76:79], v[160:163], v[140:143], v[76:79]
	s_add_u32 m0, s28, 0x8000
	s_nop 0
	global_load_lds_dwordx4 v10, s[6:7]
	v_mfma_f32_16x16x32_f16 v[80:83], v[164:167], v[140:143], v[80:83]
	v_mfma_f32_16x16x32_f16 v[84:87], v[168:171], v[140:143], v[84:87]
	s_waitcnt lgkmcnt(9)
	v_mfma_f32_16x16x32_f16 v[88:91], v[156:159], v[144:147], v[88:91]
	v_mfma_f32_16x16x32_f16 v[92:95], v[160:163], v[144:147], v[92:95]
	v_mfma_f32_16x16x32_f16 v[96:99], v[164:167], v[144:147], v[96:99]
	s_add_u32 m0, s28, 0xa000
	s_nop 0
	global_load_lds_dwordx4 v11, s[6:7]
	s_add_u32 s6, s6, s20
	s_addc_u32 s7, s7, 0
	v_mfma_f32_16x16x32_f16 v[100:103], v[168:171], v[144:147], v[100:103]
	s_waitcnt lgkmcnt(8)
	v_mfma_f32_16x16x32_f16 v[104:107], v[156:159], v[148:151], v[104:107]
	v_mfma_f32_16x16x32_f16 v[108:111], v[160:163], v[148:151], v[108:111]
	v_mfma_f32_16x16x32_f16 v[112:115], v[164:167], v[148:151], v[112:115]
	v_mfma_f32_16x16x32_f16 v[116:119], v[168:171], v[148:151], v[116:119]
	s_waitcnt vmcnt(6) lgkmcnt(0)
	s_barrier
	s_waitcnt lgkmcnt(7)
	ds_read_b128 v[136:139], v19
	ds_read_b128 v[156:159], v21
	ds_read_b128 v[160:163], v21 offset:2048
	ds_read_b128 v[164:167], v21 offset:4096
	ds_read_b128 v[168:171], v21 offset:6144
	ds_read_b128 v[140:143], v19 offset:2048
	ds_read_b128 v[144:147], v19 offset:4096
	ds_read_b128 v[148:151], v19 offset:6144
	s_waitcnt lgkmcnt(14)
	v_mfma_f32_16x16x32_f16 v[56:59], v[192:195], v[172:175], v[56:59]
	s_add_u32 m0, s28, 0xc000
	s_nop 0
	global_load_lds_dwordx4 v10, s[4:5]
	s_waitcnt lgkmcnt(13)
	v_mfma_f32_16x16x32_f16 v[60:63], v[196:199], v[172:175], v[60:63]
	s_waitcnt lgkmcnt(12)
	v_mfma_f32_16x16x32_f16 v[64:67], v[200:203], v[172:175], v[64:67]
	s_waitcnt lgkmcnt(11)
	v_mfma_f32_16x16x32_f16 v[68:71], v[204:207], v[172:175], v[68:71]
	s_waitcnt lgkmcnt(10)
	v_mfma_f32_16x16x32_f16 v[72:75], v[192:195], v[176:179], v[72:75]
	v_mfma_f32_16x16x32_f16 v[76:79], v[196:199], v[176:179], v[76:79]
	s_add_u32 m0, s28, 0xe000
	s_nop 0
	global_load_lds_dwordx4 v11, s[4:5]
	v_mfma_f32_16x16x32_f16 v[80:83], v[200:203], v[176:179], v[80:83]
	v_mfma_f32_16x16x32_f16 v[84:87], v[204:207], v[176:179], v[84:87]
	s_waitcnt lgkmcnt(9)
	v_mfma_f32_16x16x32_f16 v[88:91], v[192:195], v[180:183], v[88:91]
	v_mfma_f32_16x16x32_f16 v[92:95], v[196:199], v[180:183], v[92:95]
	v_mfma_f32_16x16x32_f16 v[96:99], v[200:203], v[180:183], v[96:99]
	s_add_u32 m0, s28, 0x10000
	s_nop 0
	global_load_lds_dwordx4 v12, s[4:5]
	v_mfma_f32_16x16x32_f16 v[100:103], v[204:207], v[180:183], v[100:103]
	s_waitcnt lgkmcnt(8)
	v_mfma_f32_16x16x32_f16 v[104:107], v[192:195], v[184:187], v[104:107]
	v_mfma_f32_16x16x32_f16 v[108:111], v[196:199], v[184:187], v[108:111]
	v_mfma_f32_16x16x32_f16 v[112:115], v[200:203], v[184:187], v[112:115]
	v_mfma_f32_16x16x32_f16 v[116:119], v[204:207], v[184:187], v[116:119]
	s_waitcnt lgkmcnt(7)
	ds_read_b128 v[172:175], v20
	ds_read_b128 v[192:195], v22
	ds_read_b128 v[196:199], v22 offset:2048
	ds_read_b128 v[200:203], v22 offset:4096
	ds_read_b128 v[204:207], v22 offset:6144
	ds_read_b128 v[176:179], v20 offset:2048
	ds_read_b128 v[180:183], v20 offset:4096
	ds_read_b128 v[184:187], v20 offset:6144
	s_waitcnt lgkmcnt(14)
	v_mfma_f32_16x16x32_f16 v[56:59], v[156:159], v[136:139], v[56:59]
	s_add_u32 m0, s28, 0x12000
	s_nop 0
	global_load_lds_dwordx4 v13, s[4:5]
	s_add_u32 s4, s4, s20
	s_addc_u32 s5, s5, 0
	s_waitcnt lgkmcnt(13)
	v_mfma_f32_16x16x32_f16 v[60:63], v[160:163], v[136:139], v[60:63]
	s_waitcnt lgkmcnt(12)
	v_mfma_f32_16x16x32_f16 v[64:67], v[164:167], v[136:139], v[64:67]
	s_waitcnt lgkmcnt(11)
	v_mfma_f32_16x16x32_f16 v[68:71], v[168:171], v[136:139], v[68:71]
	s_waitcnt lgkmcnt(10)
	v_mfma_f32_16x16x32_f16 v[72:75], v[156:159], v[140:143], v[72:75]
	v_mfma_f32_16x16x32_f16 v[76:79], v[160:163], v[140:143], v[76:79]
	s_add_u32 m0, s28, 0x14000
	s_nop 0
	global_load_lds_dwordx4 v10, s[6:7]
	v_mfma_f32_16x16x32_f16 v[80:83], v[164:167], v[140:143], v[80:83]
	v_mfma_f32_16x16x32_f16 v[84:87], v[168:171], v[140:143], v[84:87]
	s_waitcnt lgkmcnt(9)
	v_mfma_f32_16x16x32_f16 v[88:91], v[156:159], v[144:147], v[88:91]
	v_mfma_f32_16x16x32_f16 v[92:95], v[160:163], v[144:147], v[92:95]
	v_mfma_f32_16x16x32_f16 v[96:99], v[164:167], v[144:147], v[96:99]
	s_add_u32 m0, s28, 0x16000
	s_nop 0
	global_load_lds_dwordx4 v11, s[6:7]
	s_add_u32 s6, s6, s20
	s_addc_u32 s7, s7, 0
	v_mfma_f32_16x16x32_f16 v[100:103], v[168:171], v[144:147], v[100:103]
	s_waitcnt lgkmcnt(8)
	v_mfma_f32_16x16x32_f16 v[104:107], v[156:159], v[148:151], v[104:107]
	v_mfma_f32_16x16x32_f16 v[108:111], v[160:163], v[148:151], v[108:111]
	v_mfma_f32_16x16x32_f16 v[112:115], v[164:167], v[148:151], v[112:115]
	v_mfma_f32_16x16x32_f16 v[116:119], v[168:171], v[148:151], v[116:119]
	s_waitcnt vmcnt(6) lgkmcnt(0)
	s_barrier
	s_waitcnt lgkmcnt(7)
	ds_read_b128 v[136:139], v15
	ds_read_b128 v[156:159], v17
	ds_read_b128 v[160:163], v17 offset:2048
	ds_read_b128 v[164:167], v17 offset:4096
	ds_read_b128 v[168:171], v17 offset:6144
	ds_read_b128 v[140:143], v15 offset:2048
	ds_read_b128 v[144:147], v15 offset:4096
	ds_read_b128 v[148:151], v15 offset:6144
	s_waitcnt lgkmcnt(14)
	v_mfma_f32_16x16x32_f16 v[56:59], v[192:195], v[172:175], v[56:59]
	s_add_u32 m0, s28, 0x18000
	s_nop 0
	global_load_lds_dwordx4 v10, s[4:5]
	s_waitcnt lgkmcnt(13)
	v_mfma_f32_16x16x32_f16 v[60:63], v[196:199], v[172:175], v[60:63]
	s_waitcnt lgkmcnt(12)
	v_mfma_f32_16x16x32_f16 v[64:67], v[200:203], v[172:175], v[64:67]
	s_waitcnt lgkmcnt(11)
	v_mfma_f32_16x16x32_f16 v[68:71], v[204:207], v[172:175], v[68:71]
	s_waitcnt lgkmcnt(10)
	v_mfma_f32_16x16x32_f16 v[72:75], v[192:195], v[176:179], v[72:75]
	v_mfma_f32_16x16x32_f16 v[76:79], v[196:199], v[176:179], v[76:79]
	s_add_u32 m0, s28, 0x1a000
	s_nop 0
	global_load_lds_dwordx4 v11, s[4:5]
	v_mfma_f32_16x16x32_f16 v[80:83], v[200:203], v[176:179], v[80:83]
	v_mfma_f32_16x16x32_f16 v[84:87], v[204:207], v[176:179], v[84:87]
	s_waitcnt lgkmcnt(9)
	v_mfma_f32_16x16x32_f16 v[88:91], v[192:195], v[180:183], v[88:91]
	v_mfma_f32_16x16x32_f16 v[92:95], v[196:199], v[180:183], v[92:95]
	v_mfma_f32_16x16x32_f16 v[96:99], v[200:203], v[180:183], v[96:99]
	s_add_u32 m0, s28, 0x1c000
	s_nop 0
	global_load_lds_dwordx4 v12, s[4:5]
	v_mfma_f32_16x16x32_f16 v[100:103], v[204:207], v[180:183], v[100:103]
	s_waitcnt lgkmcnt(8)
	v_mfma_f32_16x16x32_f16 v[104:107], v[192:195], v[184:187], v[104:107]
	v_mfma_f32_16x16x32_f16 v[108:111], v[196:199], v[184:187], v[108:111]
	v_mfma_f32_16x16x32_f16 v[112:115], v[200:203], v[184:187], v[112:115]
	v_mfma_f32_16x16x32_f16 v[116:119], v[204:207], v[184:187], v[116:119]
	s_waitcnt lgkmcnt(7)
	ds_read_b128 v[172:175], v16
	ds_read_b128 v[192:195], v18
	ds_read_b128 v[196:199], v18 offset:2048
	ds_read_b128 v[200:203], v18 offset:4096
	ds_read_b128 v[204:207], v18 offset:6144
	ds_read_b128 v[176:179], v16 offset:2048
	ds_read_b128 v[180:183], v16 offset:4096
	ds_read_b128 v[184:187], v16 offset:6144
	s_waitcnt lgkmcnt(14)
	v_mfma_f32_16x16x32_f16 v[56:59], v[156:159], v[136:139], v[56:59]
	s_add_u32 m0, s28, 0x1e000
	s_nop 0
	global_load_lds_dwordx4 v13, s[4:5]
	s_add_u32 s4, s4, s20
	s_addc_u32 s5, s5, 0
	s_waitcnt lgkmcnt(13)
	v_mfma_f32_16x16x32_f16 v[60:63], v[160:163], v[136:139], v[60:63]
	s_waitcnt lgkmcnt(12)
	v_mfma_f32_16x16x32_f16 v[64:67], v[164:167], v[136:139], v[64:67]
	s_waitcnt lgkmcnt(11)
	v_mfma_f32_16x16x32_f16 v[68:71], v[168:171], v[136:139], v[68:71]
	s_waitcnt lgkmcnt(10)
	v_mfma_f32_16x16x32_f16 v[72:75], v[156:159], v[140:143], v[72:75]
	v_mfma_f32_16x16x32_f16 v[76:79], v[160:163], v[140:143], v[76:79]
	s_add_u32 m0, s28, 0x20000
	s_nop 0
	global_load_lds_dwordx4 v10, s[6:7]
	v_mfma_f32_16x16x32_f16 v[80:83], v[164:167], v[140:143], v[80:83]
	v_mfma_f32_16x16x32_f16 v[84:87], v[168:171], v[140:143], v[84:87]
	s_waitcnt lgkmcnt(9)
	v_mfma_f32_16x16x32_f16 v[88:91], v[156:159], v[144:147], v[88:91]
	v_mfma_f32_16x16x32_f16 v[92:95], v[160:163], v[144:147], v[92:95]
	v_mfma_f32_16x16x32_f16 v[96:99], v[164:167], v[144:147], v[96:99]
	s_add_u32 m0, s28, 0x22000
	s_nop 0
	global_load_lds_dwordx4 v11, s[6:7]
	s_add_u32 s6, s6, s20
	s_addc_u32 s7, s7, 0
	v_mfma_f32_16x16x32_f16 v[100:103], v[168:171], v[144:147], v[100:103]
	s_waitcnt lgkmcnt(8)
	v_mfma_f32_16x16x32_f16 v[104:107], v[156:159], v[148:151], v[104:107]
	v_mfma_f32_16x16x32_f16 v[108:111], v[160:163], v[148:151], v[108:111]
	v_mfma_f32_16x16x32_f16 v[112:115], v[164:167], v[148:151], v[112:115]
	v_mfma_f32_16x16x32_f16 v[116:119], v[168:171], v[148:151], v[116:119]
	s_waitcnt vmcnt(6) lgkmcnt(0)
	s_barrier
	s_waitcnt lgkmcnt(7)
	ds_read_b128 v[136:139], v15 offset:49152
	ds_read_b128 v[156:159], v17 offset:49152
	ds_read_b128 v[160:163], v17 offset:51200
	ds_read_b128 v[164:167], v17 offset:53248
	ds_read_b128 v[168:171], v17 offset:55296
	ds_read_b128 v[140:143], v15 offset:51200
	ds_read_b128 v[144:147], v15 offset:53248
	ds_read_b128 v[148:151], v15 offset:55296
	s_waitcnt lgkmcnt(14)
	v_mfma_f32_16x16x32_f16 v[56:59], v[192:195], v[172:175], v[56:59]
	s_add_u32 m0, s28, 0x0
	s_nop 0
	global_load_lds_dwordx4 v10, s[4:5]
	s_waitcnt lgkmcnt(13)
	v_mfma_f32_16x16x32_f16 v[60:63], v[196:199], v[172:175], v[60:63]
	s_waitcnt lgkmcnt(12)
	v_mfma_f32_16x16x32_f16 v[64:67], v[200:203], v[172:175], v[64:67]
	s_waitcnt lgkmcnt(11)
	v_mfma_f32_16x16x32_f16 v[68:71], v[204:207], v[172:175], v[68:71]
	s_waitcnt lgkmcnt(10)
	v_mfma_f32_16x16x32_f16 v[72:75], v[192:195], v[176:179], v[72:75]
	v_mfma_f32_16x16x32_f16 v[76:79], v[196:199], v[176:179], v[76:79]
	s_add_u32 m0, s28, 0x2000
	s_nop 0
	global_load_lds_dwordx4 v11, s[4:5]
	v_mfma_f32_16x16x32_f16 v[80:83], v[200:203], v[176:179], v[80:83]
	v_mfma_f32_16x16x32_f16 v[84:87], v[204:207], v[176:179], v[84:87]
	s_waitcnt lgkmcnt(9)
	v_mfma_f32_16x16x32_f16 v[88:91], v[192:195], v[180:183], v[88:91]
	v_mfma_f32_16x16x32_f16 v[92:95], v[196:199], v[180:183], v[92:95]
	v_mfma_f32_16x16x32_f16 v[96:99], v[200:203], v[180:183], v[96:99]
	s_add_u32 m0, s28, 0x4000
	s_nop 0
	global_load_lds_dwordx4 v12, s[4:5]
	v_mfma_f32_16x16x32_f16 v[100:103], v[204:207], v[180:183], v[100:103]
	s_waitcnt lgkmcnt(8)
	v_mfma_f32_16x16x32_f16 v[104:107], v[192:195], v[184:187], v[104:107]
	v_mfma_f32_16x16x32_f16 v[108:111], v[196:199], v[184:187], v[108:111]
	v_mfma_f32_16x16x32_f16 v[112:115], v[200:203], v[184:187], v[112:115]
	v_mfma_f32_16x16x32_f16 v[116:119], v[204:207], v[184:187], v[116:119]
	s_waitcnt lgkmcnt(7)
	ds_read_b128 v[172:175], v16 offset:49152
	ds_read_b128 v[192:195], v18 offset:49152
	ds_read_b128 v[196:199], v18 offset:51200
	ds_read_b128 v[200:203], v18 offset:53248
	ds_read_b128 v[204:207], v18 offset:55296
	ds_read_b128 v[176:179], v16 offset:51200
	ds_read_b128 v[180:183], v16 offset:53248
	ds_read_b128 v[184:187], v16 offset:55296
	s_waitcnt lgkmcnt(14)
	v_mfma_f32_16x16x32_f16 v[56:59], v[156:159], v[136:139], v[56:59]
	s_add_u32 m0, s28, 0x6000
	s_nop 0
	global_load_lds_dwordx4 v13, s[4:5]
	s_add_u32 s4, s4, s20
	s_addc_u32 s5, s5, 0
	s_waitcnt lgkmcnt(13)
	v_mfma_f32_16x16x32_f16 v[60:63], v[160:163], v[136:139], v[60:63]
	s_waitcnt lgkmcnt(12)
	v_mfma_f32_16x16x32_f16 v[64:67], v[164:167], v[136:139], v[64:67]
	s_waitcnt lgkmcnt(11)
	v_mfma_f32_16x16x32_f16 v[68:71], v[168:171], v[136:139], v[68:71]
	s_waitcnt lgkmcnt(10)
	v_mfma_f32_16x16x32_f16 v[72:75], v[156:159], v[140:143], v[72:75]
	v_mfma_f32_16x16x32_f16 v[76:79], v[160:163], v[140:143], v[76:79]
	s_add_u32 m0, s28, 0x8000
	s_nop 0
	global_load_lds_dwordx4 v10, s[6:7]
	v_mfma_f32_16x16x32_f16 v[80:83], v[164:167], v[140:143], v[80:83]
	v_mfma_f32_16x16x32_f16 v[84:87], v[168:171], v[140:143], v[84:87]
	s_waitcnt lgkmcnt(9)
	v_mfma_f32_16x16x32_f16 v[88:91], v[156:159], v[144:147], v[88:91]
	v_mfma_f32_16x16x32_f16 v[92:95], v[160:163], v[144:147], v[92:95]
	v_mfma_f32_16x16x32_f16 v[96:99], v[164:167], v[144:147], v[96:99]
	s_add_u32 m0, s28, 0xa000
	s_nop 0
	global_load_lds_dwordx4 v11, s[6:7]
	s_add_u32 s6, s6, s20
	s_addc_u32 s7, s7, 0
	v_mfma_f32_16x16x32_f16 v[100:103], v[168:171], v[144:147], v[100:103]
	s_waitcnt lgkmcnt(8)
	v_mfma_f32_16x16x32_f16 v[104:107], v[156:159], v[148:151], v[104:107]
	v_mfma_f32_16x16x32_f16 v[108:111], v[160:163], v[148:151], v[108:111]
	v_mfma_f32_16x16x32_f16 v[112:115], v[164:167], v[148:151], v[112:115]
	v_mfma_f32_16x16x32_f16 v[116:119], v[168:171], v[148:151], v[116:119]
	s_waitcnt vmcnt(6) lgkmcnt(0)
	s_barrier
	s_waitcnt lgkmcnt(7)
	ds_read_b128 v[136:139], v19
	ds_read_b128 v[156:159], v21
	ds_read_b128 v[160:163], v21 offset:2048
	ds_read_b128 v[164:167], v21 offset:4096
	ds_read_b128 v[168:171], v21 offset:6144
	ds_read_b128 v[140:143], v19 offset:2048
	ds_read_b128 v[144:147], v19 offset:4096
	ds_read_b128 v[148:151], v19 offset:6144
	s_waitcnt lgkmcnt(14)
	v_mfma_f32_16x16x32_f16 v[56:59], v[192:195], v[172:175], v[56:59]
	s_add_u32 m0, s28, 0xc000
	s_nop 0
	global_load_lds_dwordx4 v10, s[4:5]
	s_waitcnt lgkmcnt(13)
	v_mfma_f32_16x16x32_f16 v[60:63], v[196:199], v[172:175], v[60:63]
	s_waitcnt lgkmcnt(12)
	v_mfma_f32_16x16x32_f16 v[64:67], v[200:203], v[172:175], v[64:67]
	s_waitcnt lgkmcnt(11)
	v_mfma_f32_16x16x32_f16 v[68:71], v[204:207], v[172:175], v[68:71]
	s_waitcnt lgkmcnt(10)
	v_mfma_f32_16x16x32_f16 v[72:75], v[192:195], v[176:179], v[72:75]
	v_mfma_f32_16x16x32_f16 v[76:79], v[196:199], v[176:179], v[76:79]
	s_add_u32 m0, s28, 0xe000
	s_nop 0
	global_load_lds_dwordx4 v11, s[4:5]
	v_mfma_f32_16x16x32_f16 v[80:83], v[200:203], v[176:179], v[80:83]
	v_mfma_f32_16x16x32_f16 v[84:87], v[204:207], v[176:179], v[84:87]
	s_waitcnt lgkmcnt(9)
	v_mfma_f32_16x16x32_f16 v[88:91], v[192:195], v[180:183], v[88:91]
	v_mfma_f32_16x16x32_f16 v[92:95], v[196:199], v[180:183], v[92:95]
	v_mfma_f32_16x16x32_f16 v[96:99], v[200:203], v[180:183], v[96:99]
	s_add_u32 m0, s28, 0x10000
	s_nop 0
	global_load_lds_dwordx4 v12, s[4:5]
	v_mfma_f32_16x16x32_f16 v[100:103], v[204:207], v[180:183], v[100:103]
	s_waitcnt lgkmcnt(8)
	v_mfma_f32_16x16x32_f16 v[104:107], v[192:195], v[184:187], v[104:107]
	v_mfma_f32_16x16x32_f16 v[108:111], v[196:199], v[184:187], v[108:111]
	v_mfma_f32_16x16x32_f16 v[112:115], v[200:203], v[184:187], v[112:115]
	v_mfma_f32_16x16x32_f16 v[116:119], v[204:207], v[184:187], v[116:119]
	s_waitcnt lgkmcnt(7)
	ds_read_b128 v[172:175], v20
	ds_read_b128 v[192:195], v22
	ds_read_b128 v[196:199], v22 offset:2048
	ds_read_b128 v[200:203], v22 offset:4096
	ds_read_b128 v[204:207], v22 offset:6144
	ds_read_b128 v[176:179], v20 offset:2048
	ds_read_b128 v[180:183], v20 offset:4096
	ds_read_b128 v[184:187], v20 offset:6144
	s_waitcnt lgkmcnt(14)
	v_mfma_f32_16x16x32_f16 v[56:59], v[156:159], v[136:139], v[56:59]
	s_add_u32 m0, s28, 0x12000
	s_nop 0
	global_load_lds_dwordx4 v13, s[4:5]
	s_add_u32 s4, s4, s20
	s_addc_u32 s5, s5, 0
	s_waitcnt lgkmcnt(13)
	v_mfma_f32_16x16x32_f16 v[60:63], v[160:163], v[136:139], v[60:63]
	s_waitcnt lgkmcnt(12)
	v_mfma_f32_16x16x32_f16 v[64:67], v[164:167], v[136:139], v[64:67]
	s_waitcnt lgkmcnt(11)
	v_mfma_f32_16x16x32_f16 v[68:71], v[168:171], v[136:139], v[68:71]
	s_waitcnt lgkmcnt(10)
	v_mfma_f32_16x16x32_f16 v[72:75], v[156:159], v[140:143], v[72:75]
	v_mfma_f32_16x16x32_f16 v[76:79], v[160:163], v[140:143], v[76:79]
	s_add_u32 m0, s28, 0x14000
	s_nop 0
	global_load_lds_dwordx4 v10, s[6:7]
	v_mfma_f32_16x16x32_f16 v[80:83], v[164:167], v[140:143], v[80:83]
	v_mfma_f32_16x16x32_f16 v[84:87], v[168:171], v[140:143], v[84:87]
	s_waitcnt lgkmcnt(9)
	v_mfma_f32_16x16x32_f16 v[88:91], v[156:159], v[144:147], v[88:91]
	v_mfma_f32_16x16x32_f16 v[92:95], v[160:163], v[144:147], v[92:95]
	v_mfma_f32_16x16x32_f16 v[96:99], v[164:167], v[144:147], v[96:99]
	s_add_u32 m0, s28, 0x16000
	s_nop 0
	global_load_lds_dwordx4 v11, s[6:7]
	s_add_u32 s6, s6, s20
	s_addc_u32 s7, s7, 0
	v_mfma_f32_16x16x32_f16 v[100:103], v[168:171], v[144:147], v[100:103]
	s_waitcnt lgkmcnt(8)
	v_mfma_f32_16x16x32_f16 v[104:107], v[156:159], v[148:151], v[104:107]
	v_mfma_f32_16x16x32_f16 v[108:111], v[160:163], v[148:151], v[108:111]
	v_mfma_f32_16x16x32_f16 v[112:115], v[164:167], v[148:151], v[112:115]
	v_mfma_f32_16x16x32_f16 v[116:119], v[168:171], v[148:151], v[116:119]
	s_waitcnt vmcnt(6) lgkmcnt(0)
	s_barrier
	s_waitcnt lgkmcnt(7)
	ds_read_b128 v[136:139], v15
	ds_read_b128 v[156:159], v17
	ds_read_b128 v[160:163], v17 offset:2048
	ds_read_b128 v[164:167], v17 offset:4096
	ds_read_b128 v[168:171], v17 offset:6144
	ds_read_b128 v[140:143], v15 offset:2048
	ds_read_b128 v[144:147], v15 offset:4096
	ds_read_b128 v[148:151], v15 offset:6144
	s_waitcnt lgkmcnt(14)
	v_mfma_f32_16x16x32_f16 v[56:59], v[192:195], v[172:175], v[56:59]
	s_add_u32 m0, s28, 0x18000
	s_nop 0
	global_load_lds_dwordx4 v10, s[4:5]
	s_waitcnt lgkmcnt(13)
	v_mfma_f32_16x16x32_f16 v[60:63], v[196:199], v[172:175], v[60:63]
	s_waitcnt lgkmcnt(12)
	v_mfma_f32_16x16x32_f16 v[64:67], v[200:203], v[172:175], v[64:67]
	s_waitcnt lgkmcnt(11)
	v_mfma_f32_16x16x32_f16 v[68:71], v[204:207], v[172:175], v[68:71]
	s_waitcnt lgkmcnt(10)
	v_mfma_f32_16x16x32_f16 v[72:75], v[192:195], v[176:179], v[72:75]
	v_mfma_f32_16x16x32_f16 v[76:79], v[196:199], v[176:179], v[76:79]
	s_add_u32 m0, s28, 0x1a000
	s_nop 0
	global_load_lds_dwordx4 v11, s[4:5]
	v_mfma_f32_16x16x32_f16 v[80:83], v[200:203], v[176:179], v[80:83]
	v_mfma_f32_16x16x32_f16 v[84:87], v[204:207], v[176:179], v[84:87]
	s_waitcnt lgkmcnt(9)
	v_mfma_f32_16x16x32_f16 v[88:91], v[192:195], v[180:183], v[88:91]
	v_mfma_f32_16x16x32_f16 v[92:95], v[196:199], v[180:183], v[92:95]
	v_mfma_f32_16x16x32_f16 v[96:99], v[200:203], v[180:183], v[96:99]
	s_add_u32 m0, s28, 0x1c000
	s_nop 0
	global_load_lds_dwordx4 v12, s[4:5]
	v_mfma_f32_16x16x32_f16 v[100:103], v[204:207], v[180:183], v[100:103]
	s_waitcnt lgkmcnt(8)
	v_mfma_f32_16x16x32_f16 v[104:107], v[192:195], v[184:187], v[104:107]
	v_mfma_f32_16x16x32_f16 v[108:111], v[196:199], v[184:187], v[108:111]
	v_mfma_f32_16x16x32_f16 v[112:115], v[200:203], v[184:187], v[112:115]
	v_mfma_f32_16x16x32_f16 v[116:119], v[204:207], v[184:187], v[116:119]
	s_waitcnt lgkmcnt(7)
	ds_read_b128 v[172:175], v16
	ds_read_b128 v[192:195], v18
	ds_read_b128 v[196:199], v18 offset:2048
	ds_read_b128 v[200:203], v18 offset:4096
	ds_read_b128 v[204:207], v18 offset:6144
	ds_read_b128 v[176:179], v16 offset:2048
	ds_read_b128 v[180:183], v16 offset:4096
	ds_read_b128 v[184:187], v16 offset:6144
	s_waitcnt lgkmcnt(14)
	v_mfma_f32_16x16x32_f16 v[56:59], v[156:159], v[136:139], v[56:59]
	s_add_u32 m0, s28, 0x1e000
	s_nop 0
	global_load_lds_dwordx4 v13, s[4:5]
	s_add_u32 s4, s4, s20
	s_addc_u32 s5, s5, 0
	s_waitcnt lgkmcnt(13)
	v_mfma_f32_16x16x32_f16 v[60:63], v[160:163], v[136:139], v[60:63]
	s_waitcnt lgkmcnt(12)
	v_mfma_f32_16x16x32_f16 v[64:67], v[164:167], v[136:139], v[64:67]
	s_waitcnt lgkmcnt(11)
	v_mfma_f32_16x16x32_f16 v[68:71], v[168:171], v[136:139], v[68:71]
	s_waitcnt lgkmcnt(10)
	v_mfma_f32_16x16x32_f16 v[72:75], v[156:159], v[140:143], v[72:75]
	v_mfma_f32_16x16x32_f16 v[76:79], v[160:163], v[140:143], v[76:79]
	s_add_u32 m0, s28, 0x20000
	s_nop 0
	global_load_lds_dwordx4 v10, s[6:7]
	v_mfma_f32_16x16x32_f16 v[80:83], v[164:167], v[140:143], v[80:83]
	v_mfma_f32_16x16x32_f16 v[84:87], v[168:171], v[140:143], v[84:87]
	s_waitcnt lgkmcnt(9)
	v_mfma_f32_16x16x32_f16 v[88:91], v[156:159], v[144:147], v[88:91]
	v_mfma_f32_16x16x32_f16 v[92:95], v[160:163], v[144:147], v[92:95]
	v_mfma_f32_16x16x32_f16 v[96:99], v[164:167], v[144:147], v[96:99]
	s_add_u32 m0, s28, 0x22000
	s_nop 0
	global_load_lds_dwordx4 v11, s[6:7]
	s_add_u32 s6, s6, s20
	s_addc_u32 s7, s7, 0
	v_mfma_f32_16x16x32_f16 v[100:103], v[168:171], v[144:147], v[100:103]
	s_waitcnt lgkmcnt(8)
	v_mfma_f32_16x16x32_f16 v[104:107], v[156:159], v[148:151], v[104:107]
	v_mfma_f32_16x16x32_f16 v[108:111], v[160:163], v[148:151], v[108:111]
	v_mfma_f32_16x16x32_f16 v[112:115], v[164:167], v[148:151], v[112:115]
	v_mfma_f32_16x16x32_f16 v[116:119], v[168:171], v[148:151], v[116:119]
	s_waitcnt vmcnt(6) lgkmcnt(0)
	s_barrier
	s_waitcnt lgkmcnt(7)
	ds_read_b128 v[136:139], v15 offset:49152
	ds_read_b128 v[156:159], v17 offset:49152
	ds_read_b128 v[160:163], v17 offset:51200
	ds_read_b128 v[164:167], v17 offset:53248
	ds_read_b128 v[168:171], v17 offset:55296
	ds_read_b128 v[140:143], v15 offset:51200
	ds_read_b128 v[144:147], v15 offset:53248
	ds_read_b128 v[148:151], v15 offset:55296
	s_waitcnt lgkmcnt(14)
	v_mfma_f32_16x16x32_f16 v[56:59], v[192:195], v[172:175], v[56:59]
	s_add_u32 m0, s28, 0x0
	s_nop 0
	global_load_lds_dwordx4 v10, s[4:5]
	s_waitcnt lgkmcnt(13)
	v_mfma_f32_16x16x32_f16 v[60:63], v[196:199], v[172:175], v[60:63]
	s_waitcnt lgkmcnt(12)
	v_mfma_f32_16x16x32_f16 v[64:67], v[200:203], v[172:175], v[64:67]
	s_waitcnt lgkmcnt(11)
	v_mfma_f32_16x16x32_f16 v[68:71], v[204:207], v[172:175], v[68:71]
	s_waitcnt lgkmcnt(10)
	v_mfma_f32_16x16x32_f16 v[72:75], v[192:195], v[176:179], v[72:75]
	v_mfma_f32_16x16x32_f16 v[76:79], v[196:199], v[176:179], v[76:79]
	s_add_u32 m0, s28, 0x2000
	s_nop 0
	global_load_lds_dwordx4 v11, s[4:5]
	v_mfma_f32_16x16x32_f16 v[80:83], v[200:203], v[176:179], v[80:83]
	v_mfma_f32_16x16x32_f16 v[84:87], v[204:207], v[176:179], v[84:87]
	s_waitcnt lgkmcnt(9)
	v_mfma_f32_16x16x32_f16 v[88:91], v[192:195], v[180:183], v[88:91]
	v_mfma_f32_16x16x32_f16 v[92:95], v[196:199], v[180:183], v[92:95]
	v_mfma_f32_16x16x32_f16 v[96:99], v[200:203], v[180:183], v[96:99]
	s_add_u32 m0, s28, 0x4000
	s_nop 0
	global_load_lds_dwordx4 v12, s[4:5]
	v_mfma_f32_16x16x32_f16 v[100:103], v[204:207], v[180:183], v[100:103]
	s_waitcnt lgkmcnt(8)
	v_mfma_f32_16x16x32_f16 v[104:107], v[192:195], v[184:187], v[104:107]
	v_mfma_f32_16x16x32_f16 v[108:111], v[196:199], v[184:187], v[108:111]
	v_mfma_f32_16x16x32_f16 v[112:115], v[200:203], v[184:187], v[112:115]
	v_mfma_f32_16x16x32_f16 v[116:119], v[204:207], v[184:187], v[116:119]
	s_waitcnt lgkmcnt(7)
	ds_read_b128 v[172:175], v16 offset:49152
	ds_read_b128 v[192:195], v18 offset:49152
	ds_read_b128 v[196:199], v18 offset:51200
	ds_read_b128 v[200:203], v18 offset:53248
	ds_read_b128 v[204:207], v18 offset:55296
	ds_read_b128 v[176:179], v16 offset:51200
	ds_read_b128 v[180:183], v16 offset:53248
	ds_read_b128 v[184:187], v16 offset:55296
	s_waitcnt lgkmcnt(14)
	v_mfma_f32_16x16x32_f16 v[56:59], v[156:159], v[136:139], v[56:59]
	s_add_u32 m0, s28, 0x6000
	s_nop 0
	global_load_lds_dwordx4 v13, s[4:5]
	s_add_u32 s4, s4, s20
	s_addc_u32 s5, s5, 0
	s_waitcnt lgkmcnt(13)
	v_mfma_f32_16x16x32_f16 v[60:63], v[160:163], v[136:139], v[60:63]
	s_waitcnt lgkmcnt(12)
	v_mfma_f32_16x16x32_f16 v[64:67], v[164:167], v[136:139], v[64:67]
	s_waitcnt lgkmcnt(11)
	v_mfma_f32_16x16x32_f16 v[68:71], v[168:171], v[136:139], v[68:71]
	s_waitcnt lgkmcnt(10)
	v_mfma_f32_16x16x32_f16 v[72:75], v[156:159], v[140:143], v[72:75]
	v_mfma_f32_16x16x32_f16 v[76:79], v[160:163], v[140:143], v[76:79]
	s_add_u32 m0, s28, 0x8000
	s_nop 0
	global_load_lds_dwordx4 v10, s[6:7]
	v_mfma_f32_16x16x32_f16 v[80:83], v[164:167], v[140:143], v[80:83]
	v_mfma_f32_16x16x32_f16 v[84:87], v[168:171], v[140:143], v[84:87]
	s_waitcnt lgkmcnt(9)
	v_mfma_f32_16x16x32_f16 v[88:91], v[156:159], v[144:147], v[88:91]
	v_mfma_f32_16x16x32_f16 v[92:95], v[160:163], v[144:147], v[92:95]
	v_mfma_f32_16x16x32_f16 v[96:99], v[164:167], v[144:147], v[96:99]
	s_add_u32 m0, s28, 0xa000
	s_nop 0
	global_load_lds_dwordx4 v11, s[6:7]
	s_add_u32 s6, s6, s20
	s_addc_u32 s7, s7, 0
	v_mfma_f32_16x16x32_f16 v[100:103], v[168:171], v[144:147], v[100:103]
	s_waitcnt lgkmcnt(8)
	v_mfma_f32_16x16x32_f16 v[104:107], v[156:159], v[148:151], v[104:107]
	v_mfma_f32_16x16x32_f16 v[108:111], v[160:163], v[148:151], v[108:111]
	v_mfma_f32_16x16x32_f16 v[112:115], v[164:167], v[148:151], v[112:115]
	v_mfma_f32_16x16x32_f16 v[116:119], v[168:171], v[148:151], v[116:119]
	s_waitcnt vmcnt(6) lgkmcnt(0)
	s_barrier
	s_waitcnt lgkmcnt(7)
	ds_read_b128 v[136:139], v19
	ds_read_b128 v[156:159], v21
	ds_read_b128 v[160:163], v21 offset:2048
	ds_read_b128 v[164:167], v21 offset:4096
	ds_read_b128 v[168:171], v21 offset:6144
	ds_read_b128 v[140:143], v19 offset:2048
	ds_read_b128 v[144:147], v19 offset:4096
	ds_read_b128 v[148:151], v19 offset:6144
	s_waitcnt lgkmcnt(14)
	v_mfma_f32_16x16x32_f16 v[56:59], v[192:195], v[172:175], v[56:59]
	s_add_u32 m0, s28, 0xc000
	s_nop 0
	global_load_lds_dwordx4 v10, s[4:5]
	s_waitcnt lgkmcnt(13)
	v_mfma_f32_16x16x32_f16 v[60:63], v[196:199], v[172:175], v[60:63]
	s_waitcnt lgkmcnt(12)
	v_mfma_f32_16x16x32_f16 v[64:67], v[200:203], v[172:175], v[64:67]
	s_waitcnt lgkmcnt(11)
	v_mfma_f32_16x16x32_f16 v[68:71], v[204:207], v[172:175], v[68:71]
	s_waitcnt lgkmcnt(10)
	v_mfma_f32_16x16x32_f16 v[72:75], v[192:195], v[176:179], v[72:75]
	v_mfma_f32_16x16x32_f16 v[76:79], v[196:199], v[176:179], v[76:79]
	s_add_u32 m0, s28, 0xe000
	s_nop 0
	global_load_lds_dwordx4 v11, s[4:5]
	v_mfma_f32_16x16x32_f16 v[80:83], v[200:203], v[176:179], v[80:83]
	v_mfma_f32_16x16x32_f16 v[84:87], v[204:207], v[176:179], v[84:87]
	s_waitcnt lgkmcnt(9)
	v_mfma_f32_16x16x32_f16 v[88:91], v[192:195], v[180:183], v[88:91]
	v_mfma_f32_16x16x32_f16 v[92:95], v[196:199], v[180:183], v[92:95]
	v_mfma_f32_16x16x32_f16 v[96:99], v[200:203], v[180:183], v[96:99]
	s_add_u32 m0, s28, 0x10000
	s_nop 0
	global_load_lds_dwordx4 v12, s[4:5]
	v_mfma_f32_16x16x32_f16 v[100:103], v[204:207], v[180:183], v[100:103]
	s_waitcnt lgkmcnt(8)
	v_mfma_f32_16x16x32_f16 v[104:107], v[192:195], v[184:187], v[104:107]
	v_mfma_f32_16x16x32_f16 v[108:111], v[196:199], v[184:187], v[108:111]
	v_mfma_f32_16x16x32_f16 v[112:115], v[200:203], v[184:187], v[112:115]
	v_mfma_f32_16x16x32_f16 v[116:119], v[204:207], v[184:187], v[116:119]
	s_waitcnt lgkmcnt(7)
	ds_read_b128 v[172:175], v20
	ds_read_b128 v[192:195], v22
	ds_read_b128 v[196:199], v22 offset:2048
	ds_read_b128 v[200:203], v22 offset:4096
	ds_read_b128 v[204:207], v22 offset:6144
	ds_read_b128 v[176:179], v20 offset:2048
	ds_read_b128 v[180:183], v20 offset:4096
	ds_read_b128 v[184:187], v20 offset:6144
	s_waitcnt lgkmcnt(14)
	v_mfma_f32_16x16x32_f16 v[56:59], v[156:159], v[136:139], v[56:59]
	s_add_u32 m0, s28, 0x12000
	s_nop 0
	global_load_lds_dwordx4 v13, s[4:5]
	s_add_u32 s4, s4, s20
	s_addc_u32 s5, s5, 0
	s_waitcnt lgkmcnt(13)
	v_mfma_f32_16x16x32_f16 v[60:63], v[160:163], v[136:139], v[60:63]
	s_waitcnt lgkmcnt(12)
	v_mfma_f32_16x16x32_f16 v[64:67], v[164:167], v[136:139], v[64:67]
	s_waitcnt lgkmcnt(11)
	v_mfma_f32_16x16x32_f16 v[68:71], v[168:171], v[136:139], v[68:71]
	s_waitcnt lgkmcnt(10)
	v_mfma_f32_16x16x32_f16 v[72:75], v[156:159], v[140:143], v[72:75]
	v_mfma_f32_16x16x32_f16 v[76:79], v[160:163], v[140:143], v[76:79]
	s_add_u32 m0, s28, 0x14000
	s_nop 0
	global_load_lds_dwordx4 v10, s[6:7]
	v_mfma_f32_16x16x32_f16 v[80:83], v[164:167], v[140:143], v[80:83]
	v_mfma_f32_16x16x32_f16 v[84:87], v[168:171], v[140:143], v[84:87]
	s_waitcnt lgkmcnt(9)
	v_mfma_f32_16x16x32_f16 v[88:91], v[156:159], v[144:147], v[88:91]
	v_mfma_f32_16x16x32_f16 v[92:95], v[160:163], v[144:147], v[92:95]
	v_mfma_f32_16x16x32_f16 v[96:99], v[164:167], v[144:147], v[96:99]
	s_add_u32 m0, s28, 0x16000
	s_nop 0
	global_load_lds_dwordx4 v11, s[6:7]
	s_add_u32 s6, s6, s20
	s_addc_u32 s7, s7, 0
	v_mfma_f32_16x16x32_f16 v[100:103], v[168:171], v[144:147], v[100:103]
	s_waitcnt lgkmcnt(8)
	v_mfma_f32_16x16x32_f16 v[104:107], v[156:159], v[148:151], v[104:107]
	v_mfma_f32_16x16x32_f16 v[108:111], v[160:163], v[148:151], v[108:111]
	v_mfma_f32_16x16x32_f16 v[112:115], v[164:167], v[148:151], v[112:115]
	v_mfma_f32_16x16x32_f16 v[116:119], v[168:171], v[148:151], v[116:119]
	s_waitcnt vmcnt(6) lgkmcnt(0)
	s_barrier
	s_waitcnt lgkmcnt(7)
	ds_read_b128 v[136:139], v15
	ds_read_b128 v[156:159], v17
	ds_read_b128 v[160:163], v17 offset:2048
	ds_read_b128 v[164:167], v17 offset:4096
	ds_read_b128 v[168:171], v17 offset:6144
	ds_read_b128 v[140:143], v15 offset:2048
	ds_read_b128 v[144:147], v15 offset:4096
	ds_read_b128 v[148:151], v15 offset:6144
	s_waitcnt lgkmcnt(14)
	v_mfma_f32_16x16x32_f16 v[56:59], v[192:195], v[172:175], v[56:59]
	s_add_u32 m0, s28, 0x18000
	s_nop 0
	global_load_lds_dwordx4 v10, s[4:5]
	s_waitcnt lgkmcnt(13)
	v_mfma_f32_16x16x32_f16 v[60:63], v[196:199], v[172:175], v[60:63]
	s_waitcnt lgkmcnt(12)
	v_mfma_f32_16x16x32_f16 v[64:67], v[200:203], v[172:175], v[64:67]
	s_waitcnt lgkmcnt(11)
	v_mfma_f32_16x16x32_f16 v[68:71], v[204:207], v[172:175], v[68:71]
	s_waitcnt lgkmcnt(10)
	v_mfma_f32_16x16x32_f16 v[72:75], v[192:195], v[176:179], v[72:75]
	v_mfma_f32_16x16x32_f16 v[76:79], v[196:199], v[176:179], v[76:79]
	s_add_u32 m0, s28, 0x1a000
	s_nop 0
	global_load_lds_dwordx4 v11, s[4:5]
	v_mfma_f32_16x16x32_f16 v[80:83], v[200:203], v[176:179], v[80:83]
	v_mfma_f32_16x16x32_f16 v[84:87], v[204:207], v[176:179], v[84:87]
	s_waitcnt lgkmcnt(9)
	v_mfma_f32_16x16x32_f16 v[88:91], v[192:195], v[180:183], v[88:91]
	v_mfma_f32_16x16x32_f16 v[92:95], v[196:199], v[180:183], v[92:95]
	v_mfma_f32_16x16x32_f16 v[96:99], v[200:203], v[180:183], v[96:99]
	s_add_u32 m0, s28, 0x1c000
	s_nop 0
	global_load_lds_dwordx4 v12, s[4:5]
	v_mfma_f32_16x16x32_f16 v[100:103], v[204:207], v[180:183], v[100:103]
	s_waitcnt lgkmcnt(8)
	v_mfma_f32_16x16x32_f16 v[104:107], v[192:195], v[184:187], v[104:107]
	v_mfma_f32_16x16x32_f16 v[108:111], v[196:199], v[184:187], v[108:111]
	v_mfma_f32_16x16x32_f16 v[112:115], v[200:203], v[184:187], v[112:115]
	v_mfma_f32_16x16x32_f16 v[116:119], v[204:207], v[184:187], v[116:119]
	s_waitcnt lgkmcnt(7)
	ds_read_b128 v[172:175], v16
	ds_read_b128 v[192:195], v18
	ds_read_b128 v[196:199], v18 offset:2048
	ds_read_b128 v[200:203], v18 offset:4096
	ds_read_b128 v[204:207], v18 offset:6144
	ds_read_b128 v[176:179], v16 offset:2048
	ds_read_b128 v[180:183], v16 offset:4096
	ds_read_b128 v[184:187], v16 offset:6144
	s_waitcnt lgkmcnt(14)
	v_mfma_f32_16x16x32_f16 v[56:59], v[156:159], v[136:139], v[56:59]
	s_add_u32 m0, s28, 0x1e000
	s_nop 0
	global_load_lds_dwordx4 v13, s[4:5]
	s_add_u32 s4, s4, s20
	s_addc_u32 s5, s5, 0
	s_waitcnt lgkmcnt(13)
	v_mfma_f32_16x16x32_f16 v[60:63], v[160:163], v[136:139], v[60:63]
	s_waitcnt lgkmcnt(12)
	v_mfma_f32_16x16x32_f16 v[64:67], v[164:167], v[136:139], v[64:67]
	s_waitcnt lgkmcnt(11)
	v_mfma_f32_16x16x32_f16 v[68:71], v[168:171], v[136:139], v[68:71]
	s_waitcnt lgkmcnt(10)
	v_mfma_f32_16x16x32_f16 v[72:75], v[156:159], v[140:143], v[72:75]
	v_mfma_f32_16x16x32_f16 v[76:79], v[160:163], v[140:143], v[76:79]
	s_add_u32 m0, s28, 0x20000
	s_nop 0
	global_load_lds_dwordx4 v10, s[6:7]
	v_mfma_f32_16x16x32_f16 v[80:83], v[164:167], v[140:143], v[80:83]
	v_mfma_f32_16x16x32_f16 v[84:87], v[168:171], v[140:143], v[84:87]
	s_waitcnt lgkmcnt(9)
	v_mfma_f32_16x16x32_f16 v[88:91], v[156:159], v[144:147], v[88:91]
	v_mfma_f32_16x16x32_f16 v[92:95], v[160:163], v[144:147], v[92:95]
	v_mfma_f32_16x16x32_f16 v[96:99], v[164:167], v[144:147], v[96:99]
	s_add_u32 m0, s28, 0x22000
	s_nop 0
	global_load_lds_dwordx4 v11, s[6:7]
	s_add_u32 s6, s6, s20
	s_addc_u32 s7, s7, 0
	v_mfma_f32_16x16x32_f16 v[100:103], v[168:171], v[144:147], v[100:103]
	s_waitcnt lgkmcnt(8)
	v_mfma_f32_16x16x32_f16 v[104:107], v[156:159], v[148:151], v[104:107]
	v_mfma_f32_16x16x32_f16 v[108:111], v[160:163], v[148:151], v[108:111]
	v_mfma_f32_16x16x32_f16 v[112:115], v[164:167], v[148:151], v[112:115]
	v_mfma_f32_16x16x32_f16 v[116:119], v[168:171], v[148:151], v[116:119]
	s_waitcnt vmcnt(6) lgkmcnt(0)
	s_barrier
	s_waitcnt lgkmcnt(7)
	ds_read_b128 v[136:139], v15 offset:49152
	ds_read_b128 v[156:159], v17 offset:49152
	ds_read_b128 v[160:163], v17 offset:51200
	ds_read_b128 v[164:167], v17 offset:53248
	ds_read_b128 v[168:171], v17 offset:55296
	ds_read_b128 v[140:143], v15 offset:51200
	ds_read_b128 v[144:147], v15 offset:53248
	ds_read_b128 v[148:151], v15 offset:55296
	s_waitcnt lgkmcnt(14)
	v_mfma_f32_16x16x32_f16 v[56:59], v[192:195], v[172:175], v[56:59]
	s_add_u32 m0, s28, 0x0
	s_nop 0
	global_load_lds_dwordx4 v10, s[4:5]
	s_waitcnt lgkmcnt(13)
	v_mfma_f32_16x16x32_f16 v[60:63], v[196:199], v[172:175], v[60:63]
	s_waitcnt lgkmcnt(12)
	v_mfma_f32_16x16x32_f16 v[64:67], v[200:203], v[172:175], v[64:67]
	s_waitcnt lgkmcnt(11)
	v_mfma_f32_16x16x32_f16 v[68:71], v[204:207], v[172:175], v[68:71]
	s_waitcnt lgkmcnt(10)
	v_mfma_f32_16x16x32_f16 v[72:75], v[192:195], v[176:179], v[72:75]
	v_mfma_f32_16x16x32_f16 v[76:79], v[196:199], v[176:179], v[76:79]
	s_add_u32 m0, s28, 0x2000
	s_nop 0
	global_load_lds_dwordx4 v11, s[4:5]
	v_mfma_f32_16x16x32_f16 v[80:83], v[200:203], v[176:179], v[80:83]
	v_mfma_f32_16x16x32_f16 v[84:87], v[204:207], v[176:179], v[84:87]
	s_waitcnt lgkmcnt(9)
	v_mfma_f32_16x16x32_f16 v[88:91], v[192:195], v[180:183], v[88:91]
	v_mfma_f32_16x16x32_f16 v[92:95], v[196:199], v[180:183], v[92:95]
	v_mfma_f32_16x16x32_f16 v[96:99], v[200:203], v[180:183], v[96:99]
	s_add_u32 m0, s28, 0x4000
	s_nop 0
	global_load_lds_dwordx4 v12, s[4:5]
	v_mfma_f32_16x16x32_f16 v[100:103], v[204:207], v[180:183], v[100:103]
	s_waitcnt lgkmcnt(8)
	v_mfma_f32_16x16x32_f16 v[104:107], v[192:195], v[184:187], v[104:107]
	v_mfma_f32_16x16x32_f16 v[108:111], v[196:199], v[184:187], v[108:111]
	v_mfma_f32_16x16x32_f16 v[112:115], v[200:203], v[184:187], v[112:115]
	v_mfma_f32_16x16x32_f16 v[116:119], v[204:207], v[184:187], v[116:119]
	s_waitcnt lgkmcnt(7)
	ds_read_b128 v[172:175], v16 offset:49152
	ds_read_b128 v[192:195], v18 offset:49152
	ds_read_b128 v[196:199], v18 offset:51200
	ds_read_b128 v[200:203], v18 offset:53248
	ds_read_b128 v[204:207], v18 offset:55296
	ds_read_b128 v[176:179], v16 offset:51200
	ds_read_b128 v[180:183], v16 offset:53248
	ds_read_b128 v[184:187], v16 offset:55296
	s_waitcnt lgkmcnt(14)
	v_mfma_f32_16x16x32_f16 v[56:59], v[156:159], v[136:139], v[56:59]
	s_add_u32 m0, s28, 0x6000
	s_nop 0
	global_load_lds_dwordx4 v13, s[4:5]
	s_add_u32 s4, s4, s20
	s_addc_u32 s5, s5, 0
	s_waitcnt lgkmcnt(13)
	v_mfma_f32_16x16x32_f16 v[60:63], v[160:163], v[136:139], v[60:63]
	s_waitcnt lgkmcnt(12)
	v_mfma_f32_16x16x32_f16 v[64:67], v[164:167], v[136:139], v[64:67]
	s_waitcnt lgkmcnt(11)
	v_mfma_f32_16x16x32_f16 v[68:71], v[168:171], v[136:139], v[68:71]
	s_waitcnt lgkmcnt(10)
	v_mfma_f32_16x16x32_f16 v[72:75], v[156:159], v[140:143], v[72:75]
	v_mfma_f32_16x16x32_f16 v[76:79], v[160:163], v[140:143], v[76:79]
	s_add_u32 m0, s28, 0x8000
	s_nop 0
	global_load_lds_dwordx4 v10, s[6:7]
	v_mfma_f32_16x16x32_f16 v[80:83], v[164:167], v[140:143], v[80:83]
	v_mfma_f32_16x16x32_f16 v[84:87], v[168:171], v[140:143], v[84:87]
	s_waitcnt lgkmcnt(9)
	v_mfma_f32_16x16x32_f16 v[88:91], v[156:159], v[144:147], v[88:91]
	v_mfma_f32_16x16x32_f16 v[92:95], v[160:163], v[144:147], v[92:95]
	v_mfma_f32_16x16x32_f16 v[96:99], v[164:167], v[144:147], v[96:99]
	s_add_u32 m0, s28, 0xa000
	s_nop 0
	global_load_lds_dwordx4 v11, s[6:7]
	s_add_u32 s6, s6, s20
	s_addc_u32 s7, s7, 0
	v_mfma_f32_16x16x32_f16 v[100:103], v[168:171], v[144:147], v[100:103]
	s_waitcnt lgkmcnt(8)
	v_mfma_f32_16x16x32_f16 v[104:107], v[156:159], v[148:151], v[104:107]
	v_mfma_f32_16x16x32_f16 v[108:111], v[160:163], v[148:151], v[108:111]
	v_mfma_f32_16x16x32_f16 v[112:115], v[164:167], v[148:151], v[112:115]
	v_mfma_f32_16x16x32_f16 v[116:119], v[168:171], v[148:151], v[116:119]
	s_waitcnt vmcnt(6) lgkmcnt(0)
	s_barrier
	s_waitcnt lgkmcnt(7)
	ds_read_b128 v[136:139], v19
	ds_read_b128 v[156:159], v21
	ds_read_b128 v[160:163], v21 offset:2048
	ds_read_b128 v[164:167], v21 offset:4096
	ds_read_b128 v[168:171], v21 offset:6144
	ds_read_b128 v[140:143], v19 offset:2048
	ds_read_b128 v[144:147], v19 offset:4096
	ds_read_b128 v[148:151], v19 offset:6144
	s_waitcnt lgkmcnt(14)
	v_mfma_f32_16x16x32_f16 v[56:59], v[192:195], v[172:175], v[56:59]
	s_waitcnt lgkmcnt(13)
	v_mfma_f32_16x16x32_f16 v[60:63], v[196:199], v[172:175], v[60:63]
	s_waitcnt lgkmcnt(12)
	v_mfma_f32_16x16x32_f16 v[64:67], v[200:203], v[172:175], v[64:67]
	s_waitcnt lgkmcnt(11)
	v_mfma_f32_16x16x32_f16 v[68:71], v[204:207], v[172:175], v[68:71]
	s_waitcnt lgkmcnt(10)
	v_mfma_f32_16x16x32_f16 v[72:75], v[192:195], v[176:179], v[72:75]
	v_mfma_f32_16x16x32_f16 v[76:79], v[196:199], v[176:179], v[76:79]
	v_mfma_f32_16x16x32_f16 v[80:83], v[200:203], v[176:179], v[80:83]
	v_mfma_f32_16x16x32_f16 v[84:87], v[204:207], v[176:179], v[84:87]
	s_waitcnt lgkmcnt(9)
	v_mfma_f32_16x16x32_f16 v[88:91], v[192:195], v[180:183], v[88:91]
	v_mfma_f32_16x16x32_f16 v[92:95], v[196:199], v[180:183], v[92:95]
	v_mfma_f32_16x16x32_f16 v[96:99], v[200:203], v[180:183], v[96:99]
	v_mfma_f32_16x16x32_f16 v[100:103], v[204:207], v[180:183], v[100:103]
	s_waitcnt lgkmcnt(8)
	v_mfma_f32_16x16x32_f16 v[104:107], v[192:195], v[184:187], v[104:107]
	v_mfma_f32_16x16x32_f16 v[108:111], v[196:199], v[184:187], v[108:111]
	v_mfma_f32_16x16x32_f16 v[112:115], v[200:203], v[184:187], v[112:115]
	v_mfma_f32_16x16x32_f16 v[116:119], v[204:207], v[184:187], v[116:119]
	s_waitcnt lgkmcnt(7)
	ds_read_b128 v[172:175], v20
	ds_read_b128 v[192:195], v22
	ds_read_b128 v[196:199], v22 offset:2048
	ds_read_b128 v[200:203], v22 offset:4096
	ds_read_b128 v[204:207], v22 offset:6144
	ds_read_b128 v[176:179], v20 offset:2048
	ds_read_b128 v[180:183], v20 offset:4096
	ds_read_b128 v[184:187], v20 offset:6144
	s_waitcnt lgkmcnt(14)
	v_mfma_f32_16x16x32_f16 v[56:59], v[156:159], v[136:139], v[56:59]
	s_waitcnt lgkmcnt(13)
	v_mfma_f32_16x16x32_f16 v[60:63], v[160:163], v[136:139], v[60:63]
	s_waitcnt lgkmcnt(12)
	v_mfma_f32_16x16x32_f16 v[64:67], v[164:167], v[136:139], v[64:67]
	s_waitcnt lgkmcnt(11)
	v_mfma_f32_16x16x32_f16 v[68:71], v[168:171], v[136:139], v[68:71]
	s_waitcnt lgkmcnt(10)
	v_mfma_f32_16x16x32_f16 v[72:75], v[156:159], v[140:143], v[72:75]
	v_mfma_f32_16x16x32_f16 v[76:79], v[160:163], v[140:143], v[76:79]
	v_mfma_f32_16x16x32_f16 v[80:83], v[164:167], v[140:143], v[80:83]
	v_mfma_f32_16x16x32_f16 v[84:87], v[168:171], v[140:143], v[84:87]
	s_waitcnt lgkmcnt(9)
	v_mfma_f32_16x16x32_f16 v[88:91], v[156:159], v[144:147], v[88:91]
	v_mfma_f32_16x16x32_f16 v[92:95], v[160:163], v[144:147], v[92:95]
	v_mfma_f32_16x16x32_f16 v[96:99], v[164:167], v[144:147], v[96:99]
	v_mfma_f32_16x16x32_f16 v[100:103], v[168:171], v[144:147], v[100:103]
	s_waitcnt lgkmcnt(8)
	v_mfma_f32_16x16x32_f16 v[104:107], v[156:159], v[148:151], v[104:107]
	v_mfma_f32_16x16x32_f16 v[108:111], v[160:163], v[148:151], v[108:111]
	v_mfma_f32_16x16x32_f16 v[112:115], v[164:167], v[148:151], v[112:115]
	v_mfma_f32_16x16x32_f16 v[116:119], v[168:171], v[148:151], v[116:119]
	s_waitcnt vmcnt(0) lgkmcnt(0)
	s_barrier
	s_waitcnt lgkmcnt(7)
	ds_read_b128 v[136:139], v15
	ds_read_b128 v[156:159], v17
	ds_read_b128 v[160:163], v17 offset:2048
	ds_read_b128 v[164:167], v17 offset:4096
	ds_read_b128 v[168:171], v17 offset:6144
	ds_read_b128 v[140:143], v15 offset:2048
	ds_read_b128 v[144:147], v15 offset:4096
	ds_read_b128 v[148:151], v15 offset:6144
	s_waitcnt lgkmcnt(14)
	v_mfma_f32_16x16x32_f16 v[56:59], v[192:195], v[172:175], v[56:59]
	s_waitcnt lgkmcnt(13)
	v_mfma_f32_16x16x32_f16 v[60:63], v[196:199], v[172:175], v[60:63]
	s_waitcnt lgkmcnt(12)
	v_mfma_f32_16x16x32_f16 v[64:67], v[200:203], v[172:175], v[64:67]
	s_waitcnt lgkmcnt(11)
	v_mfma_f32_16x16x32_f16 v[68:71], v[204:207], v[172:175], v[68:71]
	s_waitcnt lgkmcnt(10)
	v_mfma_f32_16x16x32_f16 v[72:75], v[192:195], v[176:179], v[72:75]
	v_mfma_f32_16x16x32_f16 v[76:79], v[196:199], v[176:179], v[76:79]
	v_mfma_f32_16x16x32_f16 v[80:83], v[200:203], v[176:179], v[80:83]
	v_mfma_f32_16x16x32_f16 v[84:87], v[204:207], v[176:179], v[84:87]
	s_waitcnt lgkmcnt(9)
	v_mfma_f32_16x16x32_f16 v[88:91], v[192:195], v[180:183], v[88:91]
	v_mfma_f32_16x16x32_f16 v[92:95], v[196:199], v[180:183], v[92:95]
	v_mfma_f32_16x16x32_f16 v[96:99], v[200:203], v[180:183], v[96:99]
	v_mfma_f32_16x16x32_f16 v[100:103], v[204:207], v[180:183], v[100:103]
	s_waitcnt lgkmcnt(8)
	v_mfma_f32_16x16x32_f16 v[104:107], v[192:195], v[184:187], v[104:107]
	v_mfma_f32_16x16x32_f16 v[108:111], v[196:199], v[184:187], v[108:111]
	v_mfma_f32_16x16x32_f16 v[112:115], v[200:203], v[184:187], v[112:115]
	v_mfma_f32_16x16x32_f16 v[116:119], v[204:207], v[184:187], v[116:119]
	s_waitcnt lgkmcnt(7)
	ds_read_b128 v[172:175], v16
	ds_read_b128 v[192:195], v18
	ds_read_b128 v[196:199], v18 offset:2048
	ds_read_b128 v[200:203], v18 offset:4096
	ds_read_b128 v[204:207], v18 offset:6144
	ds_read_b128 v[176:179], v16 offset:2048
	ds_read_b128 v[180:183], v16 offset:4096
	ds_read_b128 v[184:187], v16 offset:6144
	s_waitcnt lgkmcnt(14)
	v_mfma_f32_16x16x32_f16 v[56:59], v[156:159], v[136:139], v[56:59]
	s_waitcnt lgkmcnt(13)
	v_mfma_f32_16x16x32_f16 v[60:63], v[160:163], v[136:139], v[60:63]
	s_waitcnt lgkmcnt(12)
	v_mfma_f32_16x16x32_f16 v[64:67], v[164:167], v[136:139], v[64:67]
	s_waitcnt lgkmcnt(11)
	v_mfma_f32_16x16x32_f16 v[68:71], v[168:171], v[136:139], v[68:71]
	s_waitcnt lgkmcnt(10)
	v_mfma_f32_16x16x32_f16 v[72:75], v[156:159], v[140:143], v[72:75]
	v_mfma_f32_16x16x32_f16 v[76:79], v[160:163], v[140:143], v[76:79]
	v_mfma_f32_16x16x32_f16 v[80:83], v[164:167], v[140:143], v[80:83]
	v_mfma_f32_16x16x32_f16 v[84:87], v[168:171], v[140:143], v[84:87]
	s_waitcnt lgkmcnt(9)
	v_mfma_f32_16x16x32_f16 v[88:91], v[156:159], v[144:147], v[88:91]
	v_mfma_f32_16x16x32_f16 v[92:95], v[160:163], v[144:147], v[92:95]
	v_mfma_f32_16x16x32_f16 v[96:99], v[164:167], v[144:147], v[96:99]
	v_mfma_f32_16x16x32_f16 v[100:103], v[168:171], v[144:147], v[100:103]
	s_waitcnt lgkmcnt(8)
	v_mfma_f32_16x16x32_f16 v[104:107], v[156:159], v[148:151], v[104:107]
	v_mfma_f32_16x16x32_f16 v[108:111], v[160:163], v[148:151], v[108:111]
	v_mfma_f32_16x16x32_f16 v[112:115], v[164:167], v[148:151], v[112:115]
	v_mfma_f32_16x16x32_f16 v[116:119], v[168:171], v[148:151], v[116:119]
	s_waitcnt lgkmcnt(6)
	v_mfma_f32_16x16x32_f16 v[56:59], v[192:195], v[172:175], v[56:59]
	s_waitcnt lgkmcnt(5)
	v_mfma_f32_16x16x32_f16 v[60:63], v[196:199], v[172:175], v[60:63]
	s_waitcnt lgkmcnt(4)
	v_mfma_f32_16x16x32_f16 v[64:67], v[200:203], v[172:175], v[64:67]
	s_waitcnt lgkmcnt(3)
	v_mfma_f32_16x16x32_f16 v[68:71], v[204:207], v[172:175], v[68:71]
	s_waitcnt lgkmcnt(2)
	v_mfma_f32_16x16x32_f16 v[72:75], v[192:195], v[176:179], v[72:75]
	v_mfma_f32_16x16x32_f16 v[76:79], v[196:199], v[176:179], v[76:79]
	v_mfma_f32_16x16x32_f16 v[80:83], v[200:203], v[176:179], v[80:83]
	v_mfma_f32_16x16x32_f16 v[84:87], v[204:207], v[176:179], v[84:87]
	s_waitcnt lgkmcnt(1)
	v_mfma_f32_16x16x32_f16 v[88:91], v[192:195], v[180:183], v[88:91]
	v_mfma_f32_16x16x32_f16 v[92:95], v[196:199], v[180:183], v[92:95]
	v_mfma_f32_16x16x32_f16 v[96:99], v[200:203], v[180:183], v[96:99]
	v_mfma_f32_16x16x32_f16 v[100:103], v[204:207], v[180:183], v[100:103]
	s_waitcnt lgkmcnt(0)
	v_mfma_f32_16x16x32_f16 v[104:107], v[192:195], v[184:187], v[104:107]
	v_mfma_f32_16x16x32_f16 v[108:111], v[196:199], v[184:187], v[108:111]
	v_mfma_f32_16x16x32_f16 v[112:115], v[200:203], v[184:187], v[112:115]
	v_mfma_f32_16x16x32_f16 v[116:119], v[204:207], v[184:187], v[116:119]
	s_nop 7
	s_nop 1
	v_mov_b32_e32 v211, s19
	v_add_f32_e32 v56, v56, v24
	v_add_f32_e32 v57, v57, v25
	v_add_f32_e32 v58, v58, v26
	v_add_f32_e32 v59, v59, v27
	v_add_f32_e32 v60, v60, v28
	v_add_f32_e32 v61, v61, v29
	v_add_f32_e32 v62, v62, v30
	v_add_f32_e32 v63, v63, v31
	v_add_f32_e32 v64, v64, v32
	v_add_f32_e32 v65, v65, v33
	v_add_f32_e32 v66, v66, v34
	v_add_f32_e32 v67, v67, v35
	v_add_f32_e32 v68, v68, v36
	v_add_f32_e32 v69, v69, v37
	v_add_f32_e32 v70, v70, v38
	v_add_f32_e32 v71, v71, v39
	v_mul_f32_e32 v208, v56, v56
	v_fmac_f32_e32 v208, v57, v57
	v_fmac_f32_e32 v208, v58, v58
	v_fmac_f32_e32 v208, v59, v59
	v_fmac_f32_e32 v208, v60, v60
	v_fmac_f32_e32 v208, v61, v61
	v_fmac_f32_e32 v208, v62, v62
	v_fmac_f32_e32 v208, v63, v63
	v_fmac_f32_e32 v208, v64, v64
	v_fmac_f32_e32 v208, v65, v65
	v_fmac_f32_e32 v208, v66, v66
	v_fmac_f32_e32 v208, v67, v67
	v_fmac_f32_e32 v208, v68, v68
	v_fmac_f32_e32 v208, v69, v69
	v_fmac_f32_e32 v208, v70, v70
	v_fmac_f32_e32 v208, v71, v71
	v_mov_b32_e32 v209, v208
	s_nop 1
	v_permlane16_swap_b32_e32 v208, v209
	v_add_f32_e32 v208, v208, v209
	v_mov_b32_e32 v209, v208
	s_nop 1
	v_permlane32_swap_b32_e32 v208, v209
	v_add_f32_e32 v208, v208, v209
	v_mov_b32_e32 v210, 0x358637bd
	v_fmac_f32_e32 v210, 0x3c800000, v208
	v_rsq_f32_e32 v210, v210
	s_add_u32 s24, s29, 0
	s_lshr_b32 s8, s24, 1
	s_lshl_b32 s8, s8, 12
	s_and_b32 s24, s24, 1
	s_lshl_b32 s24, s24, 8
	s_add_u32 s8, s8, s24
	v_mul_f32_e32 v210, v211, v210
	v_add_u32_e32 v212, s8, v23
	v_mul_f32_e32 v56, v56, v210
	v_mul_f32_e32 v57, v57, v210
	v_mul_f32_e32 v58, v58, v210
	v_mul_f32_e32 v59, v59, v210
	v_mul_f32_e32 v56, v56, v40
	v_mul_f32_e32 v57, v57, v41
	v_mul_f32_e32 v58, v58, v42
	v_mul_f32_e32 v59, v59, v43
	v_cvt_pk_f16_f32 v56, v56, v57
	v_cvt_pk_f16_f32 v57, v58, v59
	global_store_dwordx2 v212, v[56:57], s[22:23] offset:0
	v_mul_f32_e32 v60, v60, v210
	v_mul_f32_e32 v61, v61, v210
	v_mul_f32_e32 v62, v62, v210
	v_mul_f32_e32 v63, v63, v210
	v_mul_f32_e32 v60, v60, v44
	v_mul_f32_e32 v61, v61, v45
	v_mul_f32_e32 v62, v62, v46
	v_mul_f32_e32 v63, v63, v47
	v_cvt_pk_f16_f32 v60, v60, v61
	v_cvt_pk_f16_f32 v61, v62, v63
	global_store_dwordx2 v212, v[60:61], s[22:23] offset:1024
	v_mul_f32_e32 v64, v64, v210
	v_mul_f32_e32 v65, v65, v210
	v_mul_f32_e32 v66, v66, v210
	v_mul_f32_e32 v67, v67, v210
	v_mul_f32_e32 v64, v64, v48
	v_mul_f32_e32 v65, v65, v49
	v_mul_f32_e32 v66, v66, v50
	v_mul_f32_e32 v67, v67, v51
	v_cvt_pk_f16_f32 v64, v64, v65
	v_cvt_pk_f16_f32 v65, v66, v67
	global_store_dwordx2 v212, v[64:65], s[22:23] offset:2048
	v_mul_f32_e32 v68, v68, v210
	v_mul_f32_e32 v69, v69, v210
	v_mul_f32_e32 v70, v70, v210
	v_mul_f32_e32 v71, v71, v210
	v_mul_f32_e32 v68, v68, v52
	v_mul_f32_e32 v69, v69, v53
	v_mul_f32_e32 v70, v70, v54
	v_mul_f32_e32 v71, v71, v55
	v_cvt_pk_f16_f32 v68, v68, v69
	v_cvt_pk_f16_f32 v69, v70, v71
	global_store_dwordx2 v212, v[68:69], s[22:23] offset:3072
	v_add_f32_e32 v72, v72, v24
	v_add_f32_e32 v73, v73, v25
	v_add_f32_e32 v74, v74, v26
	v_add_f32_e32 v75, v75, v27
	v_add_f32_e32 v76, v76, v28
	v_add_f32_e32 v77, v77, v29
	v_add_f32_e32 v78, v78, v30
	v_add_f32_e32 v79, v79, v31
	v_add_f32_e32 v80, v80, v32
	v_add_f32_e32 v81, v81, v33
	v_add_f32_e32 v82, v82, v34
	v_add_f32_e32 v83, v83, v35
	v_add_f32_e32 v84, v84, v36
	v_add_f32_e32 v85, v85, v37
	v_add_f32_e32 v86, v86, v38
	v_add_f32_e32 v87, v87, v39
	v_mul_f32_e32 v208, v72, v72
	v_fmac_f32_e32 v208, v73, v73
	v_fmac_f32_e32 v208, v74, v74
	v_fmac_f32_e32 v208, v75, v75
	v_fmac_f32_e32 v208, v76, v76
	v_fmac_f32_e32 v208, v77, v77
	v_fmac_f32_e32 v208, v78, v78
	v_fmac_f32_e32 v208, v79, v79
	v_fmac_f32_e32 v208, v80, v80
	v_fmac_f32_e32 v208, v81, v81
	v_fmac_f32_e32 v208, v82, v82
	v_fmac_f32_e32 v208, v83, v83
	v_fmac_f32_e32 v208, v84, v84
	v_fmac_f32_e32 v208, v85, v85
	v_fmac_f32_e32 v208, v86, v86
	v_fmac_f32_e32 v208, v87, v87
	v_mov_b32_e32 v209, v208
	s_nop 1
	v_permlane16_swap_b32_e32 v208, v209
	v_add_f32_e32 v208, v208, v209
	v_mov_b32_e32 v209, v208
	s_nop 1
	v_permlane32_swap_b32_e32 v208, v209
	v_add_f32_e32 v208, v208, v209
	v_mov_b32_e32 v210, 0x358637bd
	v_fmac_f32_e32 v210, 0x3c800000, v208
	v_rsq_f32_e32 v210, v210
	s_add_u32 s24, s29, 1
	s_lshr_b32 s8, s24, 1
	s_lshl_b32 s8, s8, 12
	s_and_b32 s24, s24, 1
	s_lshl_b32 s24, s24, 8
	s_add_u32 s8, s8, s24
	v_mul_f32_e32 v210, v211, v210
	v_add_u32_e32 v212, s8, v23
	v_mul_f32_e32 v72, v72, v210
	v_mul_f32_e32 v73, v73, v210
	v_mul_f32_e32 v74, v74, v210
	v_mul_f32_e32 v75, v75, v210
	v_mul_f32_e32 v72, v72, v40
	v_mul_f32_e32 v73, v73, v41
	v_mul_f32_e32 v74, v74, v42
	v_mul_f32_e32 v75, v75, v43
	v_cvt_pk_f16_f32 v72, v72, v73
	v_cvt_pk_f16_f32 v73, v74, v75
	global_store_dwordx2 v212, v[72:73], s[22:23] offset:0
	v_mul_f32_e32 v76, v76, v210
	v_mul_f32_e32 v77, v77, v210
	v_mul_f32_e32 v78, v78, v210
	v_mul_f32_e32 v79, v79, v210
	v_mul_f32_e32 v76, v76, v44
	v_mul_f32_e32 v77, v77, v45
	v_mul_f32_e32 v78, v78, v46
	v_mul_f32_e32 v79, v79, v47
	v_cvt_pk_f16_f32 v76, v76, v77
	v_cvt_pk_f16_f32 v77, v78, v79
	global_store_dwordx2 v212, v[76:77], s[22:23] offset:1024
	v_mul_f32_e32 v80, v80, v210
	v_mul_f32_e32 v81, v81, v210
	v_mul_f32_e32 v82, v82, v210
	v_mul_f32_e32 v83, v83, v210
	v_mul_f32_e32 v80, v80, v48
	v_mul_f32_e32 v81, v81, v49
	v_mul_f32_e32 v82, v82, v50
	v_mul_f32_e32 v83, v83, v51
	v_cvt_pk_f16_f32 v80, v80, v81
	v_cvt_pk_f16_f32 v81, v82, v83
	global_store_dwordx2 v212, v[80:81], s[22:23] offset:2048
	v_mul_f32_e32 v84, v84, v210
	v_mul_f32_e32 v85, v85, v210
	v_mul_f32_e32 v86, v86, v210
	v_mul_f32_e32 v87, v87, v210
	v_mul_f32_e32 v84, v84, v52
	v_mul_f32_e32 v85, v85, v53
	v_mul_f32_e32 v86, v86, v54
	v_mul_f32_e32 v87, v87, v55
	v_cvt_pk_f16_f32 v84, v84, v85
	v_cvt_pk_f16_f32 v85, v86, v87
	global_store_dwordx2 v212, v[84:85], s[22:23] offset:3072
	v_add_f32_e32 v88, v88, v24
	v_add_f32_e32 v89, v89, v25
	v_add_f32_e32 v90, v90, v26
	v_add_f32_e32 v91, v91, v27
	v_add_f32_e32 v92, v92, v28
	v_add_f32_e32 v93, v93, v29
	v_add_f32_e32 v94, v94, v30
	v_add_f32_e32 v95, v95, v31
	v_add_f32_e32 v96, v96, v32
	v_add_f32_e32 v97, v97, v33
	v_add_f32_e32 v98, v98, v34
	v_add_f32_e32 v99, v99, v35
	v_add_f32_e32 v100, v100, v36
	v_add_f32_e32 v101, v101, v37
	v_add_f32_e32 v102, v102, v38
	v_add_f32_e32 v103, v103, v39
	v_mul_f32_e32 v208, v88, v88
	v_fmac_f32_e32 v208, v89, v89
	v_fmac_f32_e32 v208, v90, v90
	v_fmac_f32_e32 v208, v91, v91
	v_fmac_f32_e32 v208, v92, v92
	v_fmac_f32_e32 v208, v93, v93
	v_fmac_f32_e32 v208, v94, v94
	v_fmac_f32_e32 v208, v95, v95
	v_fmac_f32_e32 v208, v96, v96
	v_fmac_f32_e32 v208, v97, v97
	v_fmac_f32_e32 v208, v98, v98
	v_fmac_f32_e32 v208, v99, v99
	v_fmac_f32_e32 v208, v100, v100
	v_fmac_f32_e32 v208, v101, v101
	v_fmac_f32_e32 v208, v102, v102
	v_fmac_f32_e32 v208, v103, v103
	v_mov_b32_e32 v209, v208
	s_nop 1
	v_permlane16_swap_b32_e32 v208, v209
	v_add_f32_e32 v208, v208, v209
	v_mov_b32_e32 v209, v208
	s_nop 1
	v_permlane32_swap_b32_e32 v208, v209
	v_add_f32_e32 v208, v208, v209
	v_mov_b32_e32 v210, 0x358637bd
	v_fmac_f32_e32 v210, 0x3c800000, v208
	v_rsq_f32_e32 v210, v210
	s_add_u32 s24, s29, 2
	s_lshr_b32 s8, s24, 1
	s_lshl_b32 s8, s8, 12
	s_and_b32 s24, s24, 1
	s_lshl_b32 s24, s24, 8
	s_add_u32 s8, s8, s24
	v_mul_f32_e32 v210, v211, v210
	v_add_u32_e32 v212, s8, v23
	v_mul_f32_e32 v88, v88, v210
	v_mul_f32_e32 v89, v89, v210
	v_mul_f32_e32 v90, v90, v210
	v_mul_f32_e32 v91, v91, v210
	v_mul_f32_e32 v88, v88, v40
	v_mul_f32_e32 v89, v89, v41
	v_mul_f32_e32 v90, v90, v42
	v_mul_f32_e32 v91, v91, v43
	v_cvt_pk_f16_f32 v88, v88, v89
	v_cvt_pk_f16_f32 v89, v90, v91
	global_store_dwordx2 v212, v[88:89], s[22:23] offset:0
	v_mul_f32_e32 v92, v92, v210
	v_mul_f32_e32 v93, v93, v210
	v_mul_f32_e32 v94, v94, v210
	v_mul_f32_e32 v95, v95, v210
	v_mul_f32_e32 v92, v92, v44
	v_mul_f32_e32 v93, v93, v45
	v_mul_f32_e32 v94, v94, v46
	v_mul_f32_e32 v95, v95, v47
	v_cvt_pk_f16_f32 v92, v92, v93
	v_cvt_pk_f16_f32 v93, v94, v95
	global_store_dwordx2 v212, v[92:93], s[22:23] offset:1024
	v_mul_f32_e32 v96, v96, v210
	v_mul_f32_e32 v97, v97, v210
	v_mul_f32_e32 v98, v98, v210
	v_mul_f32_e32 v99, v99, v210
	v_mul_f32_e32 v96, v96, v48
	v_mul_f32_e32 v97, v97, v49
	v_mul_f32_e32 v98, v98, v50
	v_mul_f32_e32 v99, v99, v51
	v_cvt_pk_f16_f32 v96, v96, v97
	v_cvt_pk_f16_f32 v97, v98, v99
	global_store_dwordx2 v212, v[96:97], s[22:23] offset:2048
	v_mul_f32_e32 v100, v100, v210
	v_mul_f32_e32 v101, v101, v210
	v_mul_f32_e32 v102, v102, v210
	v_mul_f32_e32 v103, v103, v210
	v_mul_f32_e32 v100, v100, v52
	v_mul_f32_e32 v101, v101, v53
	v_mul_f32_e32 v102, v102, v54
	v_mul_f32_e32 v103, v103, v55
	v_cvt_pk_f16_f32 v100, v100, v101
	v_cvt_pk_f16_f32 v101, v102, v103
	global_store_dwordx2 v212, v[100:101], s[22:23] offset:3072
	v_add_f32_e32 v104, v104, v24
	v_add_f32_e32 v105, v105, v25
	v_add_f32_e32 v106, v106, v26
	v_add_f32_e32 v107, v107, v27
	v_add_f32_e32 v108, v108, v28
	v_add_f32_e32 v109, v109, v29
	v_add_f32_e32 v110, v110, v30
	v_add_f32_e32 v111, v111, v31
	v_add_f32_e32 v112, v112, v32
	v_add_f32_e32 v113, v113, v33
	v_add_f32_e32 v114, v114, v34
	v_add_f32_e32 v115, v115, v35
	v_add_f32_e32 v116, v116, v36
	v_add_f32_e32 v117, v117, v37
	v_add_f32_e32 v118, v118, v38
	v_add_f32_e32 v119, v119, v39
	v_mul_f32_e32 v208, v104, v104
	v_fmac_f32_e32 v208, v105, v105
	v_fmac_f32_e32 v208, v106, v106
	v_fmac_f32_e32 v208, v107, v107
	v_fmac_f32_e32 v208, v108, v108
	v_fmac_f32_e32 v208, v109, v109
	v_fmac_f32_e32 v208, v110, v110
	v_fmac_f32_e32 v208, v111, v111
	v_fmac_f32_e32 v208, v112, v112
	v_fmac_f32_e32 v208, v113, v113
	v_fmac_f32_e32 v208, v114, v114
	v_fmac_f32_e32 v208, v115, v115
	v_fmac_f32_e32 v208, v116, v116
	v_fmac_f32_e32 v208, v117, v117
	v_fmac_f32_e32 v208, v118, v118
	v_fmac_f32_e32 v208, v119, v119
	v_mov_b32_e32 v209, v208
	s_nop 1
	v_permlane16_swap_b32_e32 v208, v209
	v_add_f32_e32 v208, v208, v209
	v_mov_b32_e32 v209, v208
	s_nop 1
	v_permlane32_swap_b32_e32 v208, v209
	v_add_f32_e32 v208, v208, v209
	v_mov_b32_e32 v210, 0x358637bd
	v_fmac_f32_e32 v210, 0x3c800000, v208
	v_rsq_f32_e32 v210, v210
	s_add_u32 s24, s29, 3
	s_lshr_b32 s8, s24, 1
	s_lshl_b32 s8, s8, 12
	s_and_b32 s24, s24, 1
	s_lshl_b32 s24, s24, 8
	s_add_u32 s8, s8, s24
	v_mul_f32_e32 v210, v211, v210
	v_add_u32_e32 v212, s8, v23
	v_mul_f32_e32 v104, v104, v210
	v_mul_f32_e32 v105, v105, v210
	v_mul_f32_e32 v106, v106, v210
	v_mul_f32_e32 v107, v107, v210
	v_mul_f32_e32 v104, v104, v40
	v_mul_f32_e32 v105, v105, v41
	v_mul_f32_e32 v106, v106, v42
	v_mul_f32_e32 v107, v107, v43
	v_cvt_pk_f16_f32 v104, v104, v105
	v_cvt_pk_f16_f32 v105, v106, v107
	global_store_dwordx2 v212, v[104:105], s[22:23] offset:0
	v_mul_f32_e32 v108, v108, v210
	v_mul_f32_e32 v109, v109, v210
	v_mul_f32_e32 v110, v110, v210
	v_mul_f32_e32 v111, v111, v210
	v_mul_f32_e32 v108, v108, v44
	v_mul_f32_e32 v109, v109, v45
	v_mul_f32_e32 v110, v110, v46
	v_mul_f32_e32 v111, v111, v47
	v_cvt_pk_f16_f32 v108, v108, v109
	v_cvt_pk_f16_f32 v109, v110, v111
	global_store_dwordx2 v212, v[108:109], s[22:23] offset:1024
	v_mul_f32_e32 v112, v112, v210
	v_mul_f32_e32 v113, v113, v210
	v_mul_f32_e32 v114, v114, v210
	v_mul_f32_e32 v115, v115, v210
	v_mul_f32_e32 v112, v112, v48
	v_mul_f32_e32 v113, v113, v49
	v_mul_f32_e32 v114, v114, v50
	v_mul_f32_e32 v115, v115, v51
	v_cvt_pk_f16_f32 v112, v112, v113
	v_cvt_pk_f16_f32 v113, v114, v115
	global_store_dwordx2 v212, v[112:113], s[22:23] offset:2048
	v_mul_f32_e32 v116, v116, v210
	v_mul_f32_e32 v117, v117, v210
	v_mul_f32_e32 v118, v118, v210
	v_mul_f32_e32 v119, v119, v210
	v_mul_f32_e32 v116, v116, v52
	v_mul_f32_e32 v117, v117, v53
	v_mul_f32_e32 v118, v118, v54
	v_mul_f32_e32 v119, v119, v55
	v_cvt_pk_f16_f32 v116, v116, v117
	v_cvt_pk_f16_f32 v117, v118, v119
	global_store_dwordx2 v212, v[116:117], s[22:23] offset:3072
	s_branch .Lpf_done
.Lpf_vKA:
	s_add_u32 m0, s28, 0x0
	s_nop 0
	global_load_lds_dwordx4 v10, s[4:5]
	s_add_u32 m0, s28, 0x2000
	s_nop 0
	global_load_lds_dwordx4 v11, s[4:5]
	s_add_u32 m0, s28, 0x4000
	s_nop 0
	global_load_lds_dwordx4 v12, s[4:5]
	s_add_u32 m0, s28, 0x6000
	s_nop 0
	global_load_lds_dwordx4 v13, s[4:5]
	s_add_u32 m0, s28, 0x8000
	s_nop 0
	global_load_lds_dwordx4 v14, s[4:5]
	s_add_u32 s4, s4, s20
	s_addc_u32 s5, s5, 0
	s_add_u32 m0, s28, 0x9000
	s_nop 0
	global_load_lds_dwordx4 v10, s[6:7]
	s_add_u32 m0, s28, 0xb000
	s_nop 0
	global_load_lds_dwordx4 v11, s[6:7]
	s_add_u32 s6, s6, s20
	s_addc_u32 s7, s7, 0
	s_add_u32 m0, s28, 0xd000
	s_nop 0
	global_load_lds_dwordx4 v10, s[4:5]
	s_add_u32 m0, s28, 0xf000
	s_nop 0
	global_load_lds_dwordx4 v11, s[4:5]
	s_add_u32 m0, s28, 0x11000
	s_nop 0
	global_load_lds_dwordx4 v12, s[4:5]
	s_add_u32 m0, s28, 0x13000
	s_nop 0
	global_load_lds_dwordx4 v13, s[4:5]
	s_add_u32 m0, s28, 0x15000
	s_nop 0
	global_load_lds_dwordx4 v14, s[4:5]
	s_add_u32 s4, s4, s20
	s_addc_u32 s5, s5, 0
	s_add_u32 m0, s28, 0x16000
	s_nop 0
	global_load_lds_dwordx4 v10, s[6:7]
	s_add_u32 m0, s28, 0x18000
	s_nop 0
	global_load_lds_dwordx4 v11, s[6:7]
	s_add_u32 s6, s6, s20
	s_addc_u32 s7, s7, 0
	s_add_u32 m0, s28, 0x1a000
	s_nop 0
	global_load_lds_dwordx4 v10, s[4:5]
	s_add_u32 m0, s28, 0x1c000
	s_nop 0
	global_load_lds_dwordx4 v11, s[4:5]
	s_add_u32 m0, s28, 0x1e000
	s_nop 0
	global_load_lds_dwordx4 v12, s[4:5]
	s_add_u32 m0, s28, 0x20000
	s_nop 0
	global_load_lds_dwordx4 v13, s[4:5]
	s_add_u32 m0, s28, 0x22000
	s_nop 0
	global_load_lds_dwordx4 v14, s[4:5]
	s_add_u32 s4, s4, s20
	s_addc_u32 s5, s5, 0
	s_add_u32 m0, s28, 0x23000
	s_nop 0
	global_load_lds_dwordx4 v10, s[6:7]
	s_add_u32 m0, s28, 0x25000
	s_nop 0
	global_load_lds_dwordx4 v11, s[6:7]
	s_add_u32 s6, s6, s20
	s_addc_u32 s7, s7, 0
	s_waitcnt lgkmcnt(0)
	s_cmp_eq_u32 s9, 0
	s_cselect_b32 s51, s52, s53
	s_cmp_ge_i32 s10, s51
	s_cbranch_scc0 .Lpf_actKA
	s_waitcnt vmcnt(0)
	s_branch .Lpf_done
.Lpf_actKA:
	s_mul_i32 s25, s25, 0x50
	s_add_u32 s29, s10, s25
	s_lshr_b32 s29, s29, 4
	v_add_u32_e32 v5, s25, v3
	v_lshlrev_b32_e32 v5, 7, v5
	v_add_u32_e32 v15, v5, v6
	v_add_u32_e32 v16, v5, v7
	v_add_u32_e32 v5, 0x9000, v9
	v_add_u32_e32 v17, v5, v6
	v_add_u32_e32 v18, v5, v7
	v_add_u32_e32 v19, 0x1a000, v15
	v_add_u32_e32 v20, 0x1a000, v16
	v_add_u32_e32 v21, 0x1a000, v17
	v_add_u32_e32 v22, 0x1a000, v18
	v_lshlrev_b32_e32 v5, 4, v4
	global_load_dwordx4 v[24:27], v5, s[14:15] offset:0
	global_load_dwordx4 v[28:31], v5, s[14:15] offset:64
	global_load_dwordx4 v[32:35], v5, s[14:15] offset:128
	global_load_dwordx4 v[36:39], v5, s[14:15] offset:192
	global_load_dwordx4 v[40:43], v5, s[16:17] offset:0
	global_load_dwordx4 v[44:47], v5, s[16:17] offset:64
	global_load_dwordx4 v[48:51], v5, s[16:17] offset:128
	global_load_dwordx4 v[52:55], v5, s[16:17] offset:192
	s_waitcnt vmcnt(22) lgkmcnt(0)
	s_barrier
	s_waitcnt lgkmcnt(6)
	ds_read_b128 v[136:139], v15
	ds_read_b128 v[156:159], v17
	ds_read_b128 v[160:163], v17 offset:2048
	ds_read_b128 v[164:167], v17 offset:4096
	ds_read_b128 v[168:171], v17 offset:6144
	ds_read_b128 v[140:143], v15 offset:2048
	ds_read_b128 v[144:147], v15 offset:4096
	ds_read_b128 v[148:151], v15 offset:6144
	ds_read_b128 v[152:155], v15 offset:8192
	s_waitcnt lgkmcnt(6)
	ds_read_b128 v[172:175], v16
	ds_read_b128 v[192:195], v18
	ds_read_b128 v[196:199], v18 offset:2048
	ds_read_b128 v[200:203], v18 offset:4096
	ds_read_b128 v[204:207], v18 offset:6144
	ds_read_b128 v[176:179], v16 offset:2048
	ds_read_b128 v[180:183], v16 offset:4096
	ds_read_b128 v[184:187], v16 offset:6144
	ds_read_b128 v[188:191], v16 offset:8192
	v_mfma_f32_16x16x32_f16 v[56:59], v[156:159], v[136:139], 0
	s_waitcnt lgkmcnt(15)
	v_mfma_f32_16x16x32_f16 v[60:63], v[160:163], v[136:139], 0
	s_waitcnt lgkmcnt(14)
	v_mfma_f32_16x16x32_f16 v[64:67], v[164:167], v[136:139], 0
	s_waitcnt lgkmcnt(13)
	v_mfma_f32_16x16x32_f16 v[68:71], v[168:171], v[136:139], 0
	s_waitcnt lgkmcnt(12)
	v_mfma_f32_16x16x32_f16 v[72:75], v[156:159], v[140:143], 0
	v_mfma_f32_16x16x32_f16 v[76:79], v[160:163], v[140:143], 0
	v_mfma_f32_16x16x32_f16 v[80:83], v[164:167], v[140:143], 0
	v_mfma_f32_16x16x32_f16 v[84:87], v[168:171], v[140:143], 0
	s_waitcnt lgkmcnt(11)
	v_mfma_f32_16x16x32_f16 v[88:91], v[156:159], v[144:147], 0
	v_mfma_f32_16x16x32_f16 v[92:95], v[160:163], v[144:147], 0
	v_mfma_f32_16x16x32_f16 v[96:99], v[164:167], v[144:147], 0
	v_mfma_f32_16x16x32_f16 v[100:103], v[168:171], v[144:147], 0
	s_waitcnt lgkmcnt(10)
	v_mfma_f32_16x16x32_f16 v[104:107], v[156:159], v[148:151], 0
	v_mfma_f32_16x16x32_f16 v[108:111], v[160:163], v[148:151], 0
	v_mfma_f32_16x16x32_f16 v[112:115], v[164:167], v[148:151], 0
	v_mfma_f32_16x16x32_f16 v[116:119], v[168:171], v[148:151], 0
	s_waitcnt lgkmcnt(9)
	v_mfma_f32_16x16x32_f16 v[120:123], v[156:159], v[152:155], 0
	v_mfma_f32_16x16x32_f16 v[124:127], v[160:163], v[152:155], 0
	v_mfma_f32_16x16x32_f16 v[128:131], v[164:167], v[152:155], 0
	v_mfma_f32_16x16x32_f16 v[132:135], v[168:171], v[152:155], 0
	s_waitcnt vmcnt(15) lgkmcnt(0)
	s_barrier
	s_waitcnt lgkmcnt(6)
	ds_read_b128 v[136:139], v15 offset:53248
	ds_read_b128 v[156:159], v17 offset:53248
	ds_read_b128 v[160:163], v17 offset:55296
	ds_read_b128 v[164:167], v17 offset:57344
	ds_read_b128 v[168:171], v17 offset:59392
	ds_read_b128 v[140:143], v15 offset:55296
	ds_read_b128 v[144:147], v15 offset:57344
	ds_read_b128 v[148:151], v15 offset:59392
	ds_read_b128 v[152:155], v15 offset:61440
	v_mfma_f32_16x16x32_f16 v[56:59], v[192:195], v[172:175], v[56:59]
	s_add_u32 m0, s28, 0x0
	s_nop 0
	global_load_lds_dwordx4 v10, s[4:5]
	s_waitcnt lgkmcnt(15)
	v_mfma_f32_16x16x32_f16 v[60:63], v[196:199], v[172:175], v[60:63]
	s_waitcnt lgkmcnt(14)
	v_mfma_f32_16x16x32_f16 v[64:67], v[200:203], v[172:175], v[64:67]
	s_waitcnt lgkmcnt(13)
	v_mfma_f32_16x16x32_f16 v[68:71], v[204:207], v[172:175], v[68:71]
	s_waitcnt lgkmcnt(12)
	v_mfma_f32_16x16x32_f16 v[72:75], v[192:195], v[176:179], v[72:75]
	v_mfma_f32_16x16x32_f16 v[76:79], v[196:199], v[176:179], v[76:79]
	s_add_u32 m0, s28, 0x2000
	s_nop 0
	global_load_lds_dwordx4 v11, s[4:5]
	v_mfma_f32_16x16x32_f16 v[80:83], v[200:203], v[176:179], v[80:83]
	v_mfma_f32_16x16x32_f16 v[84:87], v[204:207], v[176:179], v[84:87]
	s_waitcnt lgkmcnt(11)
	v_mfma_f32_16x16x32_f16 v[88:91], v[192:195], v[180:183], v[88:91]
	v_mfma_f32_16x16x32_f16 v[92:95], v[196:199], v[180:183], v[92:95]
	v_mfma_f32_16x16x32_f16 v[96:99], v[200:203], v[180:183], v[96:99]
	s_add_u32 m0, s28, 0x4000
	s_nop 0
	global_load_lds_dwordx4 v12, s[4:5]
	v_mfma_f32_16x16x32_f16 v[100:103], v[204:207], v[180:183], v[100:103]
	s_waitcnt lgkmcnt(10)
	v_mfma_f32_16x16x32_f16 v[104:107], v[192:195], v[184:187], v[104:107]
	v_mfma_f32_16x16x32_f16 v[108:111], v[196:199], v[184:187], v[108:111]
	v_mfma_f32_16x16x32_f16 v[112:115], v[200:203], v[184:187], v[112:115]
	v_mfma_f32_16x16x32_f16 v[116:119], v[204:207], v[184:187], v[116:119]
	s_add_u32 m0, s28, 0x6000
	s_nop 0
	global_load_lds_dwordx4 v13, s[4:5]
	s_waitcnt lgkmcnt(9)
	v_mfma_f32_16x16x32_f16 v[120:123], v[192:195], v[188:191], v[120:123]
	v_mfma_f32_16x16x32_f16 v[124:127], v[196:199], v[188:191], v[124:127]
	v_mfma_f32_16x16x32_f16 v[128:131], v[200:203], v[188:191], v[128:131]
	v_mfma_f32_16x16x32_f16 v[132:135], v[204:207], v[188:191], v[132:135]
	s_waitcnt lgkmcnt(6)
	ds_read_b128 v[172:175], v16 offset:53248
	ds_read_b128 v[192:195], v18 offset:53248
	ds_read_b128 v[196:199], v18 offset:55296
	ds_read_b128 v[200:203], v18 offset:57344
	ds_read_b128 v[204:207], v18 offset:59392
	ds_read_b128 v[176:179], v16 offset:55296
	ds_read_b128 v[180:183], v16 offset:57344
	ds_read_b128 v[184:187], v16 offset:59392
	ds_read_b128 v[188:191], v16 offset:61440
	v_mfma_f32_16x16x32_f16 v[56:59], v[156:159], v[136:139], v[56:59]
	s_add_u32 m0, s28, 0x8000
	s_nop 0
	global_load_lds_dwordx4 v14, s[4:5]
	s_add_u32 s4, s4, s20
	s_addc_u32 s5, s5, 0
	s_waitcnt lgkmcnt(15)
	v_mfma_f32_16x16x32_f16 v[60:63], v[160:163], v[136:139], v[60:63]
	s_waitcnt lgkmcnt(14)
	v_mfma_f32_16x16x32_f16 v[64:67], v[164:167], v[136:139], v[64:67]
	s_waitcnt lgkmcnt(13)
	v_mfma_f32_16x16x32_f16 v[68:71], v[168:171], v[136:139], v[68:71]
	s_waitcnt lgkmcnt(12)
	v_mfma_f32_16x16x32_f16 v[72:75], v[156:159], v[140:143], v[72:75]
	v_mfma_f32_16x16x32_f16 v[76:79], v[160:163], v[140:143], v[76:79]
	v_mfma_f32_16x16x32_f16 v[80:83], v[164:167], v[140:143], v[80:83]
	s_add_u32 m0, s28, 0x9000
	s_nop 0
	global_load_lds_dwordx4 v10, s[6:7]
	v_mfma_f32_16x16x32_f16 v[84:87], v[168:171], v[140:143], v[84:87]
	s_waitcnt lgkmcnt(11)
	v_mfma_f32_16x16x32_f16 v[88:91], v[156:159], v[144:147], v[88:91]
	v_mfma_f32_16x16x32_f16 v[92:95], v[160:163], v[144:147], v[92:95]
	v_mfma_f32_16x16x32_f16 v[96:99], v[164:167], v[144:147], v[96:99]
	v_mfma_f32_16x16x32_f16 v[100:103], v[168:171], v[144:147], v[100:103]
	s_waitcnt lgkmcnt(10)
	v_mfma_f32_16x16x32_f16 v[104:107], v[156:159], v[148:151], v[104:107]
	v_mfma_f32_16x16x32_f16 v[108:111], v[160:163], v[148:151], v[108:111]
	s_add_u32 m0, s28, 0xb000
	s_nop 0
	global_load_lds_dwordx4 v11, s[6:7]
	s_add_u32 s6, s6, s20
	s_addc_u32 s7, s7, 0
	v_mfma_f32_16x16x32_f16 v[112:115], v[164:167], v[148:151], v[112:115]
	v_mfma_f32_16x16x32_f16 v[116:119], v[168:171], v[148:151], v[116:119]
	s_waitcnt lgkmcnt(9)
	v_mfma_f32_16x16x32_f16 v[120:123], v[156:159], v[152:155], v[120:123]
	v_mfma_f32_16x16x32_f16 v[124:127], v[160:163], v[152:155], v[124:127]
	v_mfma_f32_16x16x32_f16 v[128:131], v[164:167], v[152:155], v[128:131]
	v_mfma_f32_16x16x32_f16 v[132:135], v[168:171], v[152:155], v[132:135]
	s_waitcnt vmcnt(7) lgkmcnt(0)
	s_barrier
	s_waitcnt lgkmcnt(6)
	ds_read_b128 v[136:139], v19
	ds_read_b128 v[156:159], v21
	ds_read_b128 v[160:163], v21 offset:2048
	ds_read_b128 v[164:167], v21 offset:4096
	ds_read_b128 v[168:171], v21 offset:6144
	ds_read_b128 v[140:143], v19 offset:2048
	ds_read_b128 v[144:147], v19 offset:4096
	ds_read_b128 v[148:151], v19 offset:6144
	ds_read_b128 v[152:155], v19 offset:8192
	v_mfma_f32_16x16x32_f16 v[56:59], v[192:195], v[172:175], v[56:59]
	s_add_u32 m0, s28, 0xd000
	s_nop 0
	global_load_lds_dwordx4 v10, s[4:5]
	s_waitcnt lgkmcnt(15)
	v_mfma_f32_16x16x32_f16 v[60:63], v[196:199], v[172:175], v[60:63]
	s_waitcnt lgkmcnt(14)
	v_mfma_f32_16x16x32_f16 v[64:67], v[200:203], v[172:175], v[64:67]
	s_waitcnt lgkmcnt(13)
	v_mfma_f32_16x16x32_f16 v[68:71], v[204:207], v[172:175], v[68:71]
	s_waitcnt lgkmcnt(12)
	v_mfma_f32_16x16x32_f16 v[72:75], v[192:195], v[176:179], v[72:75]
	v_mfma_f32_16x16x32_f16 v[76:79], v[196:199], v[176:179], v[76:79]
	s_add_u32 m0, s28, 0xf000
	s_nop 0
	global_load_lds_dwordx4 v11, s[4:5]
	v_mfma_f32_16x16x32_f16 v[80:83], v[200:203], v[176:179], v[80:83]
	v_mfma_f32_16x16x32_f16 v[84:87], v[204:207], v[176:179], v[84:87]
	s_waitcnt lgkmcnt(11)
	v_mfma_f32_16x16x32_f16 v[88:91], v[192:195], v[180:183], v[88:91]
	v_mfma_f32_16x16x32_f16 v[92:95], v[196:199], v[180:183], v[92:95]
	v_mfma_f32_16x16x32_f16 v[96:99], v[200:203], v[180:183], v[96:99]
	s_add_u32 m0, s28, 0x11000
	s_nop 0
	global_load_lds_dwordx4 v12, s[4:5]
	v_mfma_f32_16x16x32_f16 v[100:103], v[204:207], v[180:183], v[100:103]
	s_waitcnt lgkmcnt(10)
	v_mfma_f32_16x16x32_f16 v[104:107], v[192:195], v[184:187], v[104:107]
	v_mfma_f32_16x16x32_f16 v[108:111], v[196:199], v[184:187], v[108:111]
	v_mfma_f32_16x16x32_f16 v[112:115], v[200:203], v[184:187], v[112:115]
	v_mfma_f32_16x16x32_f16 v[116:119], v[204:207], v[184:187], v[116:119]
	s_add_u32 m0, s28, 0x13000
	s_nop 0
	global_load_lds_dwordx4 v13, s[4:5]
	s_waitcnt lgkmcnt(9)
	v_mfma_f32_16x16x32_f16 v[120:123], v[192:195], v[188:191], v[120:123]
	v_mfma_f32_16x16x32_f16 v[124:127], v[196:199], v[188:191], v[124:127]
	v_mfma_f32_16x16x32_f16 v[128:131], v[200:203], v[188:191], v[128:131]
	v_mfma_f32_16x16x32_f16 v[132:135], v[204:207], v[188:191], v[132:135]
	s_waitcnt lgkmcnt(6)
	ds_read_b128 v[172:175], v20
	ds_read_b128 v[192:195], v22
	ds_read_b128 v[196:199], v22 offset:2048
	ds_read_b128 v[200:203], v22 offset:4096
	ds_read_b128 v[204:207], v22 offset:6144
	ds_read_b128 v[176:179], v20 offset:2048
	ds_read_b128 v[180:183], v20 offset:4096
	ds_read_b128 v[184:187], v20 offset:6144
	ds_read_b128 v[188:191], v20 offset:8192
	v_mfma_f32_16x16x32_f16 v[56:59], v[156:159], v[136:139], v[56:59]
	s_add_u32 m0, s28, 0x15000
	s_nop 0
	global_load_lds_dwordx4 v14, s[4:5]
	s_add_u32 s4, s4, s20
	s_addc_u32 s5, s5, 0
	s_waitcnt lgkmcnt(15)
	v_mfma_f32_16x16x32_f16 v[60:63], v[160:163], v[136:139], v[60:63]
	s_waitcnt lgkmcnt(14)
	v_mfma_f32_16x16x32_f16 v[64:67], v[164:167], v[136:139], v[64:67]
	s_waitcnt lgkmcnt(13)
	v_mfma_f32_16x16x32_f16 v[68:71], v[168:171], v[136:139], v[68:71]
	s_waitcnt lgkmcnt(12)
	v_mfma_f32_16x16x32_f16 v[72:75], v[156:159], v[140:143], v[72:75]
	v_mfma_f32_16x16x32_f16 v[76:79], v[160:163], v[140:143], v[76:79]
	v_mfma_f32_16x16x32_f16 v[80:83], v[164:167], v[140:143], v[80:83]
	s_add_u32 m0, s28, 0x16000
	s_nop 0
	global_load_lds_dwordx4 v10, s[6:7]
	v_mfma_f32_16x16x32_f16 v[84:87], v[168:171], v[140:143], v[84:87]
	s_waitcnt lgkmcnt(11)
	v_mfma_f32_16x16x32_f16 v[88:91], v[156:159], v[144:147], v[88:91]
	v_mfma_f32_16x16x32_f16 v[92:95], v[160:163], v[144:147], v[92:95]
	v_mfma_f32_16x16x32_f16 v[96:99], v[164:167], v[144:147], v[96:99]
	v_mfma_f32_16x16x32_f16 v[100:103], v[168:171], v[144:147], v[100:103]
	s_waitcnt lgkmcnt(10)
	v_mfma_f32_16x16x32_f16 v[104:107], v[156:159], v[148:151], v[104:107]
	v_mfma_f32_16x16x32_f16 v[108:111], v[160:163], v[148:151], v[108:111]
	s_add_u32 m0, s28, 0x18000
	s_nop 0
	global_load_lds_dwordx4 v11, s[6:7]
	s_add_u32 s6, s6, s20
	s_addc_u32 s7, s7, 0
	v_mfma_f32_16x16x32_f16 v[112:115], v[164:167], v[148:151], v[112:115]
	v_mfma_f32_16x16x32_f16 v[116:119], v[168:171], v[148:151], v[116:119]
	s_waitcnt lgkmcnt(9)
	v_mfma_f32_16x16x32_f16 v[120:123], v[156:159], v[152:155], v[120:123]
	v_mfma_f32_16x16x32_f16 v[124:127], v[160:163], v[152:155], v[124:127]
	v_mfma_f32_16x16x32_f16 v[128:131], v[164:167], v[152:155], v[128:131]
	v_mfma_f32_16x16x32_f16 v[132:135], v[168:171], v[152:155], v[132:135]
	s_waitcnt vmcnt(7) lgkmcnt(0)
	s_barrier
	s_waitcnt lgkmcnt(6)
	ds_read_b128 v[136:139], v15
	ds_read_b128 v[156:159], v17
	ds_read_b128 v[160:163], v17 offset:2048
	ds_read_b128 v[164:167], v17 offset:4096
	ds_read_b128 v[168:171], v17 offset:6144
	ds_read_b128 v[140:143], v15 offset:2048
	ds_read_b128 v[144:147], v15 offset:4096
	ds_read_b128 v[148:151], v15 offset:6144
	ds_read_b128 v[152:155], v15 offset:8192
	v_mfma_f32_16x16x32_f16 v[56:59], v[192:195], v[172:175], v[56:59]
	s_add_u32 m0, s28, 0x1a000
	s_nop 0
	global_load_lds_dwordx4 v10, s[4:5]
	s_waitcnt lgkmcnt(15)
	v_mfma_f32_16x16x32_f16 v[60:63], v[196:199], v[172:175], v[60:63]
	s_waitcnt lgkmcnt(14)
	v_mfma_f32_16x16x32_f16 v[64:67], v[200:203], v[172:175], v[64:67]
	s_waitcnt lgkmcnt(13)
	v_mfma_f32_16x16x32_f16 v[68:71], v[204:207], v[172:175], v[68:71]
	s_waitcnt lgkmcnt(12)
	v_mfma_f32_16x16x32_f16 v[72:75], v[192:195], v[176:179], v[72:75]
	v_mfma_f32_16x16x32_f16 v[76:79], v[196:199], v[176:179], v[76:79]
	s_add_u32 m0, s28, 0x1c000
	s_nop 0
	global_load_lds_dwordx4 v11, s[4:5]
	v_mfma_f32_16x16x32_f16 v[80:83], v[200:203], v[176:179], v[80:83]
	v_mfma_f32_16x16x32_f16 v[84:87], v[204:207], v[176:179], v[84:87]
	s_waitcnt lgkmcnt(11)
	v_mfma_f32_16x16x32_f16 v[88:91], v[192:195], v[180:183], v[88:91]
	v_mfma_f32_16x16x32_f16 v[92:95], v[196:199], v[180:183], v[92:95]
	v_mfma_f32_16x16x32_f16 v[96:99], v[200:203], v[180:183], v[96:99]
	s_add_u32 m0, s28, 0x1e000
	s_nop 0
	global_load_lds_dwordx4 v12, s[4:5]
	v_mfma_f32_16x16x32_f16 v[100:103], v[204:207], v[180:183], v[100:103]
	s_waitcnt lgkmcnt(10)
	v_mfma_f32_16x16x32_f16 v[104:107], v[192:195], v[184:187], v[104:107]
	v_mfma_f32_16x16x32_f16 v[108:111], v[196:199], v[184:187], v[108:111]
	v_mfma_f32_16x16x32_f16 v[112:115], v[200:203], v[184:187], v[112:115]
	v_mfma_f32_16x16x32_f16 v[116:119], v[204:207], v[184:187], v[116:119]
	s_add_u32 m0, s28, 0x20000
	s_nop 0
	global_load_lds_dwordx4 v13, s[4:5]
	s_waitcnt lgkmcnt(9)
	v_mfma_f32_16x16x32_f16 v[120:123], v[192:195], v[188:191], v[120:123]
	v_mfma_f32_16x16x32_f16 v[124:127], v[196:199], v[188:191], v[124:127]
	v_mfma_f32_16x16x32_f16 v[128:131], v[200:203], v[188:191], v[128:131]
	v_mfma_f32_16x16x32_f16 v[132:135], v[204:207], v[188:191], v[132:135]
	s_waitcnt lgkmcnt(6)
	ds_read_b128 v[172:175], v16
	ds_read_b128 v[192:195], v18
	ds_read_b128 v[196:199], v18 offset:2048
	ds_read_b128 v[200:203], v18 offset:4096
	ds_read_b128 v[204:207], v18 offset:6144
	ds_read_b128 v[176:179], v16 offset:2048
	ds_read_b128 v[180:183], v16 offset:4096
	ds_read_b128 v[184:187], v16 offset:6144
	ds_read_b128 v[188:191], v16 offset:8192
	v_mfma_f32_16x16x32_f16 v[56:59], v[156:159], v[136:139], v[56:59]
	s_add_u32 m0, s28, 0x22000
	s_nop 0
	global_load_lds_dwordx4 v14, s[4:5]
	s_add_u32 s4, s4, s20
	s_addc_u32 s5, s5, 0
	s_waitcnt lgkmcnt(15)
	v_mfma_f32_16x16x32_f16 v[60:63], v[160:163], v[136:139], v[60:63]
	s_waitcnt lgkmcnt(14)
	v_mfma_f32_16x16x32_f16 v[64:67], v[164:167], v[136:139], v[64:67]
	s_waitcnt lgkmcnt(13)
	v_mfma_f32_16x16x32_f16 v[68:71], v[168:171], v[136:139], v[68:71]
	s_waitcnt lgkmcnt(12)
	v_mfma_f32_16x16x32_f16 v[72:75], v[156:159], v[140:143], v[72:75]
	v_mfma_f32_16x16x32_f16 v[76:79], v[160:163], v[140:143], v[76:79]
	v_mfma_f32_16x16x32_f16 v[80:83], v[164:167], v[140:143], v[80:83]
	s_add_u32 m0, s28, 0x23000
	s_nop 0
	global_load_lds_dwordx4 v10, s[6:7]
	v_mfma_f32_16x16x32_f16 v[84:87], v[168:171], v[140:143], v[84:87]
	s_waitcnt lgkmcnt(11)
	v_mfma_f32_16x16x32_f16 v[88:91], v[156:159], v[144:147], v[88:91]
	v_mfma_f32_16x16x32_f16 v[92:95], v[160:163], v[144:147], v[92:95]
	v_mfma_f32_16x16x32_f16 v[96:99], v[164:167], v[144:147], v[96:99]
	v_mfma_f32_16x16x32_f16 v[100:103], v[168:171], v[144:147], v[100:103]
	s_waitcnt lgkmcnt(10)
	v_mfma_f32_16x16x32_f16 v[104:107], v[156:159], v[148:151], v[104:107]
	v_mfma_f32_16x16x32_f16 v[108:111], v[160:163], v[148:151], v[108:111]
	s_add_u32 m0, s28, 0x25000
	s_nop 0
	global_load_lds_dwordx4 v11, s[6:7]
	s_add_u32 s6, s6, s20
	s_addc_u32 s7, s7, 0
	v_mfma_f32_16x16x32_f16 v[112:115], v[164:167], v[148:151], v[112:115]
	v_mfma_f32_16x16x32_f16 v[116:119], v[168:171], v[148:151], v[116:119]
	s_waitcnt lgkmcnt(9)
	v_mfma_f32_16x16x32_f16 v[120:123], v[156:159], v[152:155], v[120:123]
	v_mfma_f32_16x16x32_f16 v[124:127], v[160:163], v[152:155], v[124:127]
	v_mfma_f32_16x16x32_f16 v[128:131], v[164:167], v[152:155], v[128:131]
	v_mfma_f32_16x16x32_f16 v[132:135], v[168:171], v[152:155], v[132:135]
	s_waitcnt vmcnt(7) lgkmcnt(0)
	s_barrier
	s_waitcnt lgkmcnt(6)
	ds_read_b128 v[136:139], v15 offset:53248
	ds_read_b128 v[156:159], v17 offset:53248
	ds_read_b128 v[160:163], v17 offset:55296
	ds_read_b128 v[164:167], v17 offset:57344
	ds_read_b128 v[168:171], v17 offset:59392
	ds_read_b128 v[140:143], v15 offset:55296
	ds_read_b128 v[144:147], v15 offset:57344
	ds_read_b128 v[148:151], v15 offset:59392
	ds_read_b128 v[152:155], v15 offset:61440
	v_mfma_f32_16x16x32_f16 v[56:59], v[192:195], v[172:175], v[56:59]
	s_add_u32 m0, s28, 0x0
	s_nop 0
	global_load_lds_dwordx4 v10, s[4:5]
	s_waitcnt lgkmcnt(15)
	v_mfma_f32_16x16x32_f16 v[60:63], v[196:199], v[172:175], v[60:63]
	s_waitcnt lgkmcnt(14)
	v_mfma_f32_16x16x32_f16 v[64:67], v[200:203], v[172:175], v[64:67]
	s_waitcnt lgkmcnt(13)
	v_mfma_f32_16x16x32_f16 v[68:71], v[204:207], v[172:175], v[68:71]
	s_waitcnt lgkmcnt(12)
	v_mfma_f32_16x16x32_f16 v[72:75], v[192:195], v[176:179], v[72:75]
	v_mfma_f32_16x16x32_f16 v[76:79], v[196:199], v[176:179], v[76:79]
	s_add_u32 m0, s28, 0x2000
	s_nop 0
	global_load_lds_dwordx4 v11, s[4:5]
	v_mfma_f32_16x16x32_f16 v[80:83], v[200:203], v[176:179], v[80:83]
	v_mfma_f32_16x16x32_f16 v[84:87], v[204:207], v[176:179], v[84:87]
	s_waitcnt lgkmcnt(11)
	v_mfma_f32_16x16x32_f16 v[88:91], v[192:195], v[180:183], v[88:91]
	v_mfma_f32_16x16x32_f16 v[92:95], v[196:199], v[180:183], v[92:95]
	v_mfma_f32_16x16x32_f16 v[96:99], v[200:203], v[180:183], v[96:99]
	s_add_u32 m0, s28, 0x4000
	s_nop 0
	global_load_lds_dwordx4 v12, s[4:5]
	v_mfma_f32_16x16x32_f16 v[100:103], v[204:207], v[180:183], v[100:103]
	s_waitcnt lgkmcnt(10)
	v_mfma_f32_16x16x32_f16 v[104:107], v[192:195], v[184:187], v[104:107]
	v_mfma_f32_16x16x32_f16 v[108:111], v[196:199], v[184:187], v[108:111]
	v_mfma_f32_16x16x32_f16 v[112:115], v[200:203], v[184:187], v[112:115]
	v_mfma_f32_16x16x32_f16 v[116:119], v[204:207], v[184:187], v[116:119]
	s_add_u32 m0, s28, 0x6000
	s_nop 0
	global_load_lds_dwordx4 v13, s[4:5]
	s_waitcnt lgkmcnt(9)
	v_mfma_f32_16x16x32_f16 v[120:123], v[192:195], v[188:191], v[120:123]
	v_mfma_f32_16x16x32_f16 v[124:127], v[196:199], v[188:191], v[124:127]
	v_mfma_f32_16x16x32_f16 v[128:131], v[200:203], v[188:191], v[128:131]
	v_mfma_f32_16x16x32_f16 v[132:135], v[204:207], v[188:191], v[132:135]
	s_waitcnt lgkmcnt(6)
	ds_read_b128 v[172:175], v16 offset:53248
	ds_read_b128 v[192:195], v18 offset:53248
	ds_read_b128 v[196:199], v18 offset:55296
	ds_read_b128 v[200:203], v18 offset:57344
	ds_read_b128 v[204:207], v18 offset:59392
	ds_read_b128 v[176:179], v16 offset:55296
	ds_read_b128 v[180:183], v16 offset:57344
	ds_read_b128 v[184:187], v16 offset:59392
	ds_read_b128 v[188:191], v16 offset:61440
	v_mfma_f32_16x16x32_f16 v[56:59], v[156:159], v[136:139], v[56:59]
	s_add_u32 m0, s28, 0x8000
	s_nop 0
	global_load_lds_dwordx4 v14, s[4:5]
	s_add_u32 s4, s4, s20
	s_addc_u32 s5, s5, 0
	s_waitcnt lgkmcnt(15)
	v_mfma_f32_16x16x32_f16 v[60:63], v[160:163], v[136:139], v[60:63]
	s_waitcnt lgkmcnt(14)
	v_mfma_f32_16x16x32_f16 v[64:67], v[164:167], v[136:139], v[64:67]
	s_waitcnt lgkmcnt(13)
	v_mfma_f32_16x16x32_f16 v[68:71], v[168:171], v[136:139], v[68:71]
	s_waitcnt lgkmcnt(12)
	v_mfma_f32_16x16x32_f16 v[72:75], v[156:159], v[140:143], v[72:75]
	v_mfma_f32_16x16x32_f16 v[76:79], v[160:163], v[140:143], v[76:79]
	v_mfma_f32_16x16x32_f16 v[80:83], v[164:167], v[140:143], v[80:83]
	s_add_u32 m0, s28, 0x9000
	s_nop 0
	global_load_lds_dwordx4 v10, s[6:7]
	v_mfma_f32_16x16x32_f16 v[84:87], v[168:171], v[140:143], v[84:87]
	s_waitcnt lgkmcnt(11)
	v_mfma_f32_16x16x32_f16 v[88:91], v[156:159], v[144:147], v[88:91]
	v_mfma_f32_16x16x32_f16 v[92:95], v[160:163], v[144:147], v[92:95]
	v_mfma_f32_16x16x32_f16 v[96:99], v[164:167], v[144:147], v[96:99]
	v_mfma_f32_16x16x32_f16 v[100:103], v[168:171], v[144:147], v[100:103]
	s_waitcnt lgkmcnt(10)
	v_mfma_f32_16x16x32_f16 v[104:107], v[156:159], v[148:151], v[104:107]
	v_mfma_f32_16x16x32_f16 v[108:111], v[160:163], v[148:151], v[108:111]
	s_add_u32 m0, s28, 0xb000
	s_nop 0
	global_load_lds_dwordx4 v11, s[6:7]
	s_add_u32 s6, s6, s20
	s_addc_u32 s7, s7, 0
	v_mfma_f32_16x16x32_f16 v[112:115], v[164:167], v[148:151], v[112:115]
	v_mfma_f32_16x16x32_f16 v[116:119], v[168:171], v[148:151], v[116:119]
	s_waitcnt lgkmcnt(9)
	v_mfma_f32_16x16x32_f16 v[120:123], v[156:159], v[152:155], v[120:123]
	v_mfma_f32_16x16x32_f16 v[124:127], v[160:163], v[152:155], v[124:127]
	v_mfma_f32_16x16x32_f16 v[128:131], v[164:167], v[152:155], v[128:131]
	v_mfma_f32_16x16x32_f16 v[132:135], v[168:171], v[152:155], v[132:135]
	s_waitcnt vmcnt(7) lgkmcnt(0)
	s_barrier
	s_waitcnt lgkmcnt(6)
	ds_read_b128 v[136:139], v19
	ds_read_b128 v[156:159], v21
	ds_read_b128 v[160:163], v21 offset:2048
	ds_read_b128 v[164:167], v21 offset:4096
	ds_read_b128 v[168:171], v21 offset:6144
	ds_read_b128 v[140:143], v19 offset:2048
	ds_read_b128 v[144:147], v19 offset:4096
	ds_read_b128 v[148:151], v19 offset:6144
	ds_read_b128 v[152:155], v19 offset:8192
	v_mfma_f32_16x16x32_f16 v[56:59], v[192:195], v[172:175], v[56:59]
	s_add_u32 m0, s28, 0xd000
	s_nop 0
	global_load_lds_dwordx4 v10, s[4:5]
	s_waitcnt lgkmcnt(15)
	v_mfma_f32_16x16x32_f16 v[60:63], v[196:199], v[172:175], v[60:63]
	s_waitcnt lgkmcnt(14)
	v_mfma_f32_16x16x32_f16 v[64:67], v[200:203], v[172:175], v[64:67]
	s_waitcnt lgkmcnt(13)
	v_mfma_f32_16x16x32_f16 v[68:71], v[204:207], v[172:175], v[68:71]
	s_waitcnt lgkmcnt(12)
	v_mfma_f32_16x16x32_f16 v[72:75], v[192:195], v[176:179], v[72:75]
	v_mfma_f32_16x16x32_f16 v[76:79], v[196:199], v[176:179], v[76:79]
	s_add_u32 m0, s28, 0xf000
	s_nop 0
	global_load_lds_dwordx4 v11, s[4:5]
	v_mfma_f32_16x16x32_f16 v[80:83], v[200:203], v[176:179], v[80:83]
	v_mfma_f32_16x16x32_f16 v[84:87], v[204:207], v[176:179], v[84:87]
	s_waitcnt lgkmcnt(11)
	v_mfma_f32_16x16x32_f16 v[88:91], v[192:195], v[180:183], v[88:91]
	v_mfma_f32_16x16x32_f16 v[92:95], v[196:199], v[180:183], v[92:95]
	v_mfma_f32_16x16x32_f16 v[96:99], v[200:203], v[180:183], v[96:99]
	s_add_u32 m0, s28, 0x11000
	s_nop 0
	global_load_lds_dwordx4 v12, s[4:5]
	v_mfma_f32_16x16x32_f16 v[100:103], v[204:207], v[180:183], v[100:103]
	s_waitcnt lgkmcnt(10)
	v_mfma_f32_16x16x32_f16 v[104:107], v[192:195], v[184:187], v[104:107]
	v_mfma_f32_16x16x32_f16 v[108:111], v[196:199], v[184:187], v[108:111]
	v_mfma_f32_16x16x32_f16 v[112:115], v[200:203], v[184:187], v[112:115]
	v_mfma_f32_16x16x32_f16 v[116:119], v[204:207], v[184:187], v[116:119]
	s_add_u32 m0, s28, 0x13000
	s_nop 0
	global_load_lds_dwordx4 v13, s[4:5]
	s_waitcnt lgkmcnt(9)
	v_mfma_f32_16x16x32_f16 v[120:123], v[192:195], v[188:191], v[120:123]
	v_mfma_f32_16x16x32_f16 v[124:127], v[196:199], v[188:191], v[124:127]
	v_mfma_f32_16x16x32_f16 v[128:131], v[200:203], v[188:191], v[128:131]
	v_mfma_f32_16x16x32_f16 v[132:135], v[204:207], v[188:191], v[132:135]
	s_waitcnt lgkmcnt(6)
	ds_read_b128 v[172:175], v20
	ds_read_b128 v[192:195], v22
	ds_read_b128 v[196:199], v22 offset:2048
	ds_read_b128 v[200:203], v22 offset:4096
	ds_read_b128 v[204:207], v22 offset:6144
	ds_read_b128 v[176:179], v20 offset:2048
	ds_read_b128 v[180:183], v20 offset:4096
	ds_read_b128 v[184:187], v20 offset:6144
	ds_read_b128 v[188:191], v20 offset:8192
	v_mfma_f32_16x16x32_f16 v[56:59], v[156:159], v[136:139], v[56:59]
	s_add_u32 m0, s28, 0x15000
	s_nop 0
	global_load_lds_dwordx4 v14, s[4:5]
	s_add_u32 s4, s4, s20
	s_addc_u32 s5, s5, 0
	s_waitcnt lgkmcnt(15)
	v_mfma_f32_16x16x32_f16 v[60:63], v[160:163], v[136:139], v[60:63]
	s_waitcnt lgkmcnt(14)
	v_mfma_f32_16x16x32_f16 v[64:67], v[164:167], v[136:139], v[64:67]
	s_waitcnt lgkmcnt(13)
	v_mfma_f32_16x16x32_f16 v[68:71], v[168:171], v[136:139], v[68:71]
	s_waitcnt lgkmcnt(12)
	v_mfma_f32_16x16x32_f16 v[72:75], v[156:159], v[140:143], v[72:75]
	v_mfma_f32_16x16x32_f16 v[76:79], v[160:163], v[140:143], v[76:79]
	v_mfma_f32_16x16x32_f16 v[80:83], v[164:167], v[140:143], v[80:83]
	s_add_u32 m0, s28, 0x16000
	s_nop 0
	global_load_lds_dwordx4 v10, s[6:7]
	v_mfma_f32_16x16x32_f16 v[84:87], v[168:171], v[140:143], v[84:87]
	s_waitcnt lgkmcnt(11)
	v_mfma_f32_16x16x32_f16 v[88:91], v[156:159], v[144:147], v[88:91]
	v_mfma_f32_16x16x32_f16 v[92:95], v[160:163], v[144:147], v[92:95]
	v_mfma_f32_16x16x32_f16 v[96:99], v[164:167], v[144:147], v[96:99]
	v_mfma_f32_16x16x32_f16 v[100:103], v[168:171], v[144:147], v[100:103]
	s_waitcnt lgkmcnt(10)
	v_mfma_f32_16x16x32_f16 v[104:107], v[156:159], v[148:151], v[104:107]
	v_mfma_f32_16x16x32_f16 v[108:111], v[160:163], v[148:151], v[108:111]
	s_add_u32 m0, s28, 0x18000
	s_nop 0
	global_load_lds_dwordx4 v11, s[6:7]
	s_add_u32 s6, s6, s20
	s_addc_u32 s7, s7, 0
	v_mfma_f32_16x16x32_f16 v[112:115], v[164:167], v[148:151], v[112:115]
	v_mfma_f32_16x16x32_f16 v[116:119], v[168:171], v[148:151], v[116:119]
	s_waitcnt lgkmcnt(9)
	v_mfma_f32_16x16x32_f16 v[120:123], v[156:159], v[152:155], v[120:123]
	v_mfma_f32_16x16x32_f16 v[124:127], v[160:163], v[152:155], v[124:127]
	v_mfma_f32_16x16x32_f16 v[128:131], v[164:167], v[152:155], v[128:131]
	v_mfma_f32_16x16x32_f16 v[132:135], v[168:171], v[152:155], v[132:135]
	s_waitcnt vmcnt(7) lgkmcnt(0)
	s_barrier
	s_waitcnt lgkmcnt(6)
	ds_read_b128 v[136:139], v15
	ds_read_b128 v[156:159], v17
	ds_read_b128 v[160:163], v17 offset:2048
	ds_read_b128 v[164:167], v17 offset:4096
	ds_read_b128 v[168:171], v17 offset:6144
	ds_read_b128 v[140:143], v15 offset:2048
	ds_read_b128 v[144:147], v15 offset:4096
	ds_read_b128 v[148:151], v15 offset:6144
	ds_read_b128 v[152:155], v15 offset:8192
	v_mfma_f32_16x16x32_f16 v[56:59], v[192:195], v[172:175], v[56:59]
	s_add_u32 m0, s28, 0x1a000
	s_nop 0
	global_load_lds_dwordx4 v10, s[4:5]
	s_waitcnt lgkmcnt(15)
	v_mfma_f32_16x16x32_f16 v[60:63], v[196:199], v[172:175], v[60:63]
	s_waitcnt lgkmcnt(14)
	v_mfma_f32_16x16x32_f16 v[64:67], v[200:203], v[172:175], v[64:67]
	s_waitcnt lgkmcnt(13)
	v_mfma_f32_16x16x32_f16 v[68:71], v[204:207], v[172:175], v[68:71]
	s_waitcnt lgkmcnt(12)
	v_mfma_f32_16x16x32_f16 v[72:75], v[192:195], v[176:179], v[72:75]
	v_mfma_f32_16x16x32_f16 v[76:79], v[196:199], v[176:179], v[76:79]
	s_add_u32 m0, s28, 0x1c000
	s_nop 0
	global_load_lds_dwordx4 v11, s[4:5]
	v_mfma_f32_16x16x32_f16 v[80:83], v[200:203], v[176:179], v[80:83]
	v_mfma_f32_16x16x32_f16 v[84:87], v[204:207], v[176:179], v[84:87]
	s_waitcnt lgkmcnt(11)
	v_mfma_f32_16x16x32_f16 v[88:91], v[192:195], v[180:183], v[88:91]
	v_mfma_f32_16x16x32_f16 v[92:95], v[196:199], v[180:183], v[92:95]
	v_mfma_f32_16x16x32_f16 v[96:99], v[200:203], v[180:183], v[96:99]
	s_add_u32 m0, s28, 0x1e000
	s_nop 0
	global_load_lds_dwordx4 v12, s[4:5]
	v_mfma_f32_16x16x32_f16 v[100:103], v[204:207], v[180:183], v[100:103]
	s_waitcnt lgkmcnt(10)
	v_mfma_f32_16x16x32_f16 v[104:107], v[192:195], v[184:187], v[104:107]
	v_mfma_f32_16x16x32_f16 v[108:111], v[196:199], v[184:187], v[108:111]
	v_mfma_f32_16x16x32_f16 v[112:115], v[200:203], v[184:187], v[112:115]
	v_mfma_f32_16x16x32_f16 v[116:119], v[204:207], v[184:187], v[116:119]
	s_add_u32 m0, s28, 0x20000
	s_nop 0
	global_load_lds_dwordx4 v13, s[4:5]
	s_waitcnt lgkmcnt(9)
	v_mfma_f32_16x16x32_f16 v[120:123], v[192:195], v[188:191], v[120:123]
	v_mfma_f32_16x16x32_f16 v[124:127], v[196:199], v[188:191], v[124:127]
	v_mfma_f32_16x16x32_f16 v[128:131], v[200:203], v[188:191], v[128:131]
	v_mfma_f32_16x16x32_f16 v[132:135], v[204:207], v[188:191], v[132:135]
	s_waitcnt lgkmcnt(6)
	ds_read_b128 v[172:175], v16
	ds_read_b128 v[192:195], v18
	ds_read_b128 v[196:199], v18 offset:2048
	ds_read_b128 v[200:203], v18 offset:4096
	ds_read_b128 v[204:207], v18 offset:6144
	ds_read_b128 v[176:179], v16 offset:2048
	ds_read_b128 v[180:183], v16 offset:4096
	ds_read_b128 v[184:187], v16 offset:6144
	ds_read_b128 v[188:191], v16 offset:8192
	v_mfma_f32_16x16x32_f16 v[56:59], v[156:159], v[136:139], v[56:59]
	s_add_u32 m0, s28, 0x22000
	s_nop 0
	global_load_lds_dwordx4 v14, s[4:5]
	s_add_u32 s4, s4, s20
	s_addc_u32 s5, s5, 0
	s_waitcnt lgkmcnt(15)
	v_mfma_f32_16x16x32_f16 v[60:63], v[160:163], v[136:139], v[60:63]
	s_waitcnt lgkmcnt(14)
	v_mfma_f32_16x16x32_f16 v[64:67], v[164:167], v[136:139], v[64:67]
	s_waitcnt lgkmcnt(13)
	v_mfma_f32_16x16x32_f16 v[68:71], v[168:171], v[136:139], v[68:71]
	s_waitcnt lgkmcnt(12)
	v_mfma_f32_16x16x32_f16 v[72:75], v[156:159], v[140:143], v[72:75]
	v_mfma_f32_16x16x32_f16 v[76:79], v[160:163], v[140:143], v[76:79]
	v_mfma_f32_16x16x32_f16 v[80:83], v[164:167], v[140:143], v[80:83]
	s_add_u32 m0, s28, 0x23000
	s_nop 0
	global_load_lds_dwordx4 v10, s[6:7]
	v_mfma_f32_16x16x32_f16 v[84:87], v[168:171], v[140:143], v[84:87]
	s_waitcnt lgkmcnt(11)
	v_mfma_f32_16x16x32_f16 v[88:91], v[156:159], v[144:147], v[88:91]
	v_mfma_f32_16x16x32_f16 v[92:95], v[160:163], v[144:147], v[92:95]
	v_mfma_f32_16x16x32_f16 v[96:99], v[164:167], v[144:147], v[96:99]
	v_mfma_f32_16x16x32_f16 v[100:103], v[168:171], v[144:147], v[100:103]
	s_waitcnt lgkmcnt(10)
	v_mfma_f32_16x16x32_f16 v[104:107], v[156:159], v[148:151], v[104:107]
	v_mfma_f32_16x16x32_f16 v[108:111], v[160:163], v[148:151], v[108:111]
	s_add_u32 m0, s28, 0x25000
	s_nop 0
	global_load_lds_dwordx4 v11, s[6:7]
	s_add_u32 s6, s6, s20
	s_addc_u32 s7, s7, 0
	v_mfma_f32_16x16x32_f16 v[112:115], v[164:167], v[148:151], v[112:115]
	v_mfma_f32_16x16x32_f16 v[116:119], v[168:171], v[148:151], v[116:119]
	s_waitcnt lgkmcnt(9)
	v_mfma_f32_16x16x32_f16 v[120:123], v[156:159], v[152:155], v[120:123]
	v_mfma_f32_16x16x32_f16 v[124:127], v[160:163], v[152:155], v[124:127]
	v_mfma_f32_16x16x32_f16 v[128:131], v[164:167], v[152:155], v[128:131]
	v_mfma_f32_16x16x32_f16 v[132:135], v[168:171], v[152:155], v[132:135]
	s_waitcnt vmcnt(7) lgkmcnt(0)
	s_barrier
	s_waitcnt lgkmcnt(6)
	ds_read_b128 v[136:139], v15 offset:53248
	ds_read_b128 v[156:159], v17 offset:53248
	ds_read_b128 v[160:163], v17 offset:55296
	ds_read_b128 v[164:167], v17 offset:57344
	ds_read_b128 v[168:171], v17 offset:59392
	ds_read_b128 v[140:143], v15 offset:55296
	ds_read_b128 v[144:147], v15 offset:57344
	ds_read_b128 v[148:151], v15 offset:59392
	ds_read_b128 v[152:155], v15 offset:61440
	v_mfma_f32_16x16x32_f16 v[56:59], v[192:195], v[172:175], v[56:59]
	s_add_u32 m0, s28, 0x0
	s_nop 0
	global_load_lds_dwordx4 v10, s[4:5]
	s_waitcnt lgkmcnt(15)
	v_mfma_f32_16x16x32_f16 v[60:63], v[196:199], v[172:175], v[60:63]
	s_waitcnt lgkmcnt(14)
	v_mfma_f32_16x16x32_f16 v[64:67], v[200:203], v[172:175], v[64:67]
	s_waitcnt lgkmcnt(13)
	v_mfma_f32_16x16x32_f16 v[68:71], v[204:207], v[172:175], v[68:71]
	s_waitcnt lgkmcnt(12)
	v_mfma_f32_16x16x32_f16 v[72:75], v[192:195], v[176:179], v[72:75]
	v_mfma_f32_16x16x32_f16 v[76:79], v[196:199], v[176:179], v[76:79]
	s_add_u32 m0, s28, 0x2000
	s_nop 0
	global_load_lds_dwordx4 v11, s[4:5]
	v_mfma_f32_16x16x32_f16 v[80:83], v[200:203], v[176:179], v[80:83]
	v_mfma_f32_16x16x32_f16 v[84:87], v[204:207], v[176:179], v[84:87]
	s_waitcnt lgkmcnt(11)
	v_mfma_f32_16x16x32_f16 v[88:91], v[192:195], v[180:183], v[88:91]
	v_mfma_f32_16x16x32_f16 v[92:95], v[196:199], v[180:183], v[92:95]
	v_mfma_f32_16x16x32_f16 v[96:99], v[200:203], v[180:183], v[96:99]
	s_add_u32 m0, s28, 0x4000
	s_nop 0
	global_load_lds_dwordx4 v12, s[4:5]
	v_mfma_f32_16x16x32_f16 v[100:103], v[204:207], v[180:183], v[100:103]
	s_waitcnt lgkmcnt(10)
	v_mfma_f32_16x16x32_f16 v[104:107], v[192:195], v[184:187], v[104:107]
	v_mfma_f32_16x16x32_f16 v[108:111], v[196:199], v[184:187], v[108:111]
	v_mfma_f32_16x16x32_f16 v[112:115], v[200:203], v[184:187], v[112:115]
	v_mfma_f32_16x16x32_f16 v[116:119], v[204:207], v[184:187], v[116:119]
	s_add_u32 m0, s28, 0x6000
	s_nop 0
	global_load_lds_dwordx4 v13, s[4:5]
	s_waitcnt lgkmcnt(9)
	v_mfma_f32_16x16x32_f16 v[120:123], v[192:195], v[188:191], v[120:123]
	v_mfma_f32_16x16x32_f16 v[124:127], v[196:199], v[188:191], v[124:127]
	v_mfma_f32_16x16x32_f16 v[128:131], v[200:203], v[188:191], v[128:131]
	v_mfma_f32_16x16x32_f16 v[132:135], v[204:207], v[188:191], v[132:135]
	s_waitcnt lgkmcnt(6)
	ds_read_b128 v[172:175], v16 offset:53248
	ds_read_b128 v[192:195], v18 offset:53248
	ds_read_b128 v[196:199], v18 offset:55296
	ds_read_b128 v[200:203], v18 offset:57344
	ds_read_b128 v[204:207], v18 offset:59392
	ds_read_b128 v[176:179], v16 offset:55296
	ds_read_b128 v[180:183], v16 offset:57344
	ds_read_b128 v[184:187], v16 offset:59392
	ds_read_b128 v[188:191], v16 offset:61440
	v_mfma_f32_16x16x32_f16 v[56:59], v[156:159], v[136:139], v[56:59]
	s_add_u32 m0, s28, 0x8000
	s_nop 0
	global_load_lds_dwordx4 v14, s[4:5]
	s_add_u32 s4, s4, s20
	s_addc_u32 s5, s5, 0
	s_waitcnt lgkmcnt(15)
	v_mfma_f32_16x16x32_f16 v[60:63], v[160:163], v[136:139], v[60:63]
	s_waitcnt lgkmcnt(14)
	v_mfma_f32_16x16x32_f16 v[64:67], v[164:167], v[136:139], v[64:67]
	s_waitcnt lgkmcnt(13)
	v_mfma_f32_16x16x32_f16 v[68:71], v[168:171], v[136:139], v[68:71]
	s_waitcnt lgkmcnt(12)
	v_mfma_f32_16x16x32_f16 v[72:75], v[156:159], v[140:143], v[72:75]
	v_mfma_f32_16x16x32_f16 v[76:79], v[160:163], v[140:143], v[76:79]
	v_mfma_f32_16x16x32_f16 v[80:83], v[164:167], v[140:143], v[80:83]
	s_add_u32 m0, s28, 0x9000
	s_nop 0
	global_load_lds_dwordx4 v10, s[6:7]
	v_mfma_f32_16x16x32_f16 v[84:87], v[168:171], v[140:143], v[84:87]
	s_waitcnt lgkmcnt(11)
	v_mfma_f32_16x16x32_f16 v[88:91], v[156:159], v[144:147], v[88:91]
	v_mfma_f32_16x16x32_f16 v[92:95], v[160:163], v[144:147], v[92:95]
	v_mfma_f32_16x16x32_f16 v[96:99], v[164:167], v[144:147], v[96:99]
	v_mfma_f32_16x16x32_f16 v[100:103], v[168:171], v[144:147], v[100:103]
	s_waitcnt lgkmcnt(10)
	v_mfma_f32_16x16x32_f16 v[104:107], v[156:159], v[148:151], v[104:107]
	v_mfma_f32_16x16x32_f16 v[108:111], v[160:163], v[148:151], v[108:111]
	s_add_u32 m0, s28, 0xb000
	s_nop 0
	global_load_lds_dwordx4 v11, s[6:7]
	s_add_u32 s6, s6, s20
	s_addc_u32 s7, s7, 0
	v_mfma_f32_16x16x32_f16 v[112:115], v[164:167], v[148:151], v[112:115]
	v_mfma_f32_16x16x32_f16 v[116:119], v[168:171], v[148:151], v[116:119]
	s_waitcnt lgkmcnt(9)
	v_mfma_f32_16x16x32_f16 v[120:123], v[156:159], v[152:155], v[120:123]
	v_mfma_f32_16x16x32_f16 v[124:127], v[160:163], v[152:155], v[124:127]
	v_mfma_f32_16x16x32_f16 v[128:131], v[164:167], v[152:155], v[128:131]
	v_mfma_f32_16x16x32_f16 v[132:135], v[168:171], v[152:155], v[132:135]
	s_waitcnt vmcnt(7) lgkmcnt(0)
	s_barrier
	s_waitcnt lgkmcnt(6)
	ds_read_b128 v[136:139], v19
	ds_read_b128 v[156:159], v21
	ds_read_b128 v[160:163], v21 offset:2048
	ds_read_b128 v[164:167], v21 offset:4096
	ds_read_b128 v[168:171], v21 offset:6144
	ds_read_b128 v[140:143], v19 offset:2048
	ds_read_b128 v[144:147], v19 offset:4096
	ds_read_b128 v[148:151], v19 offset:6144
	ds_read_b128 v[152:155], v19 offset:8192
	v_mfma_f32_16x16x32_f16 v[56:59], v[192:195], v[172:175], v[56:59]
	s_add_u32 m0, s28, 0xd000
	s_nop 0
	global_load_lds_dwordx4 v10, s[4:5]
	s_waitcnt lgkmcnt(15)
	v_mfma_f32_16x16x32_f16 v[60:63], v[196:199], v[172:175], v[60:63]
	s_waitcnt lgkmcnt(14)
	v_mfma_f32_16x16x32_f16 v[64:67], v[200:203], v[172:175], v[64:67]
	s_waitcnt lgkmcnt(13)
	v_mfma_f32_16x16x32_f16 v[68:71], v[204:207], v[172:175], v[68:71]
	s_waitcnt lgkmcnt(12)
	v_mfma_f32_16x16x32_f16 v[72:75], v[192:195], v[176:179], v[72:75]
	v_mfma_f32_16x16x32_f16 v[76:79], v[196:199], v[176:179], v[76:79]
	s_add_u32 m0, s28, 0xf000
	s_nop 0
	global_load_lds_dwordx4 v11, s[4:5]
	v_mfma_f32_16x16x32_f16 v[80:83], v[200:203], v[176:179], v[80:83]
	v_mfma_f32_16x16x32_f16 v[84:87], v[204:207], v[176:179], v[84:87]
	s_waitcnt lgkmcnt(11)
	v_mfma_f32_16x16x32_f16 v[88:91], v[192:195], v[180:183], v[88:91]
	v_mfma_f32_16x16x32_f16 v[92:95], v[196:199], v[180:183], v[92:95]
	v_mfma_f32_16x16x32_f16 v[96:99], v[200:203], v[180:183], v[96:99]
	s_add_u32 m0, s28, 0x11000
	s_nop 0
	global_load_lds_dwordx4 v12, s[4:5]
	v_mfma_f32_16x16x32_f16 v[100:103], v[204:207], v[180:183], v[100:103]
	s_waitcnt lgkmcnt(10)
	v_mfma_f32_16x16x32_f16 v[104:107], v[192:195], v[184:187], v[104:107]
	v_mfma_f32_16x16x32_f16 v[108:111], v[196:199], v[184:187], v[108:111]
	v_mfma_f32_16x16x32_f16 v[112:115], v[200:203], v[184:187], v[112:115]
	v_mfma_f32_16x16x32_f16 v[116:119], v[204:207], v[184:187], v[116:119]
	s_add_u32 m0, s28, 0x13000
	s_nop 0
	global_load_lds_dwordx4 v13, s[4:5]
	s_waitcnt lgkmcnt(9)
	v_mfma_f32_16x16x32_f16 v[120:123], v[192:195], v[188:191], v[120:123]
	v_mfma_f32_16x16x32_f16 v[124:127], v[196:199], v[188:191], v[124:127]
	v_mfma_f32_16x16x32_f16 v[128:131], v[200:203], v[188:191], v[128:131]
	v_mfma_f32_16x16x32_f16 v[132:135], v[204:207], v[188:191], v[132:135]
	s_waitcnt lgkmcnt(6)
	ds_read_b128 v[172:175], v20
	ds_read_b128 v[192:195], v22
	ds_read_b128 v[196:199], v22 offset:2048
	ds_read_b128 v[200:203], v22 offset:4096
	ds_read_b128 v[204:207], v22 offset:6144
	ds_read_b128 v[176:179], v20 offset:2048
	ds_read_b128 v[180:183], v20 offset:4096
	ds_read_b128 v[184:187], v20 offset:6144
	ds_read_b128 v[188:191], v20 offset:8192
	v_mfma_f32_16x16x32_f16 v[56:59], v[156:159], v[136:139], v[56:59]
	s_add_u32 m0, s28, 0x15000
	s_nop 0
	global_load_lds_dwordx4 v14, s[4:5]
	s_add_u32 s4, s4, s20
	s_addc_u32 s5, s5, 0
	s_waitcnt lgkmcnt(15)
	v_mfma_f32_16x16x32_f16 v[60:63], v[160:163], v[136:139], v[60:63]
	s_waitcnt lgkmcnt(14)
	v_mfma_f32_16x16x32_f16 v[64:67], v[164:167], v[136:139], v[64:67]
	s_waitcnt lgkmcnt(13)
	v_mfma_f32_16x16x32_f16 v[68:71], v[168:171], v[136:139], v[68:71]
	s_waitcnt lgkmcnt(12)
	v_mfma_f32_16x16x32_f16 v[72:75], v[156:159], v[140:143], v[72:75]
	v_mfma_f32_16x16x32_f16 v[76:79], v[160:163], v[140:143], v[76:79]
	v_mfma_f32_16x16x32_f16 v[80:83], v[164:167], v[140:143], v[80:83]
	s_add_u32 m0, s28, 0x16000
	s_nop 0
	global_load_lds_dwordx4 v10, s[6:7]
	v_mfma_f32_16x16x32_f16 v[84:87], v[168:171], v[140:143], v[84:87]
	s_waitcnt lgkmcnt(11)
	v_mfma_f32_16x16x32_f16 v[88:91], v[156:159], v[144:147], v[88:91]
	v_mfma_f32_16x16x32_f16 v[92:95], v[160:163], v[144:147], v[92:95]
	v_mfma_f32_16x16x32_f16 v[96:99], v[164:167], v[144:147], v[96:99]
	v_mfma_f32_16x16x32_f16 v[100:103], v[168:171], v[144:147], v[100:103]
	s_waitcnt lgkmcnt(10)
	v_mfma_f32_16x16x32_f16 v[104:107], v[156:159], v[148:151], v[104:107]
	v_mfma_f32_16x16x32_f16 v[108:111], v[160:163], v[148:151], v[108:111]
	s_add_u32 m0, s28, 0x18000
	s_nop 0
	global_load_lds_dwordx4 v11, s[6:7]
	s_add_u32 s6, s6, s20
	s_addc_u32 s7, s7, 0
	v_mfma_f32_16x16x32_f16 v[112:115], v[164:167], v[148:151], v[112:115]
	v_mfma_f32_16x16x32_f16 v[116:119], v[168:171], v[148:151], v[116:119]
	s_waitcnt lgkmcnt(9)
	v_mfma_f32_16x16x32_f16 v[120:123], v[156:159], v[152:155], v[120:123]
	v_mfma_f32_16x16x32_f16 v[124:127], v[160:163], v[152:155], v[124:127]
	v_mfma_f32_16x16x32_f16 v[128:131], v[164:167], v[152:155], v[128:131]
	v_mfma_f32_16x16x32_f16 v[132:135], v[168:171], v[152:155], v[132:135]
	s_waitcnt vmcnt(7) lgkmcnt(0)
	s_barrier
	s_waitcnt lgkmcnt(6)
	ds_read_b128 v[136:139], v15
	ds_read_b128 v[156:159], v17
	ds_read_b128 v[160:163], v17 offset:2048
	ds_read_b128 v[164:167], v17 offset:4096
	ds_read_b128 v[168:171], v17 offset:6144
	ds_read_b128 v[140:143], v15 offset:2048
	ds_read_b128 v[144:147], v15 offset:4096
	ds_read_b128 v[148:151], v15 offset:6144
	ds_read_b128 v[152:155], v15 offset:8192
	v_mfma_f32_16x16x32_f16 v[56:59], v[192:195], v[172:175], v[56:59]
	s_add_u32 m0, s28, 0x1a000
	s_nop 0
	global_load_lds_dwordx4 v10, s[4:5]
	s_waitcnt lgkmcnt(15)
	v_mfma_f32_16x16x32_f16 v[60:63], v[196:199], v[172:175], v[60:63]
	s_waitcnt lgkmcnt(14)
	v_mfma_f32_16x16x32_f16 v[64:67], v[200:203], v[172:175], v[64:67]
	s_waitcnt lgkmcnt(13)
	v_mfma_f32_16x16x32_f16 v[68:71], v[204:207], v[172:175], v[68:71]
	s_waitcnt lgkmcnt(12)
	v_mfma_f32_16x16x32_f16 v[72:75], v[192:195], v[176:179], v[72:75]
	v_mfma_f32_16x16x32_f16 v[76:79], v[196:199], v[176:179], v[76:79]
	s_add_u32 m0, s28, 0x1c000
	s_nop 0
	global_load_lds_dwordx4 v11, s[4:5]
	v_mfma_f32_16x16x32_f16 v[80:83], v[200:203], v[176:179], v[80:83]
	v_mfma_f32_16x16x32_f16 v[84:87], v[204:207], v[176:179], v[84:87]
	s_waitcnt lgkmcnt(11)
	v_mfma_f32_16x16x32_f16 v[88:91], v[192:195], v[180:183], v[88:91]
	v_mfma_f32_16x16x32_f16 v[92:95], v[196:199], v[180:183], v[92:95]
	v_mfma_f32_16x16x32_f16 v[96:99], v[200:203], v[180:183], v[96:99]
	s_add_u32 m0, s28, 0x1e000
	s_nop 0
	global_load_lds_dwordx4 v12, s[4:5]
	v_mfma_f32_16x16x32_f16 v[100:103], v[204:207], v[180:183], v[100:103]
	s_waitcnt lgkmcnt(10)
	v_mfma_f32_16x16x32_f16 v[104:107], v[192:195], v[184:187], v[104:107]
	v_mfma_f32_16x16x32_f16 v[108:111], v[196:199], v[184:187], v[108:111]
	v_mfma_f32_16x16x32_f16 v[112:115], v[200:203], v[184:187], v[112:115]
	v_mfma_f32_16x16x32_f16 v[116:119], v[204:207], v[184:187], v[116:119]
	s_add_u32 m0, s28, 0x20000
	s_nop 0
	global_load_lds_dwordx4 v13, s[4:5]
	s_waitcnt lgkmcnt(9)
	v_mfma_f32_16x16x32_f16 v[120:123], v[192:195], v[188:191], v[120:123]
	v_mfma_f32_16x16x32_f16 v[124:127], v[196:199], v[188:191], v[124:127]
	v_mfma_f32_16x16x32_f16 v[128:131], v[200:203], v[188:191], v[128:131]
	v_mfma_f32_16x16x32_f16 v[132:135], v[204:207], v[188:191], v[132:135]
	s_waitcnt lgkmcnt(6)
	ds_read_b128 v[172:175], v16
	ds_read_b128 v[192:195], v18
	ds_read_b128 v[196:199], v18 offset:2048
	ds_read_b128 v[200:203], v18 offset:4096
	ds_read_b128 v[204:207], v18 offset:6144
	ds_read_b128 v[176:179], v16 offset:2048
	ds_read_b128 v[180:183], v16 offset:4096
	ds_read_b128 v[184:187], v16 offset:6144
	ds_read_b128 v[188:191], v16 offset:8192
	v_mfma_f32_16x16x32_f16 v[56:59], v[156:159], v[136:139], v[56:59]
	s_add_u32 m0, s28, 0x22000
	s_nop 0
	global_load_lds_dwordx4 v14, s[4:5]
	s_add_u32 s4, s4, s20
	s_addc_u32 s5, s5, 0
	s_waitcnt lgkmcnt(15)
	v_mfma_f32_16x16x32_f16 v[60:63], v[160:163], v[136:139], v[60:63]
	s_waitcnt lgkmcnt(14)
	v_mfma_f32_16x16x32_f16 v[64:67], v[164:167], v[136:139], v[64:67]
	s_waitcnt lgkmcnt(13)
	v_mfma_f32_16x16x32_f16 v[68:71], v[168:171], v[136:139], v[68:71]
	s_waitcnt lgkmcnt(12)
	v_mfma_f32_16x16x32_f16 v[72:75], v[156:159], v[140:143], v[72:75]
	v_mfma_f32_16x16x32_f16 v[76:79], v[160:163], v[140:143], v[76:79]
	v_mfma_f32_16x16x32_f16 v[80:83], v[164:167], v[140:143], v[80:83]
	s_add_u32 m0, s28, 0x23000
	s_nop 0
	global_load_lds_dwordx4 v10, s[6:7]
	v_mfma_f32_16x16x32_f16 v[84:87], v[168:171], v[140:143], v[84:87]
	s_waitcnt lgkmcnt(11)
	v_mfma_f32_16x16x32_f16 v[88:91], v[156:159], v[144:147], v[88:91]
	v_mfma_f32_16x16x32_f16 v[92:95], v[160:163], v[144:147], v[92:95]
	v_mfma_f32_16x16x32_f16 v[96:99], v[164:167], v[144:147], v[96:99]
	v_mfma_f32_16x16x32_f16 v[100:103], v[168:171], v[144:147], v[100:103]
	s_waitcnt lgkmcnt(10)
	v_mfma_f32_16x16x32_f16 v[104:107], v[156:159], v[148:151], v[104:107]
	v_mfma_f32_16x16x32_f16 v[108:111], v[160:163], v[148:151], v[108:111]
	s_add_u32 m0, s28, 0x25000
	s_nop 0
	global_load_lds_dwordx4 v11, s[6:7]
	s_add_u32 s6, s6, s20
	s_addc_u32 s7, s7, 0
	v_mfma_f32_16x16x32_f16 v[112:115], v[164:167], v[148:151], v[112:115]
	v_mfma_f32_16x16x32_f16 v[116:119], v[168:171], v[148:151], v[116:119]
	s_waitcnt lgkmcnt(9)
	v_mfma_f32_16x16x32_f16 v[120:123], v[156:159], v[152:155], v[120:123]
	v_mfma_f32_16x16x32_f16 v[124:127], v[160:163], v[152:155], v[124:127]
	v_mfma_f32_16x16x32_f16 v[128:131], v[164:167], v[152:155], v[128:131]
	v_mfma_f32_16x16x32_f16 v[132:135], v[168:171], v[152:155], v[132:135]
	s_waitcnt vmcnt(7) lgkmcnt(0)
	s_barrier
	s_waitcnt lgkmcnt(6)
	ds_read_b128 v[136:139], v15 offset:53248
	ds_read_b128 v[156:159], v17 offset:53248
	ds_read_b128 v[160:163], v17 offset:55296
	ds_read_b128 v[164:167], v17 offset:57344
	ds_read_b128 v[168:171], v17 offset:59392
	ds_read_b128 v[140:143], v15 offset:55296
	ds_read_b128 v[144:147], v15 offset:57344
	ds_read_b128 v[148:151], v15 offset:59392
	ds_read_b128 v[152:155], v15 offset:61440
	v_mfma_f32_16x16x32_f16 v[56:59], v[192:195], v[172:175], v[56:59]
	s_add_u32 m0, s28, 0x0
	s_nop 0
	global_load_lds_dwordx4 v10, s[4:5]
	s_waitcnt lgkmcnt(15)
	v_mfma_f32_16x16x32_f16 v[60:63], v[196:199], v[172:175], v[60:63]
	s_waitcnt lgkmcnt(14)
	v_mfma_f32_16x16x32_f16 v[64:67], v[200:203], v[172:175], v[64:67]
	s_waitcnt lgkmcnt(13)
	v_mfma_f32_16x16x32_f16 v[68:71], v[204:207], v[172:175], v[68:71]
	s_waitcnt lgkmcnt(12)
	v_mfma_f32_16x16x32_f16 v[72:75], v[192:195], v[176:179], v[72:75]
	v_mfma_f32_16x16x32_f16 v[76:79], v[196:199], v[176:179], v[76:79]
	s_add_u32 m0, s28, 0x2000
	s_nop 0
	global_load_lds_dwordx4 v11, s[4:5]
	v_mfma_f32_16x16x32_f16 v[80:83], v[200:203], v[176:179], v[80:83]
	v_mfma_f32_16x16x32_f16 v[84:87], v[204:207], v[176:179], v[84:87]
	s_waitcnt lgkmcnt(11)
	v_mfma_f32_16x16x32_f16 v[88:91], v[192:195], v[180:183], v[88:91]
	v_mfma_f32_16x16x32_f16 v[92:95], v[196:199], v[180:183], v[92:95]
	v_mfma_f32_16x16x32_f16 v[96:99], v[200:203], v[180:183], v[96:99]
	s_add_u32 m0, s28, 0x4000
	s_nop 0
	global_load_lds_dwordx4 v12, s[4:5]
	v_mfma_f32_16x16x32_f16 v[100:103], v[204:207], v[180:183], v[100:103]
	s_waitcnt lgkmcnt(10)
	v_mfma_f32_16x16x32_f16 v[104:107], v[192:195], v[184:187], v[104:107]
	v_mfma_f32_16x16x32_f16 v[108:111], v[196:199], v[184:187], v[108:111]
	v_mfma_f32_16x16x32_f16 v[112:115], v[200:203], v[184:187], v[112:115]
	v_mfma_f32_16x16x32_f16 v[116:119], v[204:207], v[184:187], v[116:119]
	s_add_u32 m0, s28, 0x6000
	s_nop 0
	global_load_lds_dwordx4 v13, s[4:5]
	s_waitcnt lgkmcnt(9)
	v_mfma_f32_16x16x32_f16 v[120:123], v[192:195], v[188:191], v[120:123]
	v_mfma_f32_16x16x32_f16 v[124:127], v[196:199], v[188:191], v[124:127]
	v_mfma_f32_16x16x32_f16 v[128:131], v[200:203], v[188:191], v[128:131]
	v_mfma_f32_16x16x32_f16 v[132:135], v[204:207], v[188:191], v[132:135]
	s_waitcnt lgkmcnt(6)
	ds_read_b128 v[172:175], v16 offset:53248
	ds_read_b128 v[192:195], v18 offset:53248
	ds_read_b128 v[196:199], v18 offset:55296
	ds_read_b128 v[200:203], v18 offset:57344
	ds_read_b128 v[204:207], v18 offset:59392
	ds_read_b128 v[176:179], v16 offset:55296
	ds_read_b128 v[180:183], v16 offset:57344
	ds_read_b128 v[184:187], v16 offset:59392
	ds_read_b128 v[188:191], v16 offset:61440
	v_mfma_f32_16x16x32_f16 v[56:59], v[156:159], v[136:139], v[56:59]
	s_add_u32 m0, s28, 0x8000
	s_nop 0
	global_load_lds_dwordx4 v14, s[4:5]
	s_add_u32 s4, s4, s20
	s_addc_u32 s5, s5, 0
	s_waitcnt lgkmcnt(15)
	v_mfma_f32_16x16x32_f16 v[60:63], v[160:163], v[136:139], v[60:63]
	s_waitcnt lgkmcnt(14)
	v_mfma_f32_16x16x32_f16 v[64:67], v[164:167], v[136:139], v[64:67]
	s_waitcnt lgkmcnt(13)
	v_mfma_f32_16x16x32_f16 v[68:71], v[168:171], v[136:139], v[68:71]
	s_waitcnt lgkmcnt(12)
	v_mfma_f32_16x16x32_f16 v[72:75], v[156:159], v[140:143], v[72:75]
	v_mfma_f32_16x16x32_f16 v[76:79], v[160:163], v[140:143], v[76:79]
	v_mfma_f32_16x16x32_f16 v[80:83], v[164:167], v[140:143], v[80:83]
	s_add_u32 m0, s28, 0x9000
	s_nop 0
	global_load_lds_dwordx4 v10, s[6:7]
	v_mfma_f32_16x16x32_f16 v[84:87], v[168:171], v[140:143], v[84:87]
	s_waitcnt lgkmcnt(11)
	v_mfma_f32_16x16x32_f16 v[88:91], v[156:159], v[144:147], v[88:91]
	v_mfma_f32_16x16x32_f16 v[92:95], v[160:163], v[144:147], v[92:95]
	v_mfma_f32_16x16x32_f16 v[96:99], v[164:167], v[144:147], v[96:99]
	v_mfma_f32_16x16x32_f16 v[100:103], v[168:171], v[144:147], v[100:103]
	s_waitcnt lgkmcnt(10)
	v_mfma_f32_16x16x32_f16 v[104:107], v[156:159], v[148:151], v[104:107]
	v_mfma_f32_16x16x32_f16 v[108:111], v[160:163], v[148:151], v[108:111]
	s_add_u32 m0, s28, 0xb000
	s_nop 0
	global_load_lds_dwordx4 v11, s[6:7]
	s_add_u32 s6, s6, s20
	s_addc_u32 s7, s7, 0
	v_mfma_f32_16x16x32_f16 v[112:115], v[164:167], v[148:151], v[112:115]
	v_mfma_f32_16x16x32_f16 v[116:119], v[168:171], v[148:151], v[116:119]
	s_waitcnt lgkmcnt(9)
	v_mfma_f32_16x16x32_f16 v[120:123], v[156:159], v[152:155], v[120:123]
	v_mfma_f32_16x16x32_f16 v[124:127], v[160:163], v[152:155], v[124:127]
	v_mfma_f32_16x16x32_f16 v[128:131], v[164:167], v[152:155], v[128:131]
	v_mfma_f32_16x16x32_f16 v[132:135], v[168:171], v[152:155], v[132:135]
	s_waitcnt vmcnt(7) lgkmcnt(0)
	s_barrier
	s_waitcnt lgkmcnt(6)
	ds_read_b128 v[136:139], v19
	ds_read_b128 v[156:159], v21
	ds_read_b128 v[160:163], v21 offset:2048
	ds_read_b128 v[164:167], v21 offset:4096
	ds_read_b128 v[168:171], v21 offset:6144
	ds_read_b128 v[140:143], v19 offset:2048
	ds_read_b128 v[144:147], v19 offset:4096
	ds_read_b128 v[148:151], v19 offset:6144
	ds_read_b128 v[152:155], v19 offset:8192
	v_mfma_f32_16x16x32_f16 v[56:59], v[192:195], v[172:175], v[56:59]
	s_add_u32 m0, s28, 0xd000
	s_nop 0
	global_load_lds_dwordx4 v10, s[4:5]
	s_waitcnt lgkmcnt(15)
	v_mfma_f32_16x16x32_f16 v[60:63], v[196:199], v[172:175], v[60:63]
	s_waitcnt lgkmcnt(14)
	v_mfma_f32_16x16x32_f16 v[64:67], v[200:203], v[172:175], v[64:67]
	s_waitcnt lgkmcnt(13)
	v_mfma_f32_16x16x32_f16 v[68:71], v[204:207], v[172:175], v[68:71]
	s_waitcnt lgkmcnt(12)
	v_mfma_f32_16x16x32_f16 v[72:75], v[192:195], v[176:179], v[72:75]
	v_mfma_f32_16x16x32_f16 v[76:79], v[196:199], v[176:179], v[76:79]
	s_add_u32 m0, s28, 0xf000
	s_nop 0
	global_load_lds_dwordx4 v11, s[4:5]
	v_mfma_f32_16x16x32_f16 v[80:83], v[200:203], v[176:179], v[80:83]
	v_mfma_f32_16x16x32_f16 v[84:87], v[204:207], v[176:179], v[84:87]
	s_waitcnt lgkmcnt(11)
	v_mfma_f32_16x16x32_f16 v[88:91], v[192:195], v[180:183], v[88:91]
	v_mfma_f32_16x16x32_f16 v[92:95], v[196:199], v[180:183], v[92:95]
	v_mfma_f32_16x16x32_f16 v[96:99], v[200:203], v[180:183], v[96:99]
	s_add_u32 m0, s28, 0x11000
	s_nop 0
	global_load_lds_dwordx4 v12, s[4:5]
	v_mfma_f32_16x16x32_f16 v[100:103], v[204:207], v[180:183], v[100:103]
	s_waitcnt lgkmcnt(10)
	v_mfma_f32_16x16x32_f16 v[104:107], v[192:195], v[184:187], v[104:107]
	v_mfma_f32_16x16x32_f16 v[108:111], v[196:199], v[184:187], v[108:111]
	v_mfma_f32_16x16x32_f16 v[112:115], v[200:203], v[184:187], v[112:115]
	v_mfma_f32_16x16x32_f16 v[116:119], v[204:207], v[184:187], v[116:119]
	s_add_u32 m0, s28, 0x13000
	s_nop 0
	global_load_lds_dwordx4 v13, s[4:5]
	s_waitcnt lgkmcnt(9)
	v_mfma_f32_16x16x32_f16 v[120:123], v[192:195], v[188:191], v[120:123]
	v_mfma_f32_16x16x32_f16 v[124:127], v[196:199], v[188:191], v[124:127]
	v_mfma_f32_16x16x32_f16 v[128:131], v[200:203], v[188:191], v[128:131]
	v_mfma_f32_16x16x32_f16 v[132:135], v[204:207], v[188:191], v[132:135]
	s_waitcnt lgkmcnt(6)
	ds_read_b128 v[172:175], v20
	ds_read_b128 v[192:195], v22
	ds_read_b128 v[196:199], v22 offset:2048
	ds_read_b128 v[200:203], v22 offset:4096
	ds_read_b128 v[204:207], v22 offset:6144
	ds_read_b128 v[176:179], v20 offset:2048
	ds_read_b128 v[180:183], v20 offset:4096
	ds_read_b128 v[184:187], v20 offset:6144
	ds_read_b128 v[188:191], v20 offset:8192
	v_mfma_f32_16x16x32_f16 v[56:59], v[156:159], v[136:139], v[56:59]
	s_add_u32 m0, s28, 0x15000
	s_nop 0
	global_load_lds_dwordx4 v14, s[4:5]
	s_add_u32 s4, s4, s20
	s_addc_u32 s5, s5, 0
	s_waitcnt lgkmcnt(15)
	v_mfma_f32_16x16x32_f16 v[60:63], v[160:163], v[136:139], v[60:63]
	s_waitcnt lgkmcnt(14)
	v_mfma_f32_16x16x32_f16 v[64:67], v[164:167], v[136:139], v[64:67]
	s_waitcnt lgkmcnt(13)
	v_mfma_f32_16x16x32_f16 v[68:71], v[168:171], v[136:139], v[68:71]
	s_waitcnt lgkmcnt(12)
	v_mfma_f32_16x16x32_f16 v[72:75], v[156:159], v[140:143], v[72:75]
	v_mfma_f32_16x16x32_f16 v[76:79], v[160:163], v[140:143], v[76:79]
	v_mfma_f32_16x16x32_f16 v[80:83], v[164:167], v[140:143], v[80:83]
	s_add_u32 m0, s28, 0x16000
	s_nop 0
	global_load_lds_dwordx4 v10, s[6:7]
	v_mfma_f32_16x16x32_f16 v[84:87], v[168:171], v[140:143], v[84:87]
	s_waitcnt lgkmcnt(11)
	v_mfma_f32_16x16x32_f16 v[88:91], v[156:159], v[144:147], v[88:91]
	v_mfma_f32_16x16x32_f16 v[92:95], v[160:163], v[144:147], v[92:95]
	v_mfma_f32_16x16x32_f16 v[96:99], v[164:167], v[144:147], v[96:99]
	v_mfma_f32_16x16x32_f16 v[100:103], v[168:171], v[144:147], v[100:103]
	s_waitcnt lgkmcnt(10)
	v_mfma_f32_16x16x32_f16 v[104:107], v[156:159], v[148:151], v[104:107]
	v_mfma_f32_16x16x32_f16 v[108:111], v[160:163], v[148:151], v[108:111]
	s_add_u32 m0, s28, 0x18000
	s_nop 0
	global_load_lds_dwordx4 v11, s[6:7]
	s_add_u32 s6, s6, s20
	s_addc_u32 s7, s7, 0
	v_mfma_f32_16x16x32_f16 v[112:115], v[164:167], v[148:151], v[112:115]
	v_mfma_f32_16x16x32_f16 v[116:119], v[168:171], v[148:151], v[116:119]
	s_waitcnt lgkmcnt(9)
	v_mfma_f32_16x16x32_f16 v[120:123], v[156:159], v[152:155], v[120:123]
	v_mfma_f32_16x16x32_f16 v[124:127], v[160:163], v[152:155], v[124:127]
	v_mfma_f32_16x16x32_f16 v[128:131], v[164:167], v[152:155], v[128:131]
	v_mfma_f32_16x16x32_f16 v[132:135], v[168:171], v[152:155], v[132:135]
	s_waitcnt vmcnt(7) lgkmcnt(0)
	s_barrier
	s_waitcnt lgkmcnt(6)
	ds_read_b128 v[136:139], v15
	ds_read_b128 v[156:159], v17
	ds_read_b128 v[160:163], v17 offset:2048
	ds_read_b128 v[164:167], v17 offset:4096
	ds_read_b128 v[168:171], v17 offset:6144
	ds_read_b128 v[140:143], v15 offset:2048
	ds_read_b128 v[144:147], v15 offset:4096
	ds_read_b128 v[148:151], v15 offset:6144
	ds_read_b128 v[152:155], v15 offset:8192
	v_mfma_f32_16x16x32_f16 v[56:59], v[192:195], v[172:175], v[56:59]
	s_add_u32 m0, s28, 0x1a000
	s_nop 0
	global_load_lds_dwordx4 v10, s[4:5]
	s_waitcnt lgkmcnt(15)
	v_mfma_f32_16x16x32_f16 v[60:63], v[196:199], v[172:175], v[60:63]
	s_waitcnt lgkmcnt(14)
	v_mfma_f32_16x16x32_f16 v[64:67], v[200:203], v[172:175], v[64:67]
	s_waitcnt lgkmcnt(13)
	v_mfma_f32_16x16x32_f16 v[68:71], v[204:207], v[172:175], v[68:71]
	s_waitcnt lgkmcnt(12)
	v_mfma_f32_16x16x32_f16 v[72:75], v[192:195], v[176:179], v[72:75]
	v_mfma_f32_16x16x32_f16 v[76:79], v[196:199], v[176:179], v[76:79]
	s_add_u32 m0, s28, 0x1c000
	s_nop 0
	global_load_lds_dwordx4 v11, s[4:5]
	v_mfma_f32_16x16x32_f16 v[80:83], v[200:203], v[176:179], v[80:83]
	v_mfma_f32_16x16x32_f16 v[84:87], v[204:207], v[176:179], v[84:87]
	s_waitcnt lgkmcnt(11)
	v_mfma_f32_16x16x32_f16 v[88:91], v[192:195], v[180:183], v[88:91]
	v_mfma_f32_16x16x32_f16 v[92:95], v[196:199], v[180:183], v[92:95]
	v_mfma_f32_16x16x32_f16 v[96:99], v[200:203], v[180:183], v[96:99]
	s_add_u32 m0, s28, 0x1e000
	s_nop 0
	global_load_lds_dwordx4 v12, s[4:5]
	v_mfma_f32_16x16x32_f16 v[100:103], v[204:207], v[180:183], v[100:103]
	s_waitcnt lgkmcnt(10)
	v_mfma_f32_16x16x32_f16 v[104:107], v[192:195], v[184:187], v[104:107]
	v_mfma_f32_16x16x32_f16 v[108:111], v[196:199], v[184:187], v[108:111]
	v_mfma_f32_16x16x32_f16 v[112:115], v[200:203], v[184:187], v[112:115]
	v_mfma_f32_16x16x32_f16 v[116:119], v[204:207], v[184:187], v[116:119]
	s_add_u32 m0, s28, 0x20000
	s_nop 0
	global_load_lds_dwordx4 v13, s[4:5]
	s_waitcnt lgkmcnt(9)
	v_mfma_f32_16x16x32_f16 v[120:123], v[192:195], v[188:191], v[120:123]
	v_mfma_f32_16x16x32_f16 v[124:127], v[196:199], v[188:191], v[124:127]
	v_mfma_f32_16x16x32_f16 v[128:131], v[200:203], v[188:191], v[128:131]
	v_mfma_f32_16x16x32_f16 v[132:135], v[204:207], v[188:191], v[132:135]
	s_waitcnt lgkmcnt(6)
	ds_read_b128 v[172:175], v16
	ds_read_b128 v[192:195], v18
	ds_read_b128 v[196:199], v18 offset:2048
	ds_read_b128 v[200:203], v18 offset:4096
	ds_read_b128 v[204:207], v18 offset:6144
	ds_read_b128 v[176:179], v16 offset:2048
	ds_read_b128 v[180:183], v16 offset:4096
	ds_read_b128 v[184:187], v16 offset:6144
	ds_read_b128 v[188:191], v16 offset:8192
	v_mfma_f32_16x16x32_f16 v[56:59], v[156:159], v[136:139], v[56:59]
	s_add_u32 m0, s28, 0x22000
	s_nop 0
	global_load_lds_dwordx4 v14, s[4:5]
	s_add_u32 s4, s4, s20
	s_addc_u32 s5, s5, 0
	s_waitcnt lgkmcnt(15)
	v_mfma_f32_16x16x32_f16 v[60:63], v[160:163], v[136:139], v[60:63]
	s_waitcnt lgkmcnt(14)
	v_mfma_f32_16x16x32_f16 v[64:67], v[164:167], v[136:139], v[64:67]
	s_waitcnt lgkmcnt(13)
	v_mfma_f32_16x16x32_f16 v[68:71], v[168:171], v[136:139], v[68:71]
	s_waitcnt lgkmcnt(12)
	v_mfma_f32_16x16x32_f16 v[72:75], v[156:159], v[140:143], v[72:75]
	v_mfma_f32_16x16x32_f16 v[76:79], v[160:163], v[140:143], v[76:79]
	v_mfma_f32_16x16x32_f16 v[80:83], v[164:167], v[140:143], v[80:83]
	s_add_u32 m0, s28, 0x23000
	s_nop 0
	global_load_lds_dwordx4 v10, s[6:7]
	v_mfma_f32_16x16x32_f16 v[84:87], v[168:171], v[140:143], v[84:87]
	s_waitcnt lgkmcnt(11)
	v_mfma_f32_16x16x32_f16 v[88:91], v[156:159], v[144:147], v[88:91]
	v_mfma_f32_16x16x32_f16 v[92:95], v[160:163], v[144:147], v[92:95]
	v_mfma_f32_16x16x32_f16 v[96:99], v[164:167], v[144:147], v[96:99]
	v_mfma_f32_16x16x32_f16 v[100:103], v[168:171], v[144:147], v[100:103]
	s_waitcnt lgkmcnt(10)
	v_mfma_f32_16x16x32_f16 v[104:107], v[156:159], v[148:151], v[104:107]
	v_mfma_f32_16x16x32_f16 v[108:111], v[160:163], v[148:151], v[108:111]
	s_add_u32 m0, s28, 0x25000
	s_nop 0
	global_load_lds_dwordx4 v11, s[6:7]
	s_add_u32 s6, s6, s20
	s_addc_u32 s7, s7, 0
	v_mfma_f32_16x16x32_f16 v[112:115], v[164:167], v[148:151], v[112:115]
	v_mfma_f32_16x16x32_f16 v[116:119], v[168:171], v[148:151], v[116:119]
	s_waitcnt lgkmcnt(9)
	v_mfma_f32_16x16x32_f16 v[120:123], v[156:159], v[152:155], v[120:123]
	v_mfma_f32_16x16x32_f16 v[124:127], v[160:163], v[152:155], v[124:127]
	v_mfma_f32_16x16x32_f16 v[128:131], v[164:167], v[152:155], v[128:131]
	v_mfma_f32_16x16x32_f16 v[132:135], v[168:171], v[152:155], v[132:135]
	s_waitcnt vmcnt(7) lgkmcnt(0)
	s_barrier
	s_waitcnt lgkmcnt(6)
	ds_read_b128 v[136:139], v15 offset:53248
	ds_read_b128 v[156:159], v17 offset:53248
	ds_read_b128 v[160:163], v17 offset:55296
	ds_read_b128 v[164:167], v17 offset:57344
	ds_read_b128 v[168:171], v17 offset:59392
	ds_read_b128 v[140:143], v15 offset:55296
	ds_read_b128 v[144:147], v15 offset:57344
	ds_read_b128 v[148:151], v15 offset:59392
	ds_read_b128 v[152:155], v15 offset:61440
	v_mfma_f32_16x16x32_f16 v[56:59], v[192:195], v[172:175], v[56:59]
	s_add_u32 m0, s28, 0x0
	s_nop 0
	global_load_lds_dwordx4 v10, s[4:5]
	s_waitcnt lgkmcnt(15)
	v_mfma_f32_16x16x32_f16 v[60:63], v[196:199], v[172:175], v[60:63]
	s_waitcnt lgkmcnt(14)
	v_mfma_f32_16x16x32_f16 v[64:67], v[200:203], v[172:175], v[64:67]
	s_waitcnt lgkmcnt(13)
	v_mfma_f32_16x16x32_f16 v[68:71], v[204:207], v[172:175], v[68:71]
	s_waitcnt lgkmcnt(12)
	v_mfma_f32_16x16x32_f16 v[72:75], v[192:195], v[176:179], v[72:75]
	v_mfma_f32_16x16x32_f16 v[76:79], v[196:199], v[176:179], v[76:79]
	s_add_u32 m0, s28, 0x2000
	s_nop 0
	global_load_lds_dwordx4 v11, s[4:5]
	v_mfma_f32_16x16x32_f16 v[80:83], v[200:203], v[176:179], v[80:83]
	v_mfma_f32_16x16x32_f16 v[84:87], v[204:207], v[176:179], v[84:87]
	s_waitcnt lgkmcnt(11)
	v_mfma_f32_16x16x32_f16 v[88:91], v[192:195], v[180:183], v[88:91]
	v_mfma_f32_16x16x32_f16 v[92:95], v[196:199], v[180:183], v[92:95]
	v_mfma_f32_16x16x32_f16 v[96:99], v[200:203], v[180:183], v[96:99]
	s_add_u32 m0, s28, 0x4000
	s_nop 0
	global_load_lds_dwordx4 v12, s[4:5]
	v_mfma_f32_16x16x32_f16 v[100:103], v[204:207], v[180:183], v[100:103]
	s_waitcnt lgkmcnt(10)
	v_mfma_f32_16x16x32_f16 v[104:107], v[192:195], v[184:187], v[104:107]
	v_mfma_f32_16x16x32_f16 v[108:111], v[196:199], v[184:187], v[108:111]
	v_mfma_f32_16x16x32_f16 v[112:115], v[200:203], v[184:187], v[112:115]
	v_mfma_f32_16x16x32_f16 v[116:119], v[204:207], v[184:187], v[116:119]
	s_add_u32 m0, s28, 0x6000
	s_nop 0
	global_load_lds_dwordx4 v13, s[4:5]
	s_waitcnt lgkmcnt(9)
	v_mfma_f32_16x16x32_f16 v[120:123], v[192:195], v[188:191], v[120:123]
	v_mfma_f32_16x16x32_f16 v[124:127], v[196:199], v[188:191], v[124:127]
	v_mfma_f32_16x16x32_f16 v[128:131], v[200:203], v[188:191], v[128:131]
	v_mfma_f32_16x16x32_f16 v[132:135], v[204:207], v[188:191], v[132:135]
	s_waitcnt lgkmcnt(6)
	ds_read_b128 v[172:175], v16 offset:53248
	ds_read_b128 v[192:195], v18 offset:53248
	ds_read_b128 v[196:199], v18 offset:55296
	ds_read_b128 v[200:203], v18 offset:57344
	ds_read_b128 v[204:207], v18 offset:59392
	ds_read_b128 v[176:179], v16 offset:55296
	ds_read_b128 v[180:183], v16 offset:57344
	ds_read_b128 v[184:187], v16 offset:59392
	ds_read_b128 v[188:191], v16 offset:61440
	v_mfma_f32_16x16x32_f16 v[56:59], v[156:159], v[136:139], v[56:59]
	s_add_u32 m0, s28, 0x8000
	s_nop 0
	global_load_lds_dwordx4 v14, s[4:5]
	s_add_u32 s4, s4, s20
	s_addc_u32 s5, s5, 0
	s_waitcnt lgkmcnt(15)
	v_mfma_f32_16x16x32_f16 v[60:63], v[160:163], v[136:139], v[60:63]
	s_waitcnt lgkmcnt(14)
	v_mfma_f32_16x16x32_f16 v[64:67], v[164:167], v[136:139], v[64:67]
	s_waitcnt lgkmcnt(13)
	v_mfma_f32_16x16x32_f16 v[68:71], v[168:171], v[136:139], v[68:71]
	s_waitcnt lgkmcnt(12)
	v_mfma_f32_16x16x32_f16 v[72:75], v[156:159], v[140:143], v[72:75]
	v_mfma_f32_16x16x32_f16 v[76:79], v[160:163], v[140:143], v[76:79]
	v_mfma_f32_16x16x32_f16 v[80:83], v[164:167], v[140:143], v[80:83]
	s_add_u32 m0, s28, 0x9000
	s_nop 0
	global_load_lds_dwordx4 v10, s[6:7]
	v_mfma_f32_16x16x32_f16 v[84:87], v[168:171], v[140:143], v[84:87]
	s_waitcnt lgkmcnt(11)
	v_mfma_f32_16x16x32_f16 v[88:91], v[156:159], v[144:147], v[88:91]
	v_mfma_f32_16x16x32_f16 v[92:95], v[160:163], v[144:147], v[92:95]
	v_mfma_f32_16x16x32_f16 v[96:99], v[164:167], v[144:147], v[96:99]
	v_mfma_f32_16x16x32_f16 v[100:103], v[168:171], v[144:147], v[100:103]
	s_waitcnt lgkmcnt(10)
	v_mfma_f32_16x16x32_f16 v[104:107], v[156:159], v[148:151], v[104:107]
	v_mfma_f32_16x16x32_f16 v[108:111], v[160:163], v[148:151], v[108:111]
	s_add_u32 m0, s28, 0xb000
	s_nop 0
	global_load_lds_dwordx4 v11, s[6:7]
	s_add_u32 s6, s6, s20
	s_addc_u32 s7, s7, 0
	v_mfma_f32_16x16x32_f16 v[112:115], v[164:167], v[148:151], v[112:115]
	v_mfma_f32_16x16x32_f16 v[116:119], v[168:171], v[148:151], v[116:119]
	s_waitcnt lgkmcnt(9)
	v_mfma_f32_16x16x32_f16 v[120:123], v[156:159], v[152:155], v[120:123]
	v_mfma_f32_16x16x32_f16 v[124:127], v[160:163], v[152:155], v[124:127]
	v_mfma_f32_16x16x32_f16 v[128:131], v[164:167], v[152:155], v[128:131]
	v_mfma_f32_16x16x32_f16 v[132:135], v[168:171], v[152:155], v[132:135]
	s_waitcnt vmcnt(7) lgkmcnt(0)
	s_barrier
	s_waitcnt lgkmcnt(6)
	ds_read_b128 v[136:139], v19
	ds_read_b128 v[156:159], v21
	ds_read_b128 v[160:163], v21 offset:2048
	ds_read_b128 v[164:167], v21 offset:4096
	ds_read_b128 v[168:171], v21 offset:6144
	ds_read_b128 v[140:143], v19 offset:2048
	ds_read_b128 v[144:147], v19 offset:4096
	ds_read_b128 v[148:151], v19 offset:6144
	ds_read_b128 v[152:155], v19 offset:8192
	v_mfma_f32_16x16x32_f16 v[56:59], v[192:195], v[172:175], v[56:59]
	s_waitcnt lgkmcnt(15)
	v_mfma_f32_16x16x32_f16 v[60:63], v[196:199], v[172:175], v[60:63]
	s_waitcnt lgkmcnt(14)
	v_mfma_f32_16x16x32_f16 v[64:67], v[200:203], v[172:175], v[64:67]
	s_waitcnt lgkmcnt(13)
	v_mfma_f32_16x16x32_f16 v[68:71], v[204:207], v[172:175], v[68:71]
	s_waitcnt lgkmcnt(12)
	v_mfma_f32_16x16x32_f16 v[72:75], v[192:195], v[176:179], v[72:75]
	v_mfma_f32_16x16x32_f16 v[76:79], v[196:199], v[176:179], v[76:79]
	v_mfma_f32_16x16x32_f16 v[80:83], v[200:203], v[176:179], v[80:83]
	v_mfma_f32_16x16x32_f16 v[84:87], v[204:207], v[176:179], v[84:87]
	s_waitcnt lgkmcnt(11)
	v_mfma_f32_16x16x32_f16 v[88:91], v[192:195], v[180:183], v[88:91]
	v_mfma_f32_16x16x32_f16 v[92:95], v[196:199], v[180:183], v[92:95]
	v_mfma_f32_16x16x32_f16 v[96:99], v[200:203], v[180:183], v[96:99]
	v_mfma_f32_16x16x32_f16 v[100:103], v[204:207], v[180:183], v[100:103]
	s_waitcnt lgkmcnt(10)
	v_mfma_f32_16x16x32_f16 v[104:107], v[192:195], v[184:187], v[104:107]
	v_mfma_f32_16x16x32_f16 v[108:111], v[196:199], v[184:187], v[108:111]
	v_mfma_f32_16x16x32_f16 v[112:115], v[200:203], v[184:187], v[112:115]
	v_mfma_f32_16x16x32_f16 v[116:119], v[204:207], v[184:187], v[116:119]
	s_waitcnt lgkmcnt(9)
	v_mfma_f32_16x16x32_f16 v[120:123], v[192:195], v[188:191], v[120:123]
	v_mfma_f32_16x16x32_f16 v[124:127], v[196:199], v[188:191], v[124:127]
	v_mfma_f32_16x16x32_f16 v[128:131], v[200:203], v[188:191], v[128:131]
	v_mfma_f32_16x16x32_f16 v[132:135], v[204:207], v[188:191], v[132:135]
	s_waitcnt lgkmcnt(6)
	ds_read_b128 v[172:175], v20
	ds_read_b128 v[192:195], v22
	ds_read_b128 v[196:199], v22 offset:2048
	ds_read_b128 v[200:203], v22 offset:4096
	ds_read_b128 v[204:207], v22 offset:6144
	ds_read_b128 v[176:179], v20 offset:2048
	ds_read_b128 v[180:183], v20 offset:4096
	ds_read_b128 v[184:187], v20 offset:6144
	ds_read_b128 v[188:191], v20 offset:8192
	v_mfma_f32_16x16x32_f16 v[56:59], v[156:159], v[136:139], v[56:59]
	s_waitcnt lgkmcnt(15)
	v_mfma_f32_16x16x32_f16 v[60:63], v[160:163], v[136:139], v[60:63]
	s_waitcnt lgkmcnt(14)
	v_mfma_f32_16x16x32_f16 v[64:67], v[164:167], v[136:139], v[64:67]
	s_waitcnt lgkmcnt(13)
	v_mfma_f32_16x16x32_f16 v[68:71], v[168:171], v[136:139], v[68:71]
	s_waitcnt lgkmcnt(12)
	v_mfma_f32_16x16x32_f16 v[72:75], v[156:159], v[140:143], v[72:75]
	v_mfma_f32_16x16x32_f16 v[76:79], v[160:163], v[140:143], v[76:79]
	v_mfma_f32_16x16x32_f16 v[80:83], v[164:167], v[140:143], v[80:83]
	v_mfma_f32_16x16x32_f16 v[84:87], v[168:171], v[140:143], v[84:87]
	s_waitcnt lgkmcnt(11)
	v_mfma_f32_16x16x32_f16 v[88:91], v[156:159], v[144:147], v[88:91]
	v_mfma_f32_16x16x32_f16 v[92:95], v[160:163], v[144:147], v[92:95]
	v_mfma_f32_16x16x32_f16 v[96:99], v[164:167], v[144:147], v[96:99]
	v_mfma_f32_16x16x32_f16 v[100:103], v[168:171], v[144:147], v[100:103]
	s_waitcnt lgkmcnt(10)
	v_mfma_f32_16x16x32_f16 v[104:107], v[156:159], v[148:151], v[104:107]
	v_mfma_f32_16x16x32_f16 v[108:111], v[160:163], v[148:151], v[108:111]
	v_mfma_f32_16x16x32_f16 v[112:115], v[164:167], v[148:151], v[112:115]
	v_mfma_f32_16x16x32_f16 v[116:119], v[168:171], v[148:151], v[116:119]
	s_waitcnt lgkmcnt(9)
	v_mfma_f32_16x16x32_f16 v[120:123], v[156:159], v[152:155], v[120:123]
	v_mfma_f32_16x16x32_f16 v[124:127], v[160:163], v[152:155], v[124:127]
	v_mfma_f32_16x16x32_f16 v[128:131], v[164:167], v[152:155], v[128:131]
	v_mfma_f32_16x16x32_f16 v[132:135], v[168:171], v[152:155], v[132:135]
	s_waitcnt vmcnt(0) lgkmcnt(0)
	s_barrier
	s_waitcnt lgkmcnt(6)
	ds_read_b128 v[136:139], v15
	ds_read_b128 v[156:159], v17
	ds_read_b128 v[160:163], v17 offset:2048
	ds_read_b128 v[164:167], v17 offset:4096
	ds_read_b128 v[168:171], v17 offset:6144
	ds_read_b128 v[140:143], v15 offset:2048
	ds_read_b128 v[144:147], v15 offset:4096
	ds_read_b128 v[148:151], v15 offset:6144
	ds_read_b128 v[152:155], v15 offset:8192
	v_mfma_f32_16x16x32_f16 v[56:59], v[192:195], v[172:175], v[56:59]
	s_waitcnt lgkmcnt(15)
	v_mfma_f32_16x16x32_f16 v[60:63], v[196:199], v[172:175], v[60:63]
	s_waitcnt lgkmcnt(14)
	v_mfma_f32_16x16x32_f16 v[64:67], v[200:203], v[172:175], v[64:67]
	s_waitcnt lgkmcnt(13)
	v_mfma_f32_16x16x32_f16 v[68:71], v[204:207], v[172:175], v[68:71]
	s_waitcnt lgkmcnt(12)
	v_mfma_f32_16x16x32_f16 v[72:75], v[192:195], v[176:179], v[72:75]
	v_mfma_f32_16x16x32_f16 v[76:79], v[196:199], v[176:179], v[76:79]
	v_mfma_f32_16x16x32_f16 v[80:83], v[200:203], v[176:179], v[80:83]
	v_mfma_f32_16x16x32_f16 v[84:87], v[204:207], v[176:179], v[84:87]
	s_waitcnt lgkmcnt(11)
	v_mfma_f32_16x16x32_f16 v[88:91], v[192:195], v[180:183], v[88:91]
	v_mfma_f32_16x16x32_f16 v[92:95], v[196:199], v[180:183], v[92:95]
	v_mfma_f32_16x16x32_f16 v[96:99], v[200:203], v[180:183], v[96:99]
	v_mfma_f32_16x16x32_f16 v[100:103], v[204:207], v[180:183], v[100:103]
	s_waitcnt lgkmcnt(10)
	v_mfma_f32_16x16x32_f16 v[104:107], v[192:195], v[184:187], v[104:107]
	v_mfma_f32_16x16x32_f16 v[108:111], v[196:199], v[184:187], v[108:111]
	v_mfma_f32_16x16x32_f16 v[112:115], v[200:203], v[184:187], v[112:115]
	v_mfma_f32_16x16x32_f16 v[116:119], v[204:207], v[184:187], v[116:119]
	s_waitcnt lgkmcnt(9)
	v_mfma_f32_16x16x32_f16 v[120:123], v[192:195], v[188:191], v[120:123]
	v_mfma_f32_16x16x32_f16 v[124:127], v[196:199], v[188:191], v[124:127]
	v_mfma_f32_16x16x32_f16 v[128:131], v[200:203], v[188:191], v[128:131]
	v_mfma_f32_16x16x32_f16 v[132:135], v[204:207], v[188:191], v[132:135]
	s_waitcnt lgkmcnt(6)
	ds_read_b128 v[172:175], v16
	ds_read_b128 v[192:195], v18
	ds_read_b128 v[196:199], v18 offset:2048
	ds_read_b128 v[200:203], v18 offset:4096
	ds_read_b128 v[204:207], v18 offset:6144
	ds_read_b128 v[176:179], v16 offset:2048
	ds_read_b128 v[180:183], v16 offset:4096
	ds_read_b128 v[184:187], v16 offset:6144
	ds_read_b128 v[188:191], v16 offset:8192
	v_mfma_f32_16x16x32_f16 v[56:59], v[156:159], v[136:139], v[56:59]
	s_waitcnt lgkmcnt(15)
	v_mfma_f32_16x16x32_f16 v[60:63], v[160:163], v[136:139], v[60:63]
	s_waitcnt lgkmcnt(14)
	v_mfma_f32_16x16x32_f16 v[64:67], v[164:167], v[136:139], v[64:67]
	s_waitcnt lgkmcnt(13)
	v_mfma_f32_16x16x32_f16 v[68:71], v[168:171], v[136:139], v[68:71]
	s_waitcnt lgkmcnt(12)
	v_mfma_f32_16x16x32_f16 v[72:75], v[156:159], v[140:143], v[72:75]
	v_mfma_f32_16x16x32_f16 v[76:79], v[160:163], v[140:143], v[76:79]
	v_mfma_f32_16x16x32_f16 v[80:83], v[164:167], v[140:143], v[80:83]
	v_mfma_f32_16x16x32_f16 v[84:87], v[168:171], v[140:143], v[84:87]
	s_waitcnt lgkmcnt(11)
	v_mfma_f32_16x16x32_f16 v[88:91], v[156:159], v[144:147], v[88:91]
	v_mfma_f32_16x16x32_f16 v[92:95], v[160:163], v[144:147], v[92:95]
	v_mfma_f32_16x16x32_f16 v[96:99], v[164:167], v[144:147], v[96:99]
	v_mfma_f32_16x16x32_f16 v[100:103], v[168:171], v[144:147], v[100:103]
	s_waitcnt lgkmcnt(10)
	v_mfma_f32_16x16x32_f16 v[104:107], v[156:159], v[148:151], v[104:107]
	v_mfma_f32_16x16x32_f16 v[108:111], v[160:163], v[148:151], v[108:111]
	v_mfma_f32_16x16x32_f16 v[112:115], v[164:167], v[148:151], v[112:115]
	v_mfma_f32_16x16x32_f16 v[116:119], v[168:171], v[148:151], v[116:119]
	s_waitcnt lgkmcnt(9)
	v_mfma_f32_16x16x32_f16 v[120:123], v[156:159], v[152:155], v[120:123]
	v_mfma_f32_16x16x32_f16 v[124:127], v[160:163], v[152:155], v[124:127]
	v_mfma_f32_16x16x32_f16 v[128:131], v[164:167], v[152:155], v[128:131]
	v_mfma_f32_16x16x32_f16 v[132:135], v[168:171], v[152:155], v[132:135]
	s_waitcnt lgkmcnt(7)
	v_mfma_f32_16x16x32_f16 v[56:59], v[192:195], v[172:175], v[56:59]
	s_waitcnt lgkmcnt(6)
	v_mfma_f32_16x16x32_f16 v[60:63], v[196:199], v[172:175], v[60:63]
	s_waitcnt lgkmcnt(5)
	v_mfma_f32_16x16x32_f16 v[64:67], v[200:203], v[172:175], v[64:67]
	s_waitcnt lgkmcnt(4)
	v_mfma_f32_16x16x32_f16 v[68:71], v[204:207], v[172:175], v[68:71]
	s_waitcnt lgkmcnt(3)
	v_mfma_f32_16x16x32_f16 v[72:75], v[192:195], v[176:179], v[72:75]
	v_mfma_f32_16x16x32_f16 v[76:79], v[196:199], v[176:179], v[76:79]
	v_mfma_f32_16x16x32_f16 v[80:83], v[200:203], v[176:179], v[80:83]
	v_mfma_f32_16x16x32_f16 v[84:87], v[204:207], v[176:179], v[84:87]
	s_waitcnt lgkmcnt(2)
	v_mfma_f32_16x16x32_f16 v[88:91], v[192:195], v[180:183], v[88:91]
	v_mfma_f32_16x16x32_f16 v[92:95], v[196:199], v[180:183], v[92:95]
	v_mfma_f32_16x16x32_f16 v[96:99], v[200:203], v[180:183], v[96:99]
	v_mfma_f32_16x16x32_f16 v[100:103], v[204:207], v[180:183], v[100:103]
	s_waitcnt lgkmcnt(1)
	v_mfma_f32_16x16x32_f16 v[104:107], v[192:195], v[184:187], v[104:107]
	v_mfma_f32_16x16x32_f16 v[108:111], v[196:199], v[184:187], v[108:111]
	v_mfma_f32_16x16x32_f16 v[112:115], v[200:203], v[184:187], v[112:115]
	v_mfma_f32_16x16x32_f16 v[116:119], v[204:207], v[184:187], v[116:119]
	s_waitcnt lgkmcnt(0)
	v_mfma_f32_16x16x32_f16 v[120:123], v[192:195], v[188:191], v[120:123]
	v_mfma_f32_16x16x32_f16 v[124:127], v[196:199], v[188:191], v[124:127]
	v_mfma_f32_16x16x32_f16 v[128:131], v[200:203], v[188:191], v[128:131]
	v_mfma_f32_16x16x32_f16 v[132:135], v[204:207], v[188:191], v[132:135]
	s_nop 7
	s_nop 1
	v_mov_b32_e32 v211, s19
	v_add_f32_e32 v56, v56, v24
	v_add_f32_e32 v57, v57, v25
	v_add_f32_e32 v58, v58, v26
	v_add_f32_e32 v59, v59, v27
	v_add_f32_e32 v60, v60, v28
	v_add_f32_e32 v61, v61, v29
	v_add_f32_e32 v62, v62, v30
	v_add_f32_e32 v63, v63, v31
	v_add_f32_e32 v64, v64, v32
	v_add_f32_e32 v65, v65, v33
	v_add_f32_e32 v66, v66, v34
	v_add_f32_e32 v67, v67, v35
	v_add_f32_e32 v68, v68, v36
	v_add_f32_e32 v69, v69, v37
	v_add_f32_e32 v70, v70, v38
	v_add_f32_e32 v71, v71, v39
	v_mul_f32_e32 v208, v56, v56
	v_fmac_f32_e32 v208, v57, v57
	v_fmac_f32_e32 v208, v58, v58
	v_fmac_f32_e32 v208, v59, v59
	v_fmac_f32_e32 v208, v60, v60
	v_fmac_f32_e32 v208, v61, v61
	v_fmac_f32_e32 v208, v62, v62
	v_fmac_f32_e32 v208, v63, v63
	v_fmac_f32_e32 v208, v64, v64
	v_fmac_f32_e32 v208, v65, v65
	v_fmac_f32_e32 v208, v66, v66
	v_fmac_f32_e32 v208, v67, v67
	v_fmac_f32_e32 v208, v68, v68
	v_fmac_f32_e32 v208, v69, v69
	v_fmac_f32_e32 v208, v70, v70
	v_fmac_f32_e32 v208, v71, v71
	v_mov_b32_e32 v209, v208
	s_nop 1
	v_permlane16_swap_b32_e32 v208, v209
	v_add_f32_e32 v208, v208, v209
	v_mov_b32_e32 v209, v208
	s_nop 1
	v_permlane32_swap_b32_e32 v208, v209
	v_add_f32_e32 v208, v208, v209
	v_mov_b32_e32 v210, 0x358637bd
	v_fmac_f32_e32 v210, 0x3c800000, v208
	v_rsq_f32_e32 v210, v210
	s_add_u32 s24, s29, 0
	s_lshr_b32 s8, s24, 1
	s_lshl_b32 s8, s8, 12
	s_and_b32 s24, s24, 1
	s_lshl_b32 s24, s24, 8
	s_add_u32 s8, s8, s24
	v_mul_f32_e32 v210, v211, v210
	v_add_u32_e32 v212, s8, v23
	v_mul_f32_e32 v56, v56, v210
	v_mul_f32_e32 v57, v57, v210
	v_mul_f32_e32 v58, v58, v210
	v_mul_f32_e32 v59, v59, v210
	v_mul_f32_e32 v56, v56, v40
	v_mul_f32_e32 v57, v57, v41
	v_mul_f32_e32 v58, v58, v42
	v_mul_f32_e32 v59, v59, v43
	v_cvt_pk_f16_f32 v56, v56, v57
	v_cvt_pk_f16_f32 v57, v58, v59
	global_store_dwordx2 v212, v[56:57], s[22:23] offset:0
	v_mul_f32_e32 v60, v60, v210
	v_mul_f32_e32 v61, v61, v210
	v_mul_f32_e32 v62, v62, v210
	v_mul_f32_e32 v63, v63, v210
	v_mul_f32_e32 v60, v60, v44
	v_mul_f32_e32 v61, v61, v45
	v_mul_f32_e32 v62, v62, v46
	v_mul_f32_e32 v63, v63, v47
	v_cvt_pk_f16_f32 v60, v60, v61
	v_cvt_pk_f16_f32 v61, v62, v63
	global_store_dwordx2 v212, v[60:61], s[22:23] offset:1024
	v_mul_f32_e32 v64, v64, v210
	v_mul_f32_e32 v65, v65, v210
	v_mul_f32_e32 v66, v66, v210
	v_mul_f32_e32 v67, v67, v210
	v_mul_f32_e32 v64, v64, v48
	v_mul_f32_e32 v65, v65, v49
	v_mul_f32_e32 v66, v66, v50
	v_mul_f32_e32 v67, v67, v51
	v_cvt_pk_f16_f32 v64, v64, v65
	v_cvt_pk_f16_f32 v65, v66, v67
	global_store_dwordx2 v212, v[64:65], s[22:23] offset:2048
	v_mul_f32_e32 v68, v68, v210
	v_mul_f32_e32 v69, v69, v210
	v_mul_f32_e32 v70, v70, v210
	v_mul_f32_e32 v71, v71, v210
	v_mul_f32_e32 v68, v68, v52
	v_mul_f32_e32 v69, v69, v53
	v_mul_f32_e32 v70, v70, v54
	v_mul_f32_e32 v71, v71, v55
	v_cvt_pk_f16_f32 v68, v68, v69
	v_cvt_pk_f16_f32 v69, v70, v71
	global_store_dwordx2 v212, v[68:69], s[22:23] offset:3072
	v_add_f32_e32 v72, v72, v24
	v_add_f32_e32 v73, v73, v25
	v_add_f32_e32 v74, v74, v26
	v_add_f32_e32 v75, v75, v27
	v_add_f32_e32 v76, v76, v28
	v_add_f32_e32 v77, v77, v29
	v_add_f32_e32 v78, v78, v30
	v_add_f32_e32 v79, v79, v31
	v_add_f32_e32 v80, v80, v32
	v_add_f32_e32 v81, v81, v33
	v_add_f32_e32 v82, v82, v34
	v_add_f32_e32 v83, v83, v35
	v_add_f32_e32 v84, v84, v36
	v_add_f32_e32 v85, v85, v37
	v_add_f32_e32 v86, v86, v38
	v_add_f32_e32 v87, v87, v39
	v_mul_f32_e32 v208, v72, v72
	v_fmac_f32_e32 v208, v73, v73
	v_fmac_f32_e32 v208, v74, v74
	v_fmac_f32_e32 v208, v75, v75
	v_fmac_f32_e32 v208, v76, v76
	v_fmac_f32_e32 v208, v77, v77
	v_fmac_f32_e32 v208, v78, v78
	v_fmac_f32_e32 v208, v79, v79
	v_fmac_f32_e32 v208, v80, v80
	v_fmac_f32_e32 v208, v81, v81
	v_fmac_f32_e32 v208, v82, v82
	v_fmac_f32_e32 v208, v83, v83
	v_fmac_f32_e32 v208, v84, v84
	v_fmac_f32_e32 v208, v85, v85
	v_fmac_f32_e32 v208, v86, v86
	v_fmac_f32_e32 v208, v87, v87
	v_mov_b32_e32 v209, v208
	s_nop 1
	v_permlane16_swap_b32_e32 v208, v209
	v_add_f32_e32 v208, v208, v209
	v_mov_b32_e32 v209, v208
	s_nop 1
	v_permlane32_swap_b32_e32 v208, v209
	v_add_f32_e32 v208, v208, v209
	v_mov_b32_e32 v210, 0x358637bd
	v_fmac_f32_e32 v210, 0x3c800000, v208
	v_rsq_f32_e32 v210, v210
	s_add_u32 s24, s29, 1
	s_lshr_b32 s8, s24, 1
	s_lshl_b32 s8, s8, 12
	s_and_b32 s24, s24, 1
	s_lshl_b32 s24, s24, 8
	s_add_u32 s8, s8, s24
	v_mul_f32_e32 v210, v211, v210
	v_add_u32_e32 v212, s8, v23
	v_mul_f32_e32 v72, v72, v210
	v_mul_f32_e32 v73, v73, v210
	v_mul_f32_e32 v74, v74, v210
	v_mul_f32_e32 v75, v75, v210
	v_mul_f32_e32 v72, v72, v40
	v_mul_f32_e32 v73, v73, v41
	v_mul_f32_e32 v74, v74, v42
	v_mul_f32_e32 v75, v75, v43
	v_cvt_pk_f16_f32 v72, v72, v73
	v_cvt_pk_f16_f32 v73, v74, v75
	global_store_dwordx2 v212, v[72:73], s[22:23] offset:0
	v_mul_f32_e32 v76, v76, v210
	v_mul_f32_e32 v77, v77, v210
	v_mul_f32_e32 v78, v78, v210
	v_mul_f32_e32 v79, v79, v210
	v_mul_f32_e32 v76, v76, v44
	v_mul_f32_e32 v77, v77, v45
	v_mul_f32_e32 v78, v78, v46
	v_mul_f32_e32 v79, v79, v47
	v_cvt_pk_f16_f32 v76, v76, v77
	v_cvt_pk_f16_f32 v77, v78, v79
	global_store_dwordx2 v212, v[76:77], s[22:23] offset:1024
	v_mul_f32_e32 v80, v80, v210
	v_mul_f32_e32 v81, v81, v210
	v_mul_f32_e32 v82, v82, v210
	v_mul_f32_e32 v83, v83, v210
	v_mul_f32_e32 v80, v80, v48
	v_mul_f32_e32 v81, v81, v49
	v_mul_f32_e32 v82, v82, v50
	v_mul_f32_e32 v83, v83, v51
	v_cvt_pk_f16_f32 v80, v80, v81
	v_cvt_pk_f16_f32 v81, v82, v83
	global_store_dwordx2 v212, v[80:81], s[22:23] offset:2048
	v_mul_f32_e32 v84, v84, v210
	v_mul_f32_e32 v85, v85, v210
	v_mul_f32_e32 v86, v86, v210
	v_mul_f32_e32 v87, v87, v210
	v_mul_f32_e32 v84, v84, v52
	v_mul_f32_e32 v85, v85, v53
	v_mul_f32_e32 v86, v86, v54
	v_mul_f32_e32 v87, v87, v55
	v_cvt_pk_f16_f32 v84, v84, v85
	v_cvt_pk_f16_f32 v85, v86, v87
	global_store_dwordx2 v212, v[84:85], s[22:23] offset:3072
	v_add_f32_e32 v88, v88, v24
	v_add_f32_e32 v89, v89, v25
	v_add_f32_e32 v90, v90, v26
	v_add_f32_e32 v91, v91, v27
	v_add_f32_e32 v92, v92, v28
	v_add_f32_e32 v93, v93, v29
	v_add_f32_e32 v94, v94, v30
	v_add_f32_e32 v95, v95, v31
	v_add_f32_e32 v96, v96, v32
	v_add_f32_e32 v97, v97, v33
	v_add_f32_e32 v98, v98, v34
	v_add_f32_e32 v99, v99, v35
	v_add_f32_e32 v100, v100, v36
	v_add_f32_e32 v101, v101, v37
	v_add_f32_e32 v102, v102, v38
	v_add_f32_e32 v103, v103, v39
	v_mul_f32_e32 v208, v88, v88
	v_fmac_f32_e32 v208, v89, v89
	v_fmac_f32_e32 v208, v90, v90
	v_fmac_f32_e32 v208, v91, v91
	v_fmac_f32_e32 v208, v92, v92
	v_fmac_f32_e32 v208, v93, v93
	v_fmac_f32_e32 v208, v94, v94
	v_fmac_f32_e32 v208, v95, v95
	v_fmac_f32_e32 v208, v96, v96
	v_fmac_f32_e32 v208, v97, v97
	v_fmac_f32_e32 v208, v98, v98
	v_fmac_f32_e32 v208, v99, v99
	v_fmac_f32_e32 v208, v100, v100
	v_fmac_f32_e32 v208, v101, v101
	v_fmac_f32_e32 v208, v102, v102
	v_fmac_f32_e32 v208, v103, v103
	v_mov_b32_e32 v209, v208
	s_nop 1
	v_permlane16_swap_b32_e32 v208, v209
	v_add_f32_e32 v208, v208, v209
	v_mov_b32_e32 v209, v208
	s_nop 1
	v_permlane32_swap_b32_e32 v208, v209
	v_add_f32_e32 v208, v208, v209
	v_mov_b32_e32 v210, 0x358637bd
	v_fmac_f32_e32 v210, 0x3c800000, v208
	v_rsq_f32_e32 v210, v210
	s_add_u32 s24, s29, 2
	s_lshr_b32 s8, s24, 1
	s_lshl_b32 s8, s8, 12
	s_and_b32 s24, s24, 1
	s_lshl_b32 s24, s24, 8
	s_add_u32 s8, s8, s24
	v_mul_f32_e32 v210, v211, v210
	v_add_u32_e32 v212, s8, v23
	v_mul_f32_e32 v88, v88, v210
	v_mul_f32_e32 v89, v89, v210
	v_mul_f32_e32 v90, v90, v210
	v_mul_f32_e32 v91, v91, v210
	v_mul_f32_e32 v88, v88, v40
	v_mul_f32_e32 v89, v89, v41
	v_mul_f32_e32 v90, v90, v42
	v_mul_f32_e32 v91, v91, v43
	v_cvt_pk_f16_f32 v88, v88, v89
	v_cvt_pk_f16_f32 v89, v90, v91
	global_store_dwordx2 v212, v[88:89], s[22:23] offset:0
	v_mul_f32_e32 v92, v92, v210
	v_mul_f32_e32 v93, v93, v210
	v_mul_f32_e32 v94, v94, v210
	v_mul_f32_e32 v95, v95, v210
	v_mul_f32_e32 v92, v92, v44
	v_mul_f32_e32 v93, v93, v45
	v_mul_f32_e32 v94, v94, v46
	v_mul_f32_e32 v95, v95, v47
	v_cvt_pk_f16_f32 v92, v92, v93
	v_cvt_pk_f16_f32 v93, v94, v95
	global_store_dwordx2 v212, v[92:93], s[22:23] offset:1024
	v_mul_f32_e32 v96, v96, v210
	v_mul_f32_e32 v97, v97, v210
	v_mul_f32_e32 v98, v98, v210
	v_mul_f32_e32 v99, v99, v210
	v_mul_f32_e32 v96, v96, v48
	v_mul_f32_e32 v97, v97, v49
	v_mul_f32_e32 v98, v98, v50
	v_mul_f32_e32 v99, v99, v51
	v_cvt_pk_f16_f32 v96, v96, v97
	v_cvt_pk_f16_f32 v97, v98, v99
	global_store_dwordx2 v212, v[96:97], s[22:23] offset:2048
	v_mul_f32_e32 v100, v100, v210
	v_mul_f32_e32 v101, v101, v210
	v_mul_f32_e32 v102, v102, v210
	v_mul_f32_e32 v103, v103, v210
	v_mul_f32_e32 v100, v100, v52
	v_mul_f32_e32 v101, v101, v53
	v_mul_f32_e32 v102, v102, v54
	v_mul_f32_e32 v103, v103, v55
	v_cvt_pk_f16_f32 v100, v100, v101
	v_cvt_pk_f16_f32 v101, v102, v103
	global_store_dwordx2 v212, v[100:101], s[22:23] offset:3072
	v_add_f32_e32 v104, v104, v24
	v_add_f32_e32 v105, v105, v25
	v_add_f32_e32 v106, v106, v26
	v_add_f32_e32 v107, v107, v27
	v_add_f32_e32 v108, v108, v28
	v_add_f32_e32 v109, v109, v29
	v_add_f32_e32 v110, v110, v30
	v_add_f32_e32 v111, v111, v31
	v_add_f32_e32 v112, v112, v32
	v_add_f32_e32 v113, v113, v33
	v_add_f32_e32 v114, v114, v34
	v_add_f32_e32 v115, v115, v35
	v_add_f32_e32 v116, v116, v36
	v_add_f32_e32 v117, v117, v37
	v_add_f32_e32 v118, v118, v38
	v_add_f32_e32 v119, v119, v39
	v_mul_f32_e32 v208, v104, v104
	v_fmac_f32_e32 v208, v105, v105
	v_fmac_f32_e32 v208, v106, v106
	v_fmac_f32_e32 v208, v107, v107
	v_fmac_f32_e32 v208, v108, v108
	v_fmac_f32_e32 v208, v109, v109
	v_fmac_f32_e32 v208, v110, v110
	v_fmac_f32_e32 v208, v111, v111
	v_fmac_f32_e32 v208, v112, v112
	v_fmac_f32_e32 v208, v113, v113
	v_fmac_f32_e32 v208, v114, v114
	v_fmac_f32_e32 v208, v115, v115
	v_fmac_f32_e32 v208, v116, v116
	v_fmac_f32_e32 v208, v117, v117
	v_fmac_f32_e32 v208, v118, v118
	v_fmac_f32_e32 v208, v119, v119
	v_mov_b32_e32 v209, v208
	s_nop 1
	v_permlane16_swap_b32_e32 v208, v209
	v_add_f32_e32 v208, v208, v209
	v_mov_b32_e32 v209, v208
	s_nop 1
	v_permlane32_swap_b32_e32 v208, v209
	v_add_f32_e32 v208, v208, v209
	v_mov_b32_e32 v210, 0x358637bd
	v_fmac_f32_e32 v210, 0x3c800000, v208
	v_rsq_f32_e32 v210, v210
	s_add_u32 s24, s29, 3
	s_lshr_b32 s8, s24, 1
	s_lshl_b32 s8, s8, 12
	s_and_b32 s24, s24, 1
	s_lshl_b32 s24, s24, 8
	s_add_u32 s8, s8, s24
	v_mul_f32_e32 v210, v211, v210
	v_add_u32_e32 v212, s8, v23
	v_mul_f32_e32 v104, v104, v210
	v_mul_f32_e32 v105, v105, v210
	v_mul_f32_e32 v106, v106, v210
	v_mul_f32_e32 v107, v107, v210
	v_mul_f32_e32 v104, v104, v40
	v_mul_f32_e32 v105, v105, v41
	v_mul_f32_e32 v106, v106, v42
	v_mul_f32_e32 v107, v107, v43
	v_cvt_pk_f16_f32 v104, v104, v105
	v_cvt_pk_f16_f32 v105, v106, v107
	global_store_dwordx2 v212, v[104:105], s[22:23] offset:0
	v_mul_f32_e32 v108, v108, v210
	v_mul_f32_e32 v109, v109, v210
	v_mul_f32_e32 v110, v110, v210
	v_mul_f32_e32 v111, v111, v210
	v_mul_f32_e32 v108, v108, v44
	v_mul_f32_e32 v109, v109, v45
	v_mul_f32_e32 v110, v110, v46
	v_mul_f32_e32 v111, v111, v47
	v_cvt_pk_f16_f32 v108, v108, v109
	v_cvt_pk_f16_f32 v109, v110, v111
	global_store_dwordx2 v212, v[108:109], s[22:23] offset:1024
	v_mul_f32_e32 v112, v112, v210
	v_mul_f32_e32 v113, v113, v210
	v_mul_f32_e32 v114, v114, v210
	v_mul_f32_e32 v115, v115, v210
	v_mul_f32_e32 v112, v112, v48
	v_mul_f32_e32 v113, v113, v49
	v_mul_f32_e32 v114, v114, v50
	v_mul_f32_e32 v115, v115, v51
	v_cvt_pk_f16_f32 v112, v112, v113
	v_cvt_pk_f16_f32 v113, v114, v115
	global_store_dwordx2 v212, v[112:113], s[22:23] offset:2048
	v_mul_f32_e32 v116, v116, v210
	v_mul_f32_e32 v117, v117, v210
	v_mul_f32_e32 v118, v118, v210
	v_mul_f32_e32 v119, v119, v210
	v_mul_f32_e32 v116, v116, v52
	v_mul_f32_e32 v117, v117, v53
	v_mul_f32_e32 v118, v118, v54
	v_mul_f32_e32 v119, v119, v55
	v_cvt_pk_f16_f32 v116, v116, v117
	v_cvt_pk_f16_f32 v117, v118, v119
	global_store_dwordx2 v212, v[116:117], s[22:23] offset:3072
	v_add_f32_e32 v120, v120, v24
	v_add_f32_e32 v121, v121, v25
	v_add_f32_e32 v122, v122, v26
	v_add_f32_e32 v123, v123, v27
	v_add_f32_e32 v124, v124, v28
	v_add_f32_e32 v125, v125, v29
	v_add_f32_e32 v126, v126, v30
	v_add_f32_e32 v127, v127, v31
	v_add_f32_e32 v128, v128, v32
	v_add_f32_e32 v129, v129, v33
	v_add_f32_e32 v130, v130, v34
	v_add_f32_e32 v131, v131, v35
	v_add_f32_e32 v132, v132, v36
	v_add_f32_e32 v133, v133, v37
	v_add_f32_e32 v134, v134, v38
	v_add_f32_e32 v135, v135, v39
	v_mul_f32_e32 v208, v120, v120
	v_fmac_f32_e32 v208, v121, v121
	v_fmac_f32_e32 v208, v122, v122
	v_fmac_f32_e32 v208, v123, v123
	v_fmac_f32_e32 v208, v124, v124
	v_fmac_f32_e32 v208, v125, v125
	v_fmac_f32_e32 v208, v126, v126
	v_fmac_f32_e32 v208, v127, v127
	v_fmac_f32_e32 v208, v128, v128
	v_fmac_f32_e32 v208, v129, v129
	v_fmac_f32_e32 v208, v130, v130
	v_fmac_f32_e32 v208, v131, v131
	v_fmac_f32_e32 v208, v132, v132
	v_fmac_f32_e32 v208, v133, v133
	v_fmac_f32_e32 v208, v134, v134
	v_fmac_f32_e32 v208, v135, v135
	v_mov_b32_e32 v209, v208
	s_nop 1
	v_permlane16_swap_b32_e32 v208, v209
	v_add_f32_e32 v208, v208, v209
	v_mov_b32_e32 v209, v208
	s_nop 1
	v_permlane32_swap_b32_e32 v208, v209
	v_add_f32_e32 v208, v208, v209
	v_mov_b32_e32 v210, 0x358637bd
	v_fmac_f32_e32 v210, 0x3c800000, v208
	v_rsq_f32_e32 v210, v210
	s_add_u32 s24, s29, 4
	s_lshr_b32 s8, s24, 1
	s_lshl_b32 s8, s8, 12
	s_and_b32 s24, s24, 1
	s_lshl_b32 s24, s24, 8
	s_add_u32 s8, s8, s24
	v_mul_f32_e32 v210, v211, v210
	v_add_u32_e32 v212, s8, v23
	v_mul_f32_e32 v120, v120, v210
	v_mul_f32_e32 v121, v121, v210
	v_mul_f32_e32 v122, v122, v210
	v_mul_f32_e32 v123, v123, v210
	v_mul_f32_e32 v120, v120, v40
	v_mul_f32_e32 v121, v121, v41
	v_mul_f32_e32 v122, v122, v42
	v_mul_f32_e32 v123, v123, v43
	v_cvt_pk_f16_f32 v120, v120, v121
	v_cvt_pk_f16_f32 v121, v122, v123
	global_store_dwordx2 v212, v[120:121], s[22:23] offset:0
	v_mul_f32_e32 v124, v124, v210
	v_mul_f32_e32 v125, v125, v210
	v_mul_f32_e32 v126, v126, v210
	v_mul_f32_e32 v127, v127, v210
	v_mul_f32_e32 v124, v124, v44
	v_mul_f32_e32 v125, v125, v45
	v_mul_f32_e32 v126, v126, v46
	v_mul_f32_e32 v127, v127, v47
	v_cvt_pk_f16_f32 v124, v124, v125
	v_cvt_pk_f16_f32 v125, v126, v127
	global_store_dwordx2 v212, v[124:125], s[22:23] offset:1024
	v_mul_f32_e32 v128, v128, v210
	v_mul_f32_e32 v129, v129, v210
	v_mul_f32_e32 v130, v130, v210
	v_mul_f32_e32 v131, v131, v210
	v_mul_f32_e32 v128, v128, v48
	v_mul_f32_e32 v129, v129, v49
	v_mul_f32_e32 v130, v130, v50
	v_mul_f32_e32 v131, v131, v51
	v_cvt_pk_f16_f32 v128, v128, v129
	v_cvt_pk_f16_f32 v129, v130, v131
	global_store_dwordx2 v212, v[128:129], s[22:23] offset:2048
	v_mul_f32_e32 v132, v132, v210
	v_mul_f32_e32 v133, v133, v210
	v_mul_f32_e32 v134, v134, v210
	v_mul_f32_e32 v135, v135, v210
	v_mul_f32_e32 v132, v132, v52
	v_mul_f32_e32 v133, v133, v53
	v_mul_f32_e32 v134, v134, v54
	v_mul_f32_e32 v135, v135, v55
	v_cvt_pk_f16_f32 v132, v132, v133
	v_cvt_pk_f16_f32 v133, v134, v135
	global_store_dwordx2 v212, v[132:133], s[22:23] offset:3072
	s_branch .Lpf_done
.Lpf_vKB:
	s_add_u32 m0, s28, 0x0
	s_nop 0
	global_load_lds_dwordx4 v10, s[4:5]
	s_add_u32 m0, s28, 0x2000
	s_nop 0
	global_load_lds_dwordx4 v11, s[4:5]
	s_add_u32 m0, s28, 0x4000
	s_nop 0
	global_load_lds_dwordx4 v12, s[4:5]
	s_add_u32 m0, s28, 0x6000
	s_nop 0
	global_load_lds_dwordx4 v13, s[4:5]
	s_add_u32 s4, s4, s20
	s_addc_u32 s5, s5, 0
	s_add_u32 m0, s28, 0x9000
	s_nop 0
	global_load_lds_dwordx4 v10, s[6:7]
	s_add_u32 m0, s28, 0xb000
	s_nop 0
	global_load_lds_dwordx4 v11, s[6:7]
	s_add_u32 s6, s6, s20
	s_addc_u32 s7, s7, 0
	s_add_u32 m0, s28, 0xd000
	s_nop 0
	global_load_lds_dwordx4 v10, s[4:5]
	s_add_u32 m0, s28, 0xf000
	s_nop 0
	global_load_lds_dwordx4 v11, s[4:5]
	s_add_u32 m0, s28, 0x11000
	s_nop 0
	global_load_lds_dwordx4 v12, s[4:5]
	s_add_u32 m0, s28, 0x13000
	s_nop 0
	global_load_lds_dwordx4 v13, s[4:5]
	s_add_u32 s4, s4, s20
	s_addc_u32 s5, s5, 0
	s_add_u32 m0, s28, 0x16000
	s_nop 0
	global_load_lds_dwordx4 v10, s[6:7]
	s_add_u32 m0, s28, 0x18000
	s_nop 0
	global_load_lds_dwordx4 v11, s[6:7]
	s_add_u32 s6, s6, s20
	s_addc_u32 s7, s7, 0
	s_add_u32 m0, s28, 0x1a000
	s_nop 0
	global_load_lds_dwordx4 v10, s[4:5]
	s_add_u32 m0, s28, 0x1c000
	s_nop 0
	global_load_lds_dwordx4 v11, s[4:5]
	s_add_u32 m0, s28, 0x1e000
	s_nop 0
	global_load_lds_dwordx4 v12, s[4:5]
	s_add_u32 m0, s28, 0x20000
	s_nop 0
	global_load_lds_dwordx4 v13, s[4:5]
	s_add_u32 s4, s4, s20
	s_addc_u32 s5, s5, 0
	s_add_u32 m0, s28, 0x23000
	s_nop 0
	global_load_lds_dwordx4 v10, s[6:7]
	s_add_u32 m0, s28, 0x25000
	s_nop 0
	global_load_lds_dwordx4 v11, s[6:7]
	s_add_u32 s6, s6, s20
	s_addc_u32 s7, s7, 0
	s_waitcnt lgkmcnt(0)
	s_cmp_eq_u32 s9, 0
	s_cselect_b32 s51, s52, s53
	s_cmp_ge_i32 s10, s51
	s_cbranch_scc0 .Lpf_actKB
	s_waitcnt vmcnt(0)
	s_branch .Lpf_done
.Lpf_actKB:
	s_lshl_b32 s25, s25, 6
	s_add_u32 s25, s25, 32
	s_add_u32 s29, s10, s25
	s_lshr_b32 s29, s29, 4
	v_add_u32_e32 v5, s25, v3
	v_lshlrev_b32_e32 v5, 7, v5
	v_add_u32_e32 v15, v5, v6
	v_add_u32_e32 v16, v5, v7
	v_add_u32_e32 v5, 0x9000, v9
	v_add_u32_e32 v17, v5, v6
	v_add_u32_e32 v18, v5, v7
	v_add_u32_e32 v19, 0x1a000, v15
	v_add_u32_e32 v20, 0x1a000, v16
	v_add_u32_e32 v21, 0x1a000, v17
	v_add_u32_e32 v22, 0x1a000, v18
	v_lshlrev_b32_e32 v5, 4, v4
	global_load_dwordx4 v[24:27], v5, s[14:15] offset:0
	global_load_dwordx4 v[28:31], v5, s[14:15] offset:64
	global_load_dwordx4 v[32:35], v5, s[14:15] offset:128
	global_load_dwordx4 v[36:39], v5, s[14:15] offset:192
	global_load_dwordx4 v[40:43], v5, s[16:17] offset:0
	global_load_dwordx4 v[44:47], v5, s[16:17] offset:64
	global_load_dwordx4 v[48:51], v5, s[16:17] offset:128
	global_load_dwordx4 v[52:55], v5, s[16:17] offset:192
	s_waitcnt vmcnt(20) lgkmcnt(0)
	s_barrier
	s_waitcnt lgkmcnt(7)
	ds_read_b128 v[136:139], v15
	ds_read_b128 v[156:159], v17
	ds_read_b128 v[160:163], v17 offset:2048
	ds_read_b128 v[164:167], v17 offset:4096
	ds_read_b128 v[168:171], v17 offset:6144
	ds_read_b128 v[140:143], v15 offset:2048
	ds_read_b128 v[144:147], v15 offset:4096
	ds_read_b128 v[148:151], v15 offset:6144
	s_waitcnt lgkmcnt(7)
	ds_read_b128 v[172:175], v16
	ds_read_b128 v[192:195], v18
	ds_read_b128 v[196:199], v18 offset:2048
	ds_read_b128 v[200:203], v18 offset:4096
	ds_read_b128 v[204:207], v18 offset:6144
	ds_read_b128 v[176:179], v16 offset:2048
	ds_read_b128 v[180:183], v16 offset:4096
	ds_read_b128 v[184:187], v16 offset:6144
	s_waitcnt lgkmcnt(14)
	v_mfma_f32_16x16x32_f16 v[56:59], v[156:159], v[136:139], 0
	s_waitcnt lgkmcnt(13)
	v_mfma_f32_16x16x32_f16 v[60:63], v[160:163], v[136:139], 0
	s_waitcnt lgkmcnt(12)
	v_mfma_f32_16x16x32_f16 v[64:67], v[164:167], v[136:139], 0
	s_waitcnt lgkmcnt(11)
	v_mfma_f32_16x16x32_f16 v[68:71], v[168:171], v[136:139], 0
	s_waitcnt lgkmcnt(10)
	v_mfma_f32_16x16x32_f16 v[72:75], v[156:159], v[140:143], 0
	v_mfma_f32_16x16x32_f16 v[76:79], v[160:163], v[140:143], 0
	v_mfma_f32_16x16x32_f16 v[80:83], v[164:167], v[140:143], 0
	v_mfma_f32_16x16x32_f16 v[84:87], v[168:171], v[140:143], 0
	s_waitcnt lgkmcnt(9)
	v_mfma_f32_16x16x32_f16 v[88:91], v[156:159], v[144:147], 0
	v_mfma_f32_16x16x32_f16 v[92:95], v[160:163], v[144:147], 0
	v_mfma_f32_16x16x32_f16 v[96:99], v[164:167], v[144:147], 0
	v_mfma_f32_16x16x32_f16 v[100:103], v[168:171], v[144:147], 0
	s_waitcnt lgkmcnt(8)
	v_mfma_f32_16x16x32_f16 v[104:107], v[156:159], v[148:151], 0
	v_mfma_f32_16x16x32_f16 v[108:111], v[160:163], v[148:151], 0
	v_mfma_f32_16x16x32_f16 v[112:115], v[164:167], v[148:151], 0
	v_mfma_f32_16x16x32_f16 v[116:119], v[168:171], v[148:151], 0
	s_waitcnt vmcnt(14) lgkmcnt(0)
	s_barrier
	s_waitcnt lgkmcnt(7)
	ds_read_b128 v[136:139], v15 offset:53248
	ds_read_b128 v[156:159], v17 offset:53248
	ds_read_b128 v[160:163], v17 offset:55296
	ds_read_b128 v[164:167], v17 offset:57344
	ds_read_b128 v[168:171], v17 offset:59392
	ds_read_b128 v[140:143], v15 offset:55296
	ds_read_b128 v[144:147], v15 offset:57344
	ds_read_b128 v[148:151], v15 offset:59392
	s_waitcnt lgkmcnt(14)
	v_mfma_f32_16x16x32_f16 v[56:59], v[192:195], v[172:175], v[56:59]
	s_add_u32 m0, s28, 0x0
	s_nop 0
	global_load_lds_dwordx4 v10, s[4:5]
	s_waitcnt lgkmcnt(13)
	v_mfma_f32_16x16x32_f16 v[60:63], v[196:199], v[172:175], v[60:63]
	s_waitcnt lgkmcnt(12)
	v_mfma_f32_16x16x32_f16 v[64:67], v[200:203], v[172:175], v[64:67]
	s_waitcnt lgkmcnt(11)
	v_mfma_f32_16x16x32_f16 v[68:71], v[204:207], v[172:175], v[68:71]
	s_waitcnt lgkmcnt(10)
	v_mfma_f32_16x16x32_f16 v[72:75], v[192:195], v[176:179], v[72:75]
	v_mfma_f32_16x16x32_f16 v[76:79], v[196:199], v[176:179], v[76:79]
	s_add_u32 m0, s28, 0x2000
	s_nop 0
	global_load_lds_dwordx4 v11, s[4:5]
	v_mfma_f32_16x16x32_f16 v[80:83], v[200:203], v[176:179], v[80:83]
	v_mfma_f32_16x16x32_f16 v[84:87], v[204:207], v[176:179], v[84:87]
	s_waitcnt lgkmcnt(9)
	v_mfma_f32_16x16x32_f16 v[88:91], v[192:195], v[180:183], v[88:91]
	v_mfma_f32_16x16x32_f16 v[92:95], v[196:199], v[180:183], v[92:95]
	v_mfma_f32_16x16x32_f16 v[96:99], v[200:203], v[180:183], v[96:99]
	s_add_u32 m0, s28, 0x4000
	s_nop 0
	global_load_lds_dwordx4 v12, s[4:5]
	v_mfma_f32_16x16x32_f16 v[100:103], v[204:207], v[180:183], v[100:103]
	s_waitcnt lgkmcnt(8)
	v_mfma_f32_16x16x32_f16 v[104:107], v[192:195], v[184:187], v[104:107]
	v_mfma_f32_16x16x32_f16 v[108:111], v[196:199], v[184:187], v[108:111]
	v_mfma_f32_16x16x32_f16 v[112:115], v[200:203], v[184:187], v[112:115]
	v_mfma_f32_16x16x32_f16 v[116:119], v[204:207], v[184:187], v[116:119]
	s_waitcnt lgkmcnt(7)
	ds_read_b128 v[172:175], v16 offset:53248
	ds_read_b128 v[192:195], v18 offset:53248
	ds_read_b128 v[196:199], v18 offset:55296
	ds_read_b128 v[200:203], v18 offset:57344
	ds_read_b128 v[204:207], v18 offset:59392
	ds_read_b128 v[176:179], v16 offset:55296
	ds_read_b128 v[180:183], v16 offset:57344
	ds_read_b128 v[184:187], v16 offset:59392
	s_waitcnt lgkmcnt(14)
	v_mfma_f32_16x16x32_f16 v[56:59], v[156:159], v[136:139], v[56:59]
	s_add_u32 m0, s28, 0x6000
	s_nop 0
	global_load_lds_dwordx4 v13, s[4:5]
	s_add_u32 s4, s4, s20
	s_addc_u32 s5, s5, 0
	s_waitcnt lgkmcnt(13)
	v_mfma_f32_16x16x32_f16 v[60:63], v[160:163], v[136:139], v[60:63]
	s_waitcnt lgkmcnt(12)
	v_mfma_f32_16x16x32_f16 v[64:67], v[164:167], v[136:139], v[64:67]
	s_waitcnt lgkmcnt(11)
	v_mfma_f32_16x16x32_f16 v[68:71], v[168:171], v[136:139], v[68:71]
	s_waitcnt lgkmcnt(10)
	v_mfma_f32_16x16x32_f16 v[72:75], v[156:159], v[140:143], v[72:75]
	v_mfma_f32_16x16x32_f16 v[76:79], v[160:163], v[140:143], v[76:79]
	s_add_u32 m0, s28, 0x9000
	s_nop 0
	global_load_lds_dwordx4 v10, s[6:7]
	v_mfma_f32_16x16x32_f16 v[80:83], v[164:167], v[140:143], v[80:83]
	v_mfma_f32_16x16x32_f16 v[84:87], v[168:171], v[140:143], v[84:87]
	s_waitcnt lgkmcnt(9)
	v_mfma_f32_16x16x32_f16 v[88:91], v[156:159], v[144:147], v[88:91]
	v_mfma_f32_16x16x32_f16 v[92:95], v[160:163], v[144:147], v[92:95]
	v_mfma_f32_16x16x32_f16 v[96:99], v[164:167], v[144:147], v[96:99]
	s_add_u32 m0, s28, 0xb000
	s_nop 0
	global_load_lds_dwordx4 v11, s[6:7]
	s_add_u32 s6, s6, s20
	s_addc_u32 s7, s7, 0
	v_mfma_f32_16x16x32_f16 v[100:103], v[168:171], v[144:147], v[100:103]
	s_waitcnt lgkmcnt(8)
	v_mfma_f32_16x16x32_f16 v[104:107], v[156:159], v[148:151], v[104:107]
	v_mfma_f32_16x16x32_f16 v[108:111], v[160:163], v[148:151], v[108:111]
	v_mfma_f32_16x16x32_f16 v[112:115], v[164:167], v[148:151], v[112:115]
	v_mfma_f32_16x16x32_f16 v[116:119], v[168:171], v[148:151], v[116:119]
	s_waitcnt vmcnt(6) lgkmcnt(0)
	s_barrier
	s_waitcnt lgkmcnt(7)
	ds_read_b128 v[136:139], v19
	ds_read_b128 v[156:159], v21
	ds_read_b128 v[160:163], v21 offset:2048
	ds_read_b128 v[164:167], v21 offset:4096
	ds_read_b128 v[168:171], v21 offset:6144
	ds_read_b128 v[140:143], v19 offset:2048
	ds_read_b128 v[144:147], v19 offset:4096
	ds_read_b128 v[148:151], v19 offset:6144
	s_waitcnt lgkmcnt(14)
	v_mfma_f32_16x16x32_f16 v[56:59], v[192:195], v[172:175], v[56:59]
	s_add_u32 m0, s28, 0xd000
	s_nop 0
	global_load_lds_dwordx4 v10, s[4:5]
	s_waitcnt lgkmcnt(13)
	v_mfma_f32_16x16x32_f16 v[60:63], v[196:199], v[172:175], v[60:63]
	s_waitcnt lgkmcnt(12)
	v_mfma_f32_16x16x32_f16 v[64:67], v[200:203], v[172:175], v[64:67]
	s_waitcnt lgkmcnt(11)
	v_mfma_f32_16x16x32_f16 v[68:71], v[204:207], v[172:175], v[68:71]
	s_waitcnt lgkmcnt(10)
	v_mfma_f32_16x16x32_f16 v[72:75], v[192:195], v[176:179], v[72:75]
	v_mfma_f32_16x16x32_f16 v[76:79], v[196:199], v[176:179], v[76:79]
	s_add_u32 m0, s28, 0xf000
	s_nop 0
	global_load_lds_dwordx4 v11, s[4:5]
	v_mfma_f32_16x16x32_f16 v[80:83], v[200:203], v[176:179], v[80:83]
	v_mfma_f32_16x16x32_f16 v[84:87], v[204:207], v[176:179], v[84:87]
	s_waitcnt lgkmcnt(9)
	v_mfma_f32_16x16x32_f16 v[88:91], v[192:195], v[180:183], v[88:91]
	v_mfma_f32_16x16x32_f16 v[92:95], v[196:199], v[180:183], v[92:95]
	v_mfma_f32_16x16x32_f16 v[96:99], v[200:203], v[180:183], v[96:99]
	s_add_u32 m0, s28, 0x11000
	s_nop 0
	global_load_lds_dwordx4 v12, s[4:5]
	v_mfma_f32_16x16x32_f16 v[100:103], v[204:207], v[180:183], v[100:103]
	s_waitcnt lgkmcnt(8)
	v_mfma_f32_16x16x32_f16 v[104:107], v[192:195], v[184:187], v[104:107]
	v_mfma_f32_16x16x32_f16 v[108:111], v[196:199], v[184:187], v[108:111]
	v_mfma_f32_16x16x32_f16 v[112:115], v[200:203], v[184:187], v[112:115]
	v_mfma_f32_16x16x32_f16 v[116:119], v[204:207], v[184:187], v[116:119]
	s_waitcnt lgkmcnt(7)
	ds_read_b128 v[172:175], v20
	ds_read_b128 v[192:195], v22
	ds_read_b128 v[196:199], v22 offset:2048
	ds_read_b128 v[200:203], v22 offset:4096
	ds_read_b128 v[204:207], v22 offset:6144
	ds_read_b128 v[176:179], v20 offset:2048
	ds_read_b128 v[180:183], v20 offset:4096
	ds_read_b128 v[184:187], v20 offset:6144
	s_waitcnt lgkmcnt(14)
	v_mfma_f32_16x16x32_f16 v[56:59], v[156:159], v[136:139], v[56:59]
	s_add_u32 m0, s28, 0x13000
	s_nop 0
	global_load_lds_dwordx4 v13, s[4:5]
	s_add_u32 s4, s4, s20
	s_addc_u32 s5, s5, 0
	s_waitcnt lgkmcnt(13)
	v_mfma_f32_16x16x32_f16 v[60:63], v[160:163], v[136:139], v[60:63]
	s_waitcnt lgkmcnt(12)
	v_mfma_f32_16x16x32_f16 v[64:67], v[164:167], v[136:139], v[64:67]
	s_waitcnt lgkmcnt(11)
	v_mfma_f32_16x16x32_f16 v[68:71], v[168:171], v[136:139], v[68:71]
	s_waitcnt lgkmcnt(10)
	v_mfma_f32_16x16x32_f16 v[72:75], v[156:159], v[140:143], v[72:75]
	v_mfma_f32_16x16x32_f16 v[76:79], v[160:163], v[140:143], v[76:79]
	s_add_u32 m0, s28, 0x16000
	s_nop 0
	global_load_lds_dwordx4 v10, s[6:7]
	v_mfma_f32_16x16x32_f16 v[80:83], v[164:167], v[140:143], v[80:83]
	v_mfma_f32_16x16x32_f16 v[84:87], v[168:171], v[140:143], v[84:87]
	s_waitcnt lgkmcnt(9)
	v_mfma_f32_16x16x32_f16 v[88:91], v[156:159], v[144:147], v[88:91]
	v_mfma_f32_16x16x32_f16 v[92:95], v[160:163], v[144:147], v[92:95]
	v_mfma_f32_16x16x32_f16 v[96:99], v[164:167], v[144:147], v[96:99]
	s_add_u32 m0, s28, 0x18000
	s_nop 0
	global_load_lds_dwordx4 v11, s[6:7]
	s_add_u32 s6, s6, s20
	s_addc_u32 s7, s7, 0
	v_mfma_f32_16x16x32_f16 v[100:103], v[168:171], v[144:147], v[100:103]
	s_waitcnt lgkmcnt(8)
	v_mfma_f32_16x16x32_f16 v[104:107], v[156:159], v[148:151], v[104:107]
	v_mfma_f32_16x16x32_f16 v[108:111], v[160:163], v[148:151], v[108:111]
	v_mfma_f32_16x16x32_f16 v[112:115], v[164:167], v[148:151], v[112:115]
	v_mfma_f32_16x16x32_f16 v[116:119], v[168:171], v[148:151], v[116:119]
	s_waitcnt vmcnt(6) lgkmcnt(0)
	s_barrier
	s_waitcnt lgkmcnt(7)
	ds_read_b128 v[136:139], v15
	ds_read_b128 v[156:159], v17
	ds_read_b128 v[160:163], v17 offset:2048
	ds_read_b128 v[164:167], v17 offset:4096
	ds_read_b128 v[168:171], v17 offset:6144
	ds_read_b128 v[140:143], v15 offset:2048
	ds_read_b128 v[144:147], v15 offset:4096
	ds_read_b128 v[148:151], v15 offset:6144
	s_waitcnt lgkmcnt(14)
	v_mfma_f32_16x16x32_f16 v[56:59], v[192:195], v[172:175], v[56:59]
	s_add_u32 m0, s28, 0x1a000
	s_nop 0
	global_load_lds_dwordx4 v10, s[4:5]
	s_waitcnt lgkmcnt(13)
	v_mfma_f32_16x16x32_f16 v[60:63], v[196:199], v[172:175], v[60:63]
	s_waitcnt lgkmcnt(12)
	v_mfma_f32_16x16x32_f16 v[64:67], v[200:203], v[172:175], v[64:67]
	s_waitcnt lgkmcnt(11)
	v_mfma_f32_16x16x32_f16 v[68:71], v[204:207], v[172:175], v[68:71]
	s_waitcnt lgkmcnt(10)
	v_mfma_f32_16x16x32_f16 v[72:75], v[192:195], v[176:179], v[72:75]
	v_mfma_f32_16x16x32_f16 v[76:79], v[196:199], v[176:179], v[76:79]
	s_add_u32 m0, s28, 0x1c000
	s_nop 0
	global_load_lds_dwordx4 v11, s[4:5]
	v_mfma_f32_16x16x32_f16 v[80:83], v[200:203], v[176:179], v[80:83]
	v_mfma_f32_16x16x32_f16 v[84:87], v[204:207], v[176:179], v[84:87]
	s_waitcnt lgkmcnt(9)
	v_mfma_f32_16x16x32_f16 v[88:91], v[192:195], v[180:183], v[88:91]
	v_mfma_f32_16x16x32_f16 v[92:95], v[196:199], v[180:183], v[92:95]
	v_mfma_f32_16x16x32_f16 v[96:99], v[200:203], v[180:183], v[96:99]
	s_add_u32 m0, s28, 0x1e000
	s_nop 0
	global_load_lds_dwordx4 v12, s[4:5]
	v_mfma_f32_16x16x32_f16 v[100:103], v[204:207], v[180:183], v[100:103]
	s_waitcnt lgkmcnt(8)
	v_mfma_f32_16x16x32_f16 v[104:107], v[192:195], v[184:187], v[104:107]
	v_mfma_f32_16x16x32_f16 v[108:111], v[196:199], v[184:187], v[108:111]
	v_mfma_f32_16x16x32_f16 v[112:115], v[200:203], v[184:187], v[112:115]
	v_mfma_f32_16x16x32_f16 v[116:119], v[204:207], v[184:187], v[116:119]
	s_waitcnt lgkmcnt(7)
	ds_read_b128 v[172:175], v16
	ds_read_b128 v[192:195], v18
	ds_read_b128 v[196:199], v18 offset:2048
	ds_read_b128 v[200:203], v18 offset:4096
	ds_read_b128 v[204:207], v18 offset:6144
	ds_read_b128 v[176:179], v16 offset:2048
	ds_read_b128 v[180:183], v16 offset:4096
	ds_read_b128 v[184:187], v16 offset:6144
	s_waitcnt lgkmcnt(14)
	v_mfma_f32_16x16x32_f16 v[56:59], v[156:159], v[136:139], v[56:59]
	s_add_u32 m0, s28, 0x20000
	s_nop 0
	global_load_lds_dwordx4 v13, s[4:5]
	s_add_u32 s4, s4, s20
	s_addc_u32 s5, s5, 0
	s_waitcnt lgkmcnt(13)
	v_mfma_f32_16x16x32_f16 v[60:63], v[160:163], v[136:139], v[60:63]
	s_waitcnt lgkmcnt(12)
	v_mfma_f32_16x16x32_f16 v[64:67], v[164:167], v[136:139], v[64:67]
	s_waitcnt lgkmcnt(11)
	v_mfma_f32_16x16x32_f16 v[68:71], v[168:171], v[136:139], v[68:71]
	s_waitcnt lgkmcnt(10)
	v_mfma_f32_16x16x32_f16 v[72:75], v[156:159], v[140:143], v[72:75]
	v_mfma_f32_16x16x32_f16 v[76:79], v[160:163], v[140:143], v[76:79]
	s_add_u32 m0, s28, 0x23000
	s_nop 0
	global_load_lds_dwordx4 v10, s[6:7]
	v_mfma_f32_16x16x32_f16 v[80:83], v[164:167], v[140:143], v[80:83]
	v_mfma_f32_16x16x32_f16 v[84:87], v[168:171], v[140:143], v[84:87]
	s_waitcnt lgkmcnt(9)
	v_mfma_f32_16x16x32_f16 v[88:91], v[156:159], v[144:147], v[88:91]
	v_mfma_f32_16x16x32_f16 v[92:95], v[160:163], v[144:147], v[92:95]
	v_mfma_f32_16x16x32_f16 v[96:99], v[164:167], v[144:147], v[96:99]
	s_add_u32 m0, s28, 0x25000
	s_nop 0
	global_load_lds_dwordx4 v11, s[6:7]
	s_add_u32 s6, s6, s20
	s_addc_u32 s7, s7, 0
	v_mfma_f32_16x16x32_f16 v[100:103], v[168:171], v[144:147], v[100:103]
	s_waitcnt lgkmcnt(8)
	v_mfma_f32_16x16x32_f16 v[104:107], v[156:159], v[148:151], v[104:107]
	v_mfma_f32_16x16x32_f16 v[108:111], v[160:163], v[148:151], v[108:111]
	v_mfma_f32_16x16x32_f16 v[112:115], v[164:167], v[148:151], v[112:115]
	v_mfma_f32_16x16x32_f16 v[116:119], v[168:171], v[148:151], v[116:119]
	s_waitcnt vmcnt(6) lgkmcnt(0)
	s_barrier
	s_waitcnt lgkmcnt(7)
	ds_read_b128 v[136:139], v15 offset:53248
	ds_read_b128 v[156:159], v17 offset:53248
	ds_read_b128 v[160:163], v17 offset:55296
	ds_read_b128 v[164:167], v17 offset:57344
	ds_read_b128 v[168:171], v17 offset:59392
	ds_read_b128 v[140:143], v15 offset:55296
	ds_read_b128 v[144:147], v15 offset:57344
	ds_read_b128 v[148:151], v15 offset:59392
	s_waitcnt lgkmcnt(14)
	v_mfma_f32_16x16x32_f16 v[56:59], v[192:195], v[172:175], v[56:59]
	s_add_u32 m0, s28, 0x0
	s_nop 0
	global_load_lds_dwordx4 v10, s[4:5]
	s_waitcnt lgkmcnt(13)
	v_mfma_f32_16x16x32_f16 v[60:63], v[196:199], v[172:175], v[60:63]
	s_waitcnt lgkmcnt(12)
	v_mfma_f32_16x16x32_f16 v[64:67], v[200:203], v[172:175], v[64:67]
	s_waitcnt lgkmcnt(11)
	v_mfma_f32_16x16x32_f16 v[68:71], v[204:207], v[172:175], v[68:71]
	s_waitcnt lgkmcnt(10)
	v_mfma_f32_16x16x32_f16 v[72:75], v[192:195], v[176:179], v[72:75]
	v_mfma_f32_16x16x32_f16 v[76:79], v[196:199], v[176:179], v[76:79]
	s_add_u32 m0, s28, 0x2000
	s_nop 0
	global_load_lds_dwordx4 v11, s[4:5]
	v_mfma_f32_16x16x32_f16 v[80:83], v[200:203], v[176:179], v[80:83]
	v_mfma_f32_16x16x32_f16 v[84:87], v[204:207], v[176:179], v[84:87]
	s_waitcnt lgkmcnt(9)
	v_mfma_f32_16x16x32_f16 v[88:91], v[192:195], v[180:183], v[88:91]
	v_mfma_f32_16x16x32_f16 v[92:95], v[196:199], v[180:183], v[92:95]
	v_mfma_f32_16x16x32_f16 v[96:99], v[200:203], v[180:183], v[96:99]
	s_add_u32 m0, s28, 0x4000
	s_nop 0
	global_load_lds_dwordx4 v12, s[4:5]
	v_mfma_f32_16x16x32_f16 v[100:103], v[204:207], v[180:183], v[100:103]
	s_waitcnt lgkmcnt(8)
	v_mfma_f32_16x16x32_f16 v[104:107], v[192:195], v[184:187], v[104:107]
	v_mfma_f32_16x16x32_f16 v[108:111], v[196:199], v[184:187], v[108:111]
	v_mfma_f32_16x16x32_f16 v[112:115], v[200:203], v[184:187], v[112:115]
	v_mfma_f32_16x16x32_f16 v[116:119], v[204:207], v[184:187], v[116:119]
	s_waitcnt lgkmcnt(7)
	ds_read_b128 v[172:175], v16 offset:53248
	ds_read_b128 v[192:195], v18 offset:53248
	ds_read_b128 v[196:199], v18 offset:55296
	ds_read_b128 v[200:203], v18 offset:57344
	ds_read_b128 v[204:207], v18 offset:59392
	ds_read_b128 v[176:179], v16 offset:55296
	ds_read_b128 v[180:183], v16 offset:57344
	ds_read_b128 v[184:187], v16 offset:59392
	s_waitcnt lgkmcnt(14)
	v_mfma_f32_16x16x32_f16 v[56:59], v[156:159], v[136:139], v[56:59]
	s_add_u32 m0, s28, 0x6000
	s_nop 0
	global_load_lds_dwordx4 v13, s[4:5]
	s_add_u32 s4, s4, s20
	s_addc_u32 s5, s5, 0
	s_waitcnt lgkmcnt(13)
	v_mfma_f32_16x16x32_f16 v[60:63], v[160:163], v[136:139], v[60:63]
	s_waitcnt lgkmcnt(12)
	v_mfma_f32_16x16x32_f16 v[64:67], v[164:167], v[136:139], v[64:67]
	s_waitcnt lgkmcnt(11)
	v_mfma_f32_16x16x32_f16 v[68:71], v[168:171], v[136:139], v[68:71]
	s_waitcnt lgkmcnt(10)
	v_mfma_f32_16x16x32_f16 v[72:75], v[156:159], v[140:143], v[72:75]
	v_mfma_f32_16x16x32_f16 v[76:79], v[160:163], v[140:143], v[76:79]
	s_add_u32 m0, s28, 0x9000
	s_nop 0
	global_load_lds_dwordx4 v10, s[6:7]
	v_mfma_f32_16x16x32_f16 v[80:83], v[164:167], v[140:143], v[80:83]
	v_mfma_f32_16x16x32_f16 v[84:87], v[168:171], v[140:143], v[84:87]
	s_waitcnt lgkmcnt(9)
	v_mfma_f32_16x16x32_f16 v[88:91], v[156:159], v[144:147], v[88:91]
	v_mfma_f32_16x16x32_f16 v[92:95], v[160:163], v[144:147], v[92:95]
	v_mfma_f32_16x16x32_f16 v[96:99], v[164:167], v[144:147], v[96:99]
	s_add_u32 m0, s28, 0xb000
	s_nop 0
	global_load_lds_dwordx4 v11, s[6:7]
	s_add_u32 s6, s6, s20
	s_addc_u32 s7, s7, 0
	v_mfma_f32_16x16x32_f16 v[100:103], v[168:171], v[144:147], v[100:103]
	s_waitcnt lgkmcnt(8)
	v_mfma_f32_16x16x32_f16 v[104:107], v[156:159], v[148:151], v[104:107]
	v_mfma_f32_16x16x32_f16 v[108:111], v[160:163], v[148:151], v[108:111]
	v_mfma_f32_16x16x32_f16 v[112:115], v[164:167], v[148:151], v[112:115]
	v_mfma_f32_16x16x32_f16 v[116:119], v[168:171], v[148:151], v[116:119]
	s_waitcnt vmcnt(6) lgkmcnt(0)
	s_barrier
	s_waitcnt lgkmcnt(7)
	ds_read_b128 v[136:139], v19
	ds_read_b128 v[156:159], v21
	ds_read_b128 v[160:163], v21 offset:2048
	ds_read_b128 v[164:167], v21 offset:4096
	ds_read_b128 v[168:171], v21 offset:6144
	ds_read_b128 v[140:143], v19 offset:2048
	ds_read_b128 v[144:147], v19 offset:4096
	ds_read_b128 v[148:151], v19 offset:6144
	s_waitcnt lgkmcnt(14)
	v_mfma_f32_16x16x32_f16 v[56:59], v[192:195], v[172:175], v[56:59]
	s_add_u32 m0, s28, 0xd000
	s_nop 0
	global_load_lds_dwordx4 v10, s[4:5]
	s_waitcnt lgkmcnt(13)
	v_mfma_f32_16x16x32_f16 v[60:63], v[196:199], v[172:175], v[60:63]
	s_waitcnt lgkmcnt(12)
	v_mfma_f32_16x16x32_f16 v[64:67], v[200:203], v[172:175], v[64:67]
	s_waitcnt lgkmcnt(11)
	v_mfma_f32_16x16x32_f16 v[68:71], v[204:207], v[172:175], v[68:71]
	s_waitcnt lgkmcnt(10)
	v_mfma_f32_16x16x32_f16 v[72:75], v[192:195], v[176:179], v[72:75]
	v_mfma_f32_16x16x32_f16 v[76:79], v[196:199], v[176:179], v[76:79]
	s_add_u32 m0, s28, 0xf000
	s_nop 0
	global_load_lds_dwordx4 v11, s[4:5]
	v_mfma_f32_16x16x32_f16 v[80:83], v[200:203], v[176:179], v[80:83]
	v_mfma_f32_16x16x32_f16 v[84:87], v[204:207], v[176:179], v[84:87]
	s_waitcnt lgkmcnt(9)
	v_mfma_f32_16x16x32_f16 v[88:91], v[192:195], v[180:183], v[88:91]
	v_mfma_f32_16x16x32_f16 v[92:95], v[196:199], v[180:183], v[92:95]
	v_mfma_f32_16x16x32_f16 v[96:99], v[200:203], v[180:183], v[96:99]
	s_add_u32 m0, s28, 0x11000
	s_nop 0
	global_load_lds_dwordx4 v12, s[4:5]
	v_mfma_f32_16x16x32_f16 v[100:103], v[204:207], v[180:183], v[100:103]
	s_waitcnt lgkmcnt(8)
	v_mfma_f32_16x16x32_f16 v[104:107], v[192:195], v[184:187], v[104:107]
	v_mfma_f32_16x16x32_f16 v[108:111], v[196:199], v[184:187], v[108:111]
	v_mfma_f32_16x16x32_f16 v[112:115], v[200:203], v[184:187], v[112:115]
	v_mfma_f32_16x16x32_f16 v[116:119], v[204:207], v[184:187], v[116:119]
	s_waitcnt lgkmcnt(7)
	ds_read_b128 v[172:175], v20
	ds_read_b128 v[192:195], v22
	ds_read_b128 v[196:199], v22 offset:2048
	ds_read_b128 v[200:203], v22 offset:4096
	ds_read_b128 v[204:207], v22 offset:6144
	ds_read_b128 v[176:179], v20 offset:2048
	ds_read_b128 v[180:183], v20 offset:4096
	ds_read_b128 v[184:187], v20 offset:6144
	s_waitcnt lgkmcnt(14)
	v_mfma_f32_16x16x32_f16 v[56:59], v[156:159], v[136:139], v[56:59]
	s_add_u32 m0, s28, 0x13000
	s_nop 0
	global_load_lds_dwordx4 v13, s[4:5]
	s_add_u32 s4, s4, s20
	s_addc_u32 s5, s5, 0
	s_waitcnt lgkmcnt(13)
	v_mfma_f32_16x16x32_f16 v[60:63], v[160:163], v[136:139], v[60:63]
	s_waitcnt lgkmcnt(12)
	v_mfma_f32_16x16x32_f16 v[64:67], v[164:167], v[136:139], v[64:67]
	s_waitcnt lgkmcnt(11)
	v_mfma_f32_16x16x32_f16 v[68:71], v[168:171], v[136:139], v[68:71]
	s_waitcnt lgkmcnt(10)
	v_mfma_f32_16x16x32_f16 v[72:75], v[156:159], v[140:143], v[72:75]
	v_mfma_f32_16x16x32_f16 v[76:79], v[160:163], v[140:143], v[76:79]
	s_add_u32 m0, s28, 0x16000
	s_nop 0
	global_load_lds_dwordx4 v10, s[6:7]
	v_mfma_f32_16x16x32_f16 v[80:83], v[164:167], v[140:143], v[80:83]
	v_mfma_f32_16x16x32_f16 v[84:87], v[168:171], v[140:143], v[84:87]
	s_waitcnt lgkmcnt(9)
	v_mfma_f32_16x16x32_f16 v[88:91], v[156:159], v[144:147], v[88:91]
	v_mfma_f32_16x16x32_f16 v[92:95], v[160:163], v[144:147], v[92:95]
	v_mfma_f32_16x16x32_f16 v[96:99], v[164:167], v[144:147], v[96:99]
	s_add_u32 m0, s28, 0x18000
	s_nop 0
	global_load_lds_dwordx4 v11, s[6:7]
	s_add_u32 s6, s6, s20
	s_addc_u32 s7, s7, 0
	v_mfma_f32_16x16x32_f16 v[100:103], v[168:171], v[144:147], v[100:103]
	s_waitcnt lgkmcnt(8)
	v_mfma_f32_16x16x32_f16 v[104:107], v[156:159], v[148:151], v[104:107]
	v_mfma_f32_16x16x32_f16 v[108:111], v[160:163], v[148:151], v[108:111]
	v_mfma_f32_16x16x32_f16 v[112:115], v[164:167], v[148:151], v[112:115]
	v_mfma_f32_16x16x32_f16 v[116:119], v[168:171], v[148:151], v[116:119]
	s_waitcnt vmcnt(6) lgkmcnt(0)
	s_barrier
	s_waitcnt lgkmcnt(7)
	ds_read_b128 v[136:139], v15
	ds_read_b128 v[156:159], v17
	ds_read_b128 v[160:163], v17 offset:2048
	ds_read_b128 v[164:167], v17 offset:4096
	ds_read_b128 v[168:171], v17 offset:6144
	ds_read_b128 v[140:143], v15 offset:2048
	ds_read_b128 v[144:147], v15 offset:4096
	ds_read_b128 v[148:151], v15 offset:6144
	s_waitcnt lgkmcnt(14)
	v_mfma_f32_16x16x32_f16 v[56:59], v[192:195], v[172:175], v[56:59]
	s_add_u32 m0, s28, 0x1a000
	s_nop 0
	global_load_lds_dwordx4 v10, s[4:5]
	s_waitcnt lgkmcnt(13)
	v_mfma_f32_16x16x32_f16 v[60:63], v[196:199], v[172:175], v[60:63]
	s_waitcnt lgkmcnt(12)
	v_mfma_f32_16x16x32_f16 v[64:67], v[200:203], v[172:175], v[64:67]
	s_waitcnt lgkmcnt(11)
	v_mfma_f32_16x16x32_f16 v[68:71], v[204:207], v[172:175], v[68:71]
	s_waitcnt lgkmcnt(10)
	v_mfma_f32_16x16x32_f16 v[72:75], v[192:195], v[176:179], v[72:75]
	v_mfma_f32_16x16x32_f16 v[76:79], v[196:199], v[176:179], v[76:79]
	s_add_u32 m0, s28, 0x1c000
	s_nop 0
	global_load_lds_dwordx4 v11, s[4:5]
	v_mfma_f32_16x16x32_f16 v[80:83], v[200:203], v[176:179], v[80:83]
	v_mfma_f32_16x16x32_f16 v[84:87], v[204:207], v[176:179], v[84:87]
	s_waitcnt lgkmcnt(9)
	v_mfma_f32_16x16x32_f16 v[88:91], v[192:195], v[180:183], v[88:91]
	v_mfma_f32_16x16x32_f16 v[92:95], v[196:199], v[180:183], v[92:95]
	v_mfma_f32_16x16x32_f16 v[96:99], v[200:203], v[180:183], v[96:99]
	s_add_u32 m0, s28, 0x1e000
	s_nop 0
	global_load_lds_dwordx4 v12, s[4:5]
	v_mfma_f32_16x16x32_f16 v[100:103], v[204:207], v[180:183], v[100:103]
	s_waitcnt lgkmcnt(8)
	v_mfma_f32_16x16x32_f16 v[104:107], v[192:195], v[184:187], v[104:107]
	v_mfma_f32_16x16x32_f16 v[108:111], v[196:199], v[184:187], v[108:111]
	v_mfma_f32_16x16x32_f16 v[112:115], v[200:203], v[184:187], v[112:115]
	v_mfma_f32_16x16x32_f16 v[116:119], v[204:207], v[184:187], v[116:119]
	s_waitcnt lgkmcnt(7)
	ds_read_b128 v[172:175], v16
	ds_read_b128 v[192:195], v18
	ds_read_b128 v[196:199], v18 offset:2048
	ds_read_b128 v[200:203], v18 offset:4096
	ds_read_b128 v[204:207], v18 offset:6144
	ds_read_b128 v[176:179], v16 offset:2048
	ds_read_b128 v[180:183], v16 offset:4096
	ds_read_b128 v[184:187], v16 offset:6144
	s_waitcnt lgkmcnt(14)
	v_mfma_f32_16x16x32_f16 v[56:59], v[156:159], v[136:139], v[56:59]
	s_add_u32 m0, s28, 0x20000
	s_nop 0
	global_load_lds_dwordx4 v13, s[4:5]
	s_add_u32 s4, s4, s20
	s_addc_u32 s5, s5, 0
	s_waitcnt lgkmcnt(13)
	v_mfma_f32_16x16x32_f16 v[60:63], v[160:163], v[136:139], v[60:63]
	s_waitcnt lgkmcnt(12)
	v_mfma_f32_16x16x32_f16 v[64:67], v[164:167], v[136:139], v[64:67]
	s_waitcnt lgkmcnt(11)
	v_mfma_f32_16x16x32_f16 v[68:71], v[168:171], v[136:139], v[68:71]
	s_waitcnt lgkmcnt(10)
	v_mfma_f32_16x16x32_f16 v[72:75], v[156:159], v[140:143], v[72:75]
	v_mfma_f32_16x16x32_f16 v[76:79], v[160:163], v[140:143], v[76:79]
	s_add_u32 m0, s28, 0x23000
	s_nop 0
	global_load_lds_dwordx4 v10, s[6:7]
	v_mfma_f32_16x16x32_f16 v[80:83], v[164:167], v[140:143], v[80:83]
	v_mfma_f32_16x16x32_f16 v[84:87], v[168:171], v[140:143], v[84:87]
	s_waitcnt lgkmcnt(9)
	v_mfma_f32_16x16x32_f16 v[88:91], v[156:159], v[144:147], v[88:91]
	v_mfma_f32_16x16x32_f16 v[92:95], v[160:163], v[144:147], v[92:95]
	v_mfma_f32_16x16x32_f16 v[96:99], v[164:167], v[144:147], v[96:99]
	s_add_u32 m0, s28, 0x25000
	s_nop 0
	global_load_lds_dwordx4 v11, s[6:7]
	s_add_u32 s6, s6, s20
	s_addc_u32 s7, s7, 0
	v_mfma_f32_16x16x32_f16 v[100:103], v[168:171], v[144:147], v[100:103]
	s_waitcnt lgkmcnt(8)
	v_mfma_f32_16x16x32_f16 v[104:107], v[156:159], v[148:151], v[104:107]
	v_mfma_f32_16x16x32_f16 v[108:111], v[160:163], v[148:151], v[108:111]
	v_mfma_f32_16x16x32_f16 v[112:115], v[164:167], v[148:151], v[112:115]
	v_mfma_f32_16x16x32_f16 v[116:119], v[168:171], v[148:151], v[116:119]
	s_waitcnt vmcnt(6) lgkmcnt(0)
	s_barrier
	s_waitcnt lgkmcnt(7)
	ds_read_b128 v[136:139], v15 offset:53248
	ds_read_b128 v[156:159], v17 offset:53248
	ds_read_b128 v[160:163], v17 offset:55296
	ds_read_b128 v[164:167], v17 offset:57344
	ds_read_b128 v[168:171], v17 offset:59392
	ds_read_b128 v[140:143], v15 offset:55296
	ds_read_b128 v[144:147], v15 offset:57344
	ds_read_b128 v[148:151], v15 offset:59392
	s_waitcnt lgkmcnt(14)
	v_mfma_f32_16x16x32_f16 v[56:59], v[192:195], v[172:175], v[56:59]
	s_add_u32 m0, s28, 0x0
	s_nop 0
	global_load_lds_dwordx4 v10, s[4:5]
	s_waitcnt lgkmcnt(13)
	v_mfma_f32_16x16x32_f16 v[60:63], v[196:199], v[172:175], v[60:63]
	s_waitcnt lgkmcnt(12)
	v_mfma_f32_16x16x32_f16 v[64:67], v[200:203], v[172:175], v[64:67]
	s_waitcnt lgkmcnt(11)
	v_mfma_f32_16x16x32_f16 v[68:71], v[204:207], v[172:175], v[68:71]
	s_waitcnt lgkmcnt(10)
	v_mfma_f32_16x16x32_f16 v[72:75], v[192:195], v[176:179], v[72:75]
	v_mfma_f32_16x16x32_f16 v[76:79], v[196:199], v[176:179], v[76:79]
	s_add_u32 m0, s28, 0x2000
	s_nop 0
	global_load_lds_dwordx4 v11, s[4:5]
	v_mfma_f32_16x16x32_f16 v[80:83], v[200:203], v[176:179], v[80:83]
	v_mfma_f32_16x16x32_f16 v[84:87], v[204:207], v[176:179], v[84:87]
	s_waitcnt lgkmcnt(9)
	v_mfma_f32_16x16x32_f16 v[88:91], v[192:195], v[180:183], v[88:91]
	v_mfma_f32_16x16x32_f16 v[92:95], v[196:199], v[180:183], v[92:95]
	v_mfma_f32_16x16x32_f16 v[96:99], v[200:203], v[180:183], v[96:99]
	s_add_u32 m0, s28, 0x4000
	s_nop 0
	global_load_lds_dwordx4 v12, s[4:5]
	v_mfma_f32_16x16x32_f16 v[100:103], v[204:207], v[180:183], v[100:103]
	s_waitcnt lgkmcnt(8)
	v_mfma_f32_16x16x32_f16 v[104:107], v[192:195], v[184:187], v[104:107]
	v_mfma_f32_16x16x32_f16 v[108:111], v[196:199], v[184:187], v[108:111]
	v_mfma_f32_16x16x32_f16 v[112:115], v[200:203], v[184:187], v[112:115]
	v_mfma_f32_16x16x32_f16 v[116:119], v[204:207], v[184:187], v[116:119]
	s_waitcnt lgkmcnt(7)
	ds_read_b128 v[172:175], v16 offset:53248
	ds_read_b128 v[192:195], v18 offset:53248
	ds_read_b128 v[196:199], v18 offset:55296
	ds_read_b128 v[200:203], v18 offset:57344
	ds_read_b128 v[204:207], v18 offset:59392
	ds_read_b128 v[176:179], v16 offset:55296
	ds_read_b128 v[180:183], v16 offset:57344
	ds_read_b128 v[184:187], v16 offset:59392
	s_waitcnt lgkmcnt(14)
	v_mfma_f32_16x16x32_f16 v[56:59], v[156:159], v[136:139], v[56:59]
	s_add_u32 m0, s28, 0x6000
	s_nop 0
	global_load_lds_dwordx4 v13, s[4:5]
	s_add_u32 s4, s4, s20
	s_addc_u32 s5, s5, 0
	s_waitcnt lgkmcnt(13)
	v_mfma_f32_16x16x32_f16 v[60:63], v[160:163], v[136:139], v[60:63]
	s_waitcnt lgkmcnt(12)
	v_mfma_f32_16x16x32_f16 v[64:67], v[164:167], v[136:139], v[64:67]
	s_waitcnt lgkmcnt(11)
	v_mfma_f32_16x16x32_f16 v[68:71], v[168:171], v[136:139], v[68:71]
	s_waitcnt lgkmcnt(10)
	v_mfma_f32_16x16x32_f16 v[72:75], v[156:159], v[140:143], v[72:75]
	v_mfma_f32_16x16x32_f16 v[76:79], v[160:163], v[140:143], v[76:79]
	s_add_u32 m0, s28, 0x9000
	s_nop 0
	global_load_lds_dwordx4 v10, s[6:7]
	v_mfma_f32_16x16x32_f16 v[80:83], v[164:167], v[140:143], v[80:83]
	v_mfma_f32_16x16x32_f16 v[84:87], v[168:171], v[140:143], v[84:87]
	s_waitcnt lgkmcnt(9)
	v_mfma_f32_16x16x32_f16 v[88:91], v[156:159], v[144:147], v[88:91]
	v_mfma_f32_16x16x32_f16 v[92:95], v[160:163], v[144:147], v[92:95]
	v_mfma_f32_16x16x32_f16 v[96:99], v[164:167], v[144:147], v[96:99]
	s_add_u32 m0, s28, 0xb000
	s_nop 0
	global_load_lds_dwordx4 v11, s[6:7]
	s_add_u32 s6, s6, s20
	s_addc_u32 s7, s7, 0
	v_mfma_f32_16x16x32_f16 v[100:103], v[168:171], v[144:147], v[100:103]
	s_waitcnt lgkmcnt(8)
	v_mfma_f32_16x16x32_f16 v[104:107], v[156:159], v[148:151], v[104:107]
	v_mfma_f32_16x16x32_f16 v[108:111], v[160:163], v[148:151], v[108:111]
	v_mfma_f32_16x16x32_f16 v[112:115], v[164:167], v[148:151], v[112:115]
	v_mfma_f32_16x16x32_f16 v[116:119], v[168:171], v[148:151], v[116:119]
	s_waitcnt vmcnt(6) lgkmcnt(0)
	s_barrier
	s_waitcnt lgkmcnt(7)
	ds_read_b128 v[136:139], v19
	ds_read_b128 v[156:159], v21
	ds_read_b128 v[160:163], v21 offset:2048
	ds_read_b128 v[164:167], v21 offset:4096
	ds_read_b128 v[168:171], v21 offset:6144
	ds_read_b128 v[140:143], v19 offset:2048
	ds_read_b128 v[144:147], v19 offset:4096
	ds_read_b128 v[148:151], v19 offset:6144
	s_waitcnt lgkmcnt(14)
	v_mfma_f32_16x16x32_f16 v[56:59], v[192:195], v[172:175], v[56:59]
	s_add_u32 m0, s28, 0xd000
	s_nop 0
	global_load_lds_dwordx4 v10, s[4:5]
	s_waitcnt lgkmcnt(13)
	v_mfma_f32_16x16x32_f16 v[60:63], v[196:199], v[172:175], v[60:63]
	s_waitcnt lgkmcnt(12)
	v_mfma_f32_16x16x32_f16 v[64:67], v[200:203], v[172:175], v[64:67]
	s_waitcnt lgkmcnt(11)
	v_mfma_f32_16x16x32_f16 v[68:71], v[204:207], v[172:175], v[68:71]
	s_waitcnt lgkmcnt(10)
	v_mfma_f32_16x16x32_f16 v[72:75], v[192:195], v[176:179], v[72:75]
	v_mfma_f32_16x16x32_f16 v[76:79], v[196:199], v[176:179], v[76:79]
	s_add_u32 m0, s28, 0xf000
	s_nop 0
	global_load_lds_dwordx4 v11, s[4:5]
	v_mfma_f32_16x16x32_f16 v[80:83], v[200:203], v[176:179], v[80:83]
	v_mfma_f32_16x16x32_f16 v[84:87], v[204:207], v[176:179], v[84:87]
	s_waitcnt lgkmcnt(9)
	v_mfma_f32_16x16x32_f16 v[88:91], v[192:195], v[180:183], v[88:91]
	v_mfma_f32_16x16x32_f16 v[92:95], v[196:199], v[180:183], v[92:95]
	v_mfma_f32_16x16x32_f16 v[96:99], v[200:203], v[180:183], v[96:99]
	s_add_u32 m0, s28, 0x11000
	s_nop 0
	global_load_lds_dwordx4 v12, s[4:5]
	v_mfma_f32_16x16x32_f16 v[100:103], v[204:207], v[180:183], v[100:103]
	s_waitcnt lgkmcnt(8)
	v_mfma_f32_16x16x32_f16 v[104:107], v[192:195], v[184:187], v[104:107]
	v_mfma_f32_16x16x32_f16 v[108:111], v[196:199], v[184:187], v[108:111]
	v_mfma_f32_16x16x32_f16 v[112:115], v[200:203], v[184:187], v[112:115]
	v_mfma_f32_16x16x32_f16 v[116:119], v[204:207], v[184:187], v[116:119]
	s_waitcnt lgkmcnt(7)
	ds_read_b128 v[172:175], v20
	ds_read_b128 v[192:195], v22
	ds_read_b128 v[196:199], v22 offset:2048
	ds_read_b128 v[200:203], v22 offset:4096
	ds_read_b128 v[204:207], v22 offset:6144
	ds_read_b128 v[176:179], v20 offset:2048
	ds_read_b128 v[180:183], v20 offset:4096
	ds_read_b128 v[184:187], v20 offset:6144
	s_waitcnt lgkmcnt(14)
	v_mfma_f32_16x16x32_f16 v[56:59], v[156:159], v[136:139], v[56:59]
	s_add_u32 m0, s28, 0x13000
	s_nop 0
	global_load_lds_dwordx4 v13, s[4:5]
	s_add_u32 s4, s4, s20
	s_addc_u32 s5, s5, 0
	s_waitcnt lgkmcnt(13)
	v_mfma_f32_16x16x32_f16 v[60:63], v[160:163], v[136:139], v[60:63]
	s_waitcnt lgkmcnt(12)
	v_mfma_f32_16x16x32_f16 v[64:67], v[164:167], v[136:139], v[64:67]
	s_waitcnt lgkmcnt(11)
	v_mfma_f32_16x16x32_f16 v[68:71], v[168:171], v[136:139], v[68:71]
	s_waitcnt lgkmcnt(10)
	v_mfma_f32_16x16x32_f16 v[72:75], v[156:159], v[140:143], v[72:75]
	v_mfma_f32_16x16x32_f16 v[76:79], v[160:163], v[140:143], v[76:79]
	s_add_u32 m0, s28, 0x16000
	s_nop 0
	global_load_lds_dwordx4 v10, s[6:7]
	v_mfma_f32_16x16x32_f16 v[80:83], v[164:167], v[140:143], v[80:83]
	v_mfma_f32_16x16x32_f16 v[84:87], v[168:171], v[140:143], v[84:87]
	s_waitcnt lgkmcnt(9)
	v_mfma_f32_16x16x32_f16 v[88:91], v[156:159], v[144:147], v[88:91]
	v_mfma_f32_16x16x32_f16 v[92:95], v[160:163], v[144:147], v[92:95]
	v_mfma_f32_16x16x32_f16 v[96:99], v[164:167], v[144:147], v[96:99]
	s_add_u32 m0, s28, 0x18000
	s_nop 0
	global_load_lds_dwordx4 v11, s[6:7]
	s_add_u32 s6, s6, s20
	s_addc_u32 s7, s7, 0
	v_mfma_f32_16x16x32_f16 v[100:103], v[168:171], v[144:147], v[100:103]
	s_waitcnt lgkmcnt(8)
	v_mfma_f32_16x16x32_f16 v[104:107], v[156:159], v[148:151], v[104:107]
	v_mfma_f32_16x16x32_f16 v[108:111], v[160:163], v[148:151], v[108:111]
	v_mfma_f32_16x16x32_f16 v[112:115], v[164:167], v[148:151], v[112:115]
	v_mfma_f32_16x16x32_f16 v[116:119], v[168:171], v[148:151], v[116:119]
	s_waitcnt vmcnt(6) lgkmcnt(0)
	s_barrier
	s_waitcnt lgkmcnt(7)
	ds_read_b128 v[136:139], v15
	ds_read_b128 v[156:159], v17
	ds_read_b128 v[160:163], v17 offset:2048
	ds_read_b128 v[164:167], v17 offset:4096
	ds_read_b128 v[168:171], v17 offset:6144
	ds_read_b128 v[140:143], v15 offset:2048
	ds_read_b128 v[144:147], v15 offset:4096
	ds_read_b128 v[148:151], v15 offset:6144
	s_waitcnt lgkmcnt(14)
	v_mfma_f32_16x16x32_f16 v[56:59], v[192:195], v[172:175], v[56:59]
	s_add_u32 m0, s28, 0x1a000
	s_nop 0
	global_load_lds_dwordx4 v10, s[4:5]
	s_waitcnt lgkmcnt(13)
	v_mfma_f32_16x16x32_f16 v[60:63], v[196:199], v[172:175], v[60:63]
	s_waitcnt lgkmcnt(12)
	v_mfma_f32_16x16x32_f16 v[64:67], v[200:203], v[172:175], v[64:67]
	s_waitcnt lgkmcnt(11)
	v_mfma_f32_16x16x32_f16 v[68:71], v[204:207], v[172:175], v[68:71]
	s_waitcnt lgkmcnt(10)
	v_mfma_f32_16x16x32_f16 v[72:75], v[192:195], v[176:179], v[72:75]
	v_mfma_f32_16x16x32_f16 v[76:79], v[196:199], v[176:179], v[76:79]
	s_add_u32 m0, s28, 0x1c000
	s_nop 0
	global_load_lds_dwordx4 v11, s[4:5]
	v_mfma_f32_16x16x32_f16 v[80:83], v[200:203], v[176:179], v[80:83]
	v_mfma_f32_16x16x32_f16 v[84:87], v[204:207], v[176:179], v[84:87]
	s_waitcnt lgkmcnt(9)
	v_mfma_f32_16x16x32_f16 v[88:91], v[192:195], v[180:183], v[88:91]
	v_mfma_f32_16x16x32_f16 v[92:95], v[196:199], v[180:183], v[92:95]
	v_mfma_f32_16x16x32_f16 v[96:99], v[200:203], v[180:183], v[96:99]
	s_add_u32 m0, s28, 0x1e000
	s_nop 0
	global_load_lds_dwordx4 v12, s[4:5]
	v_mfma_f32_16x16x32_f16 v[100:103], v[204:207], v[180:183], v[100:103]
	s_waitcnt lgkmcnt(8)
	v_mfma_f32_16x16x32_f16 v[104:107], v[192:195], v[184:187], v[104:107]
	v_mfma_f32_16x16x32_f16 v[108:111], v[196:199], v[184:187], v[108:111]
	v_mfma_f32_16x16x32_f16 v[112:115], v[200:203], v[184:187], v[112:115]
	v_mfma_f32_16x16x32_f16 v[116:119], v[204:207], v[184:187], v[116:119]
	s_waitcnt lgkmcnt(7)
	ds_read_b128 v[172:175], v16
	ds_read_b128 v[192:195], v18
	ds_read_b128 v[196:199], v18 offset:2048
	ds_read_b128 v[200:203], v18 offset:4096
	ds_read_b128 v[204:207], v18 offset:6144
	ds_read_b128 v[176:179], v16 offset:2048
	ds_read_b128 v[180:183], v16 offset:4096
	ds_read_b128 v[184:187], v16 offset:6144
	s_waitcnt lgkmcnt(14)
	v_mfma_f32_16x16x32_f16 v[56:59], v[156:159], v[136:139], v[56:59]
	s_add_u32 m0, s28, 0x20000
	s_nop 0
	global_load_lds_dwordx4 v13, s[4:5]
	s_add_u32 s4, s4, s20
	s_addc_u32 s5, s5, 0
	s_waitcnt lgkmcnt(13)
	v_mfma_f32_16x16x32_f16 v[60:63], v[160:163], v[136:139], v[60:63]
	s_waitcnt lgkmcnt(12)
	v_mfma_f32_16x16x32_f16 v[64:67], v[164:167], v[136:139], v[64:67]
	s_waitcnt lgkmcnt(11)
	v_mfma_f32_16x16x32_f16 v[68:71], v[168:171], v[136:139], v[68:71]
	s_waitcnt lgkmcnt(10)
	v_mfma_f32_16x16x32_f16 v[72:75], v[156:159], v[140:143], v[72:75]
	v_mfma_f32_16x16x32_f16 v[76:79], v[160:163], v[140:143], v[76:79]
	s_add_u32 m0, s28, 0x23000
	s_nop 0
	global_load_lds_dwordx4 v10, s[6:7]
	v_mfma_f32_16x16x32_f16 v[80:83], v[164:167], v[140:143], v[80:83]
	v_mfma_f32_16x16x32_f16 v[84:87], v[168:171], v[140:143], v[84:87]
	s_waitcnt lgkmcnt(9)
	v_mfma_f32_16x16x32_f16 v[88:91], v[156:159], v[144:147], v[88:91]
	v_mfma_f32_16x16x32_f16 v[92:95], v[160:163], v[144:147], v[92:95]
	v_mfma_f32_16x16x32_f16 v[96:99], v[164:167], v[144:147], v[96:99]
	s_add_u32 m0, s28, 0x25000
	s_nop 0
	global_load_lds_dwordx4 v11, s[6:7]
	s_add_u32 s6, s6, s20
	s_addc_u32 s7, s7, 0
	v_mfma_f32_16x16x32_f16 v[100:103], v[168:171], v[144:147], v[100:103]
	s_waitcnt lgkmcnt(8)
	v_mfma_f32_16x16x32_f16 v[104:107], v[156:159], v[148:151], v[104:107]
	v_mfma_f32_16x16x32_f16 v[108:111], v[160:163], v[148:151], v[108:111]
	v_mfma_f32_16x16x32_f16 v[112:115], v[164:167], v[148:151], v[112:115]
	v_mfma_f32_16x16x32_f16 v[116:119], v[168:171], v[148:151], v[116:119]
	s_waitcnt vmcnt(6) lgkmcnt(0)
	s_barrier
	s_waitcnt lgkmcnt(7)
	ds_read_b128 v[136:139], v15 offset:53248
	ds_read_b128 v[156:159], v17 offset:53248
	ds_read_b128 v[160:163], v17 offset:55296
	ds_read_b128 v[164:167], v17 offset:57344
	ds_read_b128 v[168:171], v17 offset:59392
	ds_read_b128 v[140:143], v15 offset:55296
	ds_read_b128 v[144:147], v15 offset:57344
	ds_read_b128 v[148:151], v15 offset:59392
	s_waitcnt lgkmcnt(14)
	v_mfma_f32_16x16x32_f16 v[56:59], v[192:195], v[172:175], v[56:59]
	s_add_u32 m0, s28, 0x0
	s_nop 0
	global_load_lds_dwordx4 v10, s[4:5]
	s_waitcnt lgkmcnt(13)
	v_mfma_f32_16x16x32_f16 v[60:63], v[196:199], v[172:175], v[60:63]
	s_waitcnt lgkmcnt(12)
	v_mfma_f32_16x16x32_f16 v[64:67], v[200:203], v[172:175], v[64:67]
	s_waitcnt lgkmcnt(11)
	v_mfma_f32_16x16x32_f16 v[68:71], v[204:207], v[172:175], v[68:71]
	s_waitcnt lgkmcnt(10)
	v_mfma_f32_16x16x32_f16 v[72:75], v[192:195], v[176:179], v[72:75]
	v_mfma_f32_16x16x32_f16 v[76:79], v[196:199], v[176:179], v[76:79]
	s_add_u32 m0, s28, 0x2000
	s_nop 0
	global_load_lds_dwordx4 v11, s[4:5]
	v_mfma_f32_16x16x32_f16 v[80:83], v[200:203], v[176:179], v[80:83]
	v_mfma_f32_16x16x32_f16 v[84:87], v[204:207], v[176:179], v[84:87]
	s_waitcnt lgkmcnt(9)
	v_mfma_f32_16x16x32_f16 v[88:91], v[192:195], v[180:183], v[88:91]
	v_mfma_f32_16x16x32_f16 v[92:95], v[196:199], v[180:183], v[92:95]
	v_mfma_f32_16x16x32_f16 v[96:99], v[200:203], v[180:183], v[96:99]
	s_add_u32 m0, s28, 0x4000
	s_nop 0
	global_load_lds_dwordx4 v12, s[4:5]
	v_mfma_f32_16x16x32_f16 v[100:103], v[204:207], v[180:183], v[100:103]
	s_waitcnt lgkmcnt(8)
	v_mfma_f32_16x16x32_f16 v[104:107], v[192:195], v[184:187], v[104:107]
	v_mfma_f32_16x16x32_f16 v[108:111], v[196:199], v[184:187], v[108:111]
	v_mfma_f32_16x16x32_f16 v[112:115], v[200:203], v[184:187], v[112:115]
	v_mfma_f32_16x16x32_f16 v[116:119], v[204:207], v[184:187], v[116:119]
	s_waitcnt lgkmcnt(7)
	ds_read_b128 v[172:175], v16 offset:53248
	ds_read_b128 v[192:195], v18 offset:53248
	ds_read_b128 v[196:199], v18 offset:55296
	ds_read_b128 v[200:203], v18 offset:57344
	ds_read_b128 v[204:207], v18 offset:59392
	ds_read_b128 v[176:179], v16 offset:55296
	ds_read_b128 v[180:183], v16 offset:57344
	ds_read_b128 v[184:187], v16 offset:59392
	s_waitcnt lgkmcnt(14)
	v_mfma_f32_16x16x32_f16 v[56:59], v[156:159], v[136:139], v[56:59]
	s_add_u32 m0, s28, 0x6000
	s_nop 0
	global_load_lds_dwordx4 v13, s[4:5]
	s_add_u32 s4, s4, s20
	s_addc_u32 s5, s5, 0
	s_waitcnt lgkmcnt(13)
	v_mfma_f32_16x16x32_f16 v[60:63], v[160:163], v[136:139], v[60:63]
	s_waitcnt lgkmcnt(12)
	v_mfma_f32_16x16x32_f16 v[64:67], v[164:167], v[136:139], v[64:67]
	s_waitcnt lgkmcnt(11)
	v_mfma_f32_16x16x32_f16 v[68:71], v[168:171], v[136:139], v[68:71]
	s_waitcnt lgkmcnt(10)
	v_mfma_f32_16x16x32_f16 v[72:75], v[156:159], v[140:143], v[72:75]
	v_mfma_f32_16x16x32_f16 v[76:79], v[160:163], v[140:143], v[76:79]
	s_add_u32 m0, s28, 0x9000
	s_nop 0
	global_load_lds_dwordx4 v10, s[6:7]
	v_mfma_f32_16x16x32_f16 v[80:83], v[164:167], v[140:143], v[80:83]
	v_mfma_f32_16x16x32_f16 v[84:87], v[168:171], v[140:143], v[84:87]
	s_waitcnt lgkmcnt(9)
	v_mfma_f32_16x16x32_f16 v[88:91], v[156:159], v[144:147], v[88:91]
	v_mfma_f32_16x16x32_f16 v[92:95], v[160:163], v[144:147], v[92:95]
	v_mfma_f32_16x16x32_f16 v[96:99], v[164:167], v[144:147], v[96:99]
	s_add_u32 m0, s28, 0xb000
	s_nop 0
	global_load_lds_dwordx4 v11, s[6:7]
	s_add_u32 s6, s6, s20
	s_addc_u32 s7, s7, 0
	v_mfma_f32_16x16x32_f16 v[100:103], v[168:171], v[144:147], v[100:103]
	s_waitcnt lgkmcnt(8)
	v_mfma_f32_16x16x32_f16 v[104:107], v[156:159], v[148:151], v[104:107]
	v_mfma_f32_16x16x32_f16 v[108:111], v[160:163], v[148:151], v[108:111]
	v_mfma_f32_16x16x32_f16 v[112:115], v[164:167], v[148:151], v[112:115]
	v_mfma_f32_16x16x32_f16 v[116:119], v[168:171], v[148:151], v[116:119]
	s_waitcnt vmcnt(6) lgkmcnt(0)
	s_barrier
	s_waitcnt lgkmcnt(7)
	ds_read_b128 v[136:139], v19
	ds_read_b128 v[156:159], v21
	ds_read_b128 v[160:163], v21 offset:2048
	ds_read_b128 v[164:167], v21 offset:4096
	ds_read_b128 v[168:171], v21 offset:6144
	ds_read_b128 v[140:143], v19 offset:2048
	ds_read_b128 v[144:147], v19 offset:4096
	ds_read_b128 v[148:151], v19 offset:6144
	s_waitcnt lgkmcnt(14)
	v_mfma_f32_16x16x32_f16 v[56:59], v[192:195], v[172:175], v[56:59]
	s_add_u32 m0, s28, 0xd000
	s_nop 0
	global_load_lds_dwordx4 v10, s[4:5]
	s_waitcnt lgkmcnt(13)
	v_mfma_f32_16x16x32_f16 v[60:63], v[196:199], v[172:175], v[60:63]
	s_waitcnt lgkmcnt(12)
	v_mfma_f32_16x16x32_f16 v[64:67], v[200:203], v[172:175], v[64:67]
	s_waitcnt lgkmcnt(11)
	v_mfma_f32_16x16x32_f16 v[68:71], v[204:207], v[172:175], v[68:71]
	s_waitcnt lgkmcnt(10)
	v_mfma_f32_16x16x32_f16 v[72:75], v[192:195], v[176:179], v[72:75]
	v_mfma_f32_16x16x32_f16 v[76:79], v[196:199], v[176:179], v[76:79]
	s_add_u32 m0, s28, 0xf000
	s_nop 0
	global_load_lds_dwordx4 v11, s[4:5]
	v_mfma_f32_16x16x32_f16 v[80:83], v[200:203], v[176:179], v[80:83]
	v_mfma_f32_16x16x32_f16 v[84:87], v[204:207], v[176:179], v[84:87]
	s_waitcnt lgkmcnt(9)
	v_mfma_f32_16x16x32_f16 v[88:91], v[192:195], v[180:183], v[88:91]
	v_mfma_f32_16x16x32_f16 v[92:95], v[196:199], v[180:183], v[92:95]
	v_mfma_f32_16x16x32_f16 v[96:99], v[200:203], v[180:183], v[96:99]
	s_add_u32 m0, s28, 0x11000
	s_nop 0
	global_load_lds_dwordx4 v12, s[4:5]
	v_mfma_f32_16x16x32_f16 v[100:103], v[204:207], v[180:183], v[100:103]
	s_waitcnt lgkmcnt(8)
	v_mfma_f32_16x16x32_f16 v[104:107], v[192:195], v[184:187], v[104:107]
	v_mfma_f32_16x16x32_f16 v[108:111], v[196:199], v[184:187], v[108:111]
	v_mfma_f32_16x16x32_f16 v[112:115], v[200:203], v[184:187], v[112:115]
	v_mfma_f32_16x16x32_f16 v[116:119], v[204:207], v[184:187], v[116:119]
	s_waitcnt lgkmcnt(7)
	ds_read_b128 v[172:175], v20
	ds_read_b128 v[192:195], v22
	ds_read_b128 v[196:199], v22 offset:2048
	ds_read_b128 v[200:203], v22 offset:4096
	ds_read_b128 v[204:207], v22 offset:6144
	ds_read_b128 v[176:179], v20 offset:2048
	ds_read_b128 v[180:183], v20 offset:4096
	ds_read_b128 v[184:187], v20 offset:6144
	s_waitcnt lgkmcnt(14)
	v_mfma_f32_16x16x32_f16 v[56:59], v[156:159], v[136:139], v[56:59]
	s_add_u32 m0, s28, 0x13000
	s_nop 0
	global_load_lds_dwordx4 v13, s[4:5]
	s_add_u32 s4, s4, s20
	s_addc_u32 s5, s5, 0
	s_waitcnt lgkmcnt(13)
	v_mfma_f32_16x16x32_f16 v[60:63], v[160:163], v[136:139], v[60:63]
	s_waitcnt lgkmcnt(12)
	v_mfma_f32_16x16x32_f16 v[64:67], v[164:167], v[136:139], v[64:67]
	s_waitcnt lgkmcnt(11)
	v_mfma_f32_16x16x32_f16 v[68:71], v[168:171], v[136:139], v[68:71]
	s_waitcnt lgkmcnt(10)
	v_mfma_f32_16x16x32_f16 v[72:75], v[156:159], v[140:143], v[72:75]
	v_mfma_f32_16x16x32_f16 v[76:79], v[160:163], v[140:143], v[76:79]
	s_add_u32 m0, s28, 0x16000
	s_nop 0
	global_load_lds_dwordx4 v10, s[6:7]
	v_mfma_f32_16x16x32_f16 v[80:83], v[164:167], v[140:143], v[80:83]
	v_mfma_f32_16x16x32_f16 v[84:87], v[168:171], v[140:143], v[84:87]
	s_waitcnt lgkmcnt(9)
	v_mfma_f32_16x16x32_f16 v[88:91], v[156:159], v[144:147], v[88:91]
	v_mfma_f32_16x16x32_f16 v[92:95], v[160:163], v[144:147], v[92:95]
	v_mfma_f32_16x16x32_f16 v[96:99], v[164:167], v[144:147], v[96:99]
	s_add_u32 m0, s28, 0x18000
	s_nop 0
	global_load_lds_dwordx4 v11, s[6:7]
	s_add_u32 s6, s6, s20
	s_addc_u32 s7, s7, 0
	v_mfma_f32_16x16x32_f16 v[100:103], v[168:171], v[144:147], v[100:103]
	s_waitcnt lgkmcnt(8)
	v_mfma_f32_16x16x32_f16 v[104:107], v[156:159], v[148:151], v[104:107]
	v_mfma_f32_16x16x32_f16 v[108:111], v[160:163], v[148:151], v[108:111]
	v_mfma_f32_16x16x32_f16 v[112:115], v[164:167], v[148:151], v[112:115]
	v_mfma_f32_16x16x32_f16 v[116:119], v[168:171], v[148:151], v[116:119]
	s_waitcnt vmcnt(6) lgkmcnt(0)
	s_barrier
	s_waitcnt lgkmcnt(7)
	ds_read_b128 v[136:139], v15
	ds_read_b128 v[156:159], v17
	ds_read_b128 v[160:163], v17 offset:2048
	ds_read_b128 v[164:167], v17 offset:4096
	ds_read_b128 v[168:171], v17 offset:6144
	ds_read_b128 v[140:143], v15 offset:2048
	ds_read_b128 v[144:147], v15 offset:4096
	ds_read_b128 v[148:151], v15 offset:6144
	s_waitcnt lgkmcnt(14)
	v_mfma_f32_16x16x32_f16 v[56:59], v[192:195], v[172:175], v[56:59]
	s_add_u32 m0, s28, 0x1a000
	s_nop 0
	global_load_lds_dwordx4 v10, s[4:5]
	s_waitcnt lgkmcnt(13)
	v_mfma_f32_16x16x32_f16 v[60:63], v[196:199], v[172:175], v[60:63]
	s_waitcnt lgkmcnt(12)
	v_mfma_f32_16x16x32_f16 v[64:67], v[200:203], v[172:175], v[64:67]
	s_waitcnt lgkmcnt(11)
	v_mfma_f32_16x16x32_f16 v[68:71], v[204:207], v[172:175], v[68:71]
	s_waitcnt lgkmcnt(10)
	v_mfma_f32_16x16x32_f16 v[72:75], v[192:195], v[176:179], v[72:75]
	v_mfma_f32_16x16x32_f16 v[76:79], v[196:199], v[176:179], v[76:79]
	s_add_u32 m0, s28, 0x1c000
	s_nop 0
	global_load_lds_dwordx4 v11, s[4:5]
	v_mfma_f32_16x16x32_f16 v[80:83], v[200:203], v[176:179], v[80:83]
	v_mfma_f32_16x16x32_f16 v[84:87], v[204:207], v[176:179], v[84:87]
	s_waitcnt lgkmcnt(9)
	v_mfma_f32_16x16x32_f16 v[88:91], v[192:195], v[180:183], v[88:91]
	v_mfma_f32_16x16x32_f16 v[92:95], v[196:199], v[180:183], v[92:95]
	v_mfma_f32_16x16x32_f16 v[96:99], v[200:203], v[180:183], v[96:99]
	s_add_u32 m0, s28, 0x1e000
	s_nop 0
	global_load_lds_dwordx4 v12, s[4:5]
	v_mfma_f32_16x16x32_f16 v[100:103], v[204:207], v[180:183], v[100:103]
	s_waitcnt lgkmcnt(8)
	v_mfma_f32_16x16x32_f16 v[104:107], v[192:195], v[184:187], v[104:107]
	v_mfma_f32_16x16x32_f16 v[108:111], v[196:199], v[184:187], v[108:111]
	v_mfma_f32_16x16x32_f16 v[112:115], v[200:203], v[184:187], v[112:115]
	v_mfma_f32_16x16x32_f16 v[116:119], v[204:207], v[184:187], v[116:119]
	s_waitcnt lgkmcnt(7)
	ds_read_b128 v[172:175], v16
	ds_read_b128 v[192:195], v18
	ds_read_b128 v[196:199], v18 offset:2048
	ds_read_b128 v[200:203], v18 offset:4096
	ds_read_b128 v[204:207], v18 offset:6144
	ds_read_b128 v[176:179], v16 offset:2048
	ds_read_b128 v[180:183], v16 offset:4096
	ds_read_b128 v[184:187], v16 offset:6144
	s_waitcnt lgkmcnt(14)
	v_mfma_f32_16x16x32_f16 v[56:59], v[156:159], v[136:139], v[56:59]
	s_add_u32 m0, s28, 0x20000
	s_nop 0
	global_load_lds_dwordx4 v13, s[4:5]
	s_add_u32 s4, s4, s20
	s_addc_u32 s5, s5, 0
	s_waitcnt lgkmcnt(13)
	v_mfma_f32_16x16x32_f16 v[60:63], v[160:163], v[136:139], v[60:63]
	s_waitcnt lgkmcnt(12)
	v_mfma_f32_16x16x32_f16 v[64:67], v[164:167], v[136:139], v[64:67]
	s_waitcnt lgkmcnt(11)
	v_mfma_f32_16x16x32_f16 v[68:71], v[168:171], v[136:139], v[68:71]
	s_waitcnt lgkmcnt(10)
	v_mfma_f32_16x16x32_f16 v[72:75], v[156:159], v[140:143], v[72:75]
	v_mfma_f32_16x16x32_f16 v[76:79], v[160:163], v[140:143], v[76:79]
	s_add_u32 m0, s28, 0x23000
	s_nop 0
	global_load_lds_dwordx4 v10, s[6:7]
	v_mfma_f32_16x16x32_f16 v[80:83], v[164:167], v[140:143], v[80:83]
	v_mfma_f32_16x16x32_f16 v[84:87], v[168:171], v[140:143], v[84:87]
	s_waitcnt lgkmcnt(9)
	v_mfma_f32_16x16x32_f16 v[88:91], v[156:159], v[144:147], v[88:91]
	v_mfma_f32_16x16x32_f16 v[92:95], v[160:163], v[144:147], v[92:95]
	v_mfma_f32_16x16x32_f16 v[96:99], v[164:167], v[144:147], v[96:99]
	s_add_u32 m0, s28, 0x25000
	s_nop 0
	global_load_lds_dwordx4 v11, s[6:7]
	s_add_u32 s6, s6, s20
	s_addc_u32 s7, s7, 0
	v_mfma_f32_16x16x32_f16 v[100:103], v[168:171], v[144:147], v[100:103]
	s_waitcnt lgkmcnt(8)
	v_mfma_f32_16x16x32_f16 v[104:107], v[156:159], v[148:151], v[104:107]
	v_mfma_f32_16x16x32_f16 v[108:111], v[160:163], v[148:151], v[108:111]
	v_mfma_f32_16x16x32_f16 v[112:115], v[164:167], v[148:151], v[112:115]
	v_mfma_f32_16x16x32_f16 v[116:119], v[168:171], v[148:151], v[116:119]
	s_waitcnt vmcnt(6) lgkmcnt(0)
	s_barrier
	s_waitcnt lgkmcnt(7)
	ds_read_b128 v[136:139], v15 offset:53248
	ds_read_b128 v[156:159], v17 offset:53248
	ds_read_b128 v[160:163], v17 offset:55296
	ds_read_b128 v[164:167], v17 offset:57344
	ds_read_b128 v[168:171], v17 offset:59392
	ds_read_b128 v[140:143], v15 offset:55296
	ds_read_b128 v[144:147], v15 offset:57344
	ds_read_b128 v[148:151], v15 offset:59392
	s_waitcnt lgkmcnt(14)
	v_mfma_f32_16x16x32_f16 v[56:59], v[192:195], v[172:175], v[56:59]
	s_add_u32 m0, s28, 0x0
	s_nop 0
	global_load_lds_dwordx4 v10, s[4:5]
	s_waitcnt lgkmcnt(13)
	v_mfma_f32_16x16x32_f16 v[60:63], v[196:199], v[172:175], v[60:63]
	s_waitcnt lgkmcnt(12)
	v_mfma_f32_16x16x32_f16 v[64:67], v[200:203], v[172:175], v[64:67]
	s_waitcnt lgkmcnt(11)
	v_mfma_f32_16x16x32_f16 v[68:71], v[204:207], v[172:175], v[68:71]
	s_waitcnt lgkmcnt(10)
	v_mfma_f32_16x16x32_f16 v[72:75], v[192:195], v[176:179], v[72:75]
	v_mfma_f32_16x16x32_f16 v[76:79], v[196:199], v[176:179], v[76:79]
	s_add_u32 m0, s28, 0x2000
	s_nop 0
	global_load_lds_dwordx4 v11, s[4:5]
	v_mfma_f32_16x16x32_f16 v[80:83], v[200:203], v[176:179], v[80:83]
	v_mfma_f32_16x16x32_f16 v[84:87], v[204:207], v[176:179], v[84:87]
	s_waitcnt lgkmcnt(9)
	v_mfma_f32_16x16x32_f16 v[88:91], v[192:195], v[180:183], v[88:91]
	v_mfma_f32_16x16x32_f16 v[92:95], v[196:199], v[180:183], v[92:95]
	v_mfma_f32_16x16x32_f16 v[96:99], v[200:203], v[180:183], v[96:99]
	s_add_u32 m0, s28, 0x4000
	s_nop 0
	global_load_lds_dwordx4 v12, s[4:5]
	v_mfma_f32_16x16x32_f16 v[100:103], v[204:207], v[180:183], v[100:103]
	s_waitcnt lgkmcnt(8)
	v_mfma_f32_16x16x32_f16 v[104:107], v[192:195], v[184:187], v[104:107]
	v_mfma_f32_16x16x32_f16 v[108:111], v[196:199], v[184:187], v[108:111]
	v_mfma_f32_16x16x32_f16 v[112:115], v[200:203], v[184:187], v[112:115]
	v_mfma_f32_16x16x32_f16 v[116:119], v[204:207], v[184:187], v[116:119]
	s_waitcnt lgkmcnt(7)
	ds_read_b128 v[172:175], v16 offset:53248
	ds_read_b128 v[192:195], v18 offset:53248
	ds_read_b128 v[196:199], v18 offset:55296
	ds_read_b128 v[200:203], v18 offset:57344
	ds_read_b128 v[204:207], v18 offset:59392
	ds_read_b128 v[176:179], v16 offset:55296
	ds_read_b128 v[180:183], v16 offset:57344
	ds_read_b128 v[184:187], v16 offset:59392
	s_waitcnt lgkmcnt(14)
	v_mfma_f32_16x16x32_f16 v[56:59], v[156:159], v[136:139], v[56:59]
	s_add_u32 m0, s28, 0x6000
	s_nop 0
	global_load_lds_dwordx4 v13, s[4:5]
	s_add_u32 s4, s4, s20
	s_addc_u32 s5, s5, 0
	s_waitcnt lgkmcnt(13)
	v_mfma_f32_16x16x32_f16 v[60:63], v[160:163], v[136:139], v[60:63]
	s_waitcnt lgkmcnt(12)
	v_mfma_f32_16x16x32_f16 v[64:67], v[164:167], v[136:139], v[64:67]
	s_waitcnt lgkmcnt(11)
	v_mfma_f32_16x16x32_f16 v[68:71], v[168:171], v[136:139], v[68:71]
	s_waitcnt lgkmcnt(10)
	v_mfma_f32_16x16x32_f16 v[72:75], v[156:159], v[140:143], v[72:75]
	v_mfma_f32_16x16x32_f16 v[76:79], v[160:163], v[140:143], v[76:79]
	s_add_u32 m0, s28, 0x9000
	s_nop 0
	global_load_lds_dwordx4 v10, s[6:7]
	v_mfma_f32_16x16x32_f16 v[80:83], v[164:167], v[140:143], v[80:83]
	v_mfma_f32_16x16x32_f16 v[84:87], v[168:171], v[140:143], v[84:87]
	s_waitcnt lgkmcnt(9)
	v_mfma_f32_16x16x32_f16 v[88:91], v[156:159], v[144:147], v[88:91]
	v_mfma_f32_16x16x32_f16 v[92:95], v[160:163], v[144:147], v[92:95]
	v_mfma_f32_16x16x32_f16 v[96:99], v[164:167], v[144:147], v[96:99]
	s_add_u32 m0, s28, 0xb000
	s_nop 0
	global_load_lds_dwordx4 v11, s[6:7]
	s_add_u32 s6, s6, s20
	s_addc_u32 s7, s7, 0
	v_mfma_f32_16x16x32_f16 v[100:103], v[168:171], v[144:147], v[100:103]
	s_waitcnt lgkmcnt(8)
	v_mfma_f32_16x16x32_f16 v[104:107], v[156:159], v[148:151], v[104:107]
	v_mfma_f32_16x16x32_f16 v[108:111], v[160:163], v[148:151], v[108:111]
	v_mfma_f32_16x16x32_f16 v[112:115], v[164:167], v[148:151], v[112:115]
	v_mfma_f32_16x16x32_f16 v[116:119], v[168:171], v[148:151], v[116:119]
	s_waitcnt vmcnt(6) lgkmcnt(0)
	s_barrier
	s_waitcnt lgkmcnt(7)
	ds_read_b128 v[136:139], v19
	ds_read_b128 v[156:159], v21
	ds_read_b128 v[160:163], v21 offset:2048
	ds_read_b128 v[164:167], v21 offset:4096
	ds_read_b128 v[168:171], v21 offset:6144
	ds_read_b128 v[140:143], v19 offset:2048
	ds_read_b128 v[144:147], v19 offset:4096
	ds_read_b128 v[148:151], v19 offset:6144
	s_waitcnt lgkmcnt(14)
	v_mfma_f32_16x16x32_f16 v[56:59], v[192:195], v[172:175], v[56:59]
	s_waitcnt lgkmcnt(13)
	v_mfma_f32_16x16x32_f16 v[60:63], v[196:199], v[172:175], v[60:63]
	s_waitcnt lgkmcnt(12)
	v_mfma_f32_16x16x32_f16 v[64:67], v[200:203], v[172:175], v[64:67]
	s_waitcnt lgkmcnt(11)
	v_mfma_f32_16x16x32_f16 v[68:71], v[204:207], v[172:175], v[68:71]
	s_waitcnt lgkmcnt(10)
	v_mfma_f32_16x16x32_f16 v[72:75], v[192:195], v[176:179], v[72:75]
	v_mfma_f32_16x16x32_f16 v[76:79], v[196:199], v[176:179], v[76:79]
	v_mfma_f32_16x16x32_f16 v[80:83], v[200:203], v[176:179], v[80:83]
	v_mfma_f32_16x16x32_f16 v[84:87], v[204:207], v[176:179], v[84:87]
	s_waitcnt lgkmcnt(9)
	v_mfma_f32_16x16x32_f16 v[88:91], v[192:195], v[180:183], v[88:91]
	v_mfma_f32_16x16x32_f16 v[92:95], v[196:199], v[180:183], v[92:95]
	v_mfma_f32_16x16x32_f16 v[96:99], v[200:203], v[180:183], v[96:99]
	v_mfma_f32_16x16x32_f16 v[100:103], v[204:207], v[180:183], v[100:103]
	s_waitcnt lgkmcnt(8)
	v_mfma_f32_16x16x32_f16 v[104:107], v[192:195], v[184:187], v[104:107]
	v_mfma_f32_16x16x32_f16 v[108:111], v[196:199], v[184:187], v[108:111]
	v_mfma_f32_16x16x32_f16 v[112:115], v[200:203], v[184:187], v[112:115]
	v_mfma_f32_16x16x32_f16 v[116:119], v[204:207], v[184:187], v[116:119]
	s_waitcnt lgkmcnt(7)
	ds_read_b128 v[172:175], v20
	ds_read_b128 v[192:195], v22
	ds_read_b128 v[196:199], v22 offset:2048
	ds_read_b128 v[200:203], v22 offset:4096
	ds_read_b128 v[204:207], v22 offset:6144
	ds_read_b128 v[176:179], v20 offset:2048
	ds_read_b128 v[180:183], v20 offset:4096
	ds_read_b128 v[184:187], v20 offset:6144
	s_waitcnt lgkmcnt(14)
	v_mfma_f32_16x16x32_f16 v[56:59], v[156:159], v[136:139], v[56:59]
	s_waitcnt lgkmcnt(13)
	v_mfma_f32_16x16x32_f16 v[60:63], v[160:163], v[136:139], v[60:63]
	s_waitcnt lgkmcnt(12)
	v_mfma_f32_16x16x32_f16 v[64:67], v[164:167], v[136:139], v[64:67]
	s_waitcnt lgkmcnt(11)
	v_mfma_f32_16x16x32_f16 v[68:71], v[168:171], v[136:139], v[68:71]
	s_waitcnt lgkmcnt(10)
	v_mfma_f32_16x16x32_f16 v[72:75], v[156:159], v[140:143], v[72:75]
	v_mfma_f32_16x16x32_f16 v[76:79], v[160:163], v[140:143], v[76:79]
	v_mfma_f32_16x16x32_f16 v[80:83], v[164:167], v[140:143], v[80:83]
	v_mfma_f32_16x16x32_f16 v[84:87], v[168:171], v[140:143], v[84:87]
	s_waitcnt lgkmcnt(9)
	v_mfma_f32_16x16x32_f16 v[88:91], v[156:159], v[144:147], v[88:91]
	v_mfma_f32_16x16x32_f16 v[92:95], v[160:163], v[144:147], v[92:95]
	v_mfma_f32_16x16x32_f16 v[96:99], v[164:167], v[144:147], v[96:99]
	v_mfma_f32_16x16x32_f16 v[100:103], v[168:171], v[144:147], v[100:103]
	s_waitcnt lgkmcnt(8)
	v_mfma_f32_16x16x32_f16 v[104:107], v[156:159], v[148:151], v[104:107]
	v_mfma_f32_16x16x32_f16 v[108:111], v[160:163], v[148:151], v[108:111]
	v_mfma_f32_16x16x32_f16 v[112:115], v[164:167], v[148:151], v[112:115]
	v_mfma_f32_16x16x32_f16 v[116:119], v[168:171], v[148:151], v[116:119]
	s_waitcnt vmcnt(0) lgkmcnt(0)
	s_barrier
	s_waitcnt lgkmcnt(7)
	ds_read_b128 v[136:139], v15
	ds_read_b128 v[156:159], v17
	ds_read_b128 v[160:163], v17 offset:2048
	ds_read_b128 v[164:167], v17 offset:4096
	ds_read_b128 v[168:171], v17 offset:6144
	ds_read_b128 v[140:143], v15 offset:2048
	ds_read_b128 v[144:147], v15 offset:4096
	ds_read_b128 v[148:151], v15 offset:6144
	s_waitcnt lgkmcnt(14)
	v_mfma_f32_16x16x32_f16 v[56:59], v[192:195], v[172:175], v[56:59]
	s_waitcnt lgkmcnt(13)
	v_mfma_f32_16x16x32_f16 v[60:63], v[196:199], v[172:175], v[60:63]
	s_waitcnt lgkmcnt(12)
	v_mfma_f32_16x16x32_f16 v[64:67], v[200:203], v[172:175], v[64:67]
	s_waitcnt lgkmcnt(11)
	v_mfma_f32_16x16x32_f16 v[68:71], v[204:207], v[172:175], v[68:71]
	s_waitcnt lgkmcnt(10)
	v_mfma_f32_16x16x32_f16 v[72:75], v[192:195], v[176:179], v[72:75]
	v_mfma_f32_16x16x32_f16 v[76:79], v[196:199], v[176:179], v[76:79]
	v_mfma_f32_16x16x32_f16 v[80:83], v[200:203], v[176:179], v[80:83]
	v_mfma_f32_16x16x32_f16 v[84:87], v[204:207], v[176:179], v[84:87]
	s_waitcnt lgkmcnt(9)
	v_mfma_f32_16x16x32_f16 v[88:91], v[192:195], v[180:183], v[88:91]
	v_mfma_f32_16x16x32_f16 v[92:95], v[196:199], v[180:183], v[92:95]
	v_mfma_f32_16x16x32_f16 v[96:99], v[200:203], v[180:183], v[96:99]
	v_mfma_f32_16x16x32_f16 v[100:103], v[204:207], v[180:183], v[100:103]
	s_waitcnt lgkmcnt(8)
	v_mfma_f32_16x16x32_f16 v[104:107], v[192:195], v[184:187], v[104:107]
	v_mfma_f32_16x16x32_f16 v[108:111], v[196:199], v[184:187], v[108:111]
	v_mfma_f32_16x16x32_f16 v[112:115], v[200:203], v[184:187], v[112:115]
	v_mfma_f32_16x16x32_f16 v[116:119], v[204:207], v[184:187], v[116:119]
	s_waitcnt lgkmcnt(7)
	ds_read_b128 v[172:175], v16
	ds_read_b128 v[192:195], v18
	ds_read_b128 v[196:199], v18 offset:2048
	ds_read_b128 v[200:203], v18 offset:4096
	ds_read_b128 v[204:207], v18 offset:6144
	ds_read_b128 v[176:179], v16 offset:2048
	ds_read_b128 v[180:183], v16 offset:4096
	ds_read_b128 v[184:187], v16 offset:6144
	s_waitcnt lgkmcnt(14)
	v_mfma_f32_16x16x32_f16 v[56:59], v[156:159], v[136:139], v[56:59]
	s_waitcnt lgkmcnt(13)
	v_mfma_f32_16x16x32_f16 v[60:63], v[160:163], v[136:139], v[60:63]
	s_waitcnt lgkmcnt(12)
	v_mfma_f32_16x16x32_f16 v[64:67], v[164:167], v[136:139], v[64:67]
	s_waitcnt lgkmcnt(11)
	v_mfma_f32_16x16x32_f16 v[68:71], v[168:171], v[136:139], v[68:71]
	s_waitcnt lgkmcnt(10)
	v_mfma_f32_16x16x32_f16 v[72:75], v[156:159], v[140:143], v[72:75]
	v_mfma_f32_16x16x32_f16 v[76:79], v[160:163], v[140:143], v[76:79]
	v_mfma_f32_16x16x32_f16 v[80:83], v[164:167], v[140:143], v[80:83]
	v_mfma_f32_16x16x32_f16 v[84:87], v[168:171], v[140:143], v[84:87]
	s_waitcnt lgkmcnt(9)
	v_mfma_f32_16x16x32_f16 v[88:91], v[156:159], v[144:147], v[88:91]
	v_mfma_f32_16x16x32_f16 v[92:95], v[160:163], v[144:147], v[92:95]
	v_mfma_f32_16x16x32_f16 v[96:99], v[164:167], v[144:147], v[96:99]
	v_mfma_f32_16x16x32_f16 v[100:103], v[168:171], v[144:147], v[100:103]
	s_waitcnt lgkmcnt(8)
	v_mfma_f32_16x16x32_f16 v[104:107], v[156:159], v[148:151], v[104:107]
	v_mfma_f32_16x16x32_f16 v[108:111], v[160:163], v[148:151], v[108:111]
	v_mfma_f32_16x16x32_f16 v[112:115], v[164:167], v[148:151], v[112:115]
	v_mfma_f32_16x16x32_f16 v[116:119], v[168:171], v[148:151], v[116:119]
	s_waitcnt lgkmcnt(6)
	v_mfma_f32_16x16x32_f16 v[56:59], v[192:195], v[172:175], v[56:59]
	s_waitcnt lgkmcnt(5)
	v_mfma_f32_16x16x32_f16 v[60:63], v[196:199], v[172:175], v[60:63]
	s_waitcnt lgkmcnt(4)
	v_mfma_f32_16x16x32_f16 v[64:67], v[200:203], v[172:175], v[64:67]
	s_waitcnt lgkmcnt(3)
	v_mfma_f32_16x16x32_f16 v[68:71], v[204:207], v[172:175], v[68:71]
	s_waitcnt lgkmcnt(2)
	v_mfma_f32_16x16x32_f16 v[72:75], v[192:195], v[176:179], v[72:75]
	v_mfma_f32_16x16x32_f16 v[76:79], v[196:199], v[176:179], v[76:79]
	v_mfma_f32_16x16x32_f16 v[80:83], v[200:203], v[176:179], v[80:83]
	v_mfma_f32_16x16x32_f16 v[84:87], v[204:207], v[176:179], v[84:87]
	s_waitcnt lgkmcnt(1)
	v_mfma_f32_16x16x32_f16 v[88:91], v[192:195], v[180:183], v[88:91]
	v_mfma_f32_16x16x32_f16 v[92:95], v[196:199], v[180:183], v[92:95]
	v_mfma_f32_16x16x32_f16 v[96:99], v[200:203], v[180:183], v[96:99]
	v_mfma_f32_16x16x32_f16 v[100:103], v[204:207], v[180:183], v[100:103]
	s_waitcnt lgkmcnt(0)
	v_mfma_f32_16x16x32_f16 v[104:107], v[192:195], v[184:187], v[104:107]
	v_mfma_f32_16x16x32_f16 v[108:111], v[196:199], v[184:187], v[108:111]
	v_mfma_f32_16x16x32_f16 v[112:115], v[200:203], v[184:187], v[112:115]
	v_mfma_f32_16x16x32_f16 v[116:119], v[204:207], v[184:187], v[116:119]
	s_nop 7
	s_nop 1
	v_mov_b32_e32 v211, s19
	v_add_f32_e32 v56, v56, v24
	v_add_f32_e32 v57, v57, v25
	v_add_f32_e32 v58, v58, v26
	v_add_f32_e32 v59, v59, v27
	v_add_f32_e32 v60, v60, v28
	v_add_f32_e32 v61, v61, v29
	v_add_f32_e32 v62, v62, v30
	v_add_f32_e32 v63, v63, v31
	v_add_f32_e32 v64, v64, v32
	v_add_f32_e32 v65, v65, v33
	v_add_f32_e32 v66, v66, v34
	v_add_f32_e32 v67, v67, v35
	v_add_f32_e32 v68, v68, v36
	v_add_f32_e32 v69, v69, v37
	v_add_f32_e32 v70, v70, v38
	v_add_f32_e32 v71, v71, v39
	v_mul_f32_e32 v208, v56, v56
	v_fmac_f32_e32 v208, v57, v57
	v_fmac_f32_e32 v208, v58, v58
	v_fmac_f32_e32 v208, v59, v59
	v_fmac_f32_e32 v208, v60, v60
	v_fmac_f32_e32 v208, v61, v61
	v_fmac_f32_e32 v208, v62, v62
	v_fmac_f32_e32 v208, v63, v63
	v_fmac_f32_e32 v208, v64, v64
	v_fmac_f32_e32 v208, v65, v65
	v_fmac_f32_e32 v208, v66, v66
	v_fmac_f32_e32 v208, v67, v67
	v_fmac_f32_e32 v208, v68, v68
	v_fmac_f32_e32 v208, v69, v69
	v_fmac_f32_e32 v208, v70, v70
	v_fmac_f32_e32 v208, v71, v71
	v_mov_b32_e32 v209, v208
	s_nop 1
	v_permlane16_swap_b32_e32 v208, v209
	v_add_f32_e32 v208, v208, v209
	v_mov_b32_e32 v209, v208
	s_nop 1
	v_permlane32_swap_b32_e32 v208, v209
	v_add_f32_e32 v208, v208, v209
	v_mov_b32_e32 v210, 0x358637bd
	v_fmac_f32_e32 v210, 0x3c800000, v208
	v_rsq_f32_e32 v210, v210
	s_add_u32 s24, s29, 0
	s_lshr_b32 s8, s24, 1
	s_lshl_b32 s8, s8, 12
	s_and_b32 s24, s24, 1
	s_lshl_b32 s24, s24, 8
	s_add_u32 s8, s8, s24
	v_mul_f32_e32 v210, v211, v210
	v_add_u32_e32 v212, s8, v23
	v_mul_f32_e32 v56, v56, v210
	v_mul_f32_e32 v57, v57, v210
	v_mul_f32_e32 v58, v58, v210
	v_mul_f32_e32 v59, v59, v210
	v_mul_f32_e32 v56, v56, v40
	v_mul_f32_e32 v57, v57, v41
	v_mul_f32_e32 v58, v58, v42
	v_mul_f32_e32 v59, v59, v43
	v_cvt_pk_f16_f32 v56, v56, v57
	v_cvt_pk_f16_f32 v57, v58, v59
	global_store_dwordx2 v212, v[56:57], s[22:23] offset:0
	v_mul_f32_e32 v60, v60, v210
	v_mul_f32_e32 v61, v61, v210
	v_mul_f32_e32 v62, v62, v210
	v_mul_f32_e32 v63, v63, v210
	v_mul_f32_e32 v60, v60, v44
	v_mul_f32_e32 v61, v61, v45
	v_mul_f32_e32 v62, v62, v46
	v_mul_f32_e32 v63, v63, v47
	v_cvt_pk_f16_f32 v60, v60, v61
	v_cvt_pk_f16_f32 v61, v62, v63
	global_store_dwordx2 v212, v[60:61], s[22:23] offset:1024
	v_mul_f32_e32 v64, v64, v210
	v_mul_f32_e32 v65, v65, v210
	v_mul_f32_e32 v66, v66, v210
	v_mul_f32_e32 v67, v67, v210
	v_mul_f32_e32 v64, v64, v48
	v_mul_f32_e32 v65, v65, v49
	v_mul_f32_e32 v66, v66, v50
	v_mul_f32_e32 v67, v67, v51
	v_cvt_pk_f16_f32 v64, v64, v65
	v_cvt_pk_f16_f32 v65, v66, v67
	global_store_dwordx2 v212, v[64:65], s[22:23] offset:2048
	v_mul_f32_e32 v68, v68, v210
	v_mul_f32_e32 v69, v69, v210
	v_mul_f32_e32 v70, v70, v210
	v_mul_f32_e32 v71, v71, v210
	v_mul_f32_e32 v68, v68, v52
	v_mul_f32_e32 v69, v69, v53
	v_mul_f32_e32 v70, v70, v54
	v_mul_f32_e32 v71, v71, v55
	v_cvt_pk_f16_f32 v68, v68, v69
	v_cvt_pk_f16_f32 v69, v70, v71
	global_store_dwordx2 v212, v[68:69], s[22:23] offset:3072
	v_add_f32_e32 v72, v72, v24
	v_add_f32_e32 v73, v73, v25
	v_add_f32_e32 v74, v74, v26
	v_add_f32_e32 v75, v75, v27
	v_add_f32_e32 v76, v76, v28
	v_add_f32_e32 v77, v77, v29
	v_add_f32_e32 v78, v78, v30
	v_add_f32_e32 v79, v79, v31
	v_add_f32_e32 v80, v80, v32
	v_add_f32_e32 v81, v81, v33
	v_add_f32_e32 v82, v82, v34
	v_add_f32_e32 v83, v83, v35
	v_add_f32_e32 v84, v84, v36
	v_add_f32_e32 v85, v85, v37
	v_add_f32_e32 v86, v86, v38
	v_add_f32_e32 v87, v87, v39
	v_mul_f32_e32 v208, v72, v72
	v_fmac_f32_e32 v208, v73, v73
	v_fmac_f32_e32 v208, v74, v74
	v_fmac_f32_e32 v208, v75, v75
	v_fmac_f32_e32 v208, v76, v76
	v_fmac_f32_e32 v208, v77, v77
	v_fmac_f32_e32 v208, v78, v78
	v_fmac_f32_e32 v208, v79, v79
	v_fmac_f32_e32 v208, v80, v80
	v_fmac_f32_e32 v208, v81, v81
	v_fmac_f32_e32 v208, v82, v82
	v_fmac_f32_e32 v208, v83, v83
	v_fmac_f32_e32 v208, v84, v84
	v_fmac_f32_e32 v208, v85, v85
	v_fmac_f32_e32 v208, v86, v86
	v_fmac_f32_e32 v208, v87, v87
	v_mov_b32_e32 v209, v208
	s_nop 1
	v_permlane16_swap_b32_e32 v208, v209
	v_add_f32_e32 v208, v208, v209
	v_mov_b32_e32 v209, v208
	s_nop 1
	v_permlane32_swap_b32_e32 v208, v209
	v_add_f32_e32 v208, v208, v209
	v_mov_b32_e32 v210, 0x358637bd
	v_fmac_f32_e32 v210, 0x3c800000, v208
	v_rsq_f32_e32 v210, v210
	s_add_u32 s24, s29, 1
	s_lshr_b32 s8, s24, 1
	s_lshl_b32 s8, s8, 12
	s_and_b32 s24, s24, 1
	s_lshl_b32 s24, s24, 8
	s_add_u32 s8, s8, s24
	v_mul_f32_e32 v210, v211, v210
	v_add_u32_e32 v212, s8, v23
	v_mul_f32_e32 v72, v72, v210
	v_mul_f32_e32 v73, v73, v210
	v_mul_f32_e32 v74, v74, v210
	v_mul_f32_e32 v75, v75, v210
	v_mul_f32_e32 v72, v72, v40
	v_mul_f32_e32 v73, v73, v41
	v_mul_f32_e32 v74, v74, v42
	v_mul_f32_e32 v75, v75, v43
	v_cvt_pk_f16_f32 v72, v72, v73
	v_cvt_pk_f16_f32 v73, v74, v75
	global_store_dwordx2 v212, v[72:73], s[22:23] offset:0
	v_mul_f32_e32 v76, v76, v210
	v_mul_f32_e32 v77, v77, v210
	v_mul_f32_e32 v78, v78, v210
	v_mul_f32_e32 v79, v79, v210
	v_mul_f32_e32 v76, v76, v44
	v_mul_f32_e32 v77, v77, v45
	v_mul_f32_e32 v78, v78, v46
	v_mul_f32_e32 v79, v79, v47
	v_cvt_pk_f16_f32 v76, v76, v77
	v_cvt_pk_f16_f32 v77, v78, v79
	global_store_dwordx2 v212, v[76:77], s[22:23] offset:1024
	v_mul_f32_e32 v80, v80, v210
	v_mul_f32_e32 v81, v81, v210
	v_mul_f32_e32 v82, v82, v210
	v_mul_f32_e32 v83, v83, v210
	v_mul_f32_e32 v80, v80, v48
	v_mul_f32_e32 v81, v81, v49
	v_mul_f32_e32 v82, v82, v50
	v_mul_f32_e32 v83, v83, v51
	v_cvt_pk_f16_f32 v80, v80, v81
	v_cvt_pk_f16_f32 v81, v82, v83
	global_store_dwordx2 v212, v[80:81], s[22:23] offset:2048
	v_mul_f32_e32 v84, v84, v210
	v_mul_f32_e32 v85, v85, v210
	v_mul_f32_e32 v86, v86, v210
	v_mul_f32_e32 v87, v87, v210
	v_mul_f32_e32 v84, v84, v52
	v_mul_f32_e32 v85, v85, v53
	v_mul_f32_e32 v86, v86, v54
	v_mul_f32_e32 v87, v87, v55
	v_cvt_pk_f16_f32 v84, v84, v85
	v_cvt_pk_f16_f32 v85, v86, v87
	global_store_dwordx2 v212, v[84:85], s[22:23] offset:3072
	v_add_f32_e32 v88, v88, v24
	v_add_f32_e32 v89, v89, v25
	v_add_f32_e32 v90, v90, v26
	v_add_f32_e32 v91, v91, v27
	v_add_f32_e32 v92, v92, v28
	v_add_f32_e32 v93, v93, v29
	v_add_f32_e32 v94, v94, v30
	v_add_f32_e32 v95, v95, v31
	v_add_f32_e32 v96, v96, v32
	v_add_f32_e32 v97, v97, v33
	v_add_f32_e32 v98, v98, v34
	v_add_f32_e32 v99, v99, v35
	v_add_f32_e32 v100, v100, v36
	v_add_f32_e32 v101, v101, v37
	v_add_f32_e32 v102, v102, v38
	v_add_f32_e32 v103, v103, v39
	v_mul_f32_e32 v208, v88, v88
	v_fmac_f32_e32 v208, v89, v89
	v_fmac_f32_e32 v208, v90, v90
	v_fmac_f32_e32 v208, v91, v91
	v_fmac_f32_e32 v208, v92, v92
	v_fmac_f32_e32 v208, v93, v93
	v_fmac_f32_e32 v208, v94, v94
	v_fmac_f32_e32 v208, v95, v95
	v_fmac_f32_e32 v208, v96, v96
	v_fmac_f32_e32 v208, v97, v97
	v_fmac_f32_e32 v208, v98, v98
	v_fmac_f32_e32 v208, v99, v99
	v_fmac_f32_e32 v208, v100, v100
	v_fmac_f32_e32 v208, v101, v101
	v_fmac_f32_e32 v208, v102, v102
	v_fmac_f32_e32 v208, v103, v103
	v_mov_b32_e32 v209, v208
	s_nop 1
	v_permlane16_swap_b32_e32 v208, v209
	v_add_f32_e32 v208, v208, v209
	v_mov_b32_e32 v209, v208
	s_nop 1
	v_permlane32_swap_b32_e32 v208, v209
	v_add_f32_e32 v208, v208, v209
	v_mov_b32_e32 v210, 0x358637bd
	v_fmac_f32_e32 v210, 0x3c800000, v208
	v_rsq_f32_e32 v210, v210
	s_add_u32 s24, s29, 2
	s_lshr_b32 s8, s24, 1
	s_lshl_b32 s8, s8, 12
	s_and_b32 s24, s24, 1
	s_lshl_b32 s24, s24, 8
	s_add_u32 s8, s8, s24
	v_mul_f32_e32 v210, v211, v210
	v_add_u32_e32 v212, s8, v23
	v_mul_f32_e32 v88, v88, v210
	v_mul_f32_e32 v89, v89, v210
	v_mul_f32_e32 v90, v90, v210
	v_mul_f32_e32 v91, v91, v210
	v_mul_f32_e32 v88, v88, v40
	v_mul_f32_e32 v89, v89, v41
	v_mul_f32_e32 v90, v90, v42
	v_mul_f32_e32 v91, v91, v43
	v_cvt_pk_f16_f32 v88, v88, v89
	v_cvt_pk_f16_f32 v89, v90, v91
	global_store_dwordx2 v212, v[88:89], s[22:23] offset:0
	v_mul_f32_e32 v92, v92, v210
	v_mul_f32_e32 v93, v93, v210
	v_mul_f32_e32 v94, v94, v210
	v_mul_f32_e32 v95, v95, v210
	v_mul_f32_e32 v92, v92, v44
	v_mul_f32_e32 v93, v93, v45
	v_mul_f32_e32 v94, v94, v46
	v_mul_f32_e32 v95, v95, v47
	v_cvt_pk_f16_f32 v92, v92, v93
	v_cvt_pk_f16_f32 v93, v94, v95
	global_store_dwordx2 v212, v[92:93], s[22:23] offset:1024
	v_mul_f32_e32 v96, v96, v210
	v_mul_f32_e32 v97, v97, v210
	v_mul_f32_e32 v98, v98, v210
	v_mul_f32_e32 v99, v99, v210
	v_mul_f32_e32 v96, v96, v48
	v_mul_f32_e32 v97, v97, v49
	v_mul_f32_e32 v98, v98, v50
	v_mul_f32_e32 v99, v99, v51
	v_cvt_pk_f16_f32 v96, v96, v97
	v_cvt_pk_f16_f32 v97, v98, v99
	global_store_dwordx2 v212, v[96:97], s[22:23] offset:2048
	v_mul_f32_e32 v100, v100, v210
	v_mul_f32_e32 v101, v101, v210
	v_mul_f32_e32 v102, v102, v210
	v_mul_f32_e32 v103, v103, v210
	v_mul_f32_e32 v100, v100, v52
	v_mul_f32_e32 v101, v101, v53
	v_mul_f32_e32 v102, v102, v54
	v_mul_f32_e32 v103, v103, v55
	v_cvt_pk_f16_f32 v100, v100, v101
	v_cvt_pk_f16_f32 v101, v102, v103
	global_store_dwordx2 v212, v[100:101], s[22:23] offset:3072
	v_add_f32_e32 v104, v104, v24
	v_add_f32_e32 v105, v105, v25
	v_add_f32_e32 v106, v106, v26
	v_add_f32_e32 v107, v107, v27
	v_add_f32_e32 v108, v108, v28
	v_add_f32_e32 v109, v109, v29
	v_add_f32_e32 v110, v110, v30
	v_add_f32_e32 v111, v111, v31
	v_add_f32_e32 v112, v112, v32
	v_add_f32_e32 v113, v113, v33
	v_add_f32_e32 v114, v114, v34
	v_add_f32_e32 v115, v115, v35
	v_add_f32_e32 v116, v116, v36
	v_add_f32_e32 v117, v117, v37
	v_add_f32_e32 v118, v118, v38
	v_add_f32_e32 v119, v119, v39
	v_mul_f32_e32 v208, v104, v104
	v_fmac_f32_e32 v208, v105, v105
	v_fmac_f32_e32 v208, v106, v106
	v_fmac_f32_e32 v208, v107, v107
	v_fmac_f32_e32 v208, v108, v108
	v_fmac_f32_e32 v208, v109, v109
	v_fmac_f32_e32 v208, v110, v110
	v_fmac_f32_e32 v208, v111, v111
	v_fmac_f32_e32 v208, v112, v112
	v_fmac_f32_e32 v208, v113, v113
	v_fmac_f32_e32 v208, v114, v114
	v_fmac_f32_e32 v208, v115, v115
	v_fmac_f32_e32 v208, v116, v116
	v_fmac_f32_e32 v208, v117, v117
	v_fmac_f32_e32 v208, v118, v118
	v_fmac_f32_e32 v208, v119, v119
	v_mov_b32_e32 v209, v208
	s_nop 1
	v_permlane16_swap_b32_e32 v208, v209
	v_add_f32_e32 v208, v208, v209
	v_mov_b32_e32 v209, v208
	s_nop 1
	v_permlane32_swap_b32_e32 v208, v209
	v_add_f32_e32 v208, v208, v209
	v_mov_b32_e32 v210, 0x358637bd
	v_fmac_f32_e32 v210, 0x3c800000, v208
	v_rsq_f32_e32 v210, v210
	s_add_u32 s24, s29, 3
	s_lshr_b32 s8, s24, 1
	s_lshl_b32 s8, s8, 12
	s_and_b32 s24, s24, 1
	s_lshl_b32 s24, s24, 8
	s_add_u32 s8, s8, s24
	v_mul_f32_e32 v210, v211, v210
	v_add_u32_e32 v212, s8, v23
	v_mul_f32_e32 v104, v104, v210
	v_mul_f32_e32 v105, v105, v210
	v_mul_f32_e32 v106, v106, v210
	v_mul_f32_e32 v107, v107, v210
	v_mul_f32_e32 v104, v104, v40
	v_mul_f32_e32 v105, v105, v41
	v_mul_f32_e32 v106, v106, v42
	v_mul_f32_e32 v107, v107, v43
	v_cvt_pk_f16_f32 v104, v104, v105
	v_cvt_pk_f16_f32 v105, v106, v107
	global_store_dwordx2 v212, v[104:105], s[22:23] offset:0
	v_mul_f32_e32 v108, v108, v210
	v_mul_f32_e32 v109, v109, v210
	v_mul_f32_e32 v110, v110, v210
	v_mul_f32_e32 v111, v111, v210
	v_mul_f32_e32 v108, v108, v44
	v_mul_f32_e32 v109, v109, v45
	v_mul_f32_e32 v110, v110, v46
	v_mul_f32_e32 v111, v111, v47
	v_cvt_pk_f16_f32 v108, v108, v109
	v_cvt_pk_f16_f32 v109, v110, v111
	global_store_dwordx2 v212, v[108:109], s[22:23] offset:1024
	v_mul_f32_e32 v112, v112, v210
	v_mul_f32_e32 v113, v113, v210
	v_mul_f32_e32 v114, v114, v210
	v_mul_f32_e32 v115, v115, v210
	v_mul_f32_e32 v112, v112, v48
	v_mul_f32_e32 v113, v113, v49
	v_mul_f32_e32 v114, v114, v50
	v_mul_f32_e32 v115, v115, v51
	v_cvt_pk_f16_f32 v112, v112, v113
	v_cvt_pk_f16_f32 v113, v114, v115
	global_store_dwordx2 v212, v[112:113], s[22:23] offset:2048
	v_mul_f32_e32 v116, v116, v210
	v_mul_f32_e32 v117, v117, v210
	v_mul_f32_e32 v118, v118, v210
	v_mul_f32_e32 v119, v119, v210
	v_mul_f32_e32 v116, v116, v52
	v_mul_f32_e32 v117, v117, v53
	v_mul_f32_e32 v118, v118, v54
	v_mul_f32_e32 v119, v119, v55
	v_cvt_pk_f16_f32 v116, v116, v117
	v_cvt_pk_f16_f32 v117, v118, v119
	global_store_dwordx2 v212, v[116:117], s[22:23] offset:3072
	s_branch .Lpf_done

.Lpf_actVA:
	s_mul_i32 s25, s25, 0x50
	s_add_u32 s29, s10, s25
	s_lshr_b32 s29, s29, 4
	v_add_u32_e32 v5, s25, v3
	v_lshlrev_b32_e32 v5, 7, v5
	v_add_u32_e32 v15, v5, v6
	v_add_u32_e32 v16, v5, v7
	v_add_u32_e32 v5, 0x9000, v9
	v_add_u32_e32 v17, v5, v6
	v_add_u32_e32 v18, v5, v7
	v_add_u32_e32 v19, 0x1a000, v15
	v_add_u32_e32 v20, 0x1a000, v16
	v_add_u32_e32 v21, 0x1a000, v17
	v_add_u32_e32 v22, 0x1a000, v18
	v_lshlrev_b32_e32 v5, 2, v3
	global_load_dword v24, v5, s[14:15] offset:0
	global_load_dword v25, v5, s[14:15] offset:64
	global_load_dword v26, v5, s[14:15] offset:128
	global_load_dword v27, v5, s[14:15] offset:192
	s_waitcnt vmcnt(18) lgkmcnt(0)
	s_barrier
	s_waitcnt lgkmcnt(6)
	ds_read_b128 v[136:139], v15
	ds_read_b128 v[156:159], v17
	ds_read_b128 v[160:163], v17 offset:2048
	ds_read_b128 v[164:167], v17 offset:4096
	ds_read_b128 v[168:171], v17 offset:6144
	ds_read_b128 v[140:143], v15 offset:2048
	ds_read_b128 v[144:147], v15 offset:4096
	ds_read_b128 v[148:151], v15 offset:6144
	ds_read_b128 v[152:155], v15 offset:8192
	s_waitcnt lgkmcnt(6)
	ds_read_b128 v[172:175], v16
	ds_read_b128 v[192:195], v18
	ds_read_b128 v[196:199], v18 offset:2048
	ds_read_b128 v[200:203], v18 offset:4096
	ds_read_b128 v[204:207], v18 offset:6144
	ds_read_b128 v[176:179], v16 offset:2048
	ds_read_b128 v[180:183], v16 offset:4096
	ds_read_b128 v[184:187], v16 offset:6144
	ds_read_b128 v[188:191], v16 offset:8192
	v_mfma_f32_16x16x32_f16 v[56:59], v[136:139], v[156:159], 0
	s_waitcnt lgkmcnt(15)
	v_mfma_f32_16x16x32_f16 v[60:63], v[136:139], v[160:163], 0
	s_waitcnt lgkmcnt(14)
	v_mfma_f32_16x16x32_f16 v[64:67], v[136:139], v[164:167], 0
	s_waitcnt lgkmcnt(13)
	v_mfma_f32_16x16x32_f16 v[68:71], v[136:139], v[168:171], 0
	s_waitcnt lgkmcnt(12)
	v_mfma_f32_16x16x32_f16 v[72:75], v[140:143], v[156:159], 0
	v_mfma_f32_16x16x32_f16 v[76:79], v[140:143], v[160:163], 0
	v_mfma_f32_16x16x32_f16 v[80:83], v[140:143], v[164:167], 0
	v_mfma_f32_16x16x32_f16 v[84:87], v[140:143], v[168:171], 0
	s_waitcnt lgkmcnt(11)
	v_mfma_f32_16x16x32_f16 v[88:91], v[144:147], v[156:159], 0
	v_mfma_f32_16x16x32_f16 v[92:95], v[144:147], v[160:163], 0
	v_mfma_f32_16x16x32_f16 v[96:99], v[144:147], v[164:167], 0
	v_mfma_f32_16x16x32_f16 v[100:103], v[144:147], v[168:171], 0
	s_waitcnt lgkmcnt(10)
	v_mfma_f32_16x16x32_f16 v[104:107], v[148:151], v[156:159], 0
	v_mfma_f32_16x16x32_f16 v[108:111], v[148:151], v[160:163], 0
	v_mfma_f32_16x16x32_f16 v[112:115], v[148:151], v[164:167], 0
	v_mfma_f32_16x16x32_f16 v[116:119], v[148:151], v[168:171], 0
	s_waitcnt lgkmcnt(9)
	v_mfma_f32_16x16x32_f16 v[120:123], v[152:155], v[156:159], 0
	v_mfma_f32_16x16x32_f16 v[124:127], v[152:155], v[160:163], 0
	v_mfma_f32_16x16x32_f16 v[128:131], v[152:155], v[164:167], 0
	v_mfma_f32_16x16x32_f16 v[132:135], v[152:155], v[168:171], 0
	s_waitcnt vmcnt(11) lgkmcnt(0)
	s_barrier
	s_waitcnt lgkmcnt(6)
	ds_read_b128 v[136:139], v15 offset:53248
	ds_read_b128 v[156:159], v17 offset:53248
	ds_read_b128 v[160:163], v17 offset:55296
	ds_read_b128 v[164:167], v17 offset:57344
	ds_read_b128 v[168:171], v17 offset:59392
	ds_read_b128 v[140:143], v15 offset:55296
	ds_read_b128 v[144:147], v15 offset:57344
	ds_read_b128 v[148:151], v15 offset:59392
	ds_read_b128 v[152:155], v15 offset:61440
	v_mfma_f32_16x16x32_f16 v[56:59], v[172:175], v[192:195], v[56:59]
	s_add_u32 m0, s28, 0x0
	s_nop 0
	global_load_lds_dwordx4 v10, s[4:5]
	s_waitcnt lgkmcnt(15)
	v_mfma_f32_16x16x32_f16 v[60:63], v[172:175], v[196:199], v[60:63]
	s_waitcnt lgkmcnt(14)
	v_mfma_f32_16x16x32_f16 v[64:67], v[172:175], v[200:203], v[64:67]
	s_waitcnt lgkmcnt(13)
	v_mfma_f32_16x16x32_f16 v[68:71], v[172:175], v[204:207], v[68:71]
	s_waitcnt lgkmcnt(12)
	v_mfma_f32_16x16x32_f16 v[72:75], v[176:179], v[192:195], v[72:75]
	v_mfma_f32_16x16x32_f16 v[76:79], v[176:179], v[196:199], v[76:79]
	s_add_u32 m0, s28, 0x2000
	s_nop 0
	global_load_lds_dwordx4 v11, s[4:5]
	v_mfma_f32_16x16x32_f16 v[80:83], v[176:179], v[200:203], v[80:83]
	v_mfma_f32_16x16x32_f16 v[84:87], v[176:179], v[204:207], v[84:87]
	s_waitcnt lgkmcnt(11)
	v_mfma_f32_16x16x32_f16 v[88:91], v[180:183], v[192:195], v[88:91]
	v_mfma_f32_16x16x32_f16 v[92:95], v[180:183], v[196:199], v[92:95]
	v_mfma_f32_16x16x32_f16 v[96:99], v[180:183], v[200:203], v[96:99]
	s_add_u32 m0, s28, 0x4000
	s_nop 0
	global_load_lds_dwordx4 v12, s[4:5]
	v_mfma_f32_16x16x32_f16 v[100:103], v[180:183], v[204:207], v[100:103]
	s_waitcnt lgkmcnt(10)
	v_mfma_f32_16x16x32_f16 v[104:107], v[184:187], v[192:195], v[104:107]
	v_mfma_f32_16x16x32_f16 v[108:111], v[184:187], v[196:199], v[108:111]
	v_mfma_f32_16x16x32_f16 v[112:115], v[184:187], v[200:203], v[112:115]
	v_mfma_f32_16x16x32_f16 v[116:119], v[184:187], v[204:207], v[116:119]
	s_add_u32 m0, s28, 0x6000
	s_nop 0
	global_load_lds_dwordx4 v13, s[4:5]
	s_waitcnt lgkmcnt(9)
	v_mfma_f32_16x16x32_f16 v[120:123], v[188:191], v[192:195], v[120:123]
	v_mfma_f32_16x16x32_f16 v[124:127], v[188:191], v[196:199], v[124:127]
	v_mfma_f32_16x16x32_f16 v[128:131], v[188:191], v[200:203], v[128:131]
	v_mfma_f32_16x16x32_f16 v[132:135], v[188:191], v[204:207], v[132:135]
	s_waitcnt lgkmcnt(6)
	ds_read_b128 v[172:175], v16 offset:53248
	ds_read_b128 v[192:195], v18 offset:53248
	ds_read_b128 v[196:199], v18 offset:55296
	ds_read_b128 v[200:203], v18 offset:57344
	ds_read_b128 v[204:207], v18 offset:59392
	ds_read_b128 v[176:179], v16 offset:55296
	ds_read_b128 v[180:183], v16 offset:57344
	ds_read_b128 v[184:187], v16 offset:59392
	ds_read_b128 v[188:191], v16 offset:61440
	v_mfma_f32_16x16x32_f16 v[56:59], v[136:139], v[156:159], v[56:59]
	s_add_u32 m0, s28, 0x8000
	s_nop 0
	global_load_lds_dwordx4 v14, s[4:5]
	s_add_u32 s4, s4, s20
	s_addc_u32 s5, s5, 0
	s_waitcnt lgkmcnt(15)
	v_mfma_f32_16x16x32_f16 v[60:63], v[136:139], v[160:163], v[60:63]
	s_waitcnt lgkmcnt(14)
	v_mfma_f32_16x16x32_f16 v[64:67], v[136:139], v[164:167], v[64:67]
	s_waitcnt lgkmcnt(13)
	v_mfma_f32_16x16x32_f16 v[68:71], v[136:139], v[168:171], v[68:71]
	s_waitcnt lgkmcnt(12)
	v_mfma_f32_16x16x32_f16 v[72:75], v[140:143], v[156:159], v[72:75]
	v_mfma_f32_16x16x32_f16 v[76:79], v[140:143], v[160:163], v[76:79]
	v_mfma_f32_16x16x32_f16 v[80:83], v[140:143], v[164:167], v[80:83]
	s_add_u32 m0, s28, 0x9000
	s_nop 0
	global_load_lds_dwordx4 v10, s[6:7]
	v_mfma_f32_16x16x32_f16 v[84:87], v[140:143], v[168:171], v[84:87]
	s_waitcnt lgkmcnt(11)
	v_mfma_f32_16x16x32_f16 v[88:91], v[144:147], v[156:159], v[88:91]
	v_mfma_f32_16x16x32_f16 v[92:95], v[144:147], v[160:163], v[92:95]
	v_mfma_f32_16x16x32_f16 v[96:99], v[144:147], v[164:167], v[96:99]
	v_mfma_f32_16x16x32_f16 v[100:103], v[144:147], v[168:171], v[100:103]
	s_waitcnt lgkmcnt(10)
	v_mfma_f32_16x16x32_f16 v[104:107], v[148:151], v[156:159], v[104:107]
	v_mfma_f32_16x16x32_f16 v[108:111], v[148:151], v[160:163], v[108:111]
	s_add_u32 m0, s28, 0xb000
	s_nop 0
	global_load_lds_dwordx4 v11, s[6:7]
	s_add_u32 s6, s6, s20
	s_addc_u32 s7, s7, 0
	v_mfma_f32_16x16x32_f16 v[112:115], v[148:151], v[164:167], v[112:115]
	v_mfma_f32_16x16x32_f16 v[116:119], v[148:151], v[168:171], v[116:119]
	s_waitcnt lgkmcnt(9)
	v_mfma_f32_16x16x32_f16 v[120:123], v[152:155], v[156:159], v[120:123]
	v_mfma_f32_16x16x32_f16 v[124:127], v[152:155], v[160:163], v[124:127]
	v_mfma_f32_16x16x32_f16 v[128:131], v[152:155], v[164:167], v[128:131]
	v_mfma_f32_16x16x32_f16 v[132:135], v[152:155], v[168:171], v[132:135]
	s_waitcnt vmcnt(7) lgkmcnt(0)
	s_barrier
	s_waitcnt lgkmcnt(6)
	ds_read_b128 v[136:139], v19
	ds_read_b128 v[156:159], v21
	ds_read_b128 v[160:163], v21 offset:2048
	ds_read_b128 v[164:167], v21 offset:4096
	ds_read_b128 v[168:171], v21 offset:6144
	ds_read_b128 v[140:143], v19 offset:2048
	ds_read_b128 v[144:147], v19 offset:4096
	ds_read_b128 v[148:151], v19 offset:6144
	ds_read_b128 v[152:155], v19 offset:8192
	v_mfma_f32_16x16x32_f16 v[56:59], v[172:175], v[192:195], v[56:59]
	s_add_u32 m0, s28, 0xd000
	s_nop 0
	global_load_lds_dwordx4 v10, s[4:5]
	s_waitcnt lgkmcnt(15)
	v_mfma_f32_16x16x32_f16 v[60:63], v[172:175], v[196:199], v[60:63]
	s_waitcnt lgkmcnt(14)
	v_mfma_f32_16x16x32_f16 v[64:67], v[172:175], v[200:203], v[64:67]
	s_waitcnt lgkmcnt(13)
	v_mfma_f32_16x16x32_f16 v[68:71], v[172:175], v[204:207], v[68:71]
	s_waitcnt lgkmcnt(12)
	v_mfma_f32_16x16x32_f16 v[72:75], v[176:179], v[192:195], v[72:75]
	v_mfma_f32_16x16x32_f16 v[76:79], v[176:179], v[196:199], v[76:79]
	s_add_u32 m0, s28, 0xf000
	s_nop 0
	global_load_lds_dwordx4 v11, s[4:5]
	v_mfma_f32_16x16x32_f16 v[80:83], v[176:179], v[200:203], v[80:83]
	v_mfma_f32_16x16x32_f16 v[84:87], v[176:179], v[204:207], v[84:87]
	s_waitcnt lgkmcnt(11)
	v_mfma_f32_16x16x32_f16 v[88:91], v[180:183], v[192:195], v[88:91]
	v_mfma_f32_16x16x32_f16 v[92:95], v[180:183], v[196:199], v[92:95]
	v_mfma_f32_16x16x32_f16 v[96:99], v[180:183], v[200:203], v[96:99]
	s_add_u32 m0, s28, 0x11000
	s_nop 0
	global_load_lds_dwordx4 v12, s[4:5]
	v_mfma_f32_16x16x32_f16 v[100:103], v[180:183], v[204:207], v[100:103]
	s_waitcnt lgkmcnt(10)
	v_mfma_f32_16x16x32_f16 v[104:107], v[184:187], v[192:195], v[104:107]
	v_mfma_f32_16x16x32_f16 v[108:111], v[184:187], v[196:199], v[108:111]
	v_mfma_f32_16x16x32_f16 v[112:115], v[184:187], v[200:203], v[112:115]
	v_mfma_f32_16x16x32_f16 v[116:119], v[184:187], v[204:207], v[116:119]
	s_add_u32 m0, s28, 0x13000
	s_nop 0
	global_load_lds_dwordx4 v13, s[4:5]
	s_waitcnt lgkmcnt(9)
	v_mfma_f32_16x16x32_f16 v[120:123], v[188:191], v[192:195], v[120:123]
	v_mfma_f32_16x16x32_f16 v[124:127], v[188:191], v[196:199], v[124:127]
	v_mfma_f32_16x16x32_f16 v[128:131], v[188:191], v[200:203], v[128:131]
	v_mfma_f32_16x16x32_f16 v[132:135], v[188:191], v[204:207], v[132:135]
	s_waitcnt lgkmcnt(6)
	ds_read_b128 v[172:175], v20
	ds_read_b128 v[192:195], v22
	ds_read_b128 v[196:199], v22 offset:2048
	ds_read_b128 v[200:203], v22 offset:4096
	ds_read_b128 v[204:207], v22 offset:6144
	ds_read_b128 v[176:179], v20 offset:2048
	ds_read_b128 v[180:183], v20 offset:4096
	ds_read_b128 v[184:187], v20 offset:6144
	ds_read_b128 v[188:191], v20 offset:8192
	v_mfma_f32_16x16x32_f16 v[56:59], v[136:139], v[156:159], v[56:59]
	s_add_u32 m0, s28, 0x15000
	s_nop 0
	global_load_lds_dwordx4 v14, s[4:5]
	s_add_u32 s4, s4, s20
	s_addc_u32 s5, s5, 0
	s_waitcnt lgkmcnt(15)
	v_mfma_f32_16x16x32_f16 v[60:63], v[136:139], v[160:163], v[60:63]
	s_waitcnt lgkmcnt(14)
	v_mfma_f32_16x16x32_f16 v[64:67], v[136:139], v[164:167], v[64:67]
	s_waitcnt lgkmcnt(13)
	v_mfma_f32_16x16x32_f16 v[68:71], v[136:139], v[168:171], v[68:71]
	s_waitcnt lgkmcnt(12)
	v_mfma_f32_16x16x32_f16 v[72:75], v[140:143], v[156:159], v[72:75]
	v_mfma_f32_16x16x32_f16 v[76:79], v[140:143], v[160:163], v[76:79]
	v_mfma_f32_16x16x32_f16 v[80:83], v[140:143], v[164:167], v[80:83]
	s_add_u32 m0, s28, 0x16000
	s_nop 0
	global_load_lds_dwordx4 v10, s[6:7]
	v_mfma_f32_16x16x32_f16 v[84:87], v[140:143], v[168:171], v[84:87]
	s_waitcnt lgkmcnt(11)
	v_mfma_f32_16x16x32_f16 v[88:91], v[144:147], v[156:159], v[88:91]
	v_mfma_f32_16x16x32_f16 v[92:95], v[144:147], v[160:163], v[92:95]
	v_mfma_f32_16x16x32_f16 v[96:99], v[144:147], v[164:167], v[96:99]
	v_mfma_f32_16x16x32_f16 v[100:103], v[144:147], v[168:171], v[100:103]
	s_waitcnt lgkmcnt(10)
	v_mfma_f32_16x16x32_f16 v[104:107], v[148:151], v[156:159], v[104:107]
	v_mfma_f32_16x16x32_f16 v[108:111], v[148:151], v[160:163], v[108:111]
	s_add_u32 m0, s28, 0x18000
	s_nop 0
	global_load_lds_dwordx4 v11, s[6:7]
	s_add_u32 s6, s6, s20
	s_addc_u32 s7, s7, 0
	v_mfma_f32_16x16x32_f16 v[112:115], v[148:151], v[164:167], v[112:115]
	v_mfma_f32_16x16x32_f16 v[116:119], v[148:151], v[168:171], v[116:119]
	s_waitcnt lgkmcnt(9)
	v_mfma_f32_16x16x32_f16 v[120:123], v[152:155], v[156:159], v[120:123]
	v_mfma_f32_16x16x32_f16 v[124:127], v[152:155], v[160:163], v[124:127]
	v_mfma_f32_16x16x32_f16 v[128:131], v[152:155], v[164:167], v[128:131]
	v_mfma_f32_16x16x32_f16 v[132:135], v[152:155], v[168:171], v[132:135]
	s_waitcnt vmcnt(7) lgkmcnt(0)
	s_barrier
	s_waitcnt lgkmcnt(6)
	ds_read_b128 v[136:139], v15
	ds_read_b128 v[156:159], v17
	ds_read_b128 v[160:163], v17 offset:2048
	ds_read_b128 v[164:167], v17 offset:4096
	ds_read_b128 v[168:171], v17 offset:6144
	ds_read_b128 v[140:143], v15 offset:2048
	ds_read_b128 v[144:147], v15 offset:4096
	ds_read_b128 v[148:151], v15 offset:6144
	ds_read_b128 v[152:155], v15 offset:8192
	v_mfma_f32_16x16x32_f16 v[56:59], v[172:175], v[192:195], v[56:59]
	s_add_u32 m0, s28, 0x1a000
	s_nop 0
	global_load_lds_dwordx4 v10, s[4:5]
	s_waitcnt lgkmcnt(15)
	v_mfma_f32_16x16x32_f16 v[60:63], v[172:175], v[196:199], v[60:63]
	s_waitcnt lgkmcnt(14)
	v_mfma_f32_16x16x32_f16 v[64:67], v[172:175], v[200:203], v[64:67]
	s_waitcnt lgkmcnt(13)
	v_mfma_f32_16x16x32_f16 v[68:71], v[172:175], v[204:207], v[68:71]
	s_waitcnt lgkmcnt(12)
	v_mfma_f32_16x16x32_f16 v[72:75], v[176:179], v[192:195], v[72:75]
	v_mfma_f32_16x16x32_f16 v[76:79], v[176:179], v[196:199], v[76:79]
	s_add_u32 m0, s28, 0x1c000
	s_nop 0
	global_load_lds_dwordx4 v11, s[4:5]
	v_mfma_f32_16x16x32_f16 v[80:83], v[176:179], v[200:203], v[80:83]
	v_mfma_f32_16x16x32_f16 v[84:87], v[176:179], v[204:207], v[84:87]
	s_waitcnt lgkmcnt(11)
	v_mfma_f32_16x16x32_f16 v[88:91], v[180:183], v[192:195], v[88:91]
	v_mfma_f32_16x16x32_f16 v[92:95], v[180:183], v[196:199], v[92:95]
	v_mfma_f32_16x16x32_f16 v[96:99], v[180:183], v[200:203], v[96:99]
	s_add_u32 m0, s28, 0x1e000
	s_nop 0
	global_load_lds_dwordx4 v12, s[4:5]
	v_mfma_f32_16x16x32_f16 v[100:103], v[180:183], v[204:207], v[100:103]
	s_waitcnt lgkmcnt(10)
	v_mfma_f32_16x16x32_f16 v[104:107], v[184:187], v[192:195], v[104:107]
	v_mfma_f32_16x16x32_f16 v[108:111], v[184:187], v[196:199], v[108:111]
	v_mfma_f32_16x16x32_f16 v[112:115], v[184:187], v[200:203], v[112:115]
	v_mfma_f32_16x16x32_f16 v[116:119], v[184:187], v[204:207], v[116:119]
	s_add_u32 m0, s28, 0x20000
	s_nop 0
	global_load_lds_dwordx4 v13, s[4:5]
	s_waitcnt lgkmcnt(9)
	v_mfma_f32_16x16x32_f16 v[120:123], v[188:191], v[192:195], v[120:123]
	v_mfma_f32_16x16x32_f16 v[124:127], v[188:191], v[196:199], v[124:127]
	v_mfma_f32_16x16x32_f16 v[128:131], v[188:191], v[200:203], v[128:131]
	v_mfma_f32_16x16x32_f16 v[132:135], v[188:191], v[204:207], v[132:135]
	s_waitcnt lgkmcnt(6)
	ds_read_b128 v[172:175], v16
	ds_read_b128 v[192:195], v18
	ds_read_b128 v[196:199], v18 offset:2048
	ds_read_b128 v[200:203], v18 offset:4096
	ds_read_b128 v[204:207], v18 offset:6144
	ds_read_b128 v[176:179], v16 offset:2048
	ds_read_b128 v[180:183], v16 offset:4096
	ds_read_b128 v[184:187], v16 offset:6144
	ds_read_b128 v[188:191], v16 offset:8192
	v_mfma_f32_16x16x32_f16 v[56:59], v[136:139], v[156:159], v[56:59]
	s_add_u32 m0, s28, 0x22000
	s_nop 0
	global_load_lds_dwordx4 v14, s[4:5]
	s_add_u32 s4, s4, s20
	s_addc_u32 s5, s5, 0
	s_waitcnt lgkmcnt(15)
	v_mfma_f32_16x16x32_f16 v[60:63], v[136:139], v[160:163], v[60:63]
	s_waitcnt lgkmcnt(14)
	v_mfma_f32_16x16x32_f16 v[64:67], v[136:139], v[164:167], v[64:67]
	s_waitcnt lgkmcnt(13)
	v_mfma_f32_16x16x32_f16 v[68:71], v[136:139], v[168:171], v[68:71]
	s_waitcnt lgkmcnt(12)
	v_mfma_f32_16x16x32_f16 v[72:75], v[140:143], v[156:159], v[72:75]
	v_mfma_f32_16x16x32_f16 v[76:79], v[140:143], v[160:163], v[76:79]
	v_mfma_f32_16x16x32_f16 v[80:83], v[140:143], v[164:167], v[80:83]
	s_add_u32 m0, s28, 0x23000
	s_nop 0
	global_load_lds_dwordx4 v10, s[6:7]
	v_mfma_f32_16x16x32_f16 v[84:87], v[140:143], v[168:171], v[84:87]
	s_waitcnt lgkmcnt(11)
	v_mfma_f32_16x16x32_f16 v[88:91], v[144:147], v[156:159], v[88:91]
	v_mfma_f32_16x16x32_f16 v[92:95], v[144:147], v[160:163], v[92:95]
	v_mfma_f32_16x16x32_f16 v[96:99], v[144:147], v[164:167], v[96:99]
	v_mfma_f32_16x16x32_f16 v[100:103], v[144:147], v[168:171], v[100:103]
	s_waitcnt lgkmcnt(10)
	v_mfma_f32_16x16x32_f16 v[104:107], v[148:151], v[156:159], v[104:107]
	v_mfma_f32_16x16x32_f16 v[108:111], v[148:151], v[160:163], v[108:111]
	s_add_u32 m0, s28, 0x25000
	s_nop 0
	global_load_lds_dwordx4 v11, s[6:7]
	s_add_u32 s6, s6, s20
	s_addc_u32 s7, s7, 0
	v_mfma_f32_16x16x32_f16 v[112:115], v[148:151], v[164:167], v[112:115]
	v_mfma_f32_16x16x32_f16 v[116:119], v[148:151], v[168:171], v[116:119]
	s_waitcnt lgkmcnt(9)
	v_mfma_f32_16x16x32_f16 v[120:123], v[152:155], v[156:159], v[120:123]
	v_mfma_f32_16x16x32_f16 v[124:127], v[152:155], v[160:163], v[124:127]
	v_mfma_f32_16x16x32_f16 v[128:131], v[152:155], v[164:167], v[128:131]
	v_mfma_f32_16x16x32_f16 v[132:135], v[152:155], v[168:171], v[132:135]
	s_waitcnt vmcnt(7) lgkmcnt(0)
	s_barrier
	s_waitcnt lgkmcnt(6)
	ds_read_b128 v[136:139], v15 offset:53248
	ds_read_b128 v[156:159], v17 offset:53248
	ds_read_b128 v[160:163], v17 offset:55296
	ds_read_b128 v[164:167], v17 offset:57344
	ds_read_b128 v[168:171], v17 offset:59392
	ds_read_b128 v[140:143], v15 offset:55296
	ds_read_b128 v[144:147], v15 offset:57344
	ds_read_b128 v[148:151], v15 offset:59392
	ds_read_b128 v[152:155], v15 offset:61440
	v_mfma_f32_16x16x32_f16 v[56:59], v[172:175], v[192:195], v[56:59]
	s_add_u32 m0, s28, 0x0
	s_nop 0
	global_load_lds_dwordx4 v10, s[4:5]
	s_waitcnt lgkmcnt(15)
	v_mfma_f32_16x16x32_f16 v[60:63], v[172:175], v[196:199], v[60:63]
	s_waitcnt lgkmcnt(14)
	v_mfma_f32_16x16x32_f16 v[64:67], v[172:175], v[200:203], v[64:67]
	s_waitcnt lgkmcnt(13)
	v_mfma_f32_16x16x32_f16 v[68:71], v[172:175], v[204:207], v[68:71]
	s_waitcnt lgkmcnt(12)
	v_mfma_f32_16x16x32_f16 v[72:75], v[176:179], v[192:195], v[72:75]
	v_mfma_f32_16x16x32_f16 v[76:79], v[176:179], v[196:199], v[76:79]
	s_add_u32 m0, s28, 0x2000
	s_nop 0
	global_load_lds_dwordx4 v11, s[4:5]
	v_mfma_f32_16x16x32_f16 v[80:83], v[176:179], v[200:203], v[80:83]
	v_mfma_f32_16x16x32_f16 v[84:87], v[176:179], v[204:207], v[84:87]
	s_waitcnt lgkmcnt(11)
	v_mfma_f32_16x16x32_f16 v[88:91], v[180:183], v[192:195], v[88:91]
	v_mfma_f32_16x16x32_f16 v[92:95], v[180:183], v[196:199], v[92:95]
	v_mfma_f32_16x16x32_f16 v[96:99], v[180:183], v[200:203], v[96:99]
	s_add_u32 m0, s28, 0x4000
	s_nop 0
	global_load_lds_dwordx4 v12, s[4:5]
	v_mfma_f32_16x16x32_f16 v[100:103], v[180:183], v[204:207], v[100:103]
	s_waitcnt lgkmcnt(10)
	v_mfma_f32_16x16x32_f16 v[104:107], v[184:187], v[192:195], v[104:107]
	v_mfma_f32_16x16x32_f16 v[108:111], v[184:187], v[196:199], v[108:111]
	v_mfma_f32_16x16x32_f16 v[112:115], v[184:187], v[200:203], v[112:115]
	v_mfma_f32_16x16x32_f16 v[116:119], v[184:187], v[204:207], v[116:119]
	s_add_u32 m0, s28, 0x6000
	s_nop 0
	global_load_lds_dwordx4 v13, s[4:5]
	s_waitcnt lgkmcnt(9)
	v_mfma_f32_16x16x32_f16 v[120:123], v[188:191], v[192:195], v[120:123]
	v_mfma_f32_16x16x32_f16 v[124:127], v[188:191], v[196:199], v[124:127]
	v_mfma_f32_16x16x32_f16 v[128:131], v[188:191], v[200:203], v[128:131]
	v_mfma_f32_16x16x32_f16 v[132:135], v[188:191], v[204:207], v[132:135]
	s_waitcnt lgkmcnt(6)
	ds_read_b128 v[172:175], v16 offset:53248
	ds_read_b128 v[192:195], v18 offset:53248
	ds_read_b128 v[196:199], v18 offset:55296
	ds_read_b128 v[200:203], v18 offset:57344
	ds_read_b128 v[204:207], v18 offset:59392
	ds_read_b128 v[176:179], v16 offset:55296
	ds_read_b128 v[180:183], v16 offset:57344
	ds_read_b128 v[184:187], v16 offset:59392
	ds_read_b128 v[188:191], v16 offset:61440
	v_mfma_f32_16x16x32_f16 v[56:59], v[136:139], v[156:159], v[56:59]
	s_add_u32 m0, s28, 0x8000
	s_nop 0
	global_load_lds_dwordx4 v14, s[4:5]
	s_add_u32 s4, s4, s20
	s_addc_u32 s5, s5, 0
	s_waitcnt lgkmcnt(15)
	v_mfma_f32_16x16x32_f16 v[60:63], v[136:139], v[160:163], v[60:63]
	s_waitcnt lgkmcnt(14)
	v_mfma_f32_16x16x32_f16 v[64:67], v[136:139], v[164:167], v[64:67]
	s_waitcnt lgkmcnt(13)
	v_mfma_f32_16x16x32_f16 v[68:71], v[136:139], v[168:171], v[68:71]
	s_waitcnt lgkmcnt(12)
	v_mfma_f32_16x16x32_f16 v[72:75], v[140:143], v[156:159], v[72:75]
	v_mfma_f32_16x16x32_f16 v[76:79], v[140:143], v[160:163], v[76:79]
	v_mfma_f32_16x16x32_f16 v[80:83], v[140:143], v[164:167], v[80:83]
	s_add_u32 m0, s28, 0x9000
	s_nop 0
	global_load_lds_dwordx4 v10, s[6:7]
	v_mfma_f32_16x16x32_f16 v[84:87], v[140:143], v[168:171], v[84:87]
	s_waitcnt lgkmcnt(11)
	v_mfma_f32_16x16x32_f16 v[88:91], v[144:147], v[156:159], v[88:91]
	v_mfma_f32_16x16x32_f16 v[92:95], v[144:147], v[160:163], v[92:95]
	v_mfma_f32_16x16x32_f16 v[96:99], v[144:147], v[164:167], v[96:99]
	v_mfma_f32_16x16x32_f16 v[100:103], v[144:147], v[168:171], v[100:103]
	s_waitcnt lgkmcnt(10)
	v_mfma_f32_16x16x32_f16 v[104:107], v[148:151], v[156:159], v[104:107]
	v_mfma_f32_16x16x32_f16 v[108:111], v[148:151], v[160:163], v[108:111]
	s_add_u32 m0, s28, 0xb000
	s_nop 0
	global_load_lds_dwordx4 v11, s[6:7]
	s_add_u32 s6, s6, s20
	s_addc_u32 s7, s7, 0
	v_mfma_f32_16x16x32_f16 v[112:115], v[148:151], v[164:167], v[112:115]
	v_mfma_f32_16x16x32_f16 v[116:119], v[148:151], v[168:171], v[116:119]
	s_waitcnt lgkmcnt(9)
	v_mfma_f32_16x16x32_f16 v[120:123], v[152:155], v[156:159], v[120:123]
	v_mfma_f32_16x16x32_f16 v[124:127], v[152:155], v[160:163], v[124:127]
	v_mfma_f32_16x16x32_f16 v[128:131], v[152:155], v[164:167], v[128:131]
	v_mfma_f32_16x16x32_f16 v[132:135], v[152:155], v[168:171], v[132:135]
	s_waitcnt vmcnt(7) lgkmcnt(0)
	s_barrier
	s_waitcnt lgkmcnt(6)
	ds_read_b128 v[136:139], v19
	ds_read_b128 v[156:159], v21
	ds_read_b128 v[160:163], v21 offset:2048
	ds_read_b128 v[164:167], v21 offset:4096
	ds_read_b128 v[168:171], v21 offset:6144
	ds_read_b128 v[140:143], v19 offset:2048
	ds_read_b128 v[144:147], v19 offset:4096
	ds_read_b128 v[148:151], v19 offset:6144
	ds_read_b128 v[152:155], v19 offset:8192
	v_mfma_f32_16x16x32_f16 v[56:59], v[172:175], v[192:195], v[56:59]
	s_add_u32 m0, s28, 0xd000
	s_nop 0
	global_load_lds_dwordx4 v10, s[4:5]
	s_waitcnt lgkmcnt(15)
	v_mfma_f32_16x16x32_f16 v[60:63], v[172:175], v[196:199], v[60:63]
	s_waitcnt lgkmcnt(14)
	v_mfma_f32_16x16x32_f16 v[64:67], v[172:175], v[200:203], v[64:67]
	s_waitcnt lgkmcnt(13)
	v_mfma_f32_16x16x32_f16 v[68:71], v[172:175], v[204:207], v[68:71]
	s_waitcnt lgkmcnt(12)
	v_mfma_f32_16x16x32_f16 v[72:75], v[176:179], v[192:195], v[72:75]
	v_mfma_f32_16x16x32_f16 v[76:79], v[176:179], v[196:199], v[76:79]
	s_add_u32 m0, s28, 0xf000
	s_nop 0
	global_load_lds_dwordx4 v11, s[4:5]
	v_mfma_f32_16x16x32_f16 v[80:83], v[176:179], v[200:203], v[80:83]
	v_mfma_f32_16x16x32_f16 v[84:87], v[176:179], v[204:207], v[84:87]
	s_waitcnt lgkmcnt(11)
	v_mfma_f32_16x16x32_f16 v[88:91], v[180:183], v[192:195], v[88:91]
	v_mfma_f32_16x16x32_f16 v[92:95], v[180:183], v[196:199], v[92:95]
	v_mfma_f32_16x16x32_f16 v[96:99], v[180:183], v[200:203], v[96:99]
	s_add_u32 m0, s28, 0x11000
	s_nop 0
	global_load_lds_dwordx4 v12, s[4:5]
	v_mfma_f32_16x16x32_f16 v[100:103], v[180:183], v[204:207], v[100:103]
	s_waitcnt lgkmcnt(10)
	v_mfma_f32_16x16x32_f16 v[104:107], v[184:187], v[192:195], v[104:107]
	v_mfma_f32_16x16x32_f16 v[108:111], v[184:187], v[196:199], v[108:111]
	v_mfma_f32_16x16x32_f16 v[112:115], v[184:187], v[200:203], v[112:115]
	v_mfma_f32_16x16x32_f16 v[116:119], v[184:187], v[204:207], v[116:119]
	s_add_u32 m0, s28, 0x13000
	s_nop 0
	global_load_lds_dwordx4 v13, s[4:5]
	s_waitcnt lgkmcnt(9)
	v_mfma_f32_16x16x32_f16 v[120:123], v[188:191], v[192:195], v[120:123]
	v_mfma_f32_16x16x32_f16 v[124:127], v[188:191], v[196:199], v[124:127]
	v_mfma_f32_16x16x32_f16 v[128:131], v[188:191], v[200:203], v[128:131]
	v_mfma_f32_16x16x32_f16 v[132:135], v[188:191], v[204:207], v[132:135]
	s_waitcnt lgkmcnt(6)
	ds_read_b128 v[172:175], v20
	ds_read_b128 v[192:195], v22
	ds_read_b128 v[196:199], v22 offset:2048
	ds_read_b128 v[200:203], v22 offset:4096
	ds_read_b128 v[204:207], v22 offset:6144
	ds_read_b128 v[176:179], v20 offset:2048
	ds_read_b128 v[180:183], v20 offset:4096
	ds_read_b128 v[184:187], v20 offset:6144
	ds_read_b128 v[188:191], v20 offset:8192
	v_mfma_f32_16x16x32_f16 v[56:59], v[136:139], v[156:159], v[56:59]
	s_add_u32 m0, s28, 0x15000
	s_nop 0
	global_load_lds_dwordx4 v14, s[4:5]
	s_add_u32 s4, s4, s20
	s_addc_u32 s5, s5, 0
	s_waitcnt lgkmcnt(15)
	v_mfma_f32_16x16x32_f16 v[60:63], v[136:139], v[160:163], v[60:63]
	s_waitcnt lgkmcnt(14)
	v_mfma_f32_16x16x32_f16 v[64:67], v[136:139], v[164:167], v[64:67]
	s_waitcnt lgkmcnt(13)
	v_mfma_f32_16x16x32_f16 v[68:71], v[136:139], v[168:171], v[68:71]
	s_waitcnt lgkmcnt(12)
	v_mfma_f32_16x16x32_f16 v[72:75], v[140:143], v[156:159], v[72:75]
	v_mfma_f32_16x16x32_f16 v[76:79], v[140:143], v[160:163], v[76:79]
	v_mfma_f32_16x16x32_f16 v[80:83], v[140:143], v[164:167], v[80:83]
	s_add_u32 m0, s28, 0x16000
	s_nop 0
	global_load_lds_dwordx4 v10, s[6:7]
	v_mfma_f32_16x16x32_f16 v[84:87], v[140:143], v[168:171], v[84:87]
	s_waitcnt lgkmcnt(11)
	v_mfma_f32_16x16x32_f16 v[88:91], v[144:147], v[156:159], v[88:91]
	v_mfma_f32_16x16x32_f16 v[92:95], v[144:147], v[160:163], v[92:95]
	v_mfma_f32_16x16x32_f16 v[96:99], v[144:147], v[164:167], v[96:99]
	v_mfma_f32_16x16x32_f16 v[100:103], v[144:147], v[168:171], v[100:103]
	s_waitcnt lgkmcnt(10)
	v_mfma_f32_16x16x32_f16 v[104:107], v[148:151], v[156:159], v[104:107]
	v_mfma_f32_16x16x32_f16 v[108:111], v[148:151], v[160:163], v[108:111]
	s_add_u32 m0, s28, 0x18000
	s_nop 0
	global_load_lds_dwordx4 v11, s[6:7]
	s_add_u32 s6, s6, s20
	s_addc_u32 s7, s7, 0
	v_mfma_f32_16x16x32_f16 v[112:115], v[148:151], v[164:167], v[112:115]
	v_mfma_f32_16x16x32_f16 v[116:119], v[148:151], v[168:171], v[116:119]
	s_waitcnt lgkmcnt(9)
	v_mfma_f32_16x16x32_f16 v[120:123], v[152:155], v[156:159], v[120:123]
	v_mfma_f32_16x16x32_f16 v[124:127], v[152:155], v[160:163], v[124:127]
	v_mfma_f32_16x16x32_f16 v[128:131], v[152:155], v[164:167], v[128:131]
	v_mfma_f32_16x16x32_f16 v[132:135], v[152:155], v[168:171], v[132:135]
	s_waitcnt vmcnt(7) lgkmcnt(0)
	s_barrier
	s_waitcnt lgkmcnt(6)
	ds_read_b128 v[136:139], v15
	ds_read_b128 v[156:159], v17
	ds_read_b128 v[160:163], v17 offset:2048
	ds_read_b128 v[164:167], v17 offset:4096
	ds_read_b128 v[168:171], v17 offset:6144
	ds_read_b128 v[140:143], v15 offset:2048
	ds_read_b128 v[144:147], v15 offset:4096
	ds_read_b128 v[148:151], v15 offset:6144
	ds_read_b128 v[152:155], v15 offset:8192
	v_mfma_f32_16x16x32_f16 v[56:59], v[172:175], v[192:195], v[56:59]
	s_add_u32 m0, s28, 0x1a000
	s_nop 0
	global_load_lds_dwordx4 v10, s[4:5]
	s_waitcnt lgkmcnt(15)
	v_mfma_f32_16x16x32_f16 v[60:63], v[172:175], v[196:199], v[60:63]
	s_waitcnt lgkmcnt(14)
	v_mfma_f32_16x16x32_f16 v[64:67], v[172:175], v[200:203], v[64:67]
	s_waitcnt lgkmcnt(13)
	v_mfma_f32_16x16x32_f16 v[68:71], v[172:175], v[204:207], v[68:71]
	s_waitcnt lgkmcnt(12)
	v_mfma_f32_16x16x32_f16 v[72:75], v[176:179], v[192:195], v[72:75]
	v_mfma_f32_16x16x32_f16 v[76:79], v[176:179], v[196:199], v[76:79]
	s_add_u32 m0, s28, 0x1c000
	s_nop 0
	global_load_lds_dwordx4 v11, s[4:5]
	v_mfma_f32_16x16x32_f16 v[80:83], v[176:179], v[200:203], v[80:83]
	v_mfma_f32_16x16x32_f16 v[84:87], v[176:179], v[204:207], v[84:87]
	s_waitcnt lgkmcnt(11)
	v_mfma_f32_16x16x32_f16 v[88:91], v[180:183], v[192:195], v[88:91]
	v_mfma_f32_16x16x32_f16 v[92:95], v[180:183], v[196:199], v[92:95]
	v_mfma_f32_16x16x32_f16 v[96:99], v[180:183], v[200:203], v[96:99]
	s_add_u32 m0, s28, 0x1e000
	s_nop 0
	global_load_lds_dwordx4 v12, s[4:5]
	v_mfma_f32_16x16x32_f16 v[100:103], v[180:183], v[204:207], v[100:103]
	s_waitcnt lgkmcnt(10)
	v_mfma_f32_16x16x32_f16 v[104:107], v[184:187], v[192:195], v[104:107]
	v_mfma_f32_16x16x32_f16 v[108:111], v[184:187], v[196:199], v[108:111]
	v_mfma_f32_16x16x32_f16 v[112:115], v[184:187], v[200:203], v[112:115]
	v_mfma_f32_16x16x32_f16 v[116:119], v[184:187], v[204:207], v[116:119]
	s_add_u32 m0, s28, 0x20000
	s_nop 0
	global_load_lds_dwordx4 v13, s[4:5]
	s_waitcnt lgkmcnt(9)
	v_mfma_f32_16x16x32_f16 v[120:123], v[188:191], v[192:195], v[120:123]
	v_mfma_f32_16x16x32_f16 v[124:127], v[188:191], v[196:199], v[124:127]
	v_mfma_f32_16x16x32_f16 v[128:131], v[188:191], v[200:203], v[128:131]
	v_mfma_f32_16x16x32_f16 v[132:135], v[188:191], v[204:207], v[132:135]
	s_waitcnt lgkmcnt(6)
	ds_read_b128 v[172:175], v16
	ds_read_b128 v[192:195], v18
	ds_read_b128 v[196:199], v18 offset:2048
	ds_read_b128 v[200:203], v18 offset:4096
	ds_read_b128 v[204:207], v18 offset:6144
	ds_read_b128 v[176:179], v16 offset:2048
	ds_read_b128 v[180:183], v16 offset:4096
	ds_read_b128 v[184:187], v16 offset:6144
	ds_read_b128 v[188:191], v16 offset:8192
	v_mfma_f32_16x16x32_f16 v[56:59], v[136:139], v[156:159], v[56:59]
	s_add_u32 m0, s28, 0x22000
	s_nop 0
	global_load_lds_dwordx4 v14, s[4:5]
	s_add_u32 s4, s4, s20
	s_addc_u32 s5, s5, 0
	s_waitcnt lgkmcnt(15)
	v_mfma_f32_16x16x32_f16 v[60:63], v[136:139], v[160:163], v[60:63]
	s_waitcnt lgkmcnt(14)
	v_mfma_f32_16x16x32_f16 v[64:67], v[136:139], v[164:167], v[64:67]
	s_waitcnt lgkmcnt(13)
	v_mfma_f32_16x16x32_f16 v[68:71], v[136:139], v[168:171], v[68:71]
	s_waitcnt lgkmcnt(12)
	v_mfma_f32_16x16x32_f16 v[72:75], v[140:143], v[156:159], v[72:75]
	v_mfma_f32_16x16x32_f16 v[76:79], v[140:143], v[160:163], v[76:79]
	v_mfma_f32_16x16x32_f16 v[80:83], v[140:143], v[164:167], v[80:83]
	s_add_u32 m0, s28, 0x23000
	s_nop 0
	global_load_lds_dwordx4 v10, s[6:7]
	v_mfma_f32_16x16x32_f16 v[84:87], v[140:143], v[168:171], v[84:87]
	s_waitcnt lgkmcnt(11)
	v_mfma_f32_16x16x32_f16 v[88:91], v[144:147], v[156:159], v[88:91]
	v_mfma_f32_16x16x32_f16 v[92:95], v[144:147], v[160:163], v[92:95]
	v_mfma_f32_16x16x32_f16 v[96:99], v[144:147], v[164:167], v[96:99]
	v_mfma_f32_16x16x32_f16 v[100:103], v[144:147], v[168:171], v[100:103]
	s_waitcnt lgkmcnt(10)
	v_mfma_f32_16x16x32_f16 v[104:107], v[148:151], v[156:159], v[104:107]
	v_mfma_f32_16x16x32_f16 v[108:111], v[148:151], v[160:163], v[108:111]
	s_add_u32 m0, s28, 0x25000
	s_nop 0
	global_load_lds_dwordx4 v11, s[6:7]
	s_add_u32 s6, s6, s20
	s_addc_u32 s7, s7, 0
	v_mfma_f32_16x16x32_f16 v[112:115], v[148:151], v[164:167], v[112:115]
	v_mfma_f32_16x16x32_f16 v[116:119], v[148:151], v[168:171], v[116:119]
	s_waitcnt lgkmcnt(9)
	v_mfma_f32_16x16x32_f16 v[120:123], v[152:155], v[156:159], v[120:123]
	v_mfma_f32_16x16x32_f16 v[124:127], v[152:155], v[160:163], v[124:127]
	v_mfma_f32_16x16x32_f16 v[128:131], v[152:155], v[164:167], v[128:131]
	v_mfma_f32_16x16x32_f16 v[132:135], v[152:155], v[168:171], v[132:135]
	s_waitcnt vmcnt(7) lgkmcnt(0)
	s_barrier
	s_waitcnt lgkmcnt(6)
	ds_read_b128 v[136:139], v15 offset:53248
	ds_read_b128 v[156:159], v17 offset:53248
	ds_read_b128 v[160:163], v17 offset:55296
	ds_read_b128 v[164:167], v17 offset:57344
	ds_read_b128 v[168:171], v17 offset:59392
	ds_read_b128 v[140:143], v15 offset:55296
	ds_read_b128 v[144:147], v15 offset:57344
	ds_read_b128 v[148:151], v15 offset:59392
	ds_read_b128 v[152:155], v15 offset:61440
	v_mfma_f32_16x16x32_f16 v[56:59], v[172:175], v[192:195], v[56:59]
	s_add_u32 m0, s28, 0x0
	s_nop 0
	global_load_lds_dwordx4 v10, s[4:5]
	s_waitcnt lgkmcnt(15)
	v_mfma_f32_16x16x32_f16 v[60:63], v[172:175], v[196:199], v[60:63]
	s_waitcnt lgkmcnt(14)
	v_mfma_f32_16x16x32_f16 v[64:67], v[172:175], v[200:203], v[64:67]
	s_waitcnt lgkmcnt(13)
	v_mfma_f32_16x16x32_f16 v[68:71], v[172:175], v[204:207], v[68:71]
	s_waitcnt lgkmcnt(12)
	v_mfma_f32_16x16x32_f16 v[72:75], v[176:179], v[192:195], v[72:75]
	v_mfma_f32_16x16x32_f16 v[76:79], v[176:179], v[196:199], v[76:79]
	s_add_u32 m0, s28, 0x2000
	s_nop 0
	global_load_lds_dwordx4 v11, s[4:5]
	v_mfma_f32_16x16x32_f16 v[80:83], v[176:179], v[200:203], v[80:83]
	v_mfma_f32_16x16x32_f16 v[84:87], v[176:179], v[204:207], v[84:87]
	s_waitcnt lgkmcnt(11)
	v_mfma_f32_16x16x32_f16 v[88:91], v[180:183], v[192:195], v[88:91]
	v_mfma_f32_16x16x32_f16 v[92:95], v[180:183], v[196:199], v[92:95]
	v_mfma_f32_16x16x32_f16 v[96:99], v[180:183], v[200:203], v[96:99]
	s_add_u32 m0, s28, 0x4000
	s_nop 0
	global_load_lds_dwordx4 v12, s[4:5]
	v_mfma_f32_16x16x32_f16 v[100:103], v[180:183], v[204:207], v[100:103]
	s_waitcnt lgkmcnt(10)
	v_mfma_f32_16x16x32_f16 v[104:107], v[184:187], v[192:195], v[104:107]
	v_mfma_f32_16x16x32_f16 v[108:111], v[184:187], v[196:199], v[108:111]
	v_mfma_f32_16x16x32_f16 v[112:115], v[184:187], v[200:203], v[112:115]
	v_mfma_f32_16x16x32_f16 v[116:119], v[184:187], v[204:207], v[116:119]
	s_add_u32 m0, s28, 0x6000
	s_nop 0
	global_load_lds_dwordx4 v13, s[4:5]
	s_waitcnt lgkmcnt(9)
	v_mfma_f32_16x16x32_f16 v[120:123], v[188:191], v[192:195], v[120:123]
	v_mfma_f32_16x16x32_f16 v[124:127], v[188:191], v[196:199], v[124:127]
	v_mfma_f32_16x16x32_f16 v[128:131], v[188:191], v[200:203], v[128:131]
	v_mfma_f32_16x16x32_f16 v[132:135], v[188:191], v[204:207], v[132:135]
	s_waitcnt lgkmcnt(6)
	ds_read_b128 v[172:175], v16 offset:53248
	ds_read_b128 v[192:195], v18 offset:53248
	ds_read_b128 v[196:199], v18 offset:55296
	ds_read_b128 v[200:203], v18 offset:57344
	ds_read_b128 v[204:207], v18 offset:59392
	ds_read_b128 v[176:179], v16 offset:55296
	ds_read_b128 v[180:183], v16 offset:57344
	ds_read_b128 v[184:187], v16 offset:59392
	ds_read_b128 v[188:191], v16 offset:61440
	v_mfma_f32_16x16x32_f16 v[56:59], v[136:139], v[156:159], v[56:59]
	s_add_u32 m0, s28, 0x8000
	s_nop 0
	global_load_lds_dwordx4 v14, s[4:5]
	s_add_u32 s4, s4, s20
	s_addc_u32 s5, s5, 0
	s_waitcnt lgkmcnt(15)
	v_mfma_f32_16x16x32_f16 v[60:63], v[136:139], v[160:163], v[60:63]
	s_waitcnt lgkmcnt(14)
	v_mfma_f32_16x16x32_f16 v[64:67], v[136:139], v[164:167], v[64:67]
	s_waitcnt lgkmcnt(13)
	v_mfma_f32_16x16x32_f16 v[68:71], v[136:139], v[168:171], v[68:71]
	s_waitcnt lgkmcnt(12)
	v_mfma_f32_16x16x32_f16 v[72:75], v[140:143], v[156:159], v[72:75]
	v_mfma_f32_16x16x32_f16 v[76:79], v[140:143], v[160:163], v[76:79]
	v_mfma_f32_16x16x32_f16 v[80:83], v[140:143], v[164:167], v[80:83]
	s_add_u32 m0, s28, 0x9000
	s_nop 0
	global_load_lds_dwordx4 v10, s[6:7]
	v_mfma_f32_16x16x32_f16 v[84:87], v[140:143], v[168:171], v[84:87]
	s_waitcnt lgkmcnt(11)
	v_mfma_f32_16x16x32_f16 v[88:91], v[144:147], v[156:159], v[88:91]
	v_mfma_f32_16x16x32_f16 v[92:95], v[144:147], v[160:163], v[92:95]
	v_mfma_f32_16x16x32_f16 v[96:99], v[144:147], v[164:167], v[96:99]
	v_mfma_f32_16x16x32_f16 v[100:103], v[144:147], v[168:171], v[100:103]
	s_waitcnt lgkmcnt(10)
	v_mfma_f32_16x16x32_f16 v[104:107], v[148:151], v[156:159], v[104:107]
	v_mfma_f32_16x16x32_f16 v[108:111], v[148:151], v[160:163], v[108:111]
	s_add_u32 m0, s28, 0xb000
	s_nop 0
	global_load_lds_dwordx4 v11, s[6:7]
	s_add_u32 s6, s6, s20
	s_addc_u32 s7, s7, 0
	v_mfma_f32_16x16x32_f16 v[112:115], v[148:151], v[164:167], v[112:115]
	v_mfma_f32_16x16x32_f16 v[116:119], v[148:151], v[168:171], v[116:119]
	s_waitcnt lgkmcnt(9)
	v_mfma_f32_16x16x32_f16 v[120:123], v[152:155], v[156:159], v[120:123]
	v_mfma_f32_16x16x32_f16 v[124:127], v[152:155], v[160:163], v[124:127]
	v_mfma_f32_16x16x32_f16 v[128:131], v[152:155], v[164:167], v[128:131]
	v_mfma_f32_16x16x32_f16 v[132:135], v[152:155], v[168:171], v[132:135]
	s_waitcnt vmcnt(7) lgkmcnt(0)
	s_barrier
	s_waitcnt lgkmcnt(6)
	ds_read_b128 v[136:139], v19
	ds_read_b128 v[156:159], v21
	ds_read_b128 v[160:163], v21 offset:2048
	ds_read_b128 v[164:167], v21 offset:4096
	ds_read_b128 v[168:171], v21 offset:6144
	ds_read_b128 v[140:143], v19 offset:2048
	ds_read_b128 v[144:147], v19 offset:4096
	ds_read_b128 v[148:151], v19 offset:6144
	ds_read_b128 v[152:155], v19 offset:8192
	v_mfma_f32_16x16x32_f16 v[56:59], v[172:175], v[192:195], v[56:59]
	s_add_u32 m0, s28, 0xd000
	s_nop 0
	global_load_lds_dwordx4 v10, s[4:5]
	s_waitcnt lgkmcnt(15)
	v_mfma_f32_16x16x32_f16 v[60:63], v[172:175], v[196:199], v[60:63]
	s_waitcnt lgkmcnt(14)
	v_mfma_f32_16x16x32_f16 v[64:67], v[172:175], v[200:203], v[64:67]
	s_waitcnt lgkmcnt(13)
	v_mfma_f32_16x16x32_f16 v[68:71], v[172:175], v[204:207], v[68:71]
	s_waitcnt lgkmcnt(12)
	v_mfma_f32_16x16x32_f16 v[72:75], v[176:179], v[192:195], v[72:75]
	v_mfma_f32_16x16x32_f16 v[76:79], v[176:179], v[196:199], v[76:79]
	s_add_u32 m0, s28, 0xf000
	s_nop 0
	global_load_lds_dwordx4 v11, s[4:5]
	v_mfma_f32_16x16x32_f16 v[80:83], v[176:179], v[200:203], v[80:83]
	v_mfma_f32_16x16x32_f16 v[84:87], v[176:179], v[204:207], v[84:87]
	s_waitcnt lgkmcnt(11)
	v_mfma_f32_16x16x32_f16 v[88:91], v[180:183], v[192:195], v[88:91]
	v_mfma_f32_16x16x32_f16 v[92:95], v[180:183], v[196:199], v[92:95]
	v_mfma_f32_16x16x32_f16 v[96:99], v[180:183], v[200:203], v[96:99]
	s_add_u32 m0, s28, 0x11000
	s_nop 0
	global_load_lds_dwordx4 v12, s[4:5]
	v_mfma_f32_16x16x32_f16 v[100:103], v[180:183], v[204:207], v[100:103]
	s_waitcnt lgkmcnt(10)
	v_mfma_f32_16x16x32_f16 v[104:107], v[184:187], v[192:195], v[104:107]
	v_mfma_f32_16x16x32_f16 v[108:111], v[184:187], v[196:199], v[108:111]
	v_mfma_f32_16x16x32_f16 v[112:115], v[184:187], v[200:203], v[112:115]
	v_mfma_f32_16x16x32_f16 v[116:119], v[184:187], v[204:207], v[116:119]
	s_add_u32 m0, s28, 0x13000
	s_nop 0
	global_load_lds_dwordx4 v13, s[4:5]
	s_waitcnt lgkmcnt(9)
	v_mfma_f32_16x16x32_f16 v[120:123], v[188:191], v[192:195], v[120:123]
	v_mfma_f32_16x16x32_f16 v[124:127], v[188:191], v[196:199], v[124:127]
	v_mfma_f32_16x16x32_f16 v[128:131], v[188:191], v[200:203], v[128:131]
	v_mfma_f32_16x16x32_f16 v[132:135], v[188:191], v[204:207], v[132:135]
	s_waitcnt lgkmcnt(6)
	ds_read_b128 v[172:175], v20
	ds_read_b128 v[192:195], v22
	ds_read_b128 v[196:199], v22 offset:2048
	ds_read_b128 v[200:203], v22 offset:4096
	ds_read_b128 v[204:207], v22 offset:6144
	ds_read_b128 v[176:179], v20 offset:2048
	ds_read_b128 v[180:183], v20 offset:4096
	ds_read_b128 v[184:187], v20 offset:6144
	ds_read_b128 v[188:191], v20 offset:8192
	v_mfma_f32_16x16x32_f16 v[56:59], v[136:139], v[156:159], v[56:59]
	s_add_u32 m0, s28, 0x15000
	s_nop 0
	global_load_lds_dwordx4 v14, s[4:5]
	s_add_u32 s4, s4, s20
	s_addc_u32 s5, s5, 0
	s_waitcnt lgkmcnt(15)
	v_mfma_f32_16x16x32_f16 v[60:63], v[136:139], v[160:163], v[60:63]
	s_waitcnt lgkmcnt(14)
	v_mfma_f32_16x16x32_f16 v[64:67], v[136:139], v[164:167], v[64:67]
	s_waitcnt lgkmcnt(13)
	v_mfma_f32_16x16x32_f16 v[68:71], v[136:139], v[168:171], v[68:71]
	s_waitcnt lgkmcnt(12)
	v_mfma_f32_16x16x32_f16 v[72:75], v[140:143], v[156:159], v[72:75]
	v_mfma_f32_16x16x32_f16 v[76:79], v[140:143], v[160:163], v[76:79]
	v_mfma_f32_16x16x32_f16 v[80:83], v[140:143], v[164:167], v[80:83]
	s_add_u32 m0, s28, 0x16000
	s_nop 0
	global_load_lds_dwordx4 v10, s[6:7]
	v_mfma_f32_16x16x32_f16 v[84:87], v[140:143], v[168:171], v[84:87]
	s_waitcnt lgkmcnt(11)
	v_mfma_f32_16x16x32_f16 v[88:91], v[144:147], v[156:159], v[88:91]
	v_mfma_f32_16x16x32_f16 v[92:95], v[144:147], v[160:163], v[92:95]
	v_mfma_f32_16x16x32_f16 v[96:99], v[144:147], v[164:167], v[96:99]
	v_mfma_f32_16x16x32_f16 v[100:103], v[144:147], v[168:171], v[100:103]
	s_waitcnt lgkmcnt(10)
	v_mfma_f32_16x16x32_f16 v[104:107], v[148:151], v[156:159], v[104:107]
	v_mfma_f32_16x16x32_f16 v[108:111], v[148:151], v[160:163], v[108:111]
	s_add_u32 m0, s28, 0x18000
	s_nop 0
	global_load_lds_dwordx4 v11, s[6:7]
	s_add_u32 s6, s6, s20
	s_addc_u32 s7, s7, 0
	v_mfma_f32_16x16x32_f16 v[112:115], v[148:151], v[164:167], v[112:115]
	v_mfma_f32_16x16x32_f16 v[116:119], v[148:151], v[168:171], v[116:119]
	s_waitcnt lgkmcnt(9)
	v_mfma_f32_16x16x32_f16 v[120:123], v[152:155], v[156:159], v[120:123]
	v_mfma_f32_16x16x32_f16 v[124:127], v[152:155], v[160:163], v[124:127]
	v_mfma_f32_16x16x32_f16 v[128:131], v[152:155], v[164:167], v[128:131]
	v_mfma_f32_16x16x32_f16 v[132:135], v[152:155], v[168:171], v[132:135]
	s_waitcnt vmcnt(7) lgkmcnt(0)
	s_barrier
	s_waitcnt lgkmcnt(6)
	ds_read_b128 v[136:139], v15
	ds_read_b128 v[156:159], v17
	ds_read_b128 v[160:163], v17 offset:2048
	ds_read_b128 v[164:167], v17 offset:4096
	ds_read_b128 v[168:171], v17 offset:6144
	ds_read_b128 v[140:143], v15 offset:2048
	ds_read_b128 v[144:147], v15 offset:4096
	ds_read_b128 v[148:151], v15 offset:6144
	ds_read_b128 v[152:155], v15 offset:8192
	v_mfma_f32_16x16x32_f16 v[56:59], v[172:175], v[192:195], v[56:59]
	s_add_u32 m0, s28, 0x1a000
	s_nop 0
	global_load_lds_dwordx4 v10, s[4:5]
	s_waitcnt lgkmcnt(15)
	v_mfma_f32_16x16x32_f16 v[60:63], v[172:175], v[196:199], v[60:63]
	s_waitcnt lgkmcnt(14)
	v_mfma_f32_16x16x32_f16 v[64:67], v[172:175], v[200:203], v[64:67]
	s_waitcnt lgkmcnt(13)
	v_mfma_f32_16x16x32_f16 v[68:71], v[172:175], v[204:207], v[68:71]
	s_waitcnt lgkmcnt(12)
	v_mfma_f32_16x16x32_f16 v[72:75], v[176:179], v[192:195], v[72:75]
	v_mfma_f32_16x16x32_f16 v[76:79], v[176:179], v[196:199], v[76:79]
	s_add_u32 m0, s28, 0x1c000
	s_nop 0
	global_load_lds_dwordx4 v11, s[4:5]
	v_mfma_f32_16x16x32_f16 v[80:83], v[176:179], v[200:203], v[80:83]
	v_mfma_f32_16x16x32_f16 v[84:87], v[176:179], v[204:207], v[84:87]
	s_waitcnt lgkmcnt(11)
	v_mfma_f32_16x16x32_f16 v[88:91], v[180:183], v[192:195], v[88:91]
	v_mfma_f32_16x16x32_f16 v[92:95], v[180:183], v[196:199], v[92:95]
	v_mfma_f32_16x16x32_f16 v[96:99], v[180:183], v[200:203], v[96:99]
	s_add_u32 m0, s28, 0x1e000
	s_nop 0
	global_load_lds_dwordx4 v12, s[4:5]
	v_mfma_f32_16x16x32_f16 v[100:103], v[180:183], v[204:207], v[100:103]
	s_waitcnt lgkmcnt(10)
	v_mfma_f32_16x16x32_f16 v[104:107], v[184:187], v[192:195], v[104:107]
	v_mfma_f32_16x16x32_f16 v[108:111], v[184:187], v[196:199], v[108:111]
	v_mfma_f32_16x16x32_f16 v[112:115], v[184:187], v[200:203], v[112:115]
	v_mfma_f32_16x16x32_f16 v[116:119], v[184:187], v[204:207], v[116:119]
	s_add_u32 m0, s28, 0x20000
	s_nop 0
	global_load_lds_dwordx4 v13, s[4:5]
	s_waitcnt lgkmcnt(9)
	v_mfma_f32_16x16x32_f16 v[120:123], v[188:191], v[192:195], v[120:123]
	v_mfma_f32_16x16x32_f16 v[124:127], v[188:191], v[196:199], v[124:127]
	v_mfma_f32_16x16x32_f16 v[128:131], v[188:191], v[200:203], v[128:131]
	v_mfma_f32_16x16x32_f16 v[132:135], v[188:191], v[204:207], v[132:135]
	s_waitcnt lgkmcnt(6)
	ds_read_b128 v[172:175], v16
	ds_read_b128 v[192:195], v18
	ds_read_b128 v[196:199], v18 offset:2048
	ds_read_b128 v[200:203], v18 offset:4096
	ds_read_b128 v[204:207], v18 offset:6144
	ds_read_b128 v[176:179], v16 offset:2048
	ds_read_b128 v[180:183], v16 offset:4096
	ds_read_b128 v[184:187], v16 offset:6144
	ds_read_b128 v[188:191], v16 offset:8192
	v_mfma_f32_16x16x32_f16 v[56:59], v[136:139], v[156:159], v[56:59]
	s_add_u32 m0, s28, 0x22000
	s_nop 0
	global_load_lds_dwordx4 v14, s[4:5]
	s_add_u32 s4, s4, s20
	s_addc_u32 s5, s5, 0
	s_waitcnt lgkmcnt(15)
	v_mfma_f32_16x16x32_f16 v[60:63], v[136:139], v[160:163], v[60:63]
	s_waitcnt lgkmcnt(14)
	v_mfma_f32_16x16x32_f16 v[64:67], v[136:139], v[164:167], v[64:67]
	s_waitcnt lgkmcnt(13)
	v_mfma_f32_16x16x32_f16 v[68:71], v[136:139], v[168:171], v[68:71]
	s_waitcnt lgkmcnt(12)
	v_mfma_f32_16x16x32_f16 v[72:75], v[140:143], v[156:159], v[72:75]
	v_mfma_f32_16x16x32_f16 v[76:79], v[140:143], v[160:163], v[76:79]
	v_mfma_f32_16x16x32_f16 v[80:83], v[140:143], v[164:167], v[80:83]
	s_add_u32 m0, s28, 0x23000
	s_nop 0
	global_load_lds_dwordx4 v10, s[6:7]
	v_mfma_f32_16x16x32_f16 v[84:87], v[140:143], v[168:171], v[84:87]
	s_waitcnt lgkmcnt(11)
	v_mfma_f32_16x16x32_f16 v[88:91], v[144:147], v[156:159], v[88:91]
	v_mfma_f32_16x16x32_f16 v[92:95], v[144:147], v[160:163], v[92:95]
	v_mfma_f32_16x16x32_f16 v[96:99], v[144:147], v[164:167], v[96:99]
	v_mfma_f32_16x16x32_f16 v[100:103], v[144:147], v[168:171], v[100:103]
	s_waitcnt lgkmcnt(10)
	v_mfma_f32_16x16x32_f16 v[104:107], v[148:151], v[156:159], v[104:107]
	v_mfma_f32_16x16x32_f16 v[108:111], v[148:151], v[160:163], v[108:111]
	s_add_u32 m0, s28, 0x25000
	s_nop 0
	global_load_lds_dwordx4 v11, s[6:7]
	s_add_u32 s6, s6, s20
	s_addc_u32 s7, s7, 0
	v_mfma_f32_16x16x32_f16 v[112:115], v[148:151], v[164:167], v[112:115]
	v_mfma_f32_16x16x32_f16 v[116:119], v[148:151], v[168:171], v[116:119]
	s_waitcnt lgkmcnt(9)
	v_mfma_f32_16x16x32_f16 v[120:123], v[152:155], v[156:159], v[120:123]
	v_mfma_f32_16x16x32_f16 v[124:127], v[152:155], v[160:163], v[124:127]
	v_mfma_f32_16x16x32_f16 v[128:131], v[152:155], v[164:167], v[128:131]
	v_mfma_f32_16x16x32_f16 v[132:135], v[152:155], v[168:171], v[132:135]
	s_waitcnt vmcnt(7) lgkmcnt(0)
	s_barrier
	s_waitcnt lgkmcnt(6)
	ds_read_b128 v[136:139], v15 offset:53248
	ds_read_b128 v[156:159], v17 offset:53248
	ds_read_b128 v[160:163], v17 offset:55296
	ds_read_b128 v[164:167], v17 offset:57344
	ds_read_b128 v[168:171], v17 offset:59392
	ds_read_b128 v[140:143], v15 offset:55296
	ds_read_b128 v[144:147], v15 offset:57344
	ds_read_b128 v[148:151], v15 offset:59392
	ds_read_b128 v[152:155], v15 offset:61440
	v_mfma_f32_16x16x32_f16 v[56:59], v[172:175], v[192:195], v[56:59]
	s_add_u32 m0, s28, 0x0
	s_nop 0
	global_load_lds_dwordx4 v10, s[4:5]
	s_waitcnt lgkmcnt(15)
	v_mfma_f32_16x16x32_f16 v[60:63], v[172:175], v[196:199], v[60:63]
	s_waitcnt lgkmcnt(14)
	v_mfma_f32_16x16x32_f16 v[64:67], v[172:175], v[200:203], v[64:67]
	s_waitcnt lgkmcnt(13)
	v_mfma_f32_16x16x32_f16 v[68:71], v[172:175], v[204:207], v[68:71]
	s_waitcnt lgkmcnt(12)
	v_mfma_f32_16x16x32_f16 v[72:75], v[176:179], v[192:195], v[72:75]
	v_mfma_f32_16x16x32_f16 v[76:79], v[176:179], v[196:199], v[76:79]
	s_add_u32 m0, s28, 0x2000
	s_nop 0
	global_load_lds_dwordx4 v11, s[4:5]
	v_mfma_f32_16x16x32_f16 v[80:83], v[176:179], v[200:203], v[80:83]
	v_mfma_f32_16x16x32_f16 v[84:87], v[176:179], v[204:207], v[84:87]
	s_waitcnt lgkmcnt(11)
	v_mfma_f32_16x16x32_f16 v[88:91], v[180:183], v[192:195], v[88:91]
	v_mfma_f32_16x16x32_f16 v[92:95], v[180:183], v[196:199], v[92:95]
	v_mfma_f32_16x16x32_f16 v[96:99], v[180:183], v[200:203], v[96:99]
	s_add_u32 m0, s28, 0x4000
	s_nop 0
	global_load_lds_dwordx4 v12, s[4:5]
	v_mfma_f32_16x16x32_f16 v[100:103], v[180:183], v[204:207], v[100:103]
	s_waitcnt lgkmcnt(10)
	v_mfma_f32_16x16x32_f16 v[104:107], v[184:187], v[192:195], v[104:107]
	v_mfma_f32_16x16x32_f16 v[108:111], v[184:187], v[196:199], v[108:111]
	v_mfma_f32_16x16x32_f16 v[112:115], v[184:187], v[200:203], v[112:115]
	v_mfma_f32_16x16x32_f16 v[116:119], v[184:187], v[204:207], v[116:119]
	s_add_u32 m0, s28, 0x6000
	s_nop 0
	global_load_lds_dwordx4 v13, s[4:5]
	s_waitcnt lgkmcnt(9)
	v_mfma_f32_16x16x32_f16 v[120:123], v[188:191], v[192:195], v[120:123]
	v_mfma_f32_16x16x32_f16 v[124:127], v[188:191], v[196:199], v[124:127]
	v_mfma_f32_16x16x32_f16 v[128:131], v[188:191], v[200:203], v[128:131]
	v_mfma_f32_16x16x32_f16 v[132:135], v[188:191], v[204:207], v[132:135]
	s_waitcnt lgkmcnt(6)
	ds_read_b128 v[172:175], v16 offset:53248
	ds_read_b128 v[192:195], v18 offset:53248
	ds_read_b128 v[196:199], v18 offset:55296
	ds_read_b128 v[200:203], v18 offset:57344
	ds_read_b128 v[204:207], v18 offset:59392
	ds_read_b128 v[176:179], v16 offset:55296
	ds_read_b128 v[180:183], v16 offset:57344
	ds_read_b128 v[184:187], v16 offset:59392
	ds_read_b128 v[188:191], v16 offset:61440
	v_mfma_f32_16x16x32_f16 v[56:59], v[136:139], v[156:159], v[56:59]
	s_add_u32 m0, s28, 0x8000
	s_nop 0
	global_load_lds_dwordx4 v14, s[4:5]
	s_add_u32 s4, s4, s20
	s_addc_u32 s5, s5, 0
	s_waitcnt lgkmcnt(15)
	v_mfma_f32_16x16x32_f16 v[60:63], v[136:139], v[160:163], v[60:63]
	s_waitcnt lgkmcnt(14)
	v_mfma_f32_16x16x32_f16 v[64:67], v[136:139], v[164:167], v[64:67]
	s_waitcnt lgkmcnt(13)
	v_mfma_f32_16x16x32_f16 v[68:71], v[136:139], v[168:171], v[68:71]
	s_waitcnt lgkmcnt(12)
	v_mfma_f32_16x16x32_f16 v[72:75], v[140:143], v[156:159], v[72:75]
	v_mfma_f32_16x16x32_f16 v[76:79], v[140:143], v[160:163], v[76:79]
	v_mfma_f32_16x16x32_f16 v[80:83], v[140:143], v[164:167], v[80:83]
	s_add_u32 m0, s28, 0x9000
	s_nop 0
	global_load_lds_dwordx4 v10, s[6:7]
	v_mfma_f32_16x16x32_f16 v[84:87], v[140:143], v[168:171], v[84:87]
	s_waitcnt lgkmcnt(11)
	v_mfma_f32_16x16x32_f16 v[88:91], v[144:147], v[156:159], v[88:91]
	v_mfma_f32_16x16x32_f16 v[92:95], v[144:147], v[160:163], v[92:95]
	v_mfma_f32_16x16x32_f16 v[96:99], v[144:147], v[164:167], v[96:99]
	v_mfma_f32_16x16x32_f16 v[100:103], v[144:147], v[168:171], v[100:103]
	s_waitcnt lgkmcnt(10)
	v_mfma_f32_16x16x32_f16 v[104:107], v[148:151], v[156:159], v[104:107]
	v_mfma_f32_16x16x32_f16 v[108:111], v[148:151], v[160:163], v[108:111]
	s_add_u32 m0, s28, 0xb000
	s_nop 0
	global_load_lds_dwordx4 v11, s[6:7]
	s_add_u32 s6, s6, s20
	s_addc_u32 s7, s7, 0
	v_mfma_f32_16x16x32_f16 v[112:115], v[148:151], v[164:167], v[112:115]
	v_mfma_f32_16x16x32_f16 v[116:119], v[148:151], v[168:171], v[116:119]
	s_waitcnt lgkmcnt(9)
	v_mfma_f32_16x16x32_f16 v[120:123], v[152:155], v[156:159], v[120:123]
	v_mfma_f32_16x16x32_f16 v[124:127], v[152:155], v[160:163], v[124:127]
	v_mfma_f32_16x16x32_f16 v[128:131], v[152:155], v[164:167], v[128:131]
	v_mfma_f32_16x16x32_f16 v[132:135], v[152:155], v[168:171], v[132:135]
	s_waitcnt vmcnt(7) lgkmcnt(0)
	s_barrier
	s_waitcnt lgkmcnt(6)
	ds_read_b128 v[136:139], v19
	ds_read_b128 v[156:159], v21
	ds_read_b128 v[160:163], v21 offset:2048
	ds_read_b128 v[164:167], v21 offset:4096
	ds_read_b128 v[168:171], v21 offset:6144
	ds_read_b128 v[140:143], v19 offset:2048
	ds_read_b128 v[144:147], v19 offset:4096
	ds_read_b128 v[148:151], v19 offset:6144
	ds_read_b128 v[152:155], v19 offset:8192
	v_mfma_f32_16x16x32_f16 v[56:59], v[172:175], v[192:195], v[56:59]
	s_add_u32 m0, s28, 0xd000
	s_nop 0
	global_load_lds_dwordx4 v10, s[4:5]
	s_waitcnt lgkmcnt(15)
	v_mfma_f32_16x16x32_f16 v[60:63], v[172:175], v[196:199], v[60:63]
	s_waitcnt lgkmcnt(14)
	v_mfma_f32_16x16x32_f16 v[64:67], v[172:175], v[200:203], v[64:67]
	s_waitcnt lgkmcnt(13)
	v_mfma_f32_16x16x32_f16 v[68:71], v[172:175], v[204:207], v[68:71]
	s_waitcnt lgkmcnt(12)
	v_mfma_f32_16x16x32_f16 v[72:75], v[176:179], v[192:195], v[72:75]
	v_mfma_f32_16x16x32_f16 v[76:79], v[176:179], v[196:199], v[76:79]
	s_add_u32 m0, s28, 0xf000
	s_nop 0
	global_load_lds_dwordx4 v11, s[4:5]
	v_mfma_f32_16x16x32_f16 v[80:83], v[176:179], v[200:203], v[80:83]
	v_mfma_f32_16x16x32_f16 v[84:87], v[176:179], v[204:207], v[84:87]
	s_waitcnt lgkmcnt(11)
	v_mfma_f32_16x16x32_f16 v[88:91], v[180:183], v[192:195], v[88:91]
	v_mfma_f32_16x16x32_f16 v[92:95], v[180:183], v[196:199], v[92:95]
	v_mfma_f32_16x16x32_f16 v[96:99], v[180:183], v[200:203], v[96:99]
	s_add_u32 m0, s28, 0x11000
	s_nop 0
	global_load_lds_dwordx4 v12, s[4:5]
	v_mfma_f32_16x16x32_f16 v[100:103], v[180:183], v[204:207], v[100:103]
	s_waitcnt lgkmcnt(10)
	v_mfma_f32_16x16x32_f16 v[104:107], v[184:187], v[192:195], v[104:107]
	v_mfma_f32_16x16x32_f16 v[108:111], v[184:187], v[196:199], v[108:111]
	v_mfma_f32_16x16x32_f16 v[112:115], v[184:187], v[200:203], v[112:115]
	v_mfma_f32_16x16x32_f16 v[116:119], v[184:187], v[204:207], v[116:119]
	s_add_u32 m0, s28, 0x13000
	s_nop 0
	global_load_lds_dwordx4 v13, s[4:5]
	s_waitcnt lgkmcnt(9)
	v_mfma_f32_16x16x32_f16 v[120:123], v[188:191], v[192:195], v[120:123]
	v_mfma_f32_16x16x32_f16 v[124:127], v[188:191], v[196:199], v[124:127]
	v_mfma_f32_16x16x32_f16 v[128:131], v[188:191], v[200:203], v[128:131]
	v_mfma_f32_16x16x32_f16 v[132:135], v[188:191], v[204:207], v[132:135]
	s_waitcnt lgkmcnt(6)
	ds_read_b128 v[172:175], v20
	ds_read_b128 v[192:195], v22
	ds_read_b128 v[196:199], v22 offset:2048
	ds_read_b128 v[200:203], v22 offset:4096
	ds_read_b128 v[204:207], v22 offset:6144
	ds_read_b128 v[176:179], v20 offset:2048
	ds_read_b128 v[180:183], v20 offset:4096
	ds_read_b128 v[184:187], v20 offset:6144
	ds_read_b128 v[188:191], v20 offset:8192
	v_mfma_f32_16x16x32_f16 v[56:59], v[136:139], v[156:159], v[56:59]
	s_add_u32 m0, s28, 0x15000
	s_nop 0
	global_load_lds_dwordx4 v14, s[4:5]
	s_add_u32 s4, s4, s20
	s_addc_u32 s5, s5, 0
	s_waitcnt lgkmcnt(15)
	v_mfma_f32_16x16x32_f16 v[60:63], v[136:139], v[160:163], v[60:63]
	s_waitcnt lgkmcnt(14)
	v_mfma_f32_16x16x32_f16 v[64:67], v[136:139], v[164:167], v[64:67]
	s_waitcnt lgkmcnt(13)
	v_mfma_f32_16x16x32_f16 v[68:71], v[136:139], v[168:171], v[68:71]
	s_waitcnt lgkmcnt(12)
	v_mfma_f32_16x16x32_f16 v[72:75], v[140:143], v[156:159], v[72:75]
	v_mfma_f32_16x16x32_f16 v[76:79], v[140:143], v[160:163], v[76:79]
	v_mfma_f32_16x16x32_f16 v[80:83], v[140:143], v[164:167], v[80:83]
	s_add_u32 m0, s28, 0x16000
	s_nop 0
	global_load_lds_dwordx4 v10, s[6:7]
	v_mfma_f32_16x16x32_f16 v[84:87], v[140:143], v[168:171], v[84:87]
	s_waitcnt lgkmcnt(11)
	v_mfma_f32_16x16x32_f16 v[88:91], v[144:147], v[156:159], v[88:91]
	v_mfma_f32_16x16x32_f16 v[92:95], v[144:147], v[160:163], v[92:95]
	v_mfma_f32_16x16x32_f16 v[96:99], v[144:147], v[164:167], v[96:99]
	v_mfma_f32_16x16x32_f16 v[100:103], v[144:147], v[168:171], v[100:103]
	s_waitcnt lgkmcnt(10)
	v_mfma_f32_16x16x32_f16 v[104:107], v[148:151], v[156:159], v[104:107]
	v_mfma_f32_16x16x32_f16 v[108:111], v[148:151], v[160:163], v[108:111]
	s_add_u32 m0, s28, 0x18000
	s_nop 0
	global_load_lds_dwordx4 v11, s[6:7]
	s_add_u32 s6, s6, s20
	s_addc_u32 s7, s7, 0
	v_mfma_f32_16x16x32_f16 v[112:115], v[148:151], v[164:167], v[112:115]
	v_mfma_f32_16x16x32_f16 v[116:119], v[148:151], v[168:171], v[116:119]
	s_waitcnt lgkmcnt(9)
	v_mfma_f32_16x16x32_f16 v[120:123], v[152:155], v[156:159], v[120:123]
	v_mfma_f32_16x16x32_f16 v[124:127], v[152:155], v[160:163], v[124:127]
	v_mfma_f32_16x16x32_f16 v[128:131], v[152:155], v[164:167], v[128:131]
	v_mfma_f32_16x16x32_f16 v[132:135], v[152:155], v[168:171], v[132:135]
	s_waitcnt vmcnt(7) lgkmcnt(0)
	s_barrier
	s_waitcnt lgkmcnt(6)
	ds_read_b128 v[136:139], v15
	ds_read_b128 v[156:159], v17
	ds_read_b128 v[160:163], v17 offset:2048
	ds_read_b128 v[164:167], v17 offset:4096
	ds_read_b128 v[168:171], v17 offset:6144
	ds_read_b128 v[140:143], v15 offset:2048
	ds_read_b128 v[144:147], v15 offset:4096
	ds_read_b128 v[148:151], v15 offset:6144
	ds_read_b128 v[152:155], v15 offset:8192
	v_mfma_f32_16x16x32_f16 v[56:59], v[172:175], v[192:195], v[56:59]
	s_add_u32 m0, s28, 0x1a000
	s_nop 0
	global_load_lds_dwordx4 v10, s[4:5]
	s_waitcnt lgkmcnt(15)
	v_mfma_f32_16x16x32_f16 v[60:63], v[172:175], v[196:199], v[60:63]
	s_waitcnt lgkmcnt(14)
	v_mfma_f32_16x16x32_f16 v[64:67], v[172:175], v[200:203], v[64:67]
	s_waitcnt lgkmcnt(13)
	v_mfma_f32_16x16x32_f16 v[68:71], v[172:175], v[204:207], v[68:71]
	s_waitcnt lgkmcnt(12)
	v_mfma_f32_16x16x32_f16 v[72:75], v[176:179], v[192:195], v[72:75]
	v_mfma_f32_16x16x32_f16 v[76:79], v[176:179], v[196:199], v[76:79]
	s_add_u32 m0, s28, 0x1c000
	s_nop 0
	global_load_lds_dwordx4 v11, s[4:5]
	v_mfma_f32_16x16x32_f16 v[80:83], v[176:179], v[200:203], v[80:83]
	v_mfma_f32_16x16x32_f16 v[84:87], v[176:179], v[204:207], v[84:87]
	s_waitcnt lgkmcnt(11)
	v_mfma_f32_16x16x32_f16 v[88:91], v[180:183], v[192:195], v[88:91]
	v_mfma_f32_16x16x32_f16 v[92:95], v[180:183], v[196:199], v[92:95]
	v_mfma_f32_16x16x32_f16 v[96:99], v[180:183], v[200:203], v[96:99]
	s_add_u32 m0, s28, 0x1e000
	s_nop 0
	global_load_lds_dwordx4 v12, s[4:5]
	v_mfma_f32_16x16x32_f16 v[100:103], v[180:183], v[204:207], v[100:103]
	s_waitcnt lgkmcnt(10)
	v_mfma_f32_16x16x32_f16 v[104:107], v[184:187], v[192:195], v[104:107]
	v_mfma_f32_16x16x32_f16 v[108:111], v[184:187], v[196:199], v[108:111]
	v_mfma_f32_16x16x32_f16 v[112:115], v[184:187], v[200:203], v[112:115]
	v_mfma_f32_16x16x32_f16 v[116:119], v[184:187], v[204:207], v[116:119]
	s_add_u32 m0, s28, 0x20000
	s_nop 0
	global_load_lds_dwordx4 v13, s[4:5]
	s_waitcnt lgkmcnt(9)
	v_mfma_f32_16x16x32_f16 v[120:123], v[188:191], v[192:195], v[120:123]
	v_mfma_f32_16x16x32_f16 v[124:127], v[188:191], v[196:199], v[124:127]
	v_mfma_f32_16x16x32_f16 v[128:131], v[188:191], v[200:203], v[128:131]
	v_mfma_f32_16x16x32_f16 v[132:135], v[188:191], v[204:207], v[132:135]
	s_waitcnt lgkmcnt(6)
	ds_read_b128 v[172:175], v16
	ds_read_b128 v[192:195], v18
	ds_read_b128 v[196:199], v18 offset:2048
	ds_read_b128 v[200:203], v18 offset:4096
	ds_read_b128 v[204:207], v18 offset:6144
	ds_read_b128 v[176:179], v16 offset:2048
	ds_read_b128 v[180:183], v16 offset:4096
	ds_read_b128 v[184:187], v16 offset:6144
	ds_read_b128 v[188:191], v16 offset:8192
	v_mfma_f32_16x16x32_f16 v[56:59], v[136:139], v[156:159], v[56:59]
	s_add_u32 m0, s28, 0x22000
	s_nop 0
	global_load_lds_dwordx4 v14, s[4:5]
	s_add_u32 s4, s4, s20
	s_addc_u32 s5, s5, 0
	s_waitcnt lgkmcnt(15)
	v_mfma_f32_16x16x32_f16 v[60:63], v[136:139], v[160:163], v[60:63]
	s_waitcnt lgkmcnt(14)
	v_mfma_f32_16x16x32_f16 v[64:67], v[136:139], v[164:167], v[64:67]
	s_waitcnt lgkmcnt(13)
	v_mfma_f32_16x16x32_f16 v[68:71], v[136:139], v[168:171], v[68:71]
	s_waitcnt lgkmcnt(12)
	v_mfma_f32_16x16x32_f16 v[72:75], v[140:143], v[156:159], v[72:75]
	v_mfma_f32_16x16x32_f16 v[76:79], v[140:143], v[160:163], v[76:79]
	v_mfma_f32_16x16x32_f16 v[80:83], v[140:143], v[164:167], v[80:83]
	s_add_u32 m0, s28, 0x23000
	s_nop 0
	global_load_lds_dwordx4 v10, s[6:7]
	v_mfma_f32_16x16x32_f16 v[84:87], v[140:143], v[168:171], v[84:87]
	s_waitcnt lgkmcnt(11)
	v_mfma_f32_16x16x32_f16 v[88:91], v[144:147], v[156:159], v[88:91]
	v_mfma_f32_16x16x32_f16 v[92:95], v[144:147], v[160:163], v[92:95]
	v_mfma_f32_16x16x32_f16 v[96:99], v[144:147], v[164:167], v[96:99]
	v_mfma_f32_16x16x32_f16 v[100:103], v[144:147], v[168:171], v[100:103]
	s_waitcnt lgkmcnt(10)
	v_mfma_f32_16x16x32_f16 v[104:107], v[148:151], v[156:159], v[104:107]
	v_mfma_f32_16x16x32_f16 v[108:111], v[148:151], v[160:163], v[108:111]
	s_add_u32 m0, s28, 0x25000
	s_nop 0
	global_load_lds_dwordx4 v11, s[6:7]
	s_add_u32 s6, s6, s20
	s_addc_u32 s7, s7, 0
	v_mfma_f32_16x16x32_f16 v[112:115], v[148:151], v[164:167], v[112:115]
	v_mfma_f32_16x16x32_f16 v[116:119], v[148:151], v[168:171], v[116:119]
	s_waitcnt lgkmcnt(9)
	v_mfma_f32_16x16x32_f16 v[120:123], v[152:155], v[156:159], v[120:123]
	v_mfma_f32_16x16x32_f16 v[124:127], v[152:155], v[160:163], v[124:127]
	v_mfma_f32_16x16x32_f16 v[128:131], v[152:155], v[164:167], v[128:131]
	v_mfma_f32_16x16x32_f16 v[132:135], v[152:155], v[168:171], v[132:135]
	s_waitcnt vmcnt(7) lgkmcnt(0)
	s_barrier
	s_waitcnt lgkmcnt(6)
	ds_read_b128 v[136:139], v15 offset:53248
	ds_read_b128 v[156:159], v17 offset:53248
	ds_read_b128 v[160:163], v17 offset:55296
	ds_read_b128 v[164:167], v17 offset:57344
	ds_read_b128 v[168:171], v17 offset:59392
	ds_read_b128 v[140:143], v15 offset:55296
	ds_read_b128 v[144:147], v15 offset:57344
	ds_read_b128 v[148:151], v15 offset:59392
	ds_read_b128 v[152:155], v15 offset:61440
	v_mfma_f32_16x16x32_f16 v[56:59], v[172:175], v[192:195], v[56:59]
	s_add_u32 m0, s28, 0x0
	s_nop 0
	global_load_lds_dwordx4 v10, s[4:5]
	s_waitcnt lgkmcnt(15)
	v_mfma_f32_16x16x32_f16 v[60:63], v[172:175], v[196:199], v[60:63]
	s_waitcnt lgkmcnt(14)
	v_mfma_f32_16x16x32_f16 v[64:67], v[172:175], v[200:203], v[64:67]
	s_waitcnt lgkmcnt(13)
	v_mfma_f32_16x16x32_f16 v[68:71], v[172:175], v[204:207], v[68:71]
	s_waitcnt lgkmcnt(12)
	v_mfma_f32_16x16x32_f16 v[72:75], v[176:179], v[192:195], v[72:75]
	v_mfma_f32_16x16x32_f16 v[76:79], v[176:179], v[196:199], v[76:79]
	s_add_u32 m0, s28, 0x2000
	s_nop 0
	global_load_lds_dwordx4 v11, s[4:5]
	v_mfma_f32_16x16x32_f16 v[80:83], v[176:179], v[200:203], v[80:83]
	v_mfma_f32_16x16x32_f16 v[84:87], v[176:179], v[204:207], v[84:87]
	s_waitcnt lgkmcnt(11)
	v_mfma_f32_16x16x32_f16 v[88:91], v[180:183], v[192:195], v[88:91]
	v_mfma_f32_16x16x32_f16 v[92:95], v[180:183], v[196:199], v[92:95]
	v_mfma_f32_16x16x32_f16 v[96:99], v[180:183], v[200:203], v[96:99]
	s_add_u32 m0, s28, 0x4000
	s_nop 0
	global_load_lds_dwordx4 v12, s[4:5]
	v_mfma_f32_16x16x32_f16 v[100:103], v[180:183], v[204:207], v[100:103]
	s_waitcnt lgkmcnt(10)
	v_mfma_f32_16x16x32_f16 v[104:107], v[184:187], v[192:195], v[104:107]
	v_mfma_f32_16x16x32_f16 v[108:111], v[184:187], v[196:199], v[108:111]
	v_mfma_f32_16x16x32_f16 v[112:115], v[184:187], v[200:203], v[112:115]
	v_mfma_f32_16x16x32_f16 v[116:119], v[184:187], v[204:207], v[116:119]
	s_add_u32 m0, s28, 0x6000
	s_nop 0
	global_load_lds_dwordx4 v13, s[4:5]
	s_waitcnt lgkmcnt(9)
	v_mfma_f32_16x16x32_f16 v[120:123], v[188:191], v[192:195], v[120:123]
	v_mfma_f32_16x16x32_f16 v[124:127], v[188:191], v[196:199], v[124:127]
	v_mfma_f32_16x16x32_f16 v[128:131], v[188:191], v[200:203], v[128:131]
	v_mfma_f32_16x16x32_f16 v[132:135], v[188:191], v[204:207], v[132:135]
	s_waitcnt lgkmcnt(6)
	ds_read_b128 v[172:175], v16 offset:53248
	ds_read_b128 v[192:195], v18 offset:53248
	ds_read_b128 v[196:199], v18 offset:55296
	ds_read_b128 v[200:203], v18 offset:57344
	ds_read_b128 v[204:207], v18 offset:59392
	ds_read_b128 v[176:179], v16 offset:55296
	ds_read_b128 v[180:183], v16 offset:57344
	ds_read_b128 v[184:187], v16 offset:59392
	ds_read_b128 v[188:191], v16 offset:61440
	v_mfma_f32_16x16x32_f16 v[56:59], v[136:139], v[156:159], v[56:59]
	s_add_u32 m0, s28, 0x8000
	s_nop 0
	global_load_lds_dwordx4 v14, s[4:5]
	s_add_u32 s4, s4, s20
	s_addc_u32 s5, s5, 0
	s_waitcnt lgkmcnt(15)
	v_mfma_f32_16x16x32_f16 v[60:63], v[136:139], v[160:163], v[60:63]
	s_waitcnt lgkmcnt(14)
	v_mfma_f32_16x16x32_f16 v[64:67], v[136:139], v[164:167], v[64:67]
	s_waitcnt lgkmcnt(13)
	v_mfma_f32_16x16x32_f16 v[68:71], v[136:139], v[168:171], v[68:71]
	s_waitcnt lgkmcnt(12)
	v_mfma_f32_16x16x32_f16 v[72:75], v[140:143], v[156:159], v[72:75]
	v_mfma_f32_16x16x32_f16 v[76:79], v[140:143], v[160:163], v[76:79]
	v_mfma_f32_16x16x32_f16 v[80:83], v[140:143], v[164:167], v[80:83]
	s_add_u32 m0, s28, 0x9000
	s_nop 0
	global_load_lds_dwordx4 v10, s[6:7]
	v_mfma_f32_16x16x32_f16 v[84:87], v[140:143], v[168:171], v[84:87]
	s_waitcnt lgkmcnt(11)
	v_mfma_f32_16x16x32_f16 v[88:91], v[144:147], v[156:159], v[88:91]
	v_mfma_f32_16x16x32_f16 v[92:95], v[144:147], v[160:163], v[92:95]
	v_mfma_f32_16x16x32_f16 v[96:99], v[144:147], v[164:167], v[96:99]
	v_mfma_f32_16x16x32_f16 v[100:103], v[144:147], v[168:171], v[100:103]
	s_waitcnt lgkmcnt(10)
	v_mfma_f32_16x16x32_f16 v[104:107], v[148:151], v[156:159], v[104:107]
	v_mfma_f32_16x16x32_f16 v[108:111], v[148:151], v[160:163], v[108:111]
	s_add_u32 m0, s28, 0xb000
	s_nop 0
	global_load_lds_dwordx4 v11, s[6:7]
	s_add_u32 s6, s6, s20
	s_addc_u32 s7, s7, 0
	v_mfma_f32_16x16x32_f16 v[112:115], v[148:151], v[164:167], v[112:115]
	v_mfma_f32_16x16x32_f16 v[116:119], v[148:151], v[168:171], v[116:119]
	s_waitcnt lgkmcnt(9)
	v_mfma_f32_16x16x32_f16 v[120:123], v[152:155], v[156:159], v[120:123]
	v_mfma_f32_16x16x32_f16 v[124:127], v[152:155], v[160:163], v[124:127]
	v_mfma_f32_16x16x32_f16 v[128:131], v[152:155], v[164:167], v[128:131]
	v_mfma_f32_16x16x32_f16 v[132:135], v[152:155], v[168:171], v[132:135]
	s_waitcnt vmcnt(7) lgkmcnt(0)
	s_barrier
	s_waitcnt lgkmcnt(6)
	ds_read_b128 v[136:139], v19
	ds_read_b128 v[156:159], v21
	ds_read_b128 v[160:163], v21 offset:2048
	ds_read_b128 v[164:167], v21 offset:4096
	ds_read_b128 v[168:171], v21 offset:6144
	ds_read_b128 v[140:143], v19 offset:2048
	ds_read_b128 v[144:147], v19 offset:4096
	ds_read_b128 v[148:151], v19 offset:6144
	ds_read_b128 v[152:155], v19 offset:8192
	v_mfma_f32_16x16x32_f16 v[56:59], v[172:175], v[192:195], v[56:59]
	s_waitcnt lgkmcnt(15)
	v_mfma_f32_16x16x32_f16 v[60:63], v[172:175], v[196:199], v[60:63]
	s_waitcnt lgkmcnt(14)
	v_mfma_f32_16x16x32_f16 v[64:67], v[172:175], v[200:203], v[64:67]
	s_waitcnt lgkmcnt(13)
	v_mfma_f32_16x16x32_f16 v[68:71], v[172:175], v[204:207], v[68:71]
	s_waitcnt lgkmcnt(12)
	v_mfma_f32_16x16x32_f16 v[72:75], v[176:179], v[192:195], v[72:75]
	v_mfma_f32_16x16x32_f16 v[76:79], v[176:179], v[196:199], v[76:79]
	v_mfma_f32_16x16x32_f16 v[80:83], v[176:179], v[200:203], v[80:83]
	v_mfma_f32_16x16x32_f16 v[84:87], v[176:179], v[204:207], v[84:87]
	s_waitcnt lgkmcnt(11)
	v_mfma_f32_16x16x32_f16 v[88:91], v[180:183], v[192:195], v[88:91]
	v_mfma_f32_16x16x32_f16 v[92:95], v[180:183], v[196:199], v[92:95]
	v_mfma_f32_16x16x32_f16 v[96:99], v[180:183], v[200:203], v[96:99]
	v_mfma_f32_16x16x32_f16 v[100:103], v[180:183], v[204:207], v[100:103]
	s_waitcnt lgkmcnt(10)
	v_mfma_f32_16x16x32_f16 v[104:107], v[184:187], v[192:195], v[104:107]
	v_mfma_f32_16x16x32_f16 v[108:111], v[184:187], v[196:199], v[108:111]
	v_mfma_f32_16x16x32_f16 v[112:115], v[184:187], v[200:203], v[112:115]
	v_mfma_f32_16x16x32_f16 v[116:119], v[184:187], v[204:207], v[116:119]
	s_waitcnt lgkmcnt(9)
	v_mfma_f32_16x16x32_f16 v[120:123], v[188:191], v[192:195], v[120:123]
	v_mfma_f32_16x16x32_f16 v[124:127], v[188:191], v[196:199], v[124:127]
	v_mfma_f32_16x16x32_f16 v[128:131], v[188:191], v[200:203], v[128:131]
	v_mfma_f32_16x16x32_f16 v[132:135], v[188:191], v[204:207], v[132:135]
	s_waitcnt lgkmcnt(6)
	ds_read_b128 v[172:175], v20
	ds_read_b128 v[192:195], v22
	ds_read_b128 v[196:199], v22 offset:2048
	ds_read_b128 v[200:203], v22 offset:4096
	ds_read_b128 v[204:207], v22 offset:6144
	ds_read_b128 v[176:179], v20 offset:2048
	ds_read_b128 v[180:183], v20 offset:4096
	ds_read_b128 v[184:187], v20 offset:6144
	ds_read_b128 v[188:191], v20 offset:8192
	v_mfma_f32_16x16x32_f16 v[56:59], v[136:139], v[156:159], v[56:59]
	s_waitcnt lgkmcnt(15)
	v_mfma_f32_16x16x32_f16 v[60:63], v[136:139], v[160:163], v[60:63]
	s_waitcnt lgkmcnt(14)
	v_mfma_f32_16x16x32_f16 v[64:67], v[136:139], v[164:167], v[64:67]
	s_waitcnt lgkmcnt(13)
	v_mfma_f32_16x16x32_f16 v[68:71], v[136:139], v[168:171], v[68:71]
	s_waitcnt lgkmcnt(12)
	v_mfma_f32_16x16x32_f16 v[72:75], v[140:143], v[156:159], v[72:75]
	v_mfma_f32_16x16x32_f16 v[76:79], v[140:143], v[160:163], v[76:79]
	v_mfma_f32_16x16x32_f16 v[80:83], v[140:143], v[164:167], v[80:83]
	v_mfma_f32_16x16x32_f16 v[84:87], v[140:143], v[168:171], v[84:87]
	s_waitcnt lgkmcnt(11)
	v_mfma_f32_16x16x32_f16 v[88:91], v[144:147], v[156:159], v[88:91]
	v_mfma_f32_16x16x32_f16 v[92:95], v[144:147], v[160:163], v[92:95]
	v_mfma_f32_16x16x32_f16 v[96:99], v[144:147], v[164:167], v[96:99]
	v_mfma_f32_16x16x32_f16 v[100:103], v[144:147], v[168:171], v[100:103]
	s_waitcnt lgkmcnt(10)
	v_mfma_f32_16x16x32_f16 v[104:107], v[148:151], v[156:159], v[104:107]
	v_mfma_f32_16x16x32_f16 v[108:111], v[148:151], v[160:163], v[108:111]
	v_mfma_f32_16x16x32_f16 v[112:115], v[148:151], v[164:167], v[112:115]
	v_mfma_f32_16x16x32_f16 v[116:119], v[148:151], v[168:171], v[116:119]
	s_waitcnt lgkmcnt(9)
	v_mfma_f32_16x16x32_f16 v[120:123], v[152:155], v[156:159], v[120:123]
	v_mfma_f32_16x16x32_f16 v[124:127], v[152:155], v[160:163], v[124:127]
	v_mfma_f32_16x16x32_f16 v[128:131], v[152:155], v[164:167], v[128:131]
	v_mfma_f32_16x16x32_f16 v[132:135], v[152:155], v[168:171], v[132:135]
	s_waitcnt vmcnt(0) lgkmcnt(0)
	s_barrier
	s_waitcnt lgkmcnt(6)
	ds_read_b128 v[136:139], v15
	ds_read_b128 v[156:159], v17
	ds_read_b128 v[160:163], v17 offset:2048
	ds_read_b128 v[164:167], v17 offset:4096
	ds_read_b128 v[168:171], v17 offset:6144
	ds_read_b128 v[140:143], v15 offset:2048
	ds_read_b128 v[144:147], v15 offset:4096
	ds_read_b128 v[148:151], v15 offset:6144
	ds_read_b128 v[152:155], v15 offset:8192
	v_mfma_f32_16x16x32_f16 v[56:59], v[172:175], v[192:195], v[56:59]
	s_waitcnt lgkmcnt(15)
	v_mfma_f32_16x16x32_f16 v[60:63], v[172:175], v[196:199], v[60:63]
	s_waitcnt lgkmcnt(14)
	v_mfma_f32_16x16x32_f16 v[64:67], v[172:175], v[200:203], v[64:67]
	s_waitcnt lgkmcnt(13)
	v_mfma_f32_16x16x32_f16 v[68:71], v[172:175], v[204:207], v[68:71]
	s_waitcnt lgkmcnt(12)
	v_mfma_f32_16x16x32_f16 v[72:75], v[176:179], v[192:195], v[72:75]
	v_mfma_f32_16x16x32_f16 v[76:79], v[176:179], v[196:199], v[76:79]
	v_mfma_f32_16x16x32_f16 v[80:83], v[176:179], v[200:203], v[80:83]
	v_mfma_f32_16x16x32_f16 v[84:87], v[176:179], v[204:207], v[84:87]
	s_waitcnt lgkmcnt(11)
	v_mfma_f32_16x16x32_f16 v[88:91], v[180:183], v[192:195], v[88:91]
	v_mfma_f32_16x16x32_f16 v[92:95], v[180:183], v[196:199], v[92:95]
	v_mfma_f32_16x16x32_f16 v[96:99], v[180:183], v[200:203], v[96:99]
	v_mfma_f32_16x16x32_f16 v[100:103], v[180:183], v[204:207], v[100:103]
	s_waitcnt lgkmcnt(10)
	v_mfma_f32_16x16x32_f16 v[104:107], v[184:187], v[192:195], v[104:107]
	v_mfma_f32_16x16x32_f16 v[108:111], v[184:187], v[196:199], v[108:111]
	v_mfma_f32_16x16x32_f16 v[112:115], v[184:187], v[200:203], v[112:115]
	v_mfma_f32_16x16x32_f16 v[116:119], v[184:187], v[204:207], v[116:119]
	s_waitcnt lgkmcnt(9)
	v_mfma_f32_16x16x32_f16 v[120:123], v[188:191], v[192:195], v[120:123]
	v_mfma_f32_16x16x32_f16 v[124:127], v[188:191], v[196:199], v[124:127]
	v_mfma_f32_16x16x32_f16 v[128:131], v[188:191], v[200:203], v[128:131]
	v_mfma_f32_16x16x32_f16 v[132:135], v[188:191], v[204:207], v[132:135]
	s_waitcnt lgkmcnt(6)
	ds_read_b128 v[172:175], v16
	ds_read_b128 v[192:195], v18
	ds_read_b128 v[196:199], v18 offset:2048
	ds_read_b128 v[200:203], v18 offset:4096
	ds_read_b128 v[204:207], v18 offset:6144
	ds_read_b128 v[176:179], v16 offset:2048
	ds_read_b128 v[180:183], v16 offset:4096
	ds_read_b128 v[184:187], v16 offset:6144
	ds_read_b128 v[188:191], v16 offset:8192
	v_mfma_f32_16x16x32_f16 v[56:59], v[136:139], v[156:159], v[56:59]
	s_waitcnt lgkmcnt(15)
	v_mfma_f32_16x16x32_f16 v[60:63], v[136:139], v[160:163], v[60:63]
	s_waitcnt lgkmcnt(14)
	v_mfma_f32_16x16x32_f16 v[64:67], v[136:139], v[164:167], v[64:67]
	s_waitcnt lgkmcnt(13)
	v_mfma_f32_16x16x32_f16 v[68:71], v[136:139], v[168:171], v[68:71]
	s_waitcnt lgkmcnt(12)
	v_mfma_f32_16x16x32_f16 v[72:75], v[140:143], v[156:159], v[72:75]
	v_mfma_f32_16x16x32_f16 v[76:79], v[140:143], v[160:163], v[76:79]
	v_mfma_f32_16x16x32_f16 v[80:83], v[140:143], v[164:167], v[80:83]
	v_mfma_f32_16x16x32_f16 v[84:87], v[140:143], v[168:171], v[84:87]
	s_waitcnt lgkmcnt(11)
	v_mfma_f32_16x16x32_f16 v[88:91], v[144:147], v[156:159], v[88:91]
	v_mfma_f32_16x16x32_f16 v[92:95], v[144:147], v[160:163], v[92:95]
	v_mfma_f32_16x16x32_f16 v[96:99], v[144:147], v[164:167], v[96:99]
	v_mfma_f32_16x16x32_f16 v[100:103], v[144:147], v[168:171], v[100:103]
	s_waitcnt lgkmcnt(10)
	v_mfma_f32_16x16x32_f16 v[104:107], v[148:151], v[156:159], v[104:107]
	v_mfma_f32_16x16x32_f16 v[108:111], v[148:151], v[160:163], v[108:111]
	v_mfma_f32_16x16x32_f16 v[112:115], v[148:151], v[164:167], v[112:115]
	v_mfma_f32_16x16x32_f16 v[116:119], v[148:151], v[168:171], v[116:119]
	s_waitcnt lgkmcnt(9)
	v_mfma_f32_16x16x32_f16 v[120:123], v[152:155], v[156:159], v[120:123]
	v_mfma_f32_16x16x32_f16 v[124:127], v[152:155], v[160:163], v[124:127]
	v_mfma_f32_16x16x32_f16 v[128:131], v[152:155], v[164:167], v[128:131]
	v_mfma_f32_16x16x32_f16 v[132:135], v[152:155], v[168:171], v[132:135]
	s_waitcnt lgkmcnt(7)
	v_mfma_f32_16x16x32_f16 v[56:59], v[172:175], v[192:195], v[56:59]
	s_waitcnt lgkmcnt(6)
	v_mfma_f32_16x16x32_f16 v[60:63], v[172:175], v[196:199], v[60:63]
	s_waitcnt lgkmcnt(5)
	v_mfma_f32_16x16x32_f16 v[64:67], v[172:175], v[200:203], v[64:67]
	s_waitcnt lgkmcnt(4)
	v_mfma_f32_16x16x32_f16 v[68:71], v[172:175], v[204:207], v[68:71]
	s_waitcnt lgkmcnt(3)
	v_mfma_f32_16x16x32_f16 v[72:75], v[176:179], v[192:195], v[72:75]
	v_mfma_f32_16x16x32_f16 v[76:79], v[176:179], v[196:199], v[76:79]
	v_mfma_f32_16x16x32_f16 v[80:83], v[176:179], v[200:203], v[80:83]
	v_mfma_f32_16x16x32_f16 v[84:87], v[176:179], v[204:207], v[84:87]
	s_waitcnt lgkmcnt(2)
	v_mfma_f32_16x16x32_f16 v[88:91], v[180:183], v[192:195], v[88:91]
	v_mfma_f32_16x16x32_f16 v[92:95], v[180:183], v[196:199], v[92:95]
	v_mfma_f32_16x16x32_f16 v[96:99], v[180:183], v[200:203], v[96:99]
	v_mfma_f32_16x16x32_f16 v[100:103], v[180:183], v[204:207], v[100:103]
	s_waitcnt lgkmcnt(1)
	v_mfma_f32_16x16x32_f16 v[104:107], v[184:187], v[192:195], v[104:107]
	v_mfma_f32_16x16x32_f16 v[108:111], v[184:187], v[196:199], v[108:111]
	v_mfma_f32_16x16x32_f16 v[112:115], v[184:187], v[200:203], v[112:115]
	v_mfma_f32_16x16x32_f16 v[116:119], v[184:187], v[204:207], v[116:119]
	s_waitcnt lgkmcnt(0)
	v_mfma_f32_16x16x32_f16 v[120:123], v[188:191], v[192:195], v[120:123]
	v_mfma_f32_16x16x32_f16 v[124:127], v[188:191], v[196:199], v[124:127]
	v_mfma_f32_16x16x32_f16 v[128:131], v[188:191], v[200:203], v[128:131]
	v_mfma_f32_16x16x32_f16 v[132:135], v[188:191], v[204:207], v[132:135]
	s_nop 7
	s_nop 1
	s_add_u32 s24, s29, 0
	s_lshl_b32 s8, s24, 11
	s_nop 0
	v_add_u32_e32 v212, s8, v23
	v_add_f32_e32 v56, v56, v24
	v_add_f32_e32 v57, v57, v24
	v_add_f32_e32 v58, v58, v24
	v_add_f32_e32 v59, v59, v24
	v_cvt_pk_f16_f32 v56, v56, v57
	v_cvt_pk_f16_f32 v57, v58, v59
	global_store_dwordx2 v212, v[56:57], s[22:23] offset:0
	v_add_f32_e32 v60, v60, v25
	v_add_f32_e32 v61, v61, v25
	v_add_f32_e32 v62, v62, v25
	v_add_f32_e32 v63, v63, v25
	v_cvt_pk_f16_f32 v60, v60, v61
	v_cvt_pk_f16_f32 v61, v62, v63
	global_store_dwordx2 v212, v[60:61], s[22:23] offset:256
	v_add_f32_e32 v64, v64, v26
	v_add_f32_e32 v65, v65, v26
	v_add_f32_e32 v66, v66, v26
	v_add_f32_e32 v67, v67, v26
	v_cvt_pk_f16_f32 v64, v64, v65
	v_cvt_pk_f16_f32 v65, v66, v67
	global_store_dwordx2 v212, v[64:65], s[22:23] offset:1024
	v_add_f32_e32 v68, v68, v27
	v_add_f32_e32 v69, v69, v27
	v_add_f32_e32 v70, v70, v27
	v_add_f32_e32 v71, v71, v27
	v_cvt_pk_f16_f32 v68, v68, v69
	v_cvt_pk_f16_f32 v69, v70, v71
	global_store_dwordx2 v212, v[68:69], s[22:23] offset:1280
	s_add_u32 s24, s29, 1
	s_lshl_b32 s8, s24, 11
	s_nop 0
	v_add_u32_e32 v212, s8, v23
	v_add_f32_e32 v72, v72, v24
	v_add_f32_e32 v73, v73, v24
	v_add_f32_e32 v74, v74, v24
	v_add_f32_e32 v75, v75, v24
	v_cvt_pk_f16_f32 v72, v72, v73
	v_cvt_pk_f16_f32 v73, v74, v75
	global_store_dwordx2 v212, v[72:73], s[22:23] offset:0
	v_add_f32_e32 v76, v76, v25
	v_add_f32_e32 v77, v77, v25
	v_add_f32_e32 v78, v78, v25
	v_add_f32_e32 v79, v79, v25
	v_cvt_pk_f16_f32 v76, v76, v77
	v_cvt_pk_f16_f32 v77, v78, v79
	global_store_dwordx2 v212, v[76:77], s[22:23] offset:256
	v_add_f32_e32 v80, v80, v26
	v_add_f32_e32 v81, v81, v26
	v_add_f32_e32 v82, v82, v26
	v_add_f32_e32 v83, v83, v26
	v_cvt_pk_f16_f32 v80, v80, v81
	v_cvt_pk_f16_f32 v81, v82, v83
	global_store_dwordx2 v212, v[80:81], s[22:23] offset:1024
	v_add_f32_e32 v84, v84, v27
	v_add_f32_e32 v85, v85, v27
	v_add_f32_e32 v86, v86, v27
	v_add_f32_e32 v87, v87, v27
	v_cvt_pk_f16_f32 v84, v84, v85
	v_cvt_pk_f16_f32 v85, v86, v87
	global_store_dwordx2 v212, v[84:85], s[22:23] offset:1280
	s_add_u32 s24, s29, 2
	s_lshl_b32 s8, s24, 11
	s_nop 0
	v_add_u32_e32 v212, s8, v23
	v_add_f32_e32 v88, v88, v24
	v_add_f32_e32 v89, v89, v24
	v_add_f32_e32 v90, v90, v24
	v_add_f32_e32 v91, v91, v24
	v_cvt_pk_f16_f32 v88, v88, v89
	v_cvt_pk_f16_f32 v89, v90, v91
	global_store_dwordx2 v212, v[88:89], s[22:23] offset:0
	v_add_f32_e32 v92, v92, v25
	v_add_f32_e32 v93, v93, v25
	v_add_f32_e32 v94, v94, v25
	v_add_f32_e32 v95, v95, v25
	v_cvt_pk_f16_f32 v92, v92, v93
	v_cvt_pk_f16_f32 v93, v94, v95
	global_store_dwordx2 v212, v[92:93], s[22:23] offset:256
	v_add_f32_e32 v96, v96, v26
	v_add_f32_e32 v97, v97, v26
	v_add_f32_e32 v98, v98, v26
	v_add_f32_e32 v99, v99, v26
	v_cvt_pk_f16_f32 v96, v96, v97
	v_cvt_pk_f16_f32 v97, v98, v99
	global_store_dwordx2 v212, v[96:97], s[22:23] offset:1024
	v_add_f32_e32 v100, v100, v27
	v_add_f32_e32 v101, v101, v27
	v_add_f32_e32 v102, v102, v27
	v_add_f32_e32 v103, v103, v27
	v_cvt_pk_f16_f32 v100, v100, v101
	v_cvt_pk_f16_f32 v101, v102, v103
	global_store_dwordx2 v212, v[100:101], s[22:23] offset:1280
	s_add_u32 s24, s29, 3
	s_lshl_b32 s8, s24, 11
	s_nop 0
	v_add_u32_e32 v212, s8, v23
	v_add_f32_e32 v104, v104, v24
	v_add_f32_e32 v105, v105, v24
	v_add_f32_e32 v106, v106, v24
	v_add_f32_e32 v107, v107, v24
	v_cvt_pk_f16_f32 v104, v104, v105
	v_cvt_pk_f16_f32 v105, v106, v107
	global_store_dwordx2 v212, v[104:105], s[22:23] offset:0
	v_add_f32_e32 v108, v108, v25
	v_add_f32_e32 v109, v109, v25
	v_add_f32_e32 v110, v110, v25
	v_add_f32_e32 v111, v111, v25
	v_cvt_pk_f16_f32 v108, v108, v109
	v_cvt_pk_f16_f32 v109, v110, v111
	global_store_dwordx2 v212, v[108:109], s[22:23] offset:256
	v_add_f32_e32 v112, v112, v26
	v_add_f32_e32 v113, v113, v26
	v_add_f32_e32 v114, v114, v26
	v_add_f32_e32 v115, v115, v26
	v_cvt_pk_f16_f32 v112, v112, v113
	v_cvt_pk_f16_f32 v113, v114, v115
	global_store_dwordx2 v212, v[112:113], s[22:23] offset:1024
	v_add_f32_e32 v116, v116, v27
	v_add_f32_e32 v117, v117, v27
	v_add_f32_e32 v118, v118, v27
	v_add_f32_e32 v119, v119, v27
	v_cvt_pk_f16_f32 v116, v116, v117
	v_cvt_pk_f16_f32 v117, v118, v119
	global_store_dwordx2 v212, v[116:117], s[22:23] offset:1280
	s_add_u32 s24, s29, 4
	s_lshl_b32 s8, s24, 11
	s_nop 0
	v_add_u32_e32 v212, s8, v23
	v_add_f32_e32 v120, v120, v24
	v_add_f32_e32 v121, v121, v24
	v_add_f32_e32 v122, v122, v24
	v_add_f32_e32 v123, v123, v24
	v_cvt_pk_f16_f32 v120, v120, v121
	v_cvt_pk_f16_f32 v121, v122, v123
	global_store_dwordx2 v212, v[120:121], s[22:23] offset:0
	v_add_f32_e32 v124, v124, v25
	v_add_f32_e32 v125, v125, v25
	v_add_f32_e32 v126, v126, v25
	v_add_f32_e32 v127, v127, v25
	v_cvt_pk_f16_f32 v124, v124, v125
	v_cvt_pk_f16_f32 v125, v126, v127
	global_store_dwordx2 v212, v[124:125], s[22:23] offset:256
	v_add_f32_e32 v128, v128, v26
	v_add_f32_e32 v129, v129, v26
	v_add_f32_e32 v130, v130, v26
	v_add_f32_e32 v131, v131, v26
	v_cvt_pk_f16_f32 v128, v128, v129
	v_cvt_pk_f16_f32 v129, v130, v131
	global_store_dwordx2 v212, v[128:129], s[22:23] offset:1024
	v_add_f32_e32 v132, v132, v27
	v_add_f32_e32 v133, v133, v27
	v_add_f32_e32 v134, v134, v27
	v_add_f32_e32 v135, v135, v27
	v_cvt_pk_f16_f32 v132, v132, v133
	v_cvt_pk_f16_f32 v133, v134, v135
	global_store_dwordx2 v212, v[132:133], s[22:23] offset:1280
	s_branch .Lpf_done

.Lpf_actVB:
	s_lshl_b32 s25, s25, 6
	s_add_u32 s25, s25, 32
	s_add_u32 s29, s10, s25
	s_lshr_b32 s29, s29, 4
	v_add_u32_e32 v5, s25, v3
	v_lshlrev_b32_e32 v5, 7, v5
	v_add_u32_e32 v15, v5, v6
	v_add_u32_e32 v16, v5, v7
	v_add_u32_e32 v5, 0x9000, v9
	v_add_u32_e32 v17, v5, v6
	v_add_u32_e32 v18, v5, v7
	v_add_u32_e32 v19, 0x1a000, v15
	v_add_u32_e32 v20, 0x1a000, v16
	v_add_u32_e32 v21, 0x1a000, v17
	v_add_u32_e32 v22, 0x1a000, v18
	v_lshlrev_b32_e32 v5, 2, v3
	global_load_dword v24, v5, s[14:15] offset:0
	global_load_dword v25, v5, s[14:15] offset:64
	global_load_dword v26, v5, s[14:15] offset:128
	global_load_dword v27, v5, s[14:15] offset:192
	s_waitcnt vmcnt(16) lgkmcnt(0)
	s_barrier
	s_waitcnt lgkmcnt(7)
	ds_read_b128 v[136:139], v15
	ds_read_b128 v[156:159], v17
	ds_read_b128 v[160:163], v17 offset:2048
	ds_read_b128 v[164:167], v17 offset:4096
	ds_read_b128 v[168:171], v17 offset:6144
	ds_read_b128 v[140:143], v15 offset:2048
	ds_read_b128 v[144:147], v15 offset:4096
	ds_read_b128 v[148:151], v15 offset:6144
	s_waitcnt lgkmcnt(7)
	ds_read_b128 v[172:175], v16
	ds_read_b128 v[192:195], v18
	ds_read_b128 v[196:199], v18 offset:2048
	ds_read_b128 v[200:203], v18 offset:4096
	ds_read_b128 v[204:207], v18 offset:6144
	ds_read_b128 v[176:179], v16 offset:2048
	ds_read_b128 v[180:183], v16 offset:4096
	ds_read_b128 v[184:187], v16 offset:6144
	s_waitcnt lgkmcnt(14)
	v_mfma_f32_16x16x32_f16 v[56:59], v[136:139], v[156:159], 0
	s_waitcnt lgkmcnt(13)
	v_mfma_f32_16x16x32_f16 v[60:63], v[136:139], v[160:163], 0
	s_waitcnt lgkmcnt(12)
	v_mfma_f32_16x16x32_f16 v[64:67], v[136:139], v[164:167], 0
	s_waitcnt lgkmcnt(11)
	v_mfma_f32_16x16x32_f16 v[68:71], v[136:139], v[168:171], 0
	s_waitcnt lgkmcnt(10)
	v_mfma_f32_16x16x32_f16 v[72:75], v[140:143], v[156:159], 0
	v_mfma_f32_16x16x32_f16 v[76:79], v[140:143], v[160:163], 0
	v_mfma_f32_16x16x32_f16 v[80:83], v[140:143], v[164:167], 0
	v_mfma_f32_16x16x32_f16 v[84:87], v[140:143], v[168:171], 0
	s_waitcnt lgkmcnt(9)
	v_mfma_f32_16x16x32_f16 v[88:91], v[144:147], v[156:159], 0
	v_mfma_f32_16x16x32_f16 v[92:95], v[144:147], v[160:163], 0
	v_mfma_f32_16x16x32_f16 v[96:99], v[144:147], v[164:167], 0
	v_mfma_f32_16x16x32_f16 v[100:103], v[144:147], v[168:171], 0
	s_waitcnt lgkmcnt(8)
	v_mfma_f32_16x16x32_f16 v[104:107], v[148:151], v[156:159], 0
	v_mfma_f32_16x16x32_f16 v[108:111], v[148:151], v[160:163], 0
	v_mfma_f32_16x16x32_f16 v[112:115], v[148:151], v[164:167], 0
	v_mfma_f32_16x16x32_f16 v[116:119], v[148:151], v[168:171], 0
	s_waitcnt vmcnt(10) lgkmcnt(0)
	s_barrier
	s_waitcnt lgkmcnt(7)
	ds_read_b128 v[136:139], v15 offset:53248
	ds_read_b128 v[156:159], v17 offset:53248
	ds_read_b128 v[160:163], v17 offset:55296
	ds_read_b128 v[164:167], v17 offset:57344
	ds_read_b128 v[168:171], v17 offset:59392
	ds_read_b128 v[140:143], v15 offset:55296
	ds_read_b128 v[144:147], v15 offset:57344
	ds_read_b128 v[148:151], v15 offset:59392
	s_waitcnt lgkmcnt(14)
	v_mfma_f32_16x16x32_f16 v[56:59], v[172:175], v[192:195], v[56:59]
	s_add_u32 m0, s28, 0x0
	s_nop 0
	global_load_lds_dwordx4 v10, s[4:5]
	s_waitcnt lgkmcnt(13)
	v_mfma_f32_16x16x32_f16 v[60:63], v[172:175], v[196:199], v[60:63]
	s_waitcnt lgkmcnt(12)
	v_mfma_f32_16x16x32_f16 v[64:67], v[172:175], v[200:203], v[64:67]
	s_waitcnt lgkmcnt(11)
	v_mfma_f32_16x16x32_f16 v[68:71], v[172:175], v[204:207], v[68:71]
	s_waitcnt lgkmcnt(10)
	v_mfma_f32_16x16x32_f16 v[72:75], v[176:179], v[192:195], v[72:75]
	v_mfma_f32_16x16x32_f16 v[76:79], v[176:179], v[196:199], v[76:79]
	s_add_u32 m0, s28, 0x2000
	s_nop 0
	global_load_lds_dwordx4 v11, s[4:5]
	v_mfma_f32_16x16x32_f16 v[80:83], v[176:179], v[200:203], v[80:83]
	v_mfma_f32_16x16x32_f16 v[84:87], v[176:179], v[204:207], v[84:87]
	s_waitcnt lgkmcnt(9)
	v_mfma_f32_16x16x32_f16 v[88:91], v[180:183], v[192:195], v[88:91]
	v_mfma_f32_16x16x32_f16 v[92:95], v[180:183], v[196:199], v[92:95]
	v_mfma_f32_16x16x32_f16 v[96:99], v[180:183], v[200:203], v[96:99]
	s_add_u32 m0, s28, 0x4000
	s_nop 0
	global_load_lds_dwordx4 v12, s[4:5]
	v_mfma_f32_16x16x32_f16 v[100:103], v[180:183], v[204:207], v[100:103]
	s_waitcnt lgkmcnt(8)
	v_mfma_f32_16x16x32_f16 v[104:107], v[184:187], v[192:195], v[104:107]
	v_mfma_f32_16x16x32_f16 v[108:111], v[184:187], v[196:199], v[108:111]
	v_mfma_f32_16x16x32_f16 v[112:115], v[184:187], v[200:203], v[112:115]
	v_mfma_f32_16x16x32_f16 v[116:119], v[184:187], v[204:207], v[116:119]
	s_waitcnt lgkmcnt(7)
	ds_read_b128 v[172:175], v16 offset:53248
	ds_read_b128 v[192:195], v18 offset:53248
	ds_read_b128 v[196:199], v18 offset:55296
	ds_read_b128 v[200:203], v18 offset:57344
	ds_read_b128 v[204:207], v18 offset:59392
	ds_read_b128 v[176:179], v16 offset:55296
	ds_read_b128 v[180:183], v16 offset:57344
	ds_read_b128 v[184:187], v16 offset:59392
	s_waitcnt lgkmcnt(14)
	v_mfma_f32_16x16x32_f16 v[56:59], v[136:139], v[156:159], v[56:59]
	s_add_u32 m0, s28, 0x6000
	s_nop 0
	global_load_lds_dwordx4 v13, s[4:5]
	s_add_u32 s4, s4, s20
	s_addc_u32 s5, s5, 0
	s_waitcnt lgkmcnt(13)
	v_mfma_f32_16x16x32_f16 v[60:63], v[136:139], v[160:163], v[60:63]
	s_waitcnt lgkmcnt(12)
	v_mfma_f32_16x16x32_f16 v[64:67], v[136:139], v[164:167], v[64:67]
	s_waitcnt lgkmcnt(11)
	v_mfma_f32_16x16x32_f16 v[68:71], v[136:139], v[168:171], v[68:71]
	s_waitcnt lgkmcnt(10)
	v_mfma_f32_16x16x32_f16 v[72:75], v[140:143], v[156:159], v[72:75]
	v_mfma_f32_16x16x32_f16 v[76:79], v[140:143], v[160:163], v[76:79]
	s_add_u32 m0, s28, 0x9000
	s_nop 0
	global_load_lds_dwordx4 v10, s[6:7]
	v_mfma_f32_16x16x32_f16 v[80:83], v[140:143], v[164:167], v[80:83]
	v_mfma_f32_16x16x32_f16 v[84:87], v[140:143], v[168:171], v[84:87]
	s_waitcnt lgkmcnt(9)
	v_mfma_f32_16x16x32_f16 v[88:91], v[144:147], v[156:159], v[88:91]
	v_mfma_f32_16x16x32_f16 v[92:95], v[144:147], v[160:163], v[92:95]
	v_mfma_f32_16x16x32_f16 v[96:99], v[144:147], v[164:167], v[96:99]
	s_add_u32 m0, s28, 0xb000
	s_nop 0
	global_load_lds_dwordx4 v11, s[6:7]
	s_add_u32 s6, s6, s20
	s_addc_u32 s7, s7, 0
	v_mfma_f32_16x16x32_f16 v[100:103], v[144:147], v[168:171], v[100:103]
	s_waitcnt lgkmcnt(8)
	v_mfma_f32_16x16x32_f16 v[104:107], v[148:151], v[156:159], v[104:107]
	v_mfma_f32_16x16x32_f16 v[108:111], v[148:151], v[160:163], v[108:111]
	v_mfma_f32_16x16x32_f16 v[112:115], v[148:151], v[164:167], v[112:115]
	v_mfma_f32_16x16x32_f16 v[116:119], v[148:151], v[168:171], v[116:119]
	s_waitcnt vmcnt(6) lgkmcnt(0)
	s_barrier
	s_waitcnt lgkmcnt(7)
	ds_read_b128 v[136:139], v19
	ds_read_b128 v[156:159], v21
	ds_read_b128 v[160:163], v21 offset:2048
	ds_read_b128 v[164:167], v21 offset:4096
	ds_read_b128 v[168:171], v21 offset:6144
	ds_read_b128 v[140:143], v19 offset:2048
	ds_read_b128 v[144:147], v19 offset:4096
	ds_read_b128 v[148:151], v19 offset:6144
	s_waitcnt lgkmcnt(14)
	v_mfma_f32_16x16x32_f16 v[56:59], v[172:175], v[192:195], v[56:59]
	s_add_u32 m0, s28, 0xd000
	s_nop 0
	global_load_lds_dwordx4 v10, s[4:5]
	s_waitcnt lgkmcnt(13)
	v_mfma_f32_16x16x32_f16 v[60:63], v[172:175], v[196:199], v[60:63]
	s_waitcnt lgkmcnt(12)
	v_mfma_f32_16x16x32_f16 v[64:67], v[172:175], v[200:203], v[64:67]
	s_waitcnt lgkmcnt(11)
	v_mfma_f32_16x16x32_f16 v[68:71], v[172:175], v[204:207], v[68:71]
	s_waitcnt lgkmcnt(10)
	v_mfma_f32_16x16x32_f16 v[72:75], v[176:179], v[192:195], v[72:75]
	v_mfma_f32_16x16x32_f16 v[76:79], v[176:179], v[196:199], v[76:79]
	s_add_u32 m0, s28, 0xf000
	s_nop 0
	global_load_lds_dwordx4 v11, s[4:5]
	v_mfma_f32_16x16x32_f16 v[80:83], v[176:179], v[200:203], v[80:83]
	v_mfma_f32_16x16x32_f16 v[84:87], v[176:179], v[204:207], v[84:87]
	s_waitcnt lgkmcnt(9)
	v_mfma_f32_16x16x32_f16 v[88:91], v[180:183], v[192:195], v[88:91]
	v_mfma_f32_16x16x32_f16 v[92:95], v[180:183], v[196:199], v[92:95]
	v_mfma_f32_16x16x32_f16 v[96:99], v[180:183], v[200:203], v[96:99]
	s_add_u32 m0, s28, 0x11000
	s_nop 0
	global_load_lds_dwordx4 v12, s[4:5]
	v_mfma_f32_16x16x32_f16 v[100:103], v[180:183], v[204:207], v[100:103]
	s_waitcnt lgkmcnt(8)
	v_mfma_f32_16x16x32_f16 v[104:107], v[184:187], v[192:195], v[104:107]
	v_mfma_f32_16x16x32_f16 v[108:111], v[184:187], v[196:199], v[108:111]
	v_mfma_f32_16x16x32_f16 v[112:115], v[184:187], v[200:203], v[112:115]
	v_mfma_f32_16x16x32_f16 v[116:119], v[184:187], v[204:207], v[116:119]
	s_waitcnt lgkmcnt(7)
	ds_read_b128 v[172:175], v20
	ds_read_b128 v[192:195], v22
	ds_read_b128 v[196:199], v22 offset:2048
	ds_read_b128 v[200:203], v22 offset:4096
	ds_read_b128 v[204:207], v22 offset:6144
	ds_read_b128 v[176:179], v20 offset:2048
	ds_read_b128 v[180:183], v20 offset:4096
	ds_read_b128 v[184:187], v20 offset:6144
	s_waitcnt lgkmcnt(14)
	v_mfma_f32_16x16x32_f16 v[56:59], v[136:139], v[156:159], v[56:59]
	s_add_u32 m0, s28, 0x13000
	s_nop 0
	global_load_lds_dwordx4 v13, s[4:5]
	s_add_u32 s4, s4, s20
	s_addc_u32 s5, s5, 0
	s_waitcnt lgkmcnt(13)
	v_mfma_f32_16x16x32_f16 v[60:63], v[136:139], v[160:163], v[60:63]
	s_waitcnt lgkmcnt(12)
	v_mfma_f32_16x16x32_f16 v[64:67], v[136:139], v[164:167], v[64:67]
	s_waitcnt lgkmcnt(11)
	v_mfma_f32_16x16x32_f16 v[68:71], v[136:139], v[168:171], v[68:71]
	s_waitcnt lgkmcnt(10)
	v_mfma_f32_16x16x32_f16 v[72:75], v[140:143], v[156:159], v[72:75]
	v_mfma_f32_16x16x32_f16 v[76:79], v[140:143], v[160:163], v[76:79]
	s_add_u32 m0, s28, 0x16000
	s_nop 0
	global_load_lds_dwordx4 v10, s[6:7]
	v_mfma_f32_16x16x32_f16 v[80:83], v[140:143], v[164:167], v[80:83]
	v_mfma_f32_16x16x32_f16 v[84:87], v[140:143], v[168:171], v[84:87]
	s_waitcnt lgkmcnt(9)
	v_mfma_f32_16x16x32_f16 v[88:91], v[144:147], v[156:159], v[88:91]
	v_mfma_f32_16x16x32_f16 v[92:95], v[144:147], v[160:163], v[92:95]
	v_mfma_f32_16x16x32_f16 v[96:99], v[144:147], v[164:167], v[96:99]
	s_add_u32 m0, s28, 0x18000
	s_nop 0
	global_load_lds_dwordx4 v11, s[6:7]
	s_add_u32 s6, s6, s20
	s_addc_u32 s7, s7, 0
	v_mfma_f32_16x16x32_f16 v[100:103], v[144:147], v[168:171], v[100:103]
	s_waitcnt lgkmcnt(8)
	v_mfma_f32_16x16x32_f16 v[104:107], v[148:151], v[156:159], v[104:107]
	v_mfma_f32_16x16x32_f16 v[108:111], v[148:151], v[160:163], v[108:111]
	v_mfma_f32_16x16x32_f16 v[112:115], v[148:151], v[164:167], v[112:115]
	v_mfma_f32_16x16x32_f16 v[116:119], v[148:151], v[168:171], v[116:119]
	s_waitcnt vmcnt(6) lgkmcnt(0)
	s_barrier
	s_waitcnt lgkmcnt(7)
	ds_read_b128 v[136:139], v15
	ds_read_b128 v[156:159], v17
	ds_read_b128 v[160:163], v17 offset:2048
	ds_read_b128 v[164:167], v17 offset:4096
	ds_read_b128 v[168:171], v17 offset:6144
	ds_read_b128 v[140:143], v15 offset:2048
	ds_read_b128 v[144:147], v15 offset:4096
	ds_read_b128 v[148:151], v15 offset:6144
	s_waitcnt lgkmcnt(14)
	v_mfma_f32_16x16x32_f16 v[56:59], v[172:175], v[192:195], v[56:59]
	s_add_u32 m0, s28, 0x1a000
	s_nop 0
	global_load_lds_dwordx4 v10, s[4:5]
	s_waitcnt lgkmcnt(13)
	v_mfma_f32_16x16x32_f16 v[60:63], v[172:175], v[196:199], v[60:63]
	s_waitcnt lgkmcnt(12)
	v_mfma_f32_16x16x32_f16 v[64:67], v[172:175], v[200:203], v[64:67]
	s_waitcnt lgkmcnt(11)
	v_mfma_f32_16x16x32_f16 v[68:71], v[172:175], v[204:207], v[68:71]
	s_waitcnt lgkmcnt(10)
	v_mfma_f32_16x16x32_f16 v[72:75], v[176:179], v[192:195], v[72:75]
	v_mfma_f32_16x16x32_f16 v[76:79], v[176:179], v[196:199], v[76:79]
	s_add_u32 m0, s28, 0x1c000
	s_nop 0
	global_load_lds_dwordx4 v11, s[4:5]
	v_mfma_f32_16x16x32_f16 v[80:83], v[176:179], v[200:203], v[80:83]
	v_mfma_f32_16x16x32_f16 v[84:87], v[176:179], v[204:207], v[84:87]
	s_waitcnt lgkmcnt(9)
	v_mfma_f32_16x16x32_f16 v[88:91], v[180:183], v[192:195], v[88:91]
	v_mfma_f32_16x16x32_f16 v[92:95], v[180:183], v[196:199], v[92:95]
	v_mfma_f32_16x16x32_f16 v[96:99], v[180:183], v[200:203], v[96:99]
	s_add_u32 m0, s28, 0x1e000
	s_nop 0
	global_load_lds_dwordx4 v12, s[4:5]
	v_mfma_f32_16x16x32_f16 v[100:103], v[180:183], v[204:207], v[100:103]
	s_waitcnt lgkmcnt(8)
	v_mfma_f32_16x16x32_f16 v[104:107], v[184:187], v[192:195], v[104:107]
	v_mfma_f32_16x16x32_f16 v[108:111], v[184:187], v[196:199], v[108:111]
	v_mfma_f32_16x16x32_f16 v[112:115], v[184:187], v[200:203], v[112:115]
	v_mfma_f32_16x16x32_f16 v[116:119], v[184:187], v[204:207], v[116:119]
	s_waitcnt lgkmcnt(7)
	ds_read_b128 v[172:175], v16
	ds_read_b128 v[192:195], v18
	ds_read_b128 v[196:199], v18 offset:2048
	ds_read_b128 v[200:203], v18 offset:4096
	ds_read_b128 v[204:207], v18 offset:6144
	ds_read_b128 v[176:179], v16 offset:2048
	ds_read_b128 v[180:183], v16 offset:4096
	ds_read_b128 v[184:187], v16 offset:6144
	s_waitcnt lgkmcnt(14)
	v_mfma_f32_16x16x32_f16 v[56:59], v[136:139], v[156:159], v[56:59]
	s_add_u32 m0, s28, 0x20000
	s_nop 0
	global_load_lds_dwordx4 v13, s[4:5]
	s_add_u32 s4, s4, s20
	s_addc_u32 s5, s5, 0
	s_waitcnt lgkmcnt(13)
	v_mfma_f32_16x16x32_f16 v[60:63], v[136:139], v[160:163], v[60:63]
	s_waitcnt lgkmcnt(12)
	v_mfma_f32_16x16x32_f16 v[64:67], v[136:139], v[164:167], v[64:67]
	s_waitcnt lgkmcnt(11)
	v_mfma_f32_16x16x32_f16 v[68:71], v[136:139], v[168:171], v[68:71]
	s_waitcnt lgkmcnt(10)
	v_mfma_f32_16x16x32_f16 v[72:75], v[140:143], v[156:159], v[72:75]
	v_mfma_f32_16x16x32_f16 v[76:79], v[140:143], v[160:163], v[76:79]
	s_add_u32 m0, s28, 0x23000
	s_nop 0
	global_load_lds_dwordx4 v10, s[6:7]
	v_mfma_f32_16x16x32_f16 v[80:83], v[140:143], v[164:167], v[80:83]
	v_mfma_f32_16x16x32_f16 v[84:87], v[140:143], v[168:171], v[84:87]
	s_waitcnt lgkmcnt(9)
	v_mfma_f32_16x16x32_f16 v[88:91], v[144:147], v[156:159], v[88:91]
	v_mfma_f32_16x16x32_f16 v[92:95], v[144:147], v[160:163], v[92:95]
	v_mfma_f32_16x16x32_f16 v[96:99], v[144:147], v[164:167], v[96:99]
	s_add_u32 m0, s28, 0x25000
	s_nop 0
	global_load_lds_dwordx4 v11, s[6:7]
	s_add_u32 s6, s6, s20
	s_addc_u32 s7, s7, 0
	v_mfma_f32_16x16x32_f16 v[100:103], v[144:147], v[168:171], v[100:103]
	s_waitcnt lgkmcnt(8)
	v_mfma_f32_16x16x32_f16 v[104:107], v[148:151], v[156:159], v[104:107]
	v_mfma_f32_16x16x32_f16 v[108:111], v[148:151], v[160:163], v[108:111]
	v_mfma_f32_16x16x32_f16 v[112:115], v[148:151], v[164:167], v[112:115]
	v_mfma_f32_16x16x32_f16 v[116:119], v[148:151], v[168:171], v[116:119]
	s_waitcnt vmcnt(6) lgkmcnt(0)
	s_barrier
	s_waitcnt lgkmcnt(7)
	ds_read_b128 v[136:139], v15 offset:53248
	ds_read_b128 v[156:159], v17 offset:53248
	ds_read_b128 v[160:163], v17 offset:55296
	ds_read_b128 v[164:167], v17 offset:57344
	ds_read_b128 v[168:171], v17 offset:59392
	ds_read_b128 v[140:143], v15 offset:55296
	ds_read_b128 v[144:147], v15 offset:57344
	ds_read_b128 v[148:151], v15 offset:59392
	s_waitcnt lgkmcnt(14)
	v_mfma_f32_16x16x32_f16 v[56:59], v[172:175], v[192:195], v[56:59]
	s_add_u32 m0, s28, 0x0
	s_nop 0
	global_load_lds_dwordx4 v10, s[4:5]
	s_waitcnt lgkmcnt(13)
	v_mfma_f32_16x16x32_f16 v[60:63], v[172:175], v[196:199], v[60:63]
	s_waitcnt lgkmcnt(12)
	v_mfma_f32_16x16x32_f16 v[64:67], v[172:175], v[200:203], v[64:67]
	s_waitcnt lgkmcnt(11)
	v_mfma_f32_16x16x32_f16 v[68:71], v[172:175], v[204:207], v[68:71]
	s_waitcnt lgkmcnt(10)
	v_mfma_f32_16x16x32_f16 v[72:75], v[176:179], v[192:195], v[72:75]
	v_mfma_f32_16x16x32_f16 v[76:79], v[176:179], v[196:199], v[76:79]
	s_add_u32 m0, s28, 0x2000
	s_nop 0
	global_load_lds_dwordx4 v11, s[4:5]
	v_mfma_f32_16x16x32_f16 v[80:83], v[176:179], v[200:203], v[80:83]
	v_mfma_f32_16x16x32_f16 v[84:87], v[176:179], v[204:207], v[84:87]
	s_waitcnt lgkmcnt(9)
	v_mfma_f32_16x16x32_f16 v[88:91], v[180:183], v[192:195], v[88:91]
	v_mfma_f32_16x16x32_f16 v[92:95], v[180:183], v[196:199], v[92:95]
	v_mfma_f32_16x16x32_f16 v[96:99], v[180:183], v[200:203], v[96:99]
	s_add_u32 m0, s28, 0x4000
	s_nop 0
	global_load_lds_dwordx4 v12, s[4:5]
	v_mfma_f32_16x16x32_f16 v[100:103], v[180:183], v[204:207], v[100:103]
	s_waitcnt lgkmcnt(8)
	v_mfma_f32_16x16x32_f16 v[104:107], v[184:187], v[192:195], v[104:107]
	v_mfma_f32_16x16x32_f16 v[108:111], v[184:187], v[196:199], v[108:111]
	v_mfma_f32_16x16x32_f16 v[112:115], v[184:187], v[200:203], v[112:115]
	v_mfma_f32_16x16x32_f16 v[116:119], v[184:187], v[204:207], v[116:119]
	s_waitcnt lgkmcnt(7)
	ds_read_b128 v[172:175], v16 offset:53248
	ds_read_b128 v[192:195], v18 offset:53248
	ds_read_b128 v[196:199], v18 offset:55296
	ds_read_b128 v[200:203], v18 offset:57344
	ds_read_b128 v[204:207], v18 offset:59392
	ds_read_b128 v[176:179], v16 offset:55296
	ds_read_b128 v[180:183], v16 offset:57344
	ds_read_b128 v[184:187], v16 offset:59392
	s_waitcnt lgkmcnt(14)
	v_mfma_f32_16x16x32_f16 v[56:59], v[136:139], v[156:159], v[56:59]
	s_add_u32 m0, s28, 0x6000
	s_nop 0
	global_load_lds_dwordx4 v13, s[4:5]
	s_add_u32 s4, s4, s20
	s_addc_u32 s5, s5, 0
	s_waitcnt lgkmcnt(13)
	v_mfma_f32_16x16x32_f16 v[60:63], v[136:139], v[160:163], v[60:63]
	s_waitcnt lgkmcnt(12)
	v_mfma_f32_16x16x32_f16 v[64:67], v[136:139], v[164:167], v[64:67]
	s_waitcnt lgkmcnt(11)
	v_mfma_f32_16x16x32_f16 v[68:71], v[136:139], v[168:171], v[68:71]
	s_waitcnt lgkmcnt(10)
	v_mfma_f32_16x16x32_f16 v[72:75], v[140:143], v[156:159], v[72:75]
	v_mfma_f32_16x16x32_f16 v[76:79], v[140:143], v[160:163], v[76:79]
	s_add_u32 m0, s28, 0x9000
	s_nop 0
	global_load_lds_dwordx4 v10, s[6:7]
	v_mfma_f32_16x16x32_f16 v[80:83], v[140:143], v[164:167], v[80:83]
	v_mfma_f32_16x16x32_f16 v[84:87], v[140:143], v[168:171], v[84:87]
	s_waitcnt lgkmcnt(9)
	v_mfma_f32_16x16x32_f16 v[88:91], v[144:147], v[156:159], v[88:91]
	v_mfma_f32_16x16x32_f16 v[92:95], v[144:147], v[160:163], v[92:95]
	v_mfma_f32_16x16x32_f16 v[96:99], v[144:147], v[164:167], v[96:99]
	s_add_u32 m0, s28, 0xb000
	s_nop 0
	global_load_lds_dwordx4 v11, s[6:7]
	s_add_u32 s6, s6, s20
	s_addc_u32 s7, s7, 0
	v_mfma_f32_16x16x32_f16 v[100:103], v[144:147], v[168:171], v[100:103]
	s_waitcnt lgkmcnt(8)
	v_mfma_f32_16x16x32_f16 v[104:107], v[148:151], v[156:159], v[104:107]
	v_mfma_f32_16x16x32_f16 v[108:111], v[148:151], v[160:163], v[108:111]
	v_mfma_f32_16x16x32_f16 v[112:115], v[148:151], v[164:167], v[112:115]
	v_mfma_f32_16x16x32_f16 v[116:119], v[148:151], v[168:171], v[116:119]
	s_waitcnt vmcnt(6) lgkmcnt(0)
	s_barrier
	s_waitcnt lgkmcnt(7)
	ds_read_b128 v[136:139], v19
	ds_read_b128 v[156:159], v21
	ds_read_b128 v[160:163], v21 offset:2048
	ds_read_b128 v[164:167], v21 offset:4096
	ds_read_b128 v[168:171], v21 offset:6144
	ds_read_b128 v[140:143], v19 offset:2048
	ds_read_b128 v[144:147], v19 offset:4096
	ds_read_b128 v[148:151], v19 offset:6144
	s_waitcnt lgkmcnt(14)
	v_mfma_f32_16x16x32_f16 v[56:59], v[172:175], v[192:195], v[56:59]
	s_add_u32 m0, s28, 0xd000
	s_nop 0
	global_load_lds_dwordx4 v10, s[4:5]
	s_waitcnt lgkmcnt(13)
	v_mfma_f32_16x16x32_f16 v[60:63], v[172:175], v[196:199], v[60:63]
	s_waitcnt lgkmcnt(12)
	v_mfma_f32_16x16x32_f16 v[64:67], v[172:175], v[200:203], v[64:67]
	s_waitcnt lgkmcnt(11)
	v_mfma_f32_16x16x32_f16 v[68:71], v[172:175], v[204:207], v[68:71]
	s_waitcnt lgkmcnt(10)
	v_mfma_f32_16x16x32_f16 v[72:75], v[176:179], v[192:195], v[72:75]
	v_mfma_f32_16x16x32_f16 v[76:79], v[176:179], v[196:199], v[76:79]
	s_add_u32 m0, s28, 0xf000
	s_nop 0
	global_load_lds_dwordx4 v11, s[4:5]
	v_mfma_f32_16x16x32_f16 v[80:83], v[176:179], v[200:203], v[80:83]
	v_mfma_f32_16x16x32_f16 v[84:87], v[176:179], v[204:207], v[84:87]
	s_waitcnt lgkmcnt(9)
	v_mfma_f32_16x16x32_f16 v[88:91], v[180:183], v[192:195], v[88:91]
	v_mfma_f32_16x16x32_f16 v[92:95], v[180:183], v[196:199], v[92:95]
	v_mfma_f32_16x16x32_f16 v[96:99], v[180:183], v[200:203], v[96:99]
	s_add_u32 m0, s28, 0x11000
	s_nop 0
	global_load_lds_dwordx4 v12, s[4:5]
	v_mfma_f32_16x16x32_f16 v[100:103], v[180:183], v[204:207], v[100:103]
	s_waitcnt lgkmcnt(8)
	v_mfma_f32_16x16x32_f16 v[104:107], v[184:187], v[192:195], v[104:107]
	v_mfma_f32_16x16x32_f16 v[108:111], v[184:187], v[196:199], v[108:111]
	v_mfma_f32_16x16x32_f16 v[112:115], v[184:187], v[200:203], v[112:115]
	v_mfma_f32_16x16x32_f16 v[116:119], v[184:187], v[204:207], v[116:119]
	s_waitcnt lgkmcnt(7)
	ds_read_b128 v[172:175], v20
	ds_read_b128 v[192:195], v22
	ds_read_b128 v[196:199], v22 offset:2048
	ds_read_b128 v[200:203], v22 offset:4096
	ds_read_b128 v[204:207], v22 offset:6144
	ds_read_b128 v[176:179], v20 offset:2048
	ds_read_b128 v[180:183], v20 offset:4096
	ds_read_b128 v[184:187], v20 offset:6144
	s_waitcnt lgkmcnt(14)
	v_mfma_f32_16x16x32_f16 v[56:59], v[136:139], v[156:159], v[56:59]
	s_add_u32 m0, s28, 0x13000
	s_nop 0
	global_load_lds_dwordx4 v13, s[4:5]
	s_add_u32 s4, s4, s20
	s_addc_u32 s5, s5, 0
	s_waitcnt lgkmcnt(13)
	v_mfma_f32_16x16x32_f16 v[60:63], v[136:139], v[160:163], v[60:63]
	s_waitcnt lgkmcnt(12)
	v_mfma_f32_16x16x32_f16 v[64:67], v[136:139], v[164:167], v[64:67]
	s_waitcnt lgkmcnt(11)
	v_mfma_f32_16x16x32_f16 v[68:71], v[136:139], v[168:171], v[68:71]
	s_waitcnt lgkmcnt(10)
	v_mfma_f32_16x16x32_f16 v[72:75], v[140:143], v[156:159], v[72:75]
	v_mfma_f32_16x16x32_f16 v[76:79], v[140:143], v[160:163], v[76:79]
	s_add_u32 m0, s28, 0x16000
	s_nop 0
	global_load_lds_dwordx4 v10, s[6:7]
	v_mfma_f32_16x16x32_f16 v[80:83], v[140:143], v[164:167], v[80:83]
	v_mfma_f32_16x16x32_f16 v[84:87], v[140:143], v[168:171], v[84:87]
	s_waitcnt lgkmcnt(9)
	v_mfma_f32_16x16x32_f16 v[88:91], v[144:147], v[156:159], v[88:91]
	v_mfma_f32_16x16x32_f16 v[92:95], v[144:147], v[160:163], v[92:95]
	v_mfma_f32_16x16x32_f16 v[96:99], v[144:147], v[164:167], v[96:99]
	s_add_u32 m0, s28, 0x18000
	s_nop 0
	global_load_lds_dwordx4 v11, s[6:7]
	s_add_u32 s6, s6, s20
	s_addc_u32 s7, s7, 0
	v_mfma_f32_16x16x32_f16 v[100:103], v[144:147], v[168:171], v[100:103]
	s_waitcnt lgkmcnt(8)
	v_mfma_f32_16x16x32_f16 v[104:107], v[148:151], v[156:159], v[104:107]
	v_mfma_f32_16x16x32_f16 v[108:111], v[148:151], v[160:163], v[108:111]
	v_mfma_f32_16x16x32_f16 v[112:115], v[148:151], v[164:167], v[112:115]
	v_mfma_f32_16x16x32_f16 v[116:119], v[148:151], v[168:171], v[116:119]
	s_waitcnt vmcnt(6) lgkmcnt(0)
	s_barrier
	s_waitcnt lgkmcnt(7)
	ds_read_b128 v[136:139], v15
	ds_read_b128 v[156:159], v17
	ds_read_b128 v[160:163], v17 offset:2048
	ds_read_b128 v[164:167], v17 offset:4096
	ds_read_b128 v[168:171], v17 offset:6144
	ds_read_b128 v[140:143], v15 offset:2048
	ds_read_b128 v[144:147], v15 offset:4096
	ds_read_b128 v[148:151], v15 offset:6144
	s_waitcnt lgkmcnt(14)
	v_mfma_f32_16x16x32_f16 v[56:59], v[172:175], v[192:195], v[56:59]
	s_add_u32 m0, s28, 0x1a000
	s_nop 0
	global_load_lds_dwordx4 v10, s[4:5]
	s_waitcnt lgkmcnt(13)
	v_mfma_f32_16x16x32_f16 v[60:63], v[172:175], v[196:199], v[60:63]
	s_waitcnt lgkmcnt(12)
	v_mfma_f32_16x16x32_f16 v[64:67], v[172:175], v[200:203], v[64:67]
	s_waitcnt lgkmcnt(11)
	v_mfma_f32_16x16x32_f16 v[68:71], v[172:175], v[204:207], v[68:71]
	s_waitcnt lgkmcnt(10)
	v_mfma_f32_16x16x32_f16 v[72:75], v[176:179], v[192:195], v[72:75]
	v_mfma_f32_16x16x32_f16 v[76:79], v[176:179], v[196:199], v[76:79]
	s_add_u32 m0, s28, 0x1c000
	s_nop 0
	global_load_lds_dwordx4 v11, s[4:5]
	v_mfma_f32_16x16x32_f16 v[80:83], v[176:179], v[200:203], v[80:83]
	v_mfma_f32_16x16x32_f16 v[84:87], v[176:179], v[204:207], v[84:87]
	s_waitcnt lgkmcnt(9)
	v_mfma_f32_16x16x32_f16 v[88:91], v[180:183], v[192:195], v[88:91]
	v_mfma_f32_16x16x32_f16 v[92:95], v[180:183], v[196:199], v[92:95]
	v_mfma_f32_16x16x32_f16 v[96:99], v[180:183], v[200:203], v[96:99]
	s_add_u32 m0, s28, 0x1e000
	s_nop 0
	global_load_lds_dwordx4 v12, s[4:5]
	v_mfma_f32_16x16x32_f16 v[100:103], v[180:183], v[204:207], v[100:103]
	s_waitcnt lgkmcnt(8)
	v_mfma_f32_16x16x32_f16 v[104:107], v[184:187], v[192:195], v[104:107]
	v_mfma_f32_16x16x32_f16 v[108:111], v[184:187], v[196:199], v[108:111]
	v_mfma_f32_16x16x32_f16 v[112:115], v[184:187], v[200:203], v[112:115]
	v_mfma_f32_16x16x32_f16 v[116:119], v[184:187], v[204:207], v[116:119]
	s_waitcnt lgkmcnt(7)
	ds_read_b128 v[172:175], v16
	ds_read_b128 v[192:195], v18
	ds_read_b128 v[196:199], v18 offset:2048
	ds_read_b128 v[200:203], v18 offset:4096
	ds_read_b128 v[204:207], v18 offset:6144
	ds_read_b128 v[176:179], v16 offset:2048
	ds_read_b128 v[180:183], v16 offset:4096
	ds_read_b128 v[184:187], v16 offset:6144
	s_waitcnt lgkmcnt(14)
	v_mfma_f32_16x16x32_f16 v[56:59], v[136:139], v[156:159], v[56:59]
	s_add_u32 m0, s28, 0x20000
	s_nop 0
	global_load_lds_dwordx4 v13, s[4:5]
	s_add_u32 s4, s4, s20
	s_addc_u32 s5, s5, 0
	s_waitcnt lgkmcnt(13)
	v_mfma_f32_16x16x32_f16 v[60:63], v[136:139], v[160:163], v[60:63]
	s_waitcnt lgkmcnt(12)
	v_mfma_f32_16x16x32_f16 v[64:67], v[136:139], v[164:167], v[64:67]
	s_waitcnt lgkmcnt(11)
	v_mfma_f32_16x16x32_f16 v[68:71], v[136:139], v[168:171], v[68:71]
	s_waitcnt lgkmcnt(10)
	v_mfma_f32_16x16x32_f16 v[72:75], v[140:143], v[156:159], v[72:75]
	v_mfma_f32_16x16x32_f16 v[76:79], v[140:143], v[160:163], v[76:79]
	s_add_u32 m0, s28, 0x23000
	s_nop 0
	global_load_lds_dwordx4 v10, s[6:7]
	v_mfma_f32_16x16x32_f16 v[80:83], v[140:143], v[164:167], v[80:83]
	v_mfma_f32_16x16x32_f16 v[84:87], v[140:143], v[168:171], v[84:87]
	s_waitcnt lgkmcnt(9)
	v_mfma_f32_16x16x32_f16 v[88:91], v[144:147], v[156:159], v[88:91]
	v_mfma_f32_16x16x32_f16 v[92:95], v[144:147], v[160:163], v[92:95]
	v_mfma_f32_16x16x32_f16 v[96:99], v[144:147], v[164:167], v[96:99]
	s_add_u32 m0, s28, 0x25000
	s_nop 0
	global_load_lds_dwordx4 v11, s[6:7]
	s_add_u32 s6, s6, s20
	s_addc_u32 s7, s7, 0
	v_mfma_f32_16x16x32_f16 v[100:103], v[144:147], v[168:171], v[100:103]
	s_waitcnt lgkmcnt(8)
	v_mfma_f32_16x16x32_f16 v[104:107], v[148:151], v[156:159], v[104:107]
	v_mfma_f32_16x16x32_f16 v[108:111], v[148:151], v[160:163], v[108:111]
	v_mfma_f32_16x16x32_f16 v[112:115], v[148:151], v[164:167], v[112:115]
	v_mfma_f32_16x16x32_f16 v[116:119], v[148:151], v[168:171], v[116:119]
	s_waitcnt vmcnt(6) lgkmcnt(0)
	s_barrier
	s_waitcnt lgkmcnt(7)
	ds_read_b128 v[136:139], v15 offset:53248
	ds_read_b128 v[156:159], v17 offset:53248
	ds_read_b128 v[160:163], v17 offset:55296
	ds_read_b128 v[164:167], v17 offset:57344
	ds_read_b128 v[168:171], v17 offset:59392
	ds_read_b128 v[140:143], v15 offset:55296
	ds_read_b128 v[144:147], v15 offset:57344
	ds_read_b128 v[148:151], v15 offset:59392
	s_waitcnt lgkmcnt(14)
	v_mfma_f32_16x16x32_f16 v[56:59], v[172:175], v[192:195], v[56:59]
	s_add_u32 m0, s28, 0x0
	s_nop 0
	global_load_lds_dwordx4 v10, s[4:5]
	s_waitcnt lgkmcnt(13)
	v_mfma_f32_16x16x32_f16 v[60:63], v[172:175], v[196:199], v[60:63]
	s_waitcnt lgkmcnt(12)
	v_mfma_f32_16x16x32_f16 v[64:67], v[172:175], v[200:203], v[64:67]
	s_waitcnt lgkmcnt(11)
	v_mfma_f32_16x16x32_f16 v[68:71], v[172:175], v[204:207], v[68:71]
	s_waitcnt lgkmcnt(10)
	v_mfma_f32_16x16x32_f16 v[72:75], v[176:179], v[192:195], v[72:75]
	v_mfma_f32_16x16x32_f16 v[76:79], v[176:179], v[196:199], v[76:79]
	s_add_u32 m0, s28, 0x2000
	s_nop 0
	global_load_lds_dwordx4 v11, s[4:5]
	v_mfma_f32_16x16x32_f16 v[80:83], v[176:179], v[200:203], v[80:83]
	v_mfma_f32_16x16x32_f16 v[84:87], v[176:179], v[204:207], v[84:87]
	s_waitcnt lgkmcnt(9)
	v_mfma_f32_16x16x32_f16 v[88:91], v[180:183], v[192:195], v[88:91]
	v_mfma_f32_16x16x32_f16 v[92:95], v[180:183], v[196:199], v[92:95]
	v_mfma_f32_16x16x32_f16 v[96:99], v[180:183], v[200:203], v[96:99]
	s_add_u32 m0, s28, 0x4000
	s_nop 0
	global_load_lds_dwordx4 v12, s[4:5]
	v_mfma_f32_16x16x32_f16 v[100:103], v[180:183], v[204:207], v[100:103]
	s_waitcnt lgkmcnt(8)
	v_mfma_f32_16x16x32_f16 v[104:107], v[184:187], v[192:195], v[104:107]
	v_mfma_f32_16x16x32_f16 v[108:111], v[184:187], v[196:199], v[108:111]
	v_mfma_f32_16x16x32_f16 v[112:115], v[184:187], v[200:203], v[112:115]
	v_mfma_f32_16x16x32_f16 v[116:119], v[184:187], v[204:207], v[116:119]
	s_waitcnt lgkmcnt(7)
	ds_read_b128 v[172:175], v16 offset:53248
	ds_read_b128 v[192:195], v18 offset:53248
	ds_read_b128 v[196:199], v18 offset:55296
	ds_read_b128 v[200:203], v18 offset:57344
	ds_read_b128 v[204:207], v18 offset:59392
	ds_read_b128 v[176:179], v16 offset:55296
	ds_read_b128 v[180:183], v16 offset:57344
	ds_read_b128 v[184:187], v16 offset:59392
	s_waitcnt lgkmcnt(14)
	v_mfma_f32_16x16x32_f16 v[56:59], v[136:139], v[156:159], v[56:59]
	s_add_u32 m0, s28, 0x6000
	s_nop 0
	global_load_lds_dwordx4 v13, s[4:5]
	s_add_u32 s4, s4, s20
	s_addc_u32 s5, s5, 0
	s_waitcnt lgkmcnt(13)
	v_mfma_f32_16x16x32_f16 v[60:63], v[136:139], v[160:163], v[60:63]
	s_waitcnt lgkmcnt(12)
	v_mfma_f32_16x16x32_f16 v[64:67], v[136:139], v[164:167], v[64:67]
	s_waitcnt lgkmcnt(11)
	v_mfma_f32_16x16x32_f16 v[68:71], v[136:139], v[168:171], v[68:71]
	s_waitcnt lgkmcnt(10)
	v_mfma_f32_16x16x32_f16 v[72:75], v[140:143], v[156:159], v[72:75]
	v_mfma_f32_16x16x32_f16 v[76:79], v[140:143], v[160:163], v[76:79]
	s_add_u32 m0, s28, 0x9000
	s_nop 0
	global_load_lds_dwordx4 v10, s[6:7]
	v_mfma_f32_16x16x32_f16 v[80:83], v[140:143], v[164:167], v[80:83]
	v_mfma_f32_16x16x32_f16 v[84:87], v[140:143], v[168:171], v[84:87]
	s_waitcnt lgkmcnt(9)
	v_mfma_f32_16x16x32_f16 v[88:91], v[144:147], v[156:159], v[88:91]
	v_mfma_f32_16x16x32_f16 v[92:95], v[144:147], v[160:163], v[92:95]
	v_mfma_f32_16x16x32_f16 v[96:99], v[144:147], v[164:167], v[96:99]
	s_add_u32 m0, s28, 0xb000
	s_nop 0
	global_load_lds_dwordx4 v11, s[6:7]
	s_add_u32 s6, s6, s20
	s_addc_u32 s7, s7, 0
	v_mfma_f32_16x16x32_f16 v[100:103], v[144:147], v[168:171], v[100:103]
	s_waitcnt lgkmcnt(8)
	v_mfma_f32_16x16x32_f16 v[104:107], v[148:151], v[156:159], v[104:107]
	v_mfma_f32_16x16x32_f16 v[108:111], v[148:151], v[160:163], v[108:111]
	v_mfma_f32_16x16x32_f16 v[112:115], v[148:151], v[164:167], v[112:115]
	v_mfma_f32_16x16x32_f16 v[116:119], v[148:151], v[168:171], v[116:119]
	s_waitcnt vmcnt(6) lgkmcnt(0)
	s_barrier
	s_waitcnt lgkmcnt(7)
	ds_read_b128 v[136:139], v19
	ds_read_b128 v[156:159], v21
	ds_read_b128 v[160:163], v21 offset:2048
	ds_read_b128 v[164:167], v21 offset:4096
	ds_read_b128 v[168:171], v21 offset:6144
	ds_read_b128 v[140:143], v19 offset:2048
	ds_read_b128 v[144:147], v19 offset:4096
	ds_read_b128 v[148:151], v19 offset:6144
	s_waitcnt lgkmcnt(14)
	v_mfma_f32_16x16x32_f16 v[56:59], v[172:175], v[192:195], v[56:59]
	s_add_u32 m0, s28, 0xd000
	s_nop 0
	global_load_lds_dwordx4 v10, s[4:5]
	s_waitcnt lgkmcnt(13)
	v_mfma_f32_16x16x32_f16 v[60:63], v[172:175], v[196:199], v[60:63]
	s_waitcnt lgkmcnt(12)
	v_mfma_f32_16x16x32_f16 v[64:67], v[172:175], v[200:203], v[64:67]
	s_waitcnt lgkmcnt(11)
	v_mfma_f32_16x16x32_f16 v[68:71], v[172:175], v[204:207], v[68:71]
	s_waitcnt lgkmcnt(10)
	v_mfma_f32_16x16x32_f16 v[72:75], v[176:179], v[192:195], v[72:75]
	v_mfma_f32_16x16x32_f16 v[76:79], v[176:179], v[196:199], v[76:79]
	s_add_u32 m0, s28, 0xf000
	s_nop 0
	global_load_lds_dwordx4 v11, s[4:5]
	v_mfma_f32_16x16x32_f16 v[80:83], v[176:179], v[200:203], v[80:83]
	v_mfma_f32_16x16x32_f16 v[84:87], v[176:179], v[204:207], v[84:87]
	s_waitcnt lgkmcnt(9)
	v_mfma_f32_16x16x32_f16 v[88:91], v[180:183], v[192:195], v[88:91]
	v_mfma_f32_16x16x32_f16 v[92:95], v[180:183], v[196:199], v[92:95]
	v_mfma_f32_16x16x32_f16 v[96:99], v[180:183], v[200:203], v[96:99]
	s_add_u32 m0, s28, 0x11000
	s_nop 0
	global_load_lds_dwordx4 v12, s[4:5]
	v_mfma_f32_16x16x32_f16 v[100:103], v[180:183], v[204:207], v[100:103]
	s_waitcnt lgkmcnt(8)
	v_mfma_f32_16x16x32_f16 v[104:107], v[184:187], v[192:195], v[104:107]
	v_mfma_f32_16x16x32_f16 v[108:111], v[184:187], v[196:199], v[108:111]
	v_mfma_f32_16x16x32_f16 v[112:115], v[184:187], v[200:203], v[112:115]
	v_mfma_f32_16x16x32_f16 v[116:119], v[184:187], v[204:207], v[116:119]
	s_waitcnt lgkmcnt(7)
	ds_read_b128 v[172:175], v20
	ds_read_b128 v[192:195], v22
	ds_read_b128 v[196:199], v22 offset:2048
	ds_read_b128 v[200:203], v22 offset:4096
	ds_read_b128 v[204:207], v22 offset:6144
	ds_read_b128 v[176:179], v20 offset:2048
	ds_read_b128 v[180:183], v20 offset:4096
	ds_read_b128 v[184:187], v20 offset:6144
	s_waitcnt lgkmcnt(14)
	v_mfma_f32_16x16x32_f16 v[56:59], v[136:139], v[156:159], v[56:59]
	s_add_u32 m0, s28, 0x13000
	s_nop 0
	global_load_lds_dwordx4 v13, s[4:5]
	s_add_u32 s4, s4, s20
	s_addc_u32 s5, s5, 0
	s_waitcnt lgkmcnt(13)
	v_mfma_f32_16x16x32_f16 v[60:63], v[136:139], v[160:163], v[60:63]
	s_waitcnt lgkmcnt(12)
	v_mfma_f32_16x16x32_f16 v[64:67], v[136:139], v[164:167], v[64:67]
	s_waitcnt lgkmcnt(11)
	v_mfma_f32_16x16x32_f16 v[68:71], v[136:139], v[168:171], v[68:71]
	s_waitcnt lgkmcnt(10)
	v_mfma_f32_16x16x32_f16 v[72:75], v[140:143], v[156:159], v[72:75]
	v_mfma_f32_16x16x32_f16 v[76:79], v[140:143], v[160:163], v[76:79]
	s_add_u32 m0, s28, 0x16000
	s_nop 0
	global_load_lds_dwordx4 v10, s[6:7]
	v_mfma_f32_16x16x32_f16 v[80:83], v[140:143], v[164:167], v[80:83]
	v_mfma_f32_16x16x32_f16 v[84:87], v[140:143], v[168:171], v[84:87]
	s_waitcnt lgkmcnt(9)
	v_mfma_f32_16x16x32_f16 v[88:91], v[144:147], v[156:159], v[88:91]
	v_mfma_f32_16x16x32_f16 v[92:95], v[144:147], v[160:163], v[92:95]
	v_mfma_f32_16x16x32_f16 v[96:99], v[144:147], v[164:167], v[96:99]
	s_add_u32 m0, s28, 0x18000
	s_nop 0
	global_load_lds_dwordx4 v11, s[6:7]
	s_add_u32 s6, s6, s20
	s_addc_u32 s7, s7, 0
	v_mfma_f32_16x16x32_f16 v[100:103], v[144:147], v[168:171], v[100:103]
	s_waitcnt lgkmcnt(8)
	v_mfma_f32_16x16x32_f16 v[104:107], v[148:151], v[156:159], v[104:107]
	v_mfma_f32_16x16x32_f16 v[108:111], v[148:151], v[160:163], v[108:111]
	v_mfma_f32_16x16x32_f16 v[112:115], v[148:151], v[164:167], v[112:115]
	v_mfma_f32_16x16x32_f16 v[116:119], v[148:151], v[168:171], v[116:119]
	s_waitcnt vmcnt(6) lgkmcnt(0)
	s_barrier
	s_waitcnt lgkmcnt(7)
	ds_read_b128 v[136:139], v15
	ds_read_b128 v[156:159], v17
	ds_read_b128 v[160:163], v17 offset:2048
	ds_read_b128 v[164:167], v17 offset:4096
	ds_read_b128 v[168:171], v17 offset:6144
	ds_read_b128 v[140:143], v15 offset:2048
	ds_read_b128 v[144:147], v15 offset:4096
	ds_read_b128 v[148:151], v15 offset:6144
	s_waitcnt lgkmcnt(14)
	v_mfma_f32_16x16x32_f16 v[56:59], v[172:175], v[192:195], v[56:59]
	s_add_u32 m0, s28, 0x1a000
	s_nop 0
	global_load_lds_dwordx4 v10, s[4:5]
	s_waitcnt lgkmcnt(13)
	v_mfma_f32_16x16x32_f16 v[60:63], v[172:175], v[196:199], v[60:63]
	s_waitcnt lgkmcnt(12)
	v_mfma_f32_16x16x32_f16 v[64:67], v[172:175], v[200:203], v[64:67]
	s_waitcnt lgkmcnt(11)
	v_mfma_f32_16x16x32_f16 v[68:71], v[172:175], v[204:207], v[68:71]
	s_waitcnt lgkmcnt(10)
	v_mfma_f32_16x16x32_f16 v[72:75], v[176:179], v[192:195], v[72:75]
	v_mfma_f32_16x16x32_f16 v[76:79], v[176:179], v[196:199], v[76:79]
	s_add_u32 m0, s28, 0x1c000
	s_nop 0
	global_load_lds_dwordx4 v11, s[4:5]
	v_mfma_f32_16x16x32_f16 v[80:83], v[176:179], v[200:203], v[80:83]
	v_mfma_f32_16x16x32_f16 v[84:87], v[176:179], v[204:207], v[84:87]
	s_waitcnt lgkmcnt(9)
	v_mfma_f32_16x16x32_f16 v[88:91], v[180:183], v[192:195], v[88:91]
	v_mfma_f32_16x16x32_f16 v[92:95], v[180:183], v[196:199], v[92:95]
	v_mfma_f32_16x16x32_f16 v[96:99], v[180:183], v[200:203], v[96:99]
	s_add_u32 m0, s28, 0x1e000
	s_nop 0
	global_load_lds_dwordx4 v12, s[4:5]
	v_mfma_f32_16x16x32_f16 v[100:103], v[180:183], v[204:207], v[100:103]
	s_waitcnt lgkmcnt(8)
	v_mfma_f32_16x16x32_f16 v[104:107], v[184:187], v[192:195], v[104:107]
	v_mfma_f32_16x16x32_f16 v[108:111], v[184:187], v[196:199], v[108:111]
	v_mfma_f32_16x16x32_f16 v[112:115], v[184:187], v[200:203], v[112:115]
	v_mfma_f32_16x16x32_f16 v[116:119], v[184:187], v[204:207], v[116:119]
	s_waitcnt lgkmcnt(7)
	ds_read_b128 v[172:175], v16
	ds_read_b128 v[192:195], v18
	ds_read_b128 v[196:199], v18 offset:2048
	ds_read_b128 v[200:203], v18 offset:4096
	ds_read_b128 v[204:207], v18 offset:6144
	ds_read_b128 v[176:179], v16 offset:2048
	ds_read_b128 v[180:183], v16 offset:4096
	ds_read_b128 v[184:187], v16 offset:6144
	s_waitcnt lgkmcnt(14)
	v_mfma_f32_16x16x32_f16 v[56:59], v[136:139], v[156:159], v[56:59]
	s_add_u32 m0, s28, 0x20000
	s_nop 0
	global_load_lds_dwordx4 v13, s[4:5]
	s_add_u32 s4, s4, s20
	s_addc_u32 s5, s5, 0
	s_waitcnt lgkmcnt(13)
	v_mfma_f32_16x16x32_f16 v[60:63], v[136:139], v[160:163], v[60:63]
	s_waitcnt lgkmcnt(12)
	v_mfma_f32_16x16x32_f16 v[64:67], v[136:139], v[164:167], v[64:67]
	s_waitcnt lgkmcnt(11)
	v_mfma_f32_16x16x32_f16 v[68:71], v[136:139], v[168:171], v[68:71]
	s_waitcnt lgkmcnt(10)
	v_mfma_f32_16x16x32_f16 v[72:75], v[140:143], v[156:159], v[72:75]
	v_mfma_f32_16x16x32_f16 v[76:79], v[140:143], v[160:163], v[76:79]
	s_add_u32 m0, s28, 0x23000
	s_nop 0
	global_load_lds_dwordx4 v10, s[6:7]
	v_mfma_f32_16x16x32_f16 v[80:83], v[140:143], v[164:167], v[80:83]
	v_mfma_f32_16x16x32_f16 v[84:87], v[140:143], v[168:171], v[84:87]
	s_waitcnt lgkmcnt(9)
	v_mfma_f32_16x16x32_f16 v[88:91], v[144:147], v[156:159], v[88:91]
	v_mfma_f32_16x16x32_f16 v[92:95], v[144:147], v[160:163], v[92:95]
	v_mfma_f32_16x16x32_f16 v[96:99], v[144:147], v[164:167], v[96:99]
	s_add_u32 m0, s28, 0x25000
	s_nop 0
	global_load_lds_dwordx4 v11, s[6:7]
	s_add_u32 s6, s6, s20
	s_addc_u32 s7, s7, 0
	v_mfma_f32_16x16x32_f16 v[100:103], v[144:147], v[168:171], v[100:103]
	s_waitcnt lgkmcnt(8)
	v_mfma_f32_16x16x32_f16 v[104:107], v[148:151], v[156:159], v[104:107]
	v_mfma_f32_16x16x32_f16 v[108:111], v[148:151], v[160:163], v[108:111]
	v_mfma_f32_16x16x32_f16 v[112:115], v[148:151], v[164:167], v[112:115]
	v_mfma_f32_16x16x32_f16 v[116:119], v[148:151], v[168:171], v[116:119]
	s_waitcnt vmcnt(6) lgkmcnt(0)
	s_barrier
	s_waitcnt lgkmcnt(7)
	ds_read_b128 v[136:139], v15 offset:53248
	ds_read_b128 v[156:159], v17 offset:53248
	ds_read_b128 v[160:163], v17 offset:55296
	ds_read_b128 v[164:167], v17 offset:57344
	ds_read_b128 v[168:171], v17 offset:59392
	ds_read_b128 v[140:143], v15 offset:55296
	ds_read_b128 v[144:147], v15 offset:57344
	ds_read_b128 v[148:151], v15 offset:59392
	s_waitcnt lgkmcnt(14)
	v_mfma_f32_16x16x32_f16 v[56:59], v[172:175], v[192:195], v[56:59]
	s_add_u32 m0, s28, 0x0
	s_nop 0
	global_load_lds_dwordx4 v10, s[4:5]
	s_waitcnt lgkmcnt(13)
	v_mfma_f32_16x16x32_f16 v[60:63], v[172:175], v[196:199], v[60:63]
	s_waitcnt lgkmcnt(12)
	v_mfma_f32_16x16x32_f16 v[64:67], v[172:175], v[200:203], v[64:67]
	s_waitcnt lgkmcnt(11)
	v_mfma_f32_16x16x32_f16 v[68:71], v[172:175], v[204:207], v[68:71]
	s_waitcnt lgkmcnt(10)
	v_mfma_f32_16x16x32_f16 v[72:75], v[176:179], v[192:195], v[72:75]
	v_mfma_f32_16x16x32_f16 v[76:79], v[176:179], v[196:199], v[76:79]
	s_add_u32 m0, s28, 0x2000
	s_nop 0
	global_load_lds_dwordx4 v11, s[4:5]
	v_mfma_f32_16x16x32_f16 v[80:83], v[176:179], v[200:203], v[80:83]
	v_mfma_f32_16x16x32_f16 v[84:87], v[176:179], v[204:207], v[84:87]
	s_waitcnt lgkmcnt(9)
	v_mfma_f32_16x16x32_f16 v[88:91], v[180:183], v[192:195], v[88:91]
	v_mfma_f32_16x16x32_f16 v[92:95], v[180:183], v[196:199], v[92:95]
	v_mfma_f32_16x16x32_f16 v[96:99], v[180:183], v[200:203], v[96:99]
	s_add_u32 m0, s28, 0x4000
	s_nop 0
	global_load_lds_dwordx4 v12, s[4:5]
	v_mfma_f32_16x16x32_f16 v[100:103], v[180:183], v[204:207], v[100:103]
	s_waitcnt lgkmcnt(8)
	v_mfma_f32_16x16x32_f16 v[104:107], v[184:187], v[192:195], v[104:107]
	v_mfma_f32_16x16x32_f16 v[108:111], v[184:187], v[196:199], v[108:111]
	v_mfma_f32_16x16x32_f16 v[112:115], v[184:187], v[200:203], v[112:115]
	v_mfma_f32_16x16x32_f16 v[116:119], v[184:187], v[204:207], v[116:119]
	s_waitcnt lgkmcnt(7)
	ds_read_b128 v[172:175], v16 offset:53248
	ds_read_b128 v[192:195], v18 offset:53248
	ds_read_b128 v[196:199], v18 offset:55296
	ds_read_b128 v[200:203], v18 offset:57344
	ds_read_b128 v[204:207], v18 offset:59392
	ds_read_b128 v[176:179], v16 offset:55296
	ds_read_b128 v[180:183], v16 offset:57344
	ds_read_b128 v[184:187], v16 offset:59392
	s_waitcnt lgkmcnt(14)
	v_mfma_f32_16x16x32_f16 v[56:59], v[136:139], v[156:159], v[56:59]
	s_add_u32 m0, s28, 0x6000
	s_nop 0
	global_load_lds_dwordx4 v13, s[4:5]
	s_add_u32 s4, s4, s20
	s_addc_u32 s5, s5, 0
	s_waitcnt lgkmcnt(13)
	v_mfma_f32_16x16x32_f16 v[60:63], v[136:139], v[160:163], v[60:63]
	s_waitcnt lgkmcnt(12)
	v_mfma_f32_16x16x32_f16 v[64:67], v[136:139], v[164:167], v[64:67]
	s_waitcnt lgkmcnt(11)
	v_mfma_f32_16x16x32_f16 v[68:71], v[136:139], v[168:171], v[68:71]
	s_waitcnt lgkmcnt(10)
	v_mfma_f32_16x16x32_f16 v[72:75], v[140:143], v[156:159], v[72:75]
	v_mfma_f32_16x16x32_f16 v[76:79], v[140:143], v[160:163], v[76:79]
	s_add_u32 m0, s28, 0x9000
	s_nop 0
	global_load_lds_dwordx4 v10, s[6:7]
	v_mfma_f32_16x16x32_f16 v[80:83], v[140:143], v[164:167], v[80:83]
	v_mfma_f32_16x16x32_f16 v[84:87], v[140:143], v[168:171], v[84:87]
	s_waitcnt lgkmcnt(9)
	v_mfma_f32_16x16x32_f16 v[88:91], v[144:147], v[156:159], v[88:91]
	v_mfma_f32_16x16x32_f16 v[92:95], v[144:147], v[160:163], v[92:95]
	v_mfma_f32_16x16x32_f16 v[96:99], v[144:147], v[164:167], v[96:99]
	s_add_u32 m0, s28, 0xb000
	s_nop 0
	global_load_lds_dwordx4 v11, s[6:7]
	s_add_u32 s6, s6, s20
	s_addc_u32 s7, s7, 0
	v_mfma_f32_16x16x32_f16 v[100:103], v[144:147], v[168:171], v[100:103]
	s_waitcnt lgkmcnt(8)
	v_mfma_f32_16x16x32_f16 v[104:107], v[148:151], v[156:159], v[104:107]
	v_mfma_f32_16x16x32_f16 v[108:111], v[148:151], v[160:163], v[108:111]
	v_mfma_f32_16x16x32_f16 v[112:115], v[148:151], v[164:167], v[112:115]
	v_mfma_f32_16x16x32_f16 v[116:119], v[148:151], v[168:171], v[116:119]
	s_waitcnt vmcnt(6) lgkmcnt(0)
	s_barrier
	s_waitcnt lgkmcnt(7)
	ds_read_b128 v[136:139], v19
	ds_read_b128 v[156:159], v21
	ds_read_b128 v[160:163], v21 offset:2048
	ds_read_b128 v[164:167], v21 offset:4096
	ds_read_b128 v[168:171], v21 offset:6144
	ds_read_b128 v[140:143], v19 offset:2048
	ds_read_b128 v[144:147], v19 offset:4096
	ds_read_b128 v[148:151], v19 offset:6144
	s_waitcnt lgkmcnt(14)
	v_mfma_f32_16x16x32_f16 v[56:59], v[172:175], v[192:195], v[56:59]
	s_add_u32 m0, s28, 0xd000
	s_nop 0
	global_load_lds_dwordx4 v10, s[4:5]
	s_waitcnt lgkmcnt(13)
	v_mfma_f32_16x16x32_f16 v[60:63], v[172:175], v[196:199], v[60:63]
	s_waitcnt lgkmcnt(12)
	v_mfma_f32_16x16x32_f16 v[64:67], v[172:175], v[200:203], v[64:67]
	s_waitcnt lgkmcnt(11)
	v_mfma_f32_16x16x32_f16 v[68:71], v[172:175], v[204:207], v[68:71]
	s_waitcnt lgkmcnt(10)
	v_mfma_f32_16x16x32_f16 v[72:75], v[176:179], v[192:195], v[72:75]
	v_mfma_f32_16x16x32_f16 v[76:79], v[176:179], v[196:199], v[76:79]
	s_add_u32 m0, s28, 0xf000
	s_nop 0
	global_load_lds_dwordx4 v11, s[4:5]
	v_mfma_f32_16x16x32_f16 v[80:83], v[176:179], v[200:203], v[80:83]
	v_mfma_f32_16x16x32_f16 v[84:87], v[176:179], v[204:207], v[84:87]
	s_waitcnt lgkmcnt(9)
	v_mfma_f32_16x16x32_f16 v[88:91], v[180:183], v[192:195], v[88:91]
	v_mfma_f32_16x16x32_f16 v[92:95], v[180:183], v[196:199], v[92:95]
	v_mfma_f32_16x16x32_f16 v[96:99], v[180:183], v[200:203], v[96:99]
	s_add_u32 m0, s28, 0x11000
	s_nop 0
	global_load_lds_dwordx4 v12, s[4:5]
	v_mfma_f32_16x16x32_f16 v[100:103], v[180:183], v[204:207], v[100:103]
	s_waitcnt lgkmcnt(8)
	v_mfma_f32_16x16x32_f16 v[104:107], v[184:187], v[192:195], v[104:107]
	v_mfma_f32_16x16x32_f16 v[108:111], v[184:187], v[196:199], v[108:111]
	v_mfma_f32_16x16x32_f16 v[112:115], v[184:187], v[200:203], v[112:115]
	v_mfma_f32_16x16x32_f16 v[116:119], v[184:187], v[204:207], v[116:119]
	s_waitcnt lgkmcnt(7)
	ds_read_b128 v[172:175], v20
	ds_read_b128 v[192:195], v22
	ds_read_b128 v[196:199], v22 offset:2048
	ds_read_b128 v[200:203], v22 offset:4096
	ds_read_b128 v[204:207], v22 offset:6144
	ds_read_b128 v[176:179], v20 offset:2048
	ds_read_b128 v[180:183], v20 offset:4096
	ds_read_b128 v[184:187], v20 offset:6144
	s_waitcnt lgkmcnt(14)
	v_mfma_f32_16x16x32_f16 v[56:59], v[136:139], v[156:159], v[56:59]
	s_add_u32 m0, s28, 0x13000
	s_nop 0
	global_load_lds_dwordx4 v13, s[4:5]
	s_add_u32 s4, s4, s20
	s_addc_u32 s5, s5, 0
	s_waitcnt lgkmcnt(13)
	v_mfma_f32_16x16x32_f16 v[60:63], v[136:139], v[160:163], v[60:63]
	s_waitcnt lgkmcnt(12)
	v_mfma_f32_16x16x32_f16 v[64:67], v[136:139], v[164:167], v[64:67]
	s_waitcnt lgkmcnt(11)
	v_mfma_f32_16x16x32_f16 v[68:71], v[136:139], v[168:171], v[68:71]
	s_waitcnt lgkmcnt(10)
	v_mfma_f32_16x16x32_f16 v[72:75], v[140:143], v[156:159], v[72:75]
	v_mfma_f32_16x16x32_f16 v[76:79], v[140:143], v[160:163], v[76:79]
	s_add_u32 m0, s28, 0x16000
	s_nop 0
	global_load_lds_dwordx4 v10, s[6:7]
	v_mfma_f32_16x16x32_f16 v[80:83], v[140:143], v[164:167], v[80:83]
	v_mfma_f32_16x16x32_f16 v[84:87], v[140:143], v[168:171], v[84:87]
	s_waitcnt lgkmcnt(9)
	v_mfma_f32_16x16x32_f16 v[88:91], v[144:147], v[156:159], v[88:91]
	v_mfma_f32_16x16x32_f16 v[92:95], v[144:147], v[160:163], v[92:95]
	v_mfma_f32_16x16x32_f16 v[96:99], v[144:147], v[164:167], v[96:99]
	s_add_u32 m0, s28, 0x18000
	s_nop 0
	global_load_lds_dwordx4 v11, s[6:7]
	s_add_u32 s6, s6, s20
	s_addc_u32 s7, s7, 0
	v_mfma_f32_16x16x32_f16 v[100:103], v[144:147], v[168:171], v[100:103]
	s_waitcnt lgkmcnt(8)
	v_mfma_f32_16x16x32_f16 v[104:107], v[148:151], v[156:159], v[104:107]
	v_mfma_f32_16x16x32_f16 v[108:111], v[148:151], v[160:163], v[108:111]
	v_mfma_f32_16x16x32_f16 v[112:115], v[148:151], v[164:167], v[112:115]
	v_mfma_f32_16x16x32_f16 v[116:119], v[148:151], v[168:171], v[116:119]
	s_waitcnt vmcnt(6) lgkmcnt(0)
	s_barrier
	s_waitcnt lgkmcnt(7)
	ds_read_b128 v[136:139], v15
	ds_read_b128 v[156:159], v17
	ds_read_b128 v[160:163], v17 offset:2048
	ds_read_b128 v[164:167], v17 offset:4096
	ds_read_b128 v[168:171], v17 offset:6144
	ds_read_b128 v[140:143], v15 offset:2048
	ds_read_b128 v[144:147], v15 offset:4096
	ds_read_b128 v[148:151], v15 offset:6144
	s_waitcnt lgkmcnt(14)
	v_mfma_f32_16x16x32_f16 v[56:59], v[172:175], v[192:195], v[56:59]
	s_add_u32 m0, s28, 0x1a000
	s_nop 0
	global_load_lds_dwordx4 v10, s[4:5]
	s_waitcnt lgkmcnt(13)
	v_mfma_f32_16x16x32_f16 v[60:63], v[172:175], v[196:199], v[60:63]
	s_waitcnt lgkmcnt(12)
	v_mfma_f32_16x16x32_f16 v[64:67], v[172:175], v[200:203], v[64:67]
	s_waitcnt lgkmcnt(11)
	v_mfma_f32_16x16x32_f16 v[68:71], v[172:175], v[204:207], v[68:71]
	s_waitcnt lgkmcnt(10)
	v_mfma_f32_16x16x32_f16 v[72:75], v[176:179], v[192:195], v[72:75]
	v_mfma_f32_16x16x32_f16 v[76:79], v[176:179], v[196:199], v[76:79]
	s_add_u32 m0, s28, 0x1c000
	s_nop 0
	global_load_lds_dwordx4 v11, s[4:5]
	v_mfma_f32_16x16x32_f16 v[80:83], v[176:179], v[200:203], v[80:83]
	v_mfma_f32_16x16x32_f16 v[84:87], v[176:179], v[204:207], v[84:87]
	s_waitcnt lgkmcnt(9)
	v_mfma_f32_16x16x32_f16 v[88:91], v[180:183], v[192:195], v[88:91]
	v_mfma_f32_16x16x32_f16 v[92:95], v[180:183], v[196:199], v[92:95]
	v_mfma_f32_16x16x32_f16 v[96:99], v[180:183], v[200:203], v[96:99]
	s_add_u32 m0, s28, 0x1e000
	s_nop 0
	global_load_lds_dwordx4 v12, s[4:5]
	v_mfma_f32_16x16x32_f16 v[100:103], v[180:183], v[204:207], v[100:103]
	s_waitcnt lgkmcnt(8)
	v_mfma_f32_16x16x32_f16 v[104:107], v[184:187], v[192:195], v[104:107]
	v_mfma_f32_16x16x32_f16 v[108:111], v[184:187], v[196:199], v[108:111]
	v_mfma_f32_16x16x32_f16 v[112:115], v[184:187], v[200:203], v[112:115]
	v_mfma_f32_16x16x32_f16 v[116:119], v[184:187], v[204:207], v[116:119]
	s_waitcnt lgkmcnt(7)
	ds_read_b128 v[172:175], v16
	ds_read_b128 v[192:195], v18
	ds_read_b128 v[196:199], v18 offset:2048
	ds_read_b128 v[200:203], v18 offset:4096
	ds_read_b128 v[204:207], v18 offset:6144
	ds_read_b128 v[176:179], v16 offset:2048
	ds_read_b128 v[180:183], v16 offset:4096
	ds_read_b128 v[184:187], v16 offset:6144
	s_waitcnt lgkmcnt(14)
	v_mfma_f32_16x16x32_f16 v[56:59], v[136:139], v[156:159], v[56:59]
	s_add_u32 m0, s28, 0x20000
	s_nop 0
	global_load_lds_dwordx4 v13, s[4:5]
	s_add_u32 s4, s4, s20
	s_addc_u32 s5, s5, 0
	s_waitcnt lgkmcnt(13)
	v_mfma_f32_16x16x32_f16 v[60:63], v[136:139], v[160:163], v[60:63]
	s_waitcnt lgkmcnt(12)
	v_mfma_f32_16x16x32_f16 v[64:67], v[136:139], v[164:167], v[64:67]
	s_waitcnt lgkmcnt(11)
	v_mfma_f32_16x16x32_f16 v[68:71], v[136:139], v[168:171], v[68:71]
	s_waitcnt lgkmcnt(10)
	v_mfma_f32_16x16x32_f16 v[72:75], v[140:143], v[156:159], v[72:75]
	v_mfma_f32_16x16x32_f16 v[76:79], v[140:143], v[160:163], v[76:79]
	s_add_u32 m0, s28, 0x23000
	s_nop 0
	global_load_lds_dwordx4 v10, s[6:7]
	v_mfma_f32_16x16x32_f16 v[80:83], v[140:143], v[164:167], v[80:83]
	v_mfma_f32_16x16x32_f16 v[84:87], v[140:143], v[168:171], v[84:87]
	s_waitcnt lgkmcnt(9)
	v_mfma_f32_16x16x32_f16 v[88:91], v[144:147], v[156:159], v[88:91]
	v_mfma_f32_16x16x32_f16 v[92:95], v[144:147], v[160:163], v[92:95]
	v_mfma_f32_16x16x32_f16 v[96:99], v[144:147], v[164:167], v[96:99]
	s_add_u32 m0, s28, 0x25000
	s_nop 0
	global_load_lds_dwordx4 v11, s[6:7]
	s_add_u32 s6, s6, s20
	s_addc_u32 s7, s7, 0
	v_mfma_f32_16x16x32_f16 v[100:103], v[144:147], v[168:171], v[100:103]
	s_waitcnt lgkmcnt(8)
	v_mfma_f32_16x16x32_f16 v[104:107], v[148:151], v[156:159], v[104:107]
	v_mfma_f32_16x16x32_f16 v[108:111], v[148:151], v[160:163], v[108:111]
	v_mfma_f32_16x16x32_f16 v[112:115], v[148:151], v[164:167], v[112:115]
	v_mfma_f32_16x16x32_f16 v[116:119], v[148:151], v[168:171], v[116:119]
	s_waitcnt vmcnt(6) lgkmcnt(0)
	s_barrier
	s_waitcnt lgkmcnt(7)
	ds_read_b128 v[136:139], v15 offset:53248
	ds_read_b128 v[156:159], v17 offset:53248
	ds_read_b128 v[160:163], v17 offset:55296
	ds_read_b128 v[164:167], v17 offset:57344
	ds_read_b128 v[168:171], v17 offset:59392
	ds_read_b128 v[140:143], v15 offset:55296
	ds_read_b128 v[144:147], v15 offset:57344
	ds_read_b128 v[148:151], v15 offset:59392
	s_waitcnt lgkmcnt(14)
	v_mfma_f32_16x16x32_f16 v[56:59], v[172:175], v[192:195], v[56:59]
	s_add_u32 m0, s28, 0x0
	s_nop 0
	global_load_lds_dwordx4 v10, s[4:5]
	s_waitcnt lgkmcnt(13)
	v_mfma_f32_16x16x32_f16 v[60:63], v[172:175], v[196:199], v[60:63]
	s_waitcnt lgkmcnt(12)
	v_mfma_f32_16x16x32_f16 v[64:67], v[172:175], v[200:203], v[64:67]
	s_waitcnt lgkmcnt(11)
	v_mfma_f32_16x16x32_f16 v[68:71], v[172:175], v[204:207], v[68:71]
	s_waitcnt lgkmcnt(10)
	v_mfma_f32_16x16x32_f16 v[72:75], v[176:179], v[192:195], v[72:75]
	v_mfma_f32_16x16x32_f16 v[76:79], v[176:179], v[196:199], v[76:79]
	s_add_u32 m0, s28, 0x2000
	s_nop 0
	global_load_lds_dwordx4 v11, s[4:5]
	v_mfma_f32_16x16x32_f16 v[80:83], v[176:179], v[200:203], v[80:83]
	v_mfma_f32_16x16x32_f16 v[84:87], v[176:179], v[204:207], v[84:87]
	s_waitcnt lgkmcnt(9)
	v_mfma_f32_16x16x32_f16 v[88:91], v[180:183], v[192:195], v[88:91]
	v_mfma_f32_16x16x32_f16 v[92:95], v[180:183], v[196:199], v[92:95]
	v_mfma_f32_16x16x32_f16 v[96:99], v[180:183], v[200:203], v[96:99]
	s_add_u32 m0, s28, 0x4000
	s_nop 0
	global_load_lds_dwordx4 v12, s[4:5]
	v_mfma_f32_16x16x32_f16 v[100:103], v[180:183], v[204:207], v[100:103]
	s_waitcnt lgkmcnt(8)
	v_mfma_f32_16x16x32_f16 v[104:107], v[184:187], v[192:195], v[104:107]
	v_mfma_f32_16x16x32_f16 v[108:111], v[184:187], v[196:199], v[108:111]
	v_mfma_f32_16x16x32_f16 v[112:115], v[184:187], v[200:203], v[112:115]
	v_mfma_f32_16x16x32_f16 v[116:119], v[184:187], v[204:207], v[116:119]
	s_waitcnt lgkmcnt(7)
	ds_read_b128 v[172:175], v16 offset:53248
	ds_read_b128 v[192:195], v18 offset:53248
	ds_read_b128 v[196:199], v18 offset:55296
	ds_read_b128 v[200:203], v18 offset:57344
	ds_read_b128 v[204:207], v18 offset:59392
	ds_read_b128 v[176:179], v16 offset:55296
	ds_read_b128 v[180:183], v16 offset:57344
	ds_read_b128 v[184:187], v16 offset:59392
	s_waitcnt lgkmcnt(14)
	v_mfma_f32_16x16x32_f16 v[56:59], v[136:139], v[156:159], v[56:59]
	s_add_u32 m0, s28, 0x6000
	s_nop 0
	global_load_lds_dwordx4 v13, s[4:5]
	s_add_u32 s4, s4, s20
	s_addc_u32 s5, s5, 0
	s_waitcnt lgkmcnt(13)
	v_mfma_f32_16x16x32_f16 v[60:63], v[136:139], v[160:163], v[60:63]
	s_waitcnt lgkmcnt(12)
	v_mfma_f32_16x16x32_f16 v[64:67], v[136:139], v[164:167], v[64:67]
	s_waitcnt lgkmcnt(11)
	v_mfma_f32_16x16x32_f16 v[68:71], v[136:139], v[168:171], v[68:71]
	s_waitcnt lgkmcnt(10)
	v_mfma_f32_16x16x32_f16 v[72:75], v[140:143], v[156:159], v[72:75]
	v_mfma_f32_16x16x32_f16 v[76:79], v[140:143], v[160:163], v[76:79]
	s_add_u32 m0, s28, 0x9000
	s_nop 0
	global_load_lds_dwordx4 v10, s[6:7]
	v_mfma_f32_16x16x32_f16 v[80:83], v[140:143], v[164:167], v[80:83]
	v_mfma_f32_16x16x32_f16 v[84:87], v[140:143], v[168:171], v[84:87]
	s_waitcnt lgkmcnt(9)
	v_mfma_f32_16x16x32_f16 v[88:91], v[144:147], v[156:159], v[88:91]
	v_mfma_f32_16x16x32_f16 v[92:95], v[144:147], v[160:163], v[92:95]
	v_mfma_f32_16x16x32_f16 v[96:99], v[144:147], v[164:167], v[96:99]
	s_add_u32 m0, s28, 0xb000
	s_nop 0
	global_load_lds_dwordx4 v11, s[6:7]
	s_add_u32 s6, s6, s20
	s_addc_u32 s7, s7, 0
	v_mfma_f32_16x16x32_f16 v[100:103], v[144:147], v[168:171], v[100:103]
	s_waitcnt lgkmcnt(8)
	v_mfma_f32_16x16x32_f16 v[104:107], v[148:151], v[156:159], v[104:107]
	v_mfma_f32_16x16x32_f16 v[108:111], v[148:151], v[160:163], v[108:111]
	v_mfma_f32_16x16x32_f16 v[112:115], v[148:151], v[164:167], v[112:115]
	v_mfma_f32_16x16x32_f16 v[116:119], v[148:151], v[168:171], v[116:119]
	s_waitcnt vmcnt(6) lgkmcnt(0)
	s_barrier
	s_waitcnt lgkmcnt(7)
	ds_read_b128 v[136:139], v19
	ds_read_b128 v[156:159], v21
	ds_read_b128 v[160:163], v21 offset:2048
	ds_read_b128 v[164:167], v21 offset:4096
	ds_read_b128 v[168:171], v21 offset:6144
	ds_read_b128 v[140:143], v19 offset:2048
	ds_read_b128 v[144:147], v19 offset:4096
	ds_read_b128 v[148:151], v19 offset:6144
	s_waitcnt lgkmcnt(14)
	v_mfma_f32_16x16x32_f16 v[56:59], v[172:175], v[192:195], v[56:59]
	s_waitcnt lgkmcnt(13)
	v_mfma_f32_16x16x32_f16 v[60:63], v[172:175], v[196:199], v[60:63]
	s_waitcnt lgkmcnt(12)
	v_mfma_f32_16x16x32_f16 v[64:67], v[172:175], v[200:203], v[64:67]
	s_waitcnt lgkmcnt(11)
	v_mfma_f32_16x16x32_f16 v[68:71], v[172:175], v[204:207], v[68:71]
	s_waitcnt lgkmcnt(10)
	v_mfma_f32_16x16x32_f16 v[72:75], v[176:179], v[192:195], v[72:75]
	v_mfma_f32_16x16x32_f16 v[76:79], v[176:179], v[196:199], v[76:79]
	v_mfma_f32_16x16x32_f16 v[80:83], v[176:179], v[200:203], v[80:83]
	v_mfma_f32_16x16x32_f16 v[84:87], v[176:179], v[204:207], v[84:87]
	s_waitcnt lgkmcnt(9)
	v_mfma_f32_16x16x32_f16 v[88:91], v[180:183], v[192:195], v[88:91]
	v_mfma_f32_16x16x32_f16 v[92:95], v[180:183], v[196:199], v[92:95]
	v_mfma_f32_16x16x32_f16 v[96:99], v[180:183], v[200:203], v[96:99]
	v_mfma_f32_16x16x32_f16 v[100:103], v[180:183], v[204:207], v[100:103]
	s_waitcnt lgkmcnt(8)
	v_mfma_f32_16x16x32_f16 v[104:107], v[184:187], v[192:195], v[104:107]
	v_mfma_f32_16x16x32_f16 v[108:111], v[184:187], v[196:199], v[108:111]
	v_mfma_f32_16x16x32_f16 v[112:115], v[184:187], v[200:203], v[112:115]
	v_mfma_f32_16x16x32_f16 v[116:119], v[184:187], v[204:207], v[116:119]
	s_waitcnt lgkmcnt(7)
	ds_read_b128 v[172:175], v20
	ds_read_b128 v[192:195], v22
	ds_read_b128 v[196:199], v22 offset:2048
	ds_read_b128 v[200:203], v22 offset:4096
	ds_read_b128 v[204:207], v22 offset:6144
	ds_read_b128 v[176:179], v20 offset:2048
	ds_read_b128 v[180:183], v20 offset:4096
	ds_read_b128 v[184:187], v20 offset:6144
	s_waitcnt lgkmcnt(14)
	v_mfma_f32_16x16x32_f16 v[56:59], v[136:139], v[156:159], v[56:59]
	s_waitcnt lgkmcnt(13)
	v_mfma_f32_16x16x32_f16 v[60:63], v[136:139], v[160:163], v[60:63]
	s_waitcnt lgkmcnt(12)
	v_mfma_f32_16x16x32_f16 v[64:67], v[136:139], v[164:167], v[64:67]
	s_waitcnt lgkmcnt(11)
	v_mfma_f32_16x16x32_f16 v[68:71], v[136:139], v[168:171], v[68:71]
	s_waitcnt lgkmcnt(10)
	v_mfma_f32_16x16x32_f16 v[72:75], v[140:143], v[156:159], v[72:75]
	v_mfma_f32_16x16x32_f16 v[76:79], v[140:143], v[160:163], v[76:79]
	v_mfma_f32_16x16x32_f16 v[80:83], v[140:143], v[164:167], v[80:83]
	v_mfma_f32_16x16x32_f16 v[84:87], v[140:143], v[168:171], v[84:87]
	s_waitcnt lgkmcnt(9)
	v_mfma_f32_16x16x32_f16 v[88:91], v[144:147], v[156:159], v[88:91]
	v_mfma_f32_16x16x32_f16 v[92:95], v[144:147], v[160:163], v[92:95]
	v_mfma_f32_16x16x32_f16 v[96:99], v[144:147], v[164:167], v[96:99]
	v_mfma_f32_16x16x32_f16 v[100:103], v[144:147], v[168:171], v[100:103]
	s_waitcnt lgkmcnt(8)
	v_mfma_f32_16x16x32_f16 v[104:107], v[148:151], v[156:159], v[104:107]
	v_mfma_f32_16x16x32_f16 v[108:111], v[148:151], v[160:163], v[108:111]
	v_mfma_f32_16x16x32_f16 v[112:115], v[148:151], v[164:167], v[112:115]
	v_mfma_f32_16x16x32_f16 v[116:119], v[148:151], v[168:171], v[116:119]
	s_waitcnt vmcnt(0) lgkmcnt(0)
	s_barrier
	s_waitcnt lgkmcnt(7)
	ds_read_b128 v[136:139], v15
	ds_read_b128 v[156:159], v17
	ds_read_b128 v[160:163], v17 offset:2048
	ds_read_b128 v[164:167], v17 offset:4096
	ds_read_b128 v[168:171], v17 offset:6144
	ds_read_b128 v[140:143], v15 offset:2048
	ds_read_b128 v[144:147], v15 offset:4096
	ds_read_b128 v[148:151], v15 offset:6144
	s_waitcnt lgkmcnt(14)
	v_mfma_f32_16x16x32_f16 v[56:59], v[172:175], v[192:195], v[56:59]
	s_waitcnt lgkmcnt(13)
	v_mfma_f32_16x16x32_f16 v[60:63], v[172:175], v[196:199], v[60:63]
	s_waitcnt lgkmcnt(12)
	v_mfma_f32_16x16x32_f16 v[64:67], v[172:175], v[200:203], v[64:67]
	s_waitcnt lgkmcnt(11)
	v_mfma_f32_16x16x32_f16 v[68:71], v[172:175], v[204:207], v[68:71]
	s_waitcnt lgkmcnt(10)
	v_mfma_f32_16x16x32_f16 v[72:75], v[176:179], v[192:195], v[72:75]
	v_mfma_f32_16x16x32_f16 v[76:79], v[176:179], v[196:199], v[76:79]
	v_mfma_f32_16x16x32_f16 v[80:83], v[176:179], v[200:203], v[80:83]
	v_mfma_f32_16x16x32_f16 v[84:87], v[176:179], v[204:207], v[84:87]
	s_waitcnt lgkmcnt(9)
	v_mfma_f32_16x16x32_f16 v[88:91], v[180:183], v[192:195], v[88:91]
	v_mfma_f32_16x16x32_f16 v[92:95], v[180:183], v[196:199], v[92:95]
	v_mfma_f32_16x16x32_f16 v[96:99], v[180:183], v[200:203], v[96:99]
	v_mfma_f32_16x16x32_f16 v[100:103], v[180:183], v[204:207], v[100:103]
	s_waitcnt lgkmcnt(8)
	v_mfma_f32_16x16x32_f16 v[104:107], v[184:187], v[192:195], v[104:107]
	v_mfma_f32_16x16x32_f16 v[108:111], v[184:187], v[196:199], v[108:111]
	v_mfma_f32_16x16x32_f16 v[112:115], v[184:187], v[200:203], v[112:115]
	v_mfma_f32_16x16x32_f16 v[116:119], v[184:187], v[204:207], v[116:119]
	s_waitcnt lgkmcnt(7)
	ds_read_b128 v[172:175], v16
	ds_read_b128 v[192:195], v18
	ds_read_b128 v[196:199], v18 offset:2048
	ds_read_b128 v[200:203], v18 offset:4096
	ds_read_b128 v[204:207], v18 offset:6144
	ds_read_b128 v[176:179], v16 offset:2048
	ds_read_b128 v[180:183], v16 offset:4096
	ds_read_b128 v[184:187], v16 offset:6144
	s_waitcnt lgkmcnt(14)
	v_mfma_f32_16x16x32_f16 v[56:59], v[136:139], v[156:159], v[56:59]
	s_waitcnt lgkmcnt(13)
	v_mfma_f32_16x16x32_f16 v[60:63], v[136:139], v[160:163], v[60:63]
	s_waitcnt lgkmcnt(12)
	v_mfma_f32_16x16x32_f16 v[64:67], v[136:139], v[164:167], v[64:67]
	s_waitcnt lgkmcnt(11)
	v_mfma_f32_16x16x32_f16 v[68:71], v[136:139], v[168:171], v[68:71]
	s_waitcnt lgkmcnt(10)
	v_mfma_f32_16x16x32_f16 v[72:75], v[140:143], v[156:159], v[72:75]
	v_mfma_f32_16x16x32_f16 v[76:79], v[140:143], v[160:163], v[76:79]
	v_mfma_f32_16x16x32_f16 v[80:83], v[140:143], v[164:167], v[80:83]
	v_mfma_f32_16x16x32_f16 v[84:87], v[140:143], v[168:171], v[84:87]
	s_waitcnt lgkmcnt(9)
	v_mfma_f32_16x16x32_f16 v[88:91], v[144:147], v[156:159], v[88:91]
	v_mfma_f32_16x16x32_f16 v[92:95], v[144:147], v[160:163], v[92:95]
	v_mfma_f32_16x16x32_f16 v[96:99], v[144:147], v[164:167], v[96:99]
	v_mfma_f32_16x16x32_f16 v[100:103], v[144:147], v[168:171], v[100:103]
	s_waitcnt lgkmcnt(8)
	v_mfma_f32_16x16x32_f16 v[104:107], v[148:151], v[156:159], v[104:107]
	v_mfma_f32_16x16x32_f16 v[108:111], v[148:151], v[160:163], v[108:111]
	v_mfma_f32_16x16x32_f16 v[112:115], v[148:151], v[164:167], v[112:115]
	v_mfma_f32_16x16x32_f16 v[116:119], v[148:151], v[168:171], v[116:119]
	s_waitcnt lgkmcnt(6)
	v_mfma_f32_16x16x32_f16 v[56:59], v[172:175], v[192:195], v[56:59]
	s_waitcnt lgkmcnt(5)
	v_mfma_f32_16x16x32_f16 v[60:63], v[172:175], v[196:199], v[60:63]
	s_waitcnt lgkmcnt(4)
	v_mfma_f32_16x16x32_f16 v[64:67], v[172:175], v[200:203], v[64:67]
	s_waitcnt lgkmcnt(3)
	v_mfma_f32_16x16x32_f16 v[68:71], v[172:175], v[204:207], v[68:71]
	s_waitcnt lgkmcnt(2)
	v_mfma_f32_16x16x32_f16 v[72:75], v[176:179], v[192:195], v[72:75]
	v_mfma_f32_16x16x32_f16 v[76:79], v[176:179], v[196:199], v[76:79]
	v_mfma_f32_16x16x32_f16 v[80:83], v[176:179], v[200:203], v[80:83]
	v_mfma_f32_16x16x32_f16 v[84:87], v[176:179], v[204:207], v[84:87]
	s_waitcnt lgkmcnt(1)
	v_mfma_f32_16x16x32_f16 v[88:91], v[180:183], v[192:195], v[88:91]
	v_mfma_f32_16x16x32_f16 v[92:95], v[180:183], v[196:199], v[92:95]
	v_mfma_f32_16x16x32_f16 v[96:99], v[180:183], v[200:203], v[96:99]
	v_mfma_f32_16x16x32_f16 v[100:103], v[180:183], v[204:207], v[100:103]
	s_waitcnt lgkmcnt(0)
	v_mfma_f32_16x16x32_f16 v[104:107], v[184:187], v[192:195], v[104:107]
	v_mfma_f32_16x16x32_f16 v[108:111], v[184:187], v[196:199], v[108:111]
	v_mfma_f32_16x16x32_f16 v[112:115], v[184:187], v[200:203], v[112:115]
	v_mfma_f32_16x16x32_f16 v[116:119], v[184:187], v[204:207], v[116:119]
	s_nop 7
	s_nop 1
	s_add_u32 s24, s29, 0
	s_lshl_b32 s8, s24, 11
	s_nop 0
	v_add_u32_e32 v212, s8, v23
	v_add_f32_e32 v56, v56, v24
	v_add_f32_e32 v57, v57, v24
	v_add_f32_e32 v58, v58, v24
	v_add_f32_e32 v59, v59, v24
	v_cvt_pk_f16_f32 v56, v56, v57
	v_cvt_pk_f16_f32 v57, v58, v59
	global_store_dwordx2 v212, v[56:57], s[22:23] offset:0
	v_add_f32_e32 v60, v60, v25
	v_add_f32_e32 v61, v61, v25
	v_add_f32_e32 v62, v62, v25
	v_add_f32_e32 v63, v63, v25
	v_cvt_pk_f16_f32 v60, v60, v61
	v_cvt_pk_f16_f32 v61, v62, v63
	global_store_dwordx2 v212, v[60:61], s[22:23] offset:256
	v_add_f32_e32 v64, v64, v26
	v_add_f32_e32 v65, v65, v26
	v_add_f32_e32 v66, v66, v26
	v_add_f32_e32 v67, v67, v26
	v_cvt_pk_f16_f32 v64, v64, v65
	v_cvt_pk_f16_f32 v65, v66, v67
	global_store_dwordx2 v212, v[64:65], s[22:23] offset:1024
	v_add_f32_e32 v68, v68, v27
	v_add_f32_e32 v69, v69, v27
	v_add_f32_e32 v70, v70, v27
	v_add_f32_e32 v71, v71, v27
	v_cvt_pk_f16_f32 v68, v68, v69
	v_cvt_pk_f16_f32 v69, v70, v71
	global_store_dwordx2 v212, v[68:69], s[22:23] offset:1280
	s_add_u32 s24, s29, 1
	s_lshl_b32 s8, s24, 11
	s_nop 0
	v_add_u32_e32 v212, s8, v23
	v_add_f32_e32 v72, v72, v24
	v_add_f32_e32 v73, v73, v24
	v_add_f32_e32 v74, v74, v24
	v_add_f32_e32 v75, v75, v24
	v_cvt_pk_f16_f32 v72, v72, v73
	v_cvt_pk_f16_f32 v73, v74, v75
	global_store_dwordx2 v212, v[72:73], s[22:23] offset:0
	v_add_f32_e32 v76, v76, v25
	v_add_f32_e32 v77, v77, v25
	v_add_f32_e32 v78, v78, v25
	v_add_f32_e32 v79, v79, v25
	v_cvt_pk_f16_f32 v76, v76, v77
	v_cvt_pk_f16_f32 v77, v78, v79
	global_store_dwordx2 v212, v[76:77], s[22:23] offset:256
	v_add_f32_e32 v80, v80, v26
	v_add_f32_e32 v81, v81, v26
	v_add_f32_e32 v82, v82, v26
	v_add_f32_e32 v83, v83, v26
	v_cvt_pk_f16_f32 v80, v80, v81
	v_cvt_pk_f16_f32 v81, v82, v83
	global_store_dwordx2 v212, v[80:81], s[22:23] offset:1024
	v_add_f32_e32 v84, v84, v27
	v_add_f32_e32 v85, v85, v27
	v_add_f32_e32 v86, v86, v27
	v_add_f32_e32 v87, v87, v27
	v_cvt_pk_f16_f32 v84, v84, v85
	v_cvt_pk_f16_f32 v85, v86, v87
	global_store_dwordx2 v212, v[84:85], s[22:23] offset:1280
	s_add_u32 s24, s29, 2
	s_lshl_b32 s8, s24, 11
	s_nop 0
	v_add_u32_e32 v212, s8, v23
	v_add_f32_e32 v88, v88, v24
	v_add_f32_e32 v89, v89, v24
	v_add_f32_e32 v90, v90, v24
	v_add_f32_e32 v91, v91, v24
	v_cvt_pk_f16_f32 v88, v88, v89
	v_cvt_pk_f16_f32 v89, v90, v91
	global_store_dwordx2 v212, v[88:89], s[22:23] offset:0
	v_add_f32_e32 v92, v92, v25
	v_add_f32_e32 v93, v93, v25
	v_add_f32_e32 v94, v94, v25
	v_add_f32_e32 v95, v95, v25
	v_cvt_pk_f16_f32 v92, v92, v93
	v_cvt_pk_f16_f32 v93, v94, v95
	global_store_dwordx2 v212, v[92:93], s[22:23] offset:256
	v_add_f32_e32 v96, v96, v26
	v_add_f32_e32 v97, v97, v26
	v_add_f32_e32 v98, v98, v26
	v_add_f32_e32 v99, v99, v26
	v_cvt_pk_f16_f32 v96, v96, v97
	v_cvt_pk_f16_f32 v97, v98, v99
	global_store_dwordx2 v212, v[96:97], s[22:23] offset:1024
	v_add_f32_e32 v100, v100, v27
	v_add_f32_e32 v101, v101, v27
	v_add_f32_e32 v102, v102, v27
	v_add_f32_e32 v103, v103, v27
	v_cvt_pk_f16_f32 v100, v100, v101
	v_cvt_pk_f16_f32 v101, v102, v103
	global_store_dwordx2 v212, v[100:101], s[22:23] offset:1280
	s_add_u32 s24, s29, 3
	s_lshl_b32 s8, s24, 11
	s_nop 0
	v_add_u32_e32 v212, s8, v23
	v_add_f32_e32 v104, v104, v24
	v_add_f32_e32 v105, v105, v24
	v_add_f32_e32 v106, v106, v24
	v_add_f32_e32 v107, v107, v24
	v_cvt_pk_f16_f32 v104, v104, v105
	v_cvt_pk_f16_f32 v105, v106, v107
	global_store_dwordx2 v212, v[104:105], s[22:23] offset:0
	v_add_f32_e32 v108, v108, v25
	v_add_f32_e32 v109, v109, v25
	v_add_f32_e32 v110, v110, v25
	v_add_f32_e32 v111, v111, v25
	v_cvt_pk_f16_f32 v108, v108, v109
	v_cvt_pk_f16_f32 v109, v110, v111
	global_store_dwordx2 v212, v[108:109], s[22:23] offset:256
	v_add_f32_e32 v112, v112, v26
	v_add_f32_e32 v113, v113, v26
	v_add_f32_e32 v114, v114, v26
	v_add_f32_e32 v115, v115, v26
	v_cvt_pk_f16_f32 v112, v112, v113
	v_cvt_pk_f16_f32 v113, v114, v115
	global_store_dwordx2 v212, v[112:113], s[22:23] offset:1024
	v_add_f32_e32 v116, v116, v27
	v_add_f32_e32 v117, v117, v27
	v_add_f32_e32 v118, v118, v27
	v_add_f32_e32 v119, v119, v27
	v_cvt_pk_f16_f32 v116, v116, v117
	v_cvt_pk_f16_f32 v117, v118, v119
	global_store_dwordx2 v212, v[116:117], s[22:23] offset:1280
	s_branch .Lpf_done
